# group-norm phase: per-row wave sums via DPP/permlane instead of ds_bpermute, counted vmcnt wait per row, LD loads as global loads
# speedup vs baseline: 1.0022x; 1.0022x over previous
; #define GAS __attribute__((address_space(1)))
; __device__ __forceinline__ void norm_load(NormRow& R, int m, int lane, const bf16* O, const bf16* GF, const bf16* OD, const float* LD) {
;     R.oa = __builtin_nontemporal_load((const GAS v4u*)(O + (size_t)m * DM + 8 * lane));
;     if (lane < 16) { R.oc = __builtin_nontemporal_load((const GAS v4u*)(O + (size_t)m * DM + 512 + 8 * lane)); R.gc = __builtin_nontemporal_load((const GAS v4u*)(GF + (size_t)m * 384 + 256 + 8 * lane)); }
;     else { const int dc = 8 * lane - 128, hd = dc >> 6;
;         R.d0 = __builtin_nontemporal_load((const GAS v4u*)(OD + (size_t)m * 384 + dc)); R.d1 = __builtin_nontemporal_load((const GAS v4u*)(OD + OD_BRANCH + (size_t)m * 384 + dc)); R.d2 = __builtin_nontemporal_load((const GAS v4u*)(OD + 2 * OD_BRANCH + (size_t)m * 384 + dc));
;         R.l0 = LD[(size_t)m * 8 + hd]; R.l1 = LD[LD_BRANCH + (size_t)m * 8 + hd]; R.l2 = LD[2 * LD_BRANCH + (size_t)m * 8 + hd]; }
;     if (lane >= 32) R.ga = __builtin_nontemporal_load((const GAS v4u*)(GF + (size_t)m * 384 + 8 * lane - 256));
; }
; __device__ __forceinline__ void norm_phase(Frame& F, const bf16* O, const bf16* GF, const bf16* OD, const float* LD, bf16* Y) {
;     const int g = F.vcu >> 5, r = F.vcu & 31, lane = F.lane;
;     const int base = g * SEQ + ((r & 7) + ((r >> 4) << 3)) * 256 + ((r >> 3) & 1) * 128 + F.wave * 16;
;     NormRow R0, R1, R2, R3;
;     norm_load(R0, base, lane, O, GF, OD, LD); norm_load(R1, base + 1, lane, O, GF, OD, LD); norm_load(R2, base + 2, lane, O, GF, OD, LD); norm_load(R3, base + 3, lane, O, GF, OD, LD);
.LBB0_70:
	v_readlane_b32 s0, v254, 27
	s_cmp_eq_u32 s0, 2
	s_mov_b64 s[0:1], -1
	s_cbranch_scc0 .LBB0_272
	v_readlane_b32 s0, v254, 13
	v_readlane_b32 s1, v254, 14
	s_mov_b32 s12, s0
	s_ashr_i32 s0, s0, 5
	s_mul_hi_i32 s1, s0, 0x1800000
	s_mul_i32 s0, s0, 0x1800000
	s_add_u32 s0, s74, s0
	s_addc_u32 s1, s75, s1
	s_add_u32 s24, s0, 0x8000000
	s_addc_u32 s25, s1, 0
	s_add_u32 s29, s0, 0x9800000
	s_addc_u32 s30, s1, 0
	s_add_u32 s6, s74, 0x18000000
	s_addc_u32 s7, s75, 0
	s_add_u32 s0, s74, 0x19800000
	s_addc_u32 s1, s75, 0
	s_add_u32 s26, s74, 0x3800000
	s_addc_u32 s27, s75, 0
	s_lshr_b32 s10, s12, 1
	s_lshl_b32 s8, s12, 7
	s_and_b32 s9, s12, 7
	s_and_b32 s10, s10, 8
	s_and_b32 s8, s8, 0xfffff000
	s_or_b32 s9, s10, s9
	s_lshl_b32 s10, s12, 4
	s_lshl_b32 s11, s72, 4
	s_and_b32 s10, s10, 0x80
	s_add_i32 s8, s8, s11
	s_lshl_b32 s9, s9, 8
	s_add_i32 s8, s8, s10
	s_add_i32 s8, s8, s9
	s_ashr_i32 s9, s8, 31
	s_lshl_b64 s[14:15], s[8:9], 11
	s_add_u32 s10, s29, s14
	s_addc_u32 s11, s30, s15
	s_waitcnt vmcnt(0)
	v_lshlrev_b32_e32 v2, 4, v194
	global_load_dwordx4 v[102:105], v2, s[10:11] nt
	v_lshlrev_b32_e32 v0, 3, v194
	v_cmp_gt_u32_e64 s[34:35], 16, v194
	v_cmp_lt_u32_e64 s[38:39], 15, v194
	v_add_u32_e32 v114, 0xffffff80, v0
	s_mul_hi_i32 s16, s8, 0x300
	s_mul_i32 s17, s8, 0x300
	s_and_saveexec_b64 s[12:13], s[38:39]
	s_xor_b64 s[12:13], exec, s[12:13]
	s_cbranch_execz .LBB0_73
	s_add_u32 s18, s0, s17
	v_ashrrev_i32_e32 v115, 31, v114
	s_addc_u32 s19, s1, s16
	v_lshlrev_b64 v[4:5], 1, v[114:115]
	v_lshl_add_u64 v[6:7], s[18:19], 0, v[4:5]
	s_add_u32 s18, s74, s17
	s_addc_u32 s19, s75, s16
	v_lshl_add_u64 v[4:5], s[18:19], 0, v[4:5]
	s_mov_b32 s3, 0x1b000000
	global_load_dwordx4 v[82:85], v[6:7], off nt
	v_add_co_u32_e32 v6, vcc, s3, v4
	s_lshl_b64 s[18:19], s[8:9], 5
	v_ashrrev_i32_e32 v2, 6, v114
	v_addc_co_u32_e32 v7, vcc, 0, v5, vcc
	s_mov_b32 s3, 0x1c800000
	s_add_u32 s18, s26, s18
	v_add_co_u32_e32 v4, vcc, s3, v4
	v_ashrrev_i32_e32 v3, 31, v2
	s_addc_u32 s19, s27, s19
	v_addc_co_u32_e32 v5, vcc, 0, v5, vcc
	v_lshl_add_u64 v[2:3], v[2:3], 2, s[18:19]
	global_load_dwordx4 v[86:89], v[6:7], off nt
	global_load_dwordx4 v[90:93], v[4:5], off nt
	v_add_co_u32_e32 v4, vcc, 0x100000, v2
	global_load_dword v173, v[2:3], off
	s_nop 0
	v_addc_co_u32_e32 v5, vcc, 0, v3, vcc
	v_add_co_u32_e32 v2, vcc, 0x200000, v2
	global_load_dword v174, v[4:5], off
	s_nop 0
	v_addc_co_u32_e32 v3, vcc, 0, v3, vcc
	global_load_dword v175, v[2:3], off

; #define GAS __attribute__((address_space(1)))
; __device__ __forceinline__ void norm_load(NormRow& R, int m, int lane, const bf16* O, const bf16* GF, const bf16* OD, const float* LD) {
;     R.oa = __builtin_nontemporal_load((const GAS v4u*)(O + (size_t)m * DM + 8 * lane));
;     if (lane < 16) { R.oc = __builtin_nontemporal_load((const GAS v4u*)(O + (size_t)m * DM + 512 + 8 * lane)); R.gc = __builtin_nontemporal_load((const GAS v4u*)(GF + (size_t)m * 384 + 256 + 8 * lane)); }
;     else { const int dc = 8 * lane - 128, hd = dc >> 6;
;         R.d0 = __builtin_nontemporal_load((const GAS v4u*)(OD + (size_t)m * 384 + dc)); R.d1 = __builtin_nontemporal_load((const GAS v4u*)(OD + OD_BRANCH + (size_t)m * 384 + dc)); R.d2 = __builtin_nontemporal_load((const GAS v4u*)(OD + 2 * OD_BRANCH + (size_t)m * 384 + dc));
;         R.l0 = LD[(size_t)m * 8 + hd]; R.l1 = LD[LD_BRANCH + (size_t)m * 8 + hd]; R.l2 = LD[2 * LD_BRANCH + (size_t)m * 8 + hd]; }
;     if (lane >= 32) R.ga = __builtin_nontemporal_load((const GAS v4u*)(GF + (size_t)m * 384 + 8 * lane - 256));
; }
.LBB0_77:
	s_or_b64 exec, exec, s[10:11]
	s_or_b32 s18, s8, 1
	s_ashr_i32 s19, s18, 31
	s_lshl_b64 s[16:17], s[18:19], 11
	s_add_u32 s10, s29, s16
	s_addc_u32 s11, s30, s17
	global_load_dwordx4 v[106:109], v0, s[10:11] nt
	s_mul_hi_i32 s9, s18, 0x300
	s_mul_i32 s20, s18, 0x300
	s_and_saveexec_b64 s[12:13], s[38:39]
	s_xor_b64 s[12:13], exec, s[12:13]
	s_cbranch_execz .LBB0_79
	s_add_u32 s22, s0, s20
	v_ashrrev_i32_e32 v115, 31, v114
	s_addc_u32 s23, s1, s9
	v_lshlrev_b64 v[4:5], 1, v[114:115]
	v_lshl_add_u64 v[6:7], s[22:23], 0, v[4:5]
	s_add_u32 s22, s74, s20
	s_addc_u32 s23, s75, s9
	v_lshl_add_u64 v[4:5], s[22:23], 0, v[4:5]
	s_mov_b32 s3, 0x1b000000
	global_load_dwordx4 v[58:61], v[6:7], off nt
	v_add_co_u32_e32 v6, vcc, s3, v4
	s_lshl_b64 s[18:19], s[18:19], 5
	v_ashrrev_i32_e32 v2, 6, v114
	v_addc_co_u32_e32 v7, vcc, 0, v5, vcc
	s_mov_b32 s3, 0x1c800000
	s_add_u32 s18, s26, s18
	v_add_co_u32_e32 v4, vcc, s3, v4
	v_ashrrev_i32_e32 v3, 31, v2
	s_addc_u32 s19, s27, s19
	v_addc_co_u32_e32 v5, vcc, 0, v5, vcc
	v_lshl_add_u64 v[2:3], v[2:3], 2, s[18:19]
	global_load_dwordx4 v[62:65], v[6:7], off nt
	global_load_dwordx4 v[66:69], v[4:5], off nt
	v_add_co_u32_e32 v4, vcc, 0x100000, v2
	global_load_dword v170, v[2:3], off
	s_nop 0
	v_addc_co_u32_e32 v5, vcc, 0, v3, vcc
	v_add_co_u32_e32 v2, vcc, 0x200000, v2
	global_load_dword v171, v[4:5], off
	s_nop 0
	v_addc_co_u32_e32 v3, vcc, 0, v3, vcc
	global_load_dword v172, v[2:3], off

; #define GAS __attribute__((address_space(1)))
; __device__ __forceinline__ void norm_load(NormRow& R, int m, int lane, const bf16* O, const bf16* GF, const bf16* OD, const float* LD) {
;     R.oa = __builtin_nontemporal_load((const GAS v4u*)(O + (size_t)m * DM + 8 * lane));
;     if (lane < 16) { R.oc = __builtin_nontemporal_load((const GAS v4u*)(O + (size_t)m * DM + 512 + 8 * lane)); R.gc = __builtin_nontemporal_load((const GAS v4u*)(GF + (size_t)m * 384 + 256 + 8 * lane)); }
;     else { const int dc = 8 * lane - 128, hd = dc >> 6;
;         R.d0 = __builtin_nontemporal_load((const GAS v4u*)(OD + (size_t)m * 384 + dc)); R.d1 = __builtin_nontemporal_load((const GAS v4u*)(OD + OD_BRANCH + (size_t)m * 384 + dc)); R.d2 = __builtin_nontemporal_load((const GAS v4u*)(OD + 2 * OD_BRANCH + (size_t)m * 384 + dc));
;         R.l0 = LD[(size_t)m * 8 + hd]; R.l1 = LD[LD_BRANCH + (size_t)m * 8 + hd]; R.l2 = LD[2 * LD_BRANCH + (size_t)m * 8 + hd]; }
;     if (lane >= 32) R.ga = __builtin_nontemporal_load((const GAS v4u*)(GF + (size_t)m * 384 + 8 * lane - 256));
; }
.LBB0_83:
	s_or_b64 exec, exec, s[10:11]
	s_or_b32 s20, s8, 2
	s_ashr_i32 s21, s20, 31
	s_lshl_b64 s[18:19], s[20:21], 11
	s_add_u32 s10, s29, s18
	s_addc_u32 s11, s30, s19
	global_load_dwordx4 v[110:113], v0, s[10:11] nt
	s_mul_hi_i32 s9, s20, 0x300
	s_mul_i32 s22, s20, 0x300
	s_and_saveexec_b64 s[12:13], s[38:39]
	s_xor_b64 s[12:13], exec, s[12:13]
	s_cbranch_execz .LBB0_85
	s_add_u32 s40, s0, s22
	v_ashrrev_i32_e32 v115, 31, v114
	s_addc_u32 s41, s1, s9
	v_lshlrev_b64 v[4:5], 1, v[114:115]
	v_lshl_add_u64 v[6:7], s[40:41], 0, v[4:5]
	s_add_u32 s40, s74, s22
	s_addc_u32 s41, s75, s9
	v_lshl_add_u64 v[4:5], s[40:41], 0, v[4:5]
	s_mov_b32 s3, 0x1b000000
	global_load_dwordx4 v[34:37], v[6:7], off nt
	v_add_co_u32_e32 v6, vcc, s3, v4
	s_lshl_b64 s[20:21], s[20:21], 5
	v_ashrrev_i32_e32 v2, 6, v114
	v_addc_co_u32_e32 v7, vcc, 0, v5, vcc
	s_mov_b32 s3, 0x1c800000
	s_add_u32 s20, s26, s20
	v_add_co_u32_e32 v4, vcc, s3, v4
	v_ashrrev_i32_e32 v3, 31, v2
	s_addc_u32 s21, s27, s21
	v_addc_co_u32_e32 v5, vcc, 0, v5, vcc
	v_lshl_add_u64 v[2:3], v[2:3], 2, s[20:21]
	global_load_dwordx4 v[38:41], v[6:7], off nt
	global_load_dwordx4 v[42:45], v[4:5], off nt
	v_add_co_u32_e32 v4, vcc, 0x100000, v2
	global_load_dword v167, v[2:3], off
	s_nop 0
	v_addc_co_u32_e32 v5, vcc, 0, v3, vcc
	v_add_co_u32_e32 v2, vcc, 0x200000, v2
	global_load_dword v168, v[4:5], off
	s_nop 0
	v_addc_co_u32_e32 v3, vcc, 0, v3, vcc
	global_load_dword v169, v[2:3], off

; #define GAS __attribute__((address_space(1)))
; __device__ __forceinline__ void norm_load(NormRow& R, int m, int lane, const bf16* O, const bf16* GF, const bf16* OD, const float* LD) {
;     R.oa = __builtin_nontemporal_load((const GAS v4u*)(O + (size_t)m * DM + 8 * lane));
;     if (lane < 16) { R.oc = __builtin_nontemporal_load((const GAS v4u*)(O + (size_t)m * DM + 512 + 8 * lane)); R.gc = __builtin_nontemporal_load((const GAS v4u*)(GF + (size_t)m * 384 + 256 + 8 * lane)); }
;     else { const int dc = 8 * lane - 128, hd = dc >> 6;
;         R.d0 = __builtin_nontemporal_load((const GAS v4u*)(OD + (size_t)m * 384 + dc)); R.d1 = __builtin_nontemporal_load((const GAS v4u*)(OD + OD_BRANCH + (size_t)m * 384 + dc)); R.d2 = __builtin_nontemporal_load((const GAS v4u*)(OD + 2 * OD_BRANCH + (size_t)m * 384 + dc));
;         R.l0 = LD[(size_t)m * 8 + hd]; R.l1 = LD[LD_BRANCH + (size_t)m * 8 + hd]; R.l2 = LD[2 * LD_BRANCH + (size_t)m * 8 + hd]; }
;     if (lane >= 32) R.ga = __builtin_nontemporal_load((const GAS v4u*)(GF + (size_t)m * 384 + 8 * lane - 256));
; }
.LBB0_89:
	s_or_b64 exec, exec, s[10:11]
	s_or_b32 s22, s8, 3
	s_ashr_i32 s23, s22, 31
	s_lshl_b64 s[10:11], s[22:23], 11
	s_add_u32 s12, s29, s10
	s_addc_u32 s13, s30, s11
	global_load_dwordx4 v[98:101], v0, s[12:13] nt
	s_mul_hi_i32 s9, s22, 0x300
	s_mul_i32 s31, s22, 0x300
	s_and_saveexec_b64 s[20:21], s[38:39]
	s_xor_b64 s[20:21], exec, s[20:21]
	s_cbranch_execz .LBB0_91
	s_add_u32 s40, s0, s31
	v_ashrrev_i32_e32 v115, 31, v114
	s_addc_u32 s41, s1, s9
	v_lshlrev_b64 v[4:5], 1, v[114:115]
	v_lshl_add_u64 v[6:7], s[40:41], 0, v[4:5]
	s_add_u32 s40, s74, s31
	s_addc_u32 s41, s75, s9
	v_lshl_add_u64 v[4:5], s[40:41], 0, v[4:5]
	s_mov_b32 s3, 0x1b000000
	global_load_dwordx4 v[10:13], v[6:7], off nt
	v_add_co_u32_e32 v6, vcc, s3, v4
	s_lshl_b64 s[22:23], s[22:23], 5
	v_ashrrev_i32_e32 v2, 6, v114
	v_addc_co_u32_e32 v7, vcc, 0, v5, vcc
	s_mov_b32 s3, 0x1c800000
	s_add_u32 s22, s26, s22
	v_add_co_u32_e32 v4, vcc, s3, v4
	v_ashrrev_i32_e32 v3, 31, v2
	s_addc_u32 s23, s27, s23
	v_addc_co_u32_e32 v5, vcc, 0, v5, vcc
	v_lshl_add_u64 v[2:3], v[2:3], 2, s[22:23]
	global_load_dwordx4 v[14:17], v[6:7], off nt
	global_load_dwordx4 v[18:21], v[4:5], off nt
	v_add_co_u32_e32 v4, vcc, 0x100000, v2
	global_load_dword v163, v[2:3], off
	s_nop 0
	v_addc_co_u32_e32 v5, vcc, 0, v3, vcc
	v_add_co_u32_e32 v2, vcc, 0x200000, v2
	global_load_dword v165, v[4:5], off
	s_nop 0
	v_addc_co_u32_e32 v3, vcc, 0, v3, vcc
	global_load_dword v166, v[2:3], off

; __device__ __forceinline__ void unpack8(const v4u w, float* f) { f[0] = bflo(w.x); f[1] = bfhi(w.x); f[2] = bflo(w.y); f[3] = bfhi(w.y); f[4] = bflo(w.z); f[5] = bfhi(w.z); f[6] = bflo(w.w); f[7] = bfhi(w.w); }
; __device__ __forceinline__ void norm_compute(const NormRow& R, int lane, v4u& ya, v4u& yc) {
;     float fa[8], fc[8];
;     unpack8(R.oa, fa);
;     if (lane < 16) unpack8(R.oc, fc);
;     else { float f0[8], f1[8], f2[8]; unpack8(R.d0, f0); unpack8(R.d1, f1); unpack8(R.d2, f2);
;         const float inv = 1.0f / (R.l0 + R.l1 + R.l2);
; #pragma unroll
;         for (int e = 0; e < 8; ++e) fc[e] = (f0[e] + f1[e] + f2[e]) * inv; }
.LBB0_95:
	s_or_b64 exec, exec, s[12:13]
	s_and_saveexec_b64 s[12:13], s[38:39]
	s_xor_b64 s[12:13], exec, s[12:13]
	s_cbranch_execz .LBB0_97
	s_waitcnt vmcnt(26)
	v_add_f32_e32 v115, v173, v174
	v_add_f32_e32 v115, v115, v175
	v_div_scale_f32 v116, s[20:21], v115, v115, 1.0
	v_rcp_f32_e32 v117, v116
	v_and_b32_e32 v125, 0xffff0000, v86
	v_lshlrev_b32_e32 v126, 16, v90
	v_and_b32_e32 v127, 0xffff0000, v90
	v_fma_f32 v122, -v116, v117, 1.0
	v_fmac_f32_e32 v117, v122, v117
	v_div_scale_f32 v122, vcc, 1.0, v115, 1.0
	v_mul_f32_e32 v123, v122, v117
	v_fma_f32 v124, -v116, v123, v122
	v_fmac_f32_e32 v123, v124, v117
	v_fma_f32 v116, -v116, v123, v122
	v_div_fmas_f32 v116, v116, v117, v123
	v_div_fixup_f32 v122, v116, v115, 1.0
	v_lshlrev_b32_e32 v116, 16, v82
	v_and_b32_e32 v117, 0xffff0000, v82
	v_lshlrev_b32_e32 v124, 16, v86
	v_pk_add_f32 v[116:117], v[124:125], v[116:117]
	v_lshlrev_b32_e32 v128, 16, v91
	v_pk_add_f32 v[116:117], v[116:117], v[126:127]
	v_lshlrev_b32_e32 v126, 16, v87
	v_pk_mul_f32 v[124:125], v[116:117], v[122:123] op_sel_hi:[1,0]
	v_lshlrev_b32_e32 v116, 16, v83
	v_and_b32_e32 v117, 0xffff0000, v83
	v_and_b32_e32 v127, 0xffff0000, v87
	v_and_b32_e32 v129, 0xffff0000, v91
	v_pk_add_f32 v[116:117], v[126:127], v[116:117]
	v_lshlrev_b32_e32 v118, 16, v85
	v_lshlrev_b32_e32 v120, 16, v89
	v_and_b32_e32 v119, 0xffff0000, v85
	v_and_b32_e32 v121, 0xffff0000, v89
	v_pk_add_f32 v[116:117], v[116:117], v[128:129]
	v_lshlrev_b32_e32 v126, 16, v84
	v_and_b32_e32 v127, 0xffff0000, v84
	v_lshlrev_b32_e32 v128, 16, v88
	v_and_b32_e32 v129, 0xffff0000, v88
	v_lshlrev_b32_e32 v130, 16, v92
	v_and_b32_e32 v131, 0xffff0000, v92
	v_pk_add_f32 v[126:127], v[128:129], v[126:127]
	v_lshlrev_b32_e32 v128, 16, v93
	v_and_b32_e32 v129, 0xffff0000, v93
	v_pk_add_f32 v[118:119], v[120:121], v[118:119]
	v_pk_add_f32 v[126:127], v[126:127], v[130:131]
	v_pk_add_f32 v[118:119], v[118:119], v[128:129]
	v_pk_mul_f32 v[116:117], v[116:117], v[122:123] op_sel_hi:[1,0]
	v_pk_mul_f32 v[126:127], v[126:127], v[122:123] op_sel_hi:[1,0]
	v_pk_mul_f32 v[128:129], v[118:119], v[122:123] op_sel_hi:[1,0]
	v_mov_b32_e32 v130, v126
	v_mov_b32_e32 v131, v128
	v_mov_b32_e32 v128, v127
	v_mov_b32_e32 v133, v116
	v_mov_b32_e32 v116, v125
	v_mov_b32_e32 v132, v124
	s_andn2_saveexec_b64 s[12:13], s[12:13]
	s_cbranch_execnz .LBB0_98
	s_branch .LBB0_99

; __device__ __forceinline__ void unpack8(const v4u w, float* f) { f[0] = bflo(w.x); f[1] = bfhi(w.x); f[2] = bflo(w.y); f[3] = bfhi(w.y); f[4] = bflo(w.z); f[5] = bfhi(w.z); f[6] = bflo(w.w); f[7] = bfhi(w.w); }
; __device__ __forceinline__ float wave_sum(float v) {
; #pragma unroll
;     for (int o = 1; o < 64; o <<= 1) v += __shfl_xor(v, o);
;     return v;
; }
; __device__ __forceinline__ void norm_compute(const NormRow& R, int lane, v4u& ya, v4u& yc) {
;     ...
;     if (lane < 16) unpack8(R.oc, fc);
;     else { float f0[8], f1[8], f2[8]; unpack8(R.d0, f0); unpack8(R.d1, f1); unpack8(R.d2, f2);
;         const float inv = 1.0f / (R.l0 + R.l1 + R.l2);
; #pragma unroll
;         for (int e = 0; e < 8; ++e) fc[e] = (f0[e] + f1[e] + f2[e]) * inv; }
;     float sa = 0.f, sc = 0.f;
; #pragma unroll
;     for (int e = 0; e < 8; ++e) { sa += fa[e] * fa[e]; sc += fc[e] * fc[e]; }
;     const float s_moba = wave_sum(lane < 32 ? sa : 0.f), s_fox = wave_sum((lane >= 32 ? sa : 0.f) + (lane < 16 ? sc : 0.f)), s_dil = wave_sum(lane >= 16 ? sc : 0.f);
;     const float r_moba = 1.0f / sqrtf(s_moba * (1.0f / 256.0f) + EPS), r_fox = 1.0f / sqrtf(s_fox * (1.0f / 384.0f) + EPS), r_dil = 1.0f / sqrtf(s_dil * (1.0f / 384.0f) + EPS);
;     float ga[8], gc[8];
; #pragma unroll
;     for (int e = 0; e < 8; ++e) { ga[e] = 1.f; gc[e] = 1.f; }
;     if (lane >= 32) unpack8(R.ga, ga);
;     if (lane < 16) unpack8(R.gc, gc);
.LBB0_98:
	s_waitcnt vmcnt(26)
	v_lshlrev_b32_e32 v132, 16, v94
	v_and_b32_e32 v116, 0xffff0000, v94
	v_lshlrev_b32_e32 v133, 16, v95
	v_and_b32_e32 v117, 0xffff0000, v95
	v_lshlrev_b32_e32 v130, 16, v96
	v_and_b32_e32 v128, 0xffff0000, v96
	v_lshlrev_b32_e32 v131, 16, v97
	v_and_b32_e32 v129, 0xffff0000, v97
.LBB0_99:
	s_or_b64 exec, exec, s[12:13]
	v_and_b32_e32 v115, 64, v214
	v_add_u32_e32 v115, 64, v115
	v_xor_b32_e32 v118, 1, v214
	v_cmp_lt_i32_e32 vcc, v118, v115
	s_waitcnt vmcnt(26)
	v_lshlrev_b32_e32 v141, 16, v103
	v_lshlrev_b32_e32 v140, 16, v102
	v_cndmask_b32_e32 v118, v214, v118, vcc
	v_lshlrev_b32_e32 v164, 2, v118
	v_xor_b32_e32 v118, 2, v214
	v_cmp_lt_i32_e32 vcc, v118, v115
	v_and_b32_e32 v135, 0xffff0000, v103
	v_and_b32_e32 v134, 0xffff0000, v102
	v_cndmask_b32_e32 v118, v214, v118, vcc
	v_lshlrev_b32_e32 v162, 2, v118
	v_xor_b32_e32 v118, 4, v214
	v_cmp_lt_i32_e32 vcc, v118, v115
	v_lshlrev_b32_e32 v139, 16, v105
	v_lshlrev_b32_e32 v138, 16, v104
	v_cndmask_b32_e32 v118, v214, v118, vcc
	v_lshlrev_b32_e32 v161, 2, v118
	v_xor_b32_e32 v118, 8, v214
	v_cmp_lt_i32_e32 vcc, v118, v115
	v_and_b32_e32 v137, 0xffff0000, v105
	v_and_b32_e32 v136, 0xffff0000, v104
	v_cndmask_b32_e32 v118, v214, v118, vcc
	v_lshlrev_b32_e32 v160, 2, v118
	v_xor_b32_e32 v118, 16, v214
	v_cmp_lt_i32_e32 vcc, v118, v115
	v_pk_mul_f32 v[102:103], v[140:141], v[140:141]
	v_pk_mul_f32 v[104:105], v[134:135], v[134:135]
	v_cndmask_b32_e32 v118, v214, v118, vcc
	v_lshlrev_b32_e32 v159, 2, v118
	v_xor_b32_e32 v118, 32, v214
	v_add_f32_e32 v102, v102, v104
	v_cmp_lt_i32_e32 vcc, v118, v115
	v_add_f32_e32 v102, v103, v102
	v_add_f32_e32 v102, v105, v102
	v_cndmask_b32_e32 v115, v214, v118, vcc
	v_pk_mul_f32 v[118:119], v[138:139], v[138:139]
	v_pk_mul_f32 v[120:121], v[136:137], v[136:137]
	v_add_f32_e32 v102, v118, v102
	v_add_f32_e32 v102, v120, v102
	v_add_f32_e32 v102, v119, v102
	v_cmp_gt_u32_e64 s[40:41], 32, v194
	v_add_f32_e32 v102, v121, v102
	v_lshlrev_b32_e32 v158, 2, v115
	v_cndmask_b32_e64 v103, 0, v102, s[40:41]
	v_mul_f32_e32 v115, v116, v116
	v_fmac_f32_e32 v115, v132, v132
	v_fmac_f32_e32 v115, v133, v133
	v_fmac_f32_e32 v115, v117, v117
	s_nop 1
	v_add_f32_dpp v103, v103, v103 quad_perm:[1,0,3,2] row_mask:0xf bank_mask:0xf
	v_fmac_f32_e32 v115, v130, v130
	v_fmac_f32_e32 v115, v128, v128
	v_fmac_f32_e32 v115, v131, v131
	v_fmac_f32_e32 v115, v129, v129
	s_nop 1
	v_add_f32_dpp v103, v103, v103 quad_perm:[2,3,0,1] row_mask:0xf bank_mask:0xf
	v_cndmask_b32_e64 v102, 0, v102, s[36:37]
	v_cmp_lt_u32_e64 s[42:43], 15, v194
	v_mov_b32_e32 v142, 1.0
	v_mov_b32_e32 v156, 1.0
	s_nop 1
	v_add_f32_dpp v103, v103, v103 row_half_mirror row_mask:0xf bank_mask:0xf
	v_mov_b32_e32 v152, 1.0
	v_mov_b32_e32 v157, 1.0
	v_mov_b32_e32 v153, 1.0
	v_mov_b32_e32 v154, 1.0
	s_nop 1
	v_add_f32_dpp v103, v103, v103 row_mirror row_mask:0xf bank_mask:0xf
	v_mov_b32_e32 v150, 1.0
	v_mov_b32_e32 v155, 1.0
	v_mov_b32_e32 v151, 1.0
	v_mov_b32_e32 v104, v103
	s_nop 1
	v_permlane16_swap_b32_e32 v103, v104
	v_add_f32_e32 v176, v103, v104
	v_cndmask_b32_e64 v103, 0, v115, s[34:35]
	v_add_f32_e32 v102, v102, v103
	s_nop 1
	v_add_f32_dpp v102, v102, v102 quad_perm:[1,0,3,2] row_mask:0xf bank_mask:0xf
	s_nop 1
	v_add_f32_dpp v102, v102, v102 quad_perm:[2,3,0,1] row_mask:0xf bank_mask:0xf
	s_nop 1
	v_add_f32_dpp v102, v102, v102 row_half_mirror row_mask:0xf bank_mask:0xf
	s_nop 1
	v_add_f32_dpp v102, v102, v102 row_mirror row_mask:0xf bank_mask:0xf
	v_mov_b32_e32 v103, v102
	s_nop 1
	v_permlane16_swap_b32_e32 v102, v103
	v_add_f32_e32 v177, v102, v103
	v_cndmask_b32_e64 v102, 0, v115, s[42:43]
	s_nop 1
	v_add_f32_dpp v102, v102, v102 quad_perm:[1,0,3,2] row_mask:0xf bank_mask:0xf
	s_nop 1
	v_add_f32_dpp v102, v102, v102 quad_perm:[2,3,0,1] row_mask:0xf bank_mask:0xf
	s_nop 1
	v_add_f32_dpp v102, v102, v102 row_half_mirror row_mask:0xf bank_mask:0xf
	s_nop 1
	v_add_f32_dpp v102, v102, v102 row_mirror row_mask:0xf bank_mask:0xf
	v_mov_b32_e32 v103, v102
	s_nop 1
	v_permlane16_swap_b32_e32 v102, v103
	v_add_f32_e32 v180, v102, v103
	s_and_saveexec_b64 s[12:13], s[36:37]
	v_lshlrev_b32_e32 v156, 16, v78
	v_and_b32_e32 v152, 0xffff0000, v78
	v_lshlrev_b32_e32 v157, 16, v79
	v_and_b32_e32 v153, 0xffff0000, v79
	v_lshlrev_b32_e32 v154, 16, v80
	v_and_b32_e32 v150, 0xffff0000, v80
	v_lshlrev_b32_e32 v155, 16, v81
	v_and_b32_e32 v151, 0xffff0000, v81
	s_or_b64 exec, exec, s[12:13]
	v_mov_b32_e32 v148, 1.0
	v_mov_b32_e32 v143, 1.0
	v_mov_b32_e32 v149, 1.0
	v_mov_b32_e32 v146, 1.0
	v_mov_b32_e32 v144, 1.0
	v_mov_b32_e32 v147, 1.0
	v_mov_b32_e32 v145, 1.0
	s_and_saveexec_b64 s[12:13], s[34:35]
	v_lshlrev_b32_e32 v142, 16, v74
	v_and_b32_e32 v148, 0xffff0000, v74
	v_lshlrev_b32_e32 v143, 16, v75
	v_and_b32_e32 v149, 0xffff0000, v75
	v_lshlrev_b32_e32 v146, 16, v76
	v_and_b32_e32 v144, 0xffff0000, v76
	v_lshlrev_b32_e32 v147, 16, v77
	v_and_b32_e32 v145, 0xffff0000, v77
	s_or_b64 exec, exec, s[12:13]
	v_ashrrev_i32_e32 v115, 31, v114
	v_lshlrev_b64 v[102:103], 1, v[114:115]
	v_lshl_add_u64 v[124:125], s[0:1], 0, v[102:103]
	v_lshl_add_u64 v[102:103], s[74:75], 0, v[102:103]
	s_mov_b64 s[0:1], 0x1b000000
	v_lshl_add_u64 v[122:123], v[102:103], 0, s[0:1]
	s_mov_b64 s[0:1], 0x1c800000
	v_lshl_add_u64 v[120:121], v[102:103], 0, s[0:1]
	s_or_b32 s0, s8, 4
	s_ashr_i32 s1, s0, 31
	s_lshl_b64 s[12:13], s[0:1], 11
	s_add_u32 s20, s29, s12
	s_addc_u32 s21, s30, s13
	global_load_dwordx4 v[102:105], v0, s[20:21] nt
	v_ashrrev_i32_e32 v118, 6, v114
	v_ashrrev_i32_e32 v119, 31, v118
	s_and_saveexec_b64 s[22:23], s[38:39]
	s_xor_b64 s[22:23], exec, s[22:23]
	s_cbranch_execz .LBB0_759
	v_mad_i64_i32 v[82:83], s[44:45], s0, v252, v[124:125]
	v_mad_i64_i32 v[86:87], s[44:45], s0, v252, v[122:123]
	v_mad_i64_i32 v[90:91], s[44:45], s0, v252, v[120:121]
	s_lshl_b64 s[44:45], s[0:1], 5
	s_add_u32 s44, s26, s44
	s_addc_u32 s45, s27, s45
	v_lshl_add_u64 v[114:115], v[118:119], 2, s[44:45]
	v_add_co_u32_e32 v126, vcc, 0x100000, v114
	global_load_dword v173, v[114:115], off
	s_nop 0
	v_addc_co_u32_e32 v127, vcc, 0, v115, vcc
	global_load_dword v174, v[126:127], off
	v_add_co_u32_e32 v114, vcc, 0x200000, v114
	global_load_dwordx4 v[82:85], v[82:83], off nt
	s_nop 0
	v_addc_co_u32_e32 v115, vcc, 0, v115, vcc
	global_load_dwordx4 v[86:89], v[86:87], off nt
	s_nop 0
	global_load_dwordx4 v[90:93], v[90:91], off nt
	s_nop 0
	global_load_dword v175, v[114:115], off
	s_andn2_saveexec_b64 s[22:23], s[22:23]
	s_cbranch_execnz .LBB0_760

; __device__ __forceinline__ unsigned pk2(float lo, float hi) { return f2bf(lo) | (f2bf(hi) << 16); }
; __device__ __forceinline__ void unpack8(const v4u w, float* f) { f[0] = bflo(w.x); f[1] = bfhi(w.x); f[2] = bflo(w.y); f[3] = bfhi(w.y); f[4] = bflo(w.z); f[5] = bfhi(w.z); f[6] = bflo(w.w); f[7] = bfhi(w.w); }
; __device__ __forceinline__ void norm_compute(const NormRow& R, int lane, v4u& ya, v4u& yc) {
;     ...
;     const float s_moba = wave_sum(lane < 32 ? sa : 0.f), s_fox = wave_sum((lane >= 32 ? sa : 0.f) + (lane < 16 ? sc : 0.f)), s_dil = wave_sum(lane >= 16 ? sc : 0.f);
;     const float r_moba = 1.0f / sqrtf(s_moba * (1.0f / 256.0f) + EPS), r_fox = 1.0f / sqrtf(s_fox * (1.0f / 384.0f) + EPS), r_dil = 1.0f / sqrtf(s_dil * (1.0f / 384.0f) + EPS);
;     float ga[8], gc[8];
; #pragma unroll
;     for (int e = 0; e < 8; ++e) { ga[e] = 1.f; gc[e] = 1.f; }
;     if (lane >= 32) unpack8(R.ga, ga);
;     if (lane < 16) unpack8(R.gc, gc);
;     const float ra = lane < 32 ? r_moba : r_fox, rc = lane < 16 ? r_fox : r_dil;
;     ya.x = pk2(fa[0] * ra * ga[0], fa[1] * ra * ga[1]); ya.y = pk2(fa[2] * ra * ga[2], fa[3] * ra * ga[3]); ya.z = pk2(fa[4] * ra * ga[4], fa[5] * ra * ga[5]); ya.w = pk2(fa[6] * ra * ga[6], fa[7] * ra * ga[7]);
;     yc.x = pk2(fc[0] * rc * gc[0], fc[1] * rc * gc[1]); yc.y = pk2(fc[2] * rc * gc[2], fc[3] * rc * gc[3]); yc.z = pk2(fc[4] * rc * gc[4], fc[5] * rc * gc[5]); yc.w = pk2(fc[6] * rc * gc[6], fc[7] * rc * gc[7]);
; }
.LBB0_107:
	s_or_b64 exec, exec, s[20:21]
	v_mov_b32_e32 v181, v180
	s_nop 1
	v_permlane32_swap_b32_e32 v180, v181
	v_add_f32_e32 v114, v180, v181
	v_fmamk_f32 v114, v114, 0x3b2aaaab, v215
	s_mov_b32 s3, 0xf800000
	v_mul_f32_e32 v115, 0x4f800000, v114
	v_cmp_gt_f32_e32 vcc, s3, v114
	v_mov_b32_e32 v179, v177
	s_nop 1
	v_permlane32_swap_b32_e32 v177, v179
	v_add_f32_e32 v177, v177, v179
	v_fmamk_f32 v177, v177, 0x3b2aaaab, v215
	v_cndmask_b32_e32 v114, v114, v115, vcc
	v_sqrt_f32_e32 v115, v114
	v_mul_f32_e32 v179, 0x4f800000, v177
	v_mov_b32_e32 v178, v176
	s_nop 1
	v_permlane32_swap_b32_e32 v176, v178
	v_add_f32_e32 v176, v176, v178
	v_fmamk_f32 v176, v176, 0x3b800000, v215
	v_add_u32_e32 v180, -1, v115
	v_fma_f32 v182, -v180, v115, v114
	v_add_u32_e32 v181, 1, v115
	v_cmp_ge_f32_e64 s[0:1], 0, v182
	v_mul_f32_e32 v178, 0x4f800000, v176
	s_nop 0
	v_cndmask_b32_e64 v180, v115, v180, s[0:1]
	v_fma_f32 v115, -v181, v115, v114
	v_cmp_lt_f32_e64 s[0:1], 0, v115
	s_nop 1
	v_cndmask_b32_e64 v115, v180, v181, s[0:1]
	v_cmp_gt_f32_e64 s[0:1], s3, v177
	v_mul_f32_e32 v180, 0x37800000, v115
	v_cndmask_b32_e32 v115, v115, v180, vcc
	v_cndmask_b32_e64 v177, v177, v179, s[0:1]
	v_sqrt_f32_e32 v179, v177
	v_cmp_class_f32_e32 vcc, v114, v216
	s_nop 1
	v_cndmask_b32_e32 v114, v115, v114, vcc
	v_add_u32_e32 v115, -1, v179
	v_fma_f32 v180, -v115, v179, v177
	v_cmp_ge_f32_e32 vcc, 0, v180
	v_add_u32_e32 v180, 1, v179
	s_nop 0
	v_cndmask_b32_e32 v115, v179, v115, vcc
	v_fma_f32 v179, -v180, v179, v177
	v_cmp_lt_f32_e32 vcc, 0, v179
	s_nop 1
	v_cndmask_b32_e32 v115, v115, v180, vcc
	v_cmp_gt_f32_e32 vcc, s3, v176
	v_mul_f32_e32 v179, 0x37800000, v115
	v_cndmask_b32_e64 v115, v115, v179, s[0:1]
	v_cndmask_b32_e32 v176, v176, v178, vcc
	v_sqrt_f32_e32 v178, v176
	v_cmp_class_f32_e64 s[0:1], v177, v216
	s_nop 1
	v_cndmask_b32_e64 v115, v115, v177, s[0:1]
	v_add_u32_e32 v177, -1, v178
	v_fma_f32 v179, -v177, v178, v176
	v_cmp_ge_f32_e64 s[0:1], 0, v179
	v_add_u32_e32 v179, 1, v178
	s_nop 0
	v_cndmask_b32_e64 v177, v178, v177, s[0:1]
	v_fma_f32 v178, -v179, v178, v176
	v_cmp_lt_f32_e64 s[0:1], 0, v178
	s_nop 1
	v_cndmask_b32_e64 v177, v177, v179, s[0:1]
	v_div_scale_f32 v179, s[0:1], v114, v114, 1.0
	v_rcp_f32_e32 v180, v179
	v_mul_f32_e32 v178, 0x37800000, v177
	v_cndmask_b32_e32 v177, v177, v178, vcc
	v_cmp_class_f32_e32 vcc, v176, v216
	s_nop 1
	v_cndmask_b32_e32 v176, v177, v176, vcc
	v_fma_f32 v177, -v179, v180, 1.0
	v_fmac_f32_e32 v180, v177, v180
	v_div_scale_f32 v177, vcc, 1.0, v114, 1.0
	v_mul_f32_e32 v178, v177, v180
	v_fma_f32 v181, -v179, v178, v177
	v_fmac_f32_e32 v178, v181, v180
	v_fma_f32 v177, -v179, v178, v177
	v_div_scale_f32 v179, s[0:1], v115, v115, 1.0
	v_rcp_f32_e32 v181, v179
	v_div_fmas_f32 v177, v177, v180, v178
	v_div_fixup_f32 v177, v177, v114, 1.0
	v_fma_f32 v114, -v179, v181, 1.0
	v_fmac_f32_e32 v181, v114, v181
	v_div_scale_f32 v114, vcc, 1.0, v115, 1.0
	v_mul_f32_e32 v178, v114, v181
	v_fma_f32 v180, -v179, v178, v114
	v_fmac_f32_e32 v178, v180, v181
	v_fma_f32 v114, -v179, v178, v114
	v_div_scale_f32 v179, s[0:1], v176, v176, 1.0
	v_rcp_f32_e32 v180, v179
	v_div_fmas_f32 v114, v114, v181, v178
	v_div_fixup_f32 v115, v114, v115, 1.0
	s_movk_i32 s1, 0x7fff
	v_fma_f32 v114, -v179, v180, 1.0
	v_fmac_f32_e32 v180, v114, v180
	v_div_scale_f32 v114, vcc, 1.0, v176, 1.0
	v_mul_f32_e32 v178, v114, v180
	v_fma_f32 v181, -v179, v178, v114
	v_fmac_f32_e32 v178, v181, v180
	v_fma_f32 v114, -v179, v178, v114
	v_div_fmas_f32 v114, v114, v180, v178
	v_div_fixup_f32 v114, v114, v176, 1.0
	v_cndmask_b32_e64 v114, v115, v114, s[40:41]
	v_cndmask_b32_e64 v176, v177, v115, s[34:35]
	v_pk_mul_f32 v[140:141], v[114:115], v[140:141] op_sel_hi:[0,1]
	v_pk_mul_f32 v[134:135], v[114:115], v[134:135] op_sel_hi:[0,1]
	v_pk_mul_f32 v[138:139], v[114:115], v[138:139] op_sel_hi:[0,1]
	v_pk_mul_f32 v[114:115], v[114:115], v[136:137] op_sel_hi:[0,1]
	v_pk_mul_f32 v[134:135], v[134:135], v[152:153]
	v_pk_mul_f32 v[114:115], v[114:115], v[150:151]
	v_pk_mul_f32 v[140:141], v[140:141], v[156:157]
	v_pk_mul_f32 v[138:139], v[138:139], v[154:155]
	v_bfe_u32 v136, v115, 16, 1
	v_bfe_u32 v137, v114, 16, 1
	v_bfe_u32 v150, v135, 16, 1
	v_bfe_u32 v151, v134, 16, 1
	v_add3_u32 v134, v134, v151, s1
	v_add3_u32 v135, v135, v150, s1
	v_add3_u32 v114, v114, v137, s1
	v_add3_u32 v115, v115, v136, s1
	v_bfe_u32 v136, v140, 16, 1
	v_bfe_u32 v137, v141, 16, 1
	v_bfe_u32 v150, v138, 16, 1
	v_bfe_u32 v151, v139, 16, 1
	v_add3_u32 v139, v139, v151, s1
	v_add3_u32 v138, v138, v150, s1
	v_add3_u32 v137, v141, v137, s1
	v_add3_u32 v136, v140, v136, s1
	v_lshrrev_b32_e32 v140, 16, v136
	v_lshrrev_b32_e32 v141, 16, v137
	v_lshrrev_b32_e32 v136, 16, v138
	v_lshrrev_b32_e32 v137, 16, v139
	s_mov_b32 s0, 0xffff0000
	v_pk_mul_f32 v[116:117], v[116:117], v[176:177] op_sel_hi:[1,0]
	v_pk_mul_f32 v[128:129], v[128:129], v[176:177] op_sel_hi:[1,0]
	v_and_or_b32 v137, v115, s0, v137
	v_and_or_b32 v136, v114, s0, v136
	v_pk_mul_f32 v[114:115], v[132:133], v[176:177] op_sel_hi:[1,0]
	v_pk_mul_f32 v[116:117], v[116:117], v[148:149]
	v_pk_mul_f32 v[130:131], v[130:131], v[176:177] op_sel_hi:[1,0]
	v_pk_mul_f32 v[128:129], v[128:129], v[144:145]
	v_pk_mul_f32 v[114:115], v[114:115], v[142:143]
	v_pk_mul_f32 v[130:131], v[130:131], v[146:147]
	v_bfe_u32 v132, v129, 16, 1
	v_bfe_u32 v133, v128, 16, 1
	v_bfe_u32 v138, v117, 16, 1
	v_bfe_u32 v139, v116, 16, 1
	v_add3_u32 v139, v116, v139, s1
	v_add3_u32 v138, v117, v138, s1
	v_add3_u32 v116, v128, v133, s1
	v_add3_u32 v117, v129, v132, s1
	v_bfe_u32 v128, v114, 16, 1
	v_bfe_u32 v129, v115, 16, 1
	v_bfe_u32 v132, v130, 16, 1
	v_bfe_u32 v133, v131, 16, 1
	v_add3_u32 v131, v131, v133, s1
	v_add3_u32 v130, v130, v132, s1
	v_add3_u32 v115, v115, v129, s1
	v_add3_u32 v114, v114, v128, s1
	v_lshrrev_b32_e32 v114, 16, v114
	v_lshrrev_b32_e32 v115, 16, v115
	v_lshrrev_b32_e32 v128, 16, v130
	v_lshrrev_b32_e32 v129, 16, v131
	v_and_or_b32 v135, v135, s0, v141
	v_and_or_b32 v134, v134, s0, v140
	v_and_or_b32 v117, v117, s0, v129
	v_and_or_b32 v116, v116, s0, v128
	v_and_or_b32 v115, v138, s0, v115
	v_and_or_b32 v114, v139, s0, v114
	s_add_u32 s0, s24, s14
	s_addc_u32 s1, s25, s15
	global_store_dwordx4 v0, v[134:137], s[0:1]
	global_store_dwordx4 v0, v[114:117], s[0:1] offset:1024
	s_waitcnt vmcnt(28)
	s_and_saveexec_b64 s[0:1], s[38:39]
	s_xor_b64 s[0:1], exec, s[0:1]
	s_cbranch_execz .LBB0_109
; __device__ __forceinline__ void unpack8(const v4u w, float* f) { f[0] = bflo(w.x); f[1] = bfhi(w.x); f[2] = bflo(w.y); f[3] = bfhi(w.y); f[4] = bflo(w.z); f[5] = bfhi(w.z); f[6] = bflo(w.w); f[7] = bfhi(w.w); }
; __device__ __forceinline__ void norm_compute(const NormRow& R, int lane, v4u& ya, v4u& yc) {
;     ...
;     else { float f0[8], f1[8], f2[8]; unpack8(R.d0, f0); unpack8(R.d1, f1); unpack8(R.d2, f2);
;         const float inv = 1.0f / (R.l0 + R.l1 + R.l2);
; #pragma unroll
;         for (int e = 0; e < 8; ++e) fc[e] = (f0[e] + f1[e] + f2[e]) * inv; }
	v_add_f32_e32 v114, v171, v170
	v_add_f32_e32 v114, v172, v114
	v_div_scale_f32 v115, s[14:15], v114, v114, 1.0
	v_rcp_f32_e32 v130, v115
	v_lshlrev_b32_e32 v134, 16, v66
	v_and_b32_e32 v135, 0xffff0000, v66
	v_lshlrev_b32_e32 v136, 16, v67
	v_fma_f32 v131, -v115, v130, 1.0
	v_fmac_f32_e32 v130, v131, v130
	v_div_scale_f32 v131, vcc, 1.0, v114, 1.0
	v_mul_f32_e32 v132, v131, v130
	v_fma_f32 v133, -v115, v132, v131
	v_fmac_f32_e32 v132, v133, v130
	v_fma_f32 v115, -v115, v132, v131
	v_div_fmas_f32 v115, v115, v130, v132
	v_div_fixup_f32 v130, v115, v114, 1.0
	v_lshlrev_b32_e32 v114, 16, v58
	v_and_b32_e32 v115, 0xffff0000, v58
	v_lshlrev_b32_e32 v132, 16, v62
	v_and_b32_e32 v133, 0xffff0000, v62
	v_pk_add_f32 v[114:115], v[132:133], v[114:115]
	v_and_b32_e32 v137, 0xffff0000, v67
	v_pk_add_f32 v[114:115], v[114:115], v[134:135]
	v_lshlrev_b32_e32 v134, 16, v63
	v_pk_mul_f32 v[132:133], v[130:131], v[114:115] op_sel_hi:[0,1]
	v_lshlrev_b32_e32 v114, 16, v59
	v_and_b32_e32 v115, 0xffff0000, v59
	v_and_b32_e32 v135, 0xffff0000, v63
	v_pk_add_f32 v[114:115], v[134:135], v[114:115]
	v_lshlrev_b32_e32 v116, 16, v61
	v_lshlrev_b32_e32 v128, 16, v65
	v_and_b32_e32 v117, 0xffff0000, v61
	v_and_b32_e32 v129, 0xffff0000, v65
	v_pk_add_f32 v[114:115], v[114:115], v[136:137]
	v_lshlrev_b32_e32 v134, 16, v60
	v_and_b32_e32 v135, 0xffff0000, v60
	v_lshlrev_b32_e32 v136, 16, v64
	v_and_b32_e32 v137, 0xffff0000, v64
	v_lshlrev_b32_e32 v138, 16, v68
	v_and_b32_e32 v139, 0xffff0000, v68
	v_pk_add_f32 v[134:135], v[136:137], v[134:135]
	v_lshlrev_b32_e32 v136, 16, v69
	v_and_b32_e32 v137, 0xffff0000, v69
	v_pk_add_f32 v[116:117], v[128:129], v[116:117]
	v_pk_add_f32 v[134:135], v[134:135], v[138:139]
	v_pk_add_f32 v[116:117], v[116:117], v[136:137]
	v_pk_mul_f32 v[114:115], v[130:131], v[114:115] op_sel_hi:[0,1]
	v_pk_mul_f32 v[134:135], v[130:131], v[134:135] op_sel_hi:[0,1]
	v_pk_mul_f32 v[116:117], v[130:131], v[116:117] op_sel_hi:[0,1]
	v_mov_b32_e32 v129, v116
	v_mov_b32_e32 v116, v135
	v_mov_b32_e32 v128, v134
	v_mov_b32_e32 v131, v114
	v_mov_b32_e32 v114, v133
	v_mov_b32_e32 v130, v132
; __device__ __forceinline__ void unpack8(const v4u w, float* f) { f[0] = bflo(w.x); f[1] = bfhi(w.x); f[2] = bflo(w.y); f[3] = bfhi(w.y); f[4] = bflo(w.z); f[5] = bfhi(w.z); f[6] = bflo(w.w); f[7] = bfhi(w.w); }
; __device__ __forceinline__ float wave_sum(float v) {
; #pragma unroll
;     for (int o = 1; o < 64; o <<= 1) v += __shfl_xor(v, o);
;     return v;
; }
; __device__ __forceinline__ void norm_compute(const NormRow& R, int lane, v4u& ya, v4u& yc) {
;     ...
;     if (lane < 16) unpack8(R.oc, fc);
;     else { float f0[8], f1[8], f2[8]; unpack8(R.d0, f0); unpack8(R.d1, f1); unpack8(R.d2, f2);
;         const float inv = 1.0f / (R.l0 + R.l1 + R.l2);
; #pragma unroll
;         for (int e = 0; e < 8; ++e) fc[e] = (f0[e] + f1[e] + f2[e]) * inv; }
;     float sa = 0.f, sc = 0.f;
; #pragma unroll
;     for (int e = 0; e < 8; ++e) { sa += fa[e] * fa[e]; sc += fc[e] * fc[e]; }
;     const float s_moba = wave_sum(lane < 32 ? sa : 0.f), s_fox = wave_sum((lane >= 32 ? sa : 0.f) + (lane < 16 ? sc : 0.f)), s_dil = wave_sum(lane >= 16 ? sc : 0.f);
;     const float r_moba = 1.0f / sqrtf(s_moba * (1.0f / 256.0f) + EPS), r_fox = 1.0f / sqrtf(s_fox * (1.0f / 384.0f) + EPS), r_dil = 1.0f / sqrtf(s_dil * (1.0f / 384.0f) + EPS);
;     float ga[8], gc[8];
; #pragma unroll
;     for (int e = 0; e < 8; ++e) { ga[e] = 1.f; gc[e] = 1.f; }
;     if (lane >= 32) unpack8(R.ga, ga);
;     if (lane < 16) unpack8(R.gc, gc);
.LBB0_109:
	s_andn2_saveexec_b64 s[0:1], s[0:1]
	v_lshlrev_b32_e32 v130, 16, v70
	v_and_b32_e32 v114, 0xffff0000, v70
	v_lshlrev_b32_e32 v131, 16, v71
	v_and_b32_e32 v115, 0xffff0000, v71
	v_lshlrev_b32_e32 v128, 16, v72
	v_and_b32_e32 v116, 0xffff0000, v72
	v_lshlrev_b32_e32 v129, 16, v73
	v_and_b32_e32 v117, 0xffff0000, v73
	s_or_b64 exec, exec, s[0:1]
	v_lshlrev_b32_e32 v139, 16, v107
	v_lshlrev_b32_e32 v138, 16, v106
	v_and_b32_e32 v133, 0xffff0000, v107
	v_and_b32_e32 v132, 0xffff0000, v106
	v_lshlrev_b32_e32 v137, 16, v109
	v_lshlrev_b32_e32 v136, 16, v108
	v_and_b32_e32 v135, 0xffff0000, v109
	v_and_b32_e32 v134, 0xffff0000, v108
	v_pk_mul_f32 v[106:107], v[138:139], v[138:139]
	v_pk_mul_f32 v[108:109], v[132:133], v[132:133]
	v_mul_f32_e32 v144, v114, v114
	v_fmac_f32_e32 v144, v130, v130
	v_add_f32_e32 v106, v106, v108
	v_fmac_f32_e32 v144, v131, v131
	v_add_f32_e32 v106, v107, v106
	v_fmac_f32_e32 v144, v115, v115
	v_pk_mul_f32 v[140:141], v[136:137], v[136:137]
	v_add_f32_e32 v106, v109, v106
	v_fmac_f32_e32 v144, v128, v128
	v_pk_mul_f32 v[142:143], v[134:135], v[134:135]
	v_add_f32_e32 v106, v140, v106
	v_fmac_f32_e32 v144, v116, v116
	v_add_f32_e32 v106, v142, v106
	v_fmac_f32_e32 v144, v129, v129
	v_add_f32_e32 v106, v141, v106
	v_add_f32_e32 v106, v143, v106
	v_fmac_f32_e32 v144, v117, v117
	v_cndmask_b32_e64 v107, 0, v106, s[40:41]
	v_cndmask_b32_e64 v106, 0, v106, s[36:37]
	v_cndmask_b32_e64 v109, 0, v144, s[34:35]
	v_add_f32_e32 v106, v106, v109
	v_cndmask_b32_e64 v140, 0, v144, s[42:43]
	v_mov_b32_e32 v154, 1.0
	v_mov_b32_e32 v150, 1.0
	s_nop 1
	v_add_f32_dpp v107, v107, v107 quad_perm:[1,0,3,2] row_mask:0xf bank_mask:0xf
	s_nop 1
	v_add_f32_dpp v106, v106, v106 quad_perm:[1,0,3,2] row_mask:0xf bank_mask:0xf
	s_nop 1
	v_add_f32_dpp v140, v140, v140 quad_perm:[1,0,3,2] row_mask:0xf bank_mask:0xf
	v_mov_b32_e32 v155, 1.0
	v_mov_b32_e32 v151, 1.0
	s_nop 1
	v_add_f32_dpp v107, v107, v107 quad_perm:[2,3,0,1] row_mask:0xf bank_mask:0xf
	s_nop 1
	v_add_f32_dpp v106, v106, v106 quad_perm:[2,3,0,1] row_mask:0xf bank_mask:0xf
	s_nop 1
	v_add_f32_dpp v140, v140, v140 quad_perm:[2,3,0,1] row_mask:0xf bank_mask:0xf
	v_mov_b32_e32 v152, 1.0
	v_mov_b32_e32 v148, 1.0
	s_nop 1
	v_add_f32_dpp v107, v107, v107 row_half_mirror row_mask:0xf bank_mask:0xf
	s_nop 1
	v_add_f32_dpp v106, v106, v106 row_half_mirror row_mask:0xf bank_mask:0xf
	s_nop 1
	v_add_f32_dpp v140, v140, v140 row_half_mirror row_mask:0xf bank_mask:0xf
	v_mov_b32_e32 v153, 1.0
	v_mov_b32_e32 v149, 1.0
	s_nop 1
	v_add_f32_dpp v107, v107, v107 row_mirror row_mask:0xf bank_mask:0xf
	s_nop 1
	v_add_f32_dpp v106, v106, v106 row_mirror row_mask:0xf bank_mask:0xf
	s_nop 1
	v_add_f32_dpp v140, v140, v140 row_mirror row_mask:0xf bank_mask:0xf
	v_mov_b32_e32 v108, v107
	s_nop 1
	v_permlane16_swap_b32_e32 v107, v108
	v_add_f32_e32 v156, v107, v108
	v_mov_b32_e32 v109, v106
	s_nop 1
	v_permlane16_swap_b32_e32 v106, v109
	v_add_f32_e32 v176, v106, v109
	v_mov_b32_e32 v141, v140
	s_nop 1
	v_permlane16_swap_b32_e32 v140, v141
	v_add_f32_e32 v178, v140, v141
	v_mov_b32_e32 v140, 1.0
	s_and_saveexec_b64 s[0:1], s[36:37]
	v_lshlrev_b32_e32 v154, 16, v54
	v_and_b32_e32 v150, 0xffff0000, v54
	v_lshlrev_b32_e32 v155, 16, v55
	v_and_b32_e32 v151, 0xffff0000, v55
	v_lshlrev_b32_e32 v152, 16, v56
	v_and_b32_e32 v148, 0xffff0000, v56
	v_lshlrev_b32_e32 v153, 16, v57
	v_and_b32_e32 v149, 0xffff0000, v57
	s_or_b64 exec, exec, s[0:1]
	v_mov_b32_e32 v146, 1.0
	v_mov_b32_e32 v141, 1.0
	v_mov_b32_e32 v147, 1.0
	v_mov_b32_e32 v144, 1.0
	v_mov_b32_e32 v142, 1.0
	v_mov_b32_e32 v145, 1.0
	v_mov_b32_e32 v143, 1.0
	s_and_saveexec_b64 s[0:1], s[34:35]
	v_lshlrev_b32_e32 v140, 16, v50
	v_and_b32_e32 v146, 0xffff0000, v50
	v_lshlrev_b32_e32 v141, 16, v51
	v_and_b32_e32 v147, 0xffff0000, v51
	v_lshlrev_b32_e32 v144, 16, v52
	v_and_b32_e32 v142, 0xffff0000, v52
	v_lshlrev_b32_e32 v145, 16, v53
	v_and_b32_e32 v143, 0xffff0000, v53
	s_or_b64 exec, exec, s[0:1]
	s_or_b32 s0, s8, 5
	s_ashr_i32 s1, s0, 31
	s_lshl_b64 s[14:15], s[0:1], 11
	s_add_u32 s20, s29, s14
	s_addc_u32 s21, s30, s15
	global_load_dwordx4 v[106:109], v0, s[20:21] nt
	s_and_saveexec_b64 s[22:23], s[38:39]
	s_xor_b64 s[22:23], exec, s[22:23]
	s_cbranch_execz .LBB0_761
	v_mad_i64_i32 v[58:59], s[44:45], s0, v252, v[124:125]
	v_mad_i64_i32 v[62:63], s[44:45], s0, v252, v[122:123]
	v_mad_i64_i32 v[66:67], s[44:45], s0, v252, v[120:121]
	s_lshl_b64 s[44:45], s[0:1], 5
	s_add_u32 s44, s26, s44
	s_addc_u32 s45, s27, s45
	v_lshl_add_u64 v[180:181], v[118:119], 2, s[44:45]
	v_add_co_u32_e32 v182, vcc, 0x100000, v180
	global_load_dword v170, v[180:181], off
	s_nop 0
	v_addc_co_u32_e32 v183, vcc, 0, v181, vcc
	global_load_dword v171, v[182:183], off
	v_add_co_u32_e32 v180, vcc, 0x200000, v180
	global_load_dwordx4 v[58:61], v[58:59], off nt
	s_nop 0
	v_addc_co_u32_e32 v181, vcc, 0, v181, vcc
	global_load_dwordx4 v[62:65], v[62:63], off nt
	s_nop 0
	global_load_dwordx4 v[66:69], v[66:67], off nt
	s_nop 0
	global_load_dword v172, v[180:181], off
	s_andn2_saveexec_b64 s[22:23], s[22:23]
	s_cbranch_execnz .LBB0_762

; __device__ __forceinline__ unsigned pk2(float lo, float hi) { return f2bf(lo) | (f2bf(hi) << 16); }
; __device__ __forceinline__ void unpack8(const v4u w, float* f) { f[0] = bflo(w.x); f[1] = bfhi(w.x); f[2] = bflo(w.y); f[3] = bfhi(w.y); f[4] = bflo(w.z); f[5] = bfhi(w.z); f[6] = bflo(w.w); f[7] = bfhi(w.w); }
; __device__ __forceinline__ void norm_compute(const NormRow& R, int lane, v4u& ya, v4u& yc) {
;     ...
;     const float s_moba = wave_sum(lane < 32 ? sa : 0.f), s_fox = wave_sum((lane >= 32 ? sa : 0.f) + (lane < 16 ? sc : 0.f)), s_dil = wave_sum(lane >= 16 ? sc : 0.f);
;     const float r_moba = 1.0f / sqrtf(s_moba * (1.0f / 256.0f) + EPS), r_fox = 1.0f / sqrtf(s_fox * (1.0f / 384.0f) + EPS), r_dil = 1.0f / sqrtf(s_dil * (1.0f / 384.0f) + EPS);
;     float ga[8], gc[8];
; #pragma unroll
;     for (int e = 0; e < 8; ++e) { ga[e] = 1.f; gc[e] = 1.f; }
;     if (lane >= 32) unpack8(R.ga, ga);
;     if (lane < 16) unpack8(R.gc, gc);
;     const float ra = lane < 32 ? r_moba : r_fox, rc = lane < 16 ? r_fox : r_dil;
;     ya.x = pk2(fa[0] * ra * ga[0], fa[1] * ra * ga[1]); ya.y = pk2(fa[2] * ra * ga[2], fa[3] * ra * ga[3]); ya.z = pk2(fa[4] * ra * ga[4], fa[5] * ra * ga[5]); ya.w = pk2(fa[6] * ra * ga[6], fa[7] * ra * ga[7]);
;     yc.x = pk2(fc[0] * rc * gc[0], fc[1] * rc * gc[1]); yc.y = pk2(fc[2] * rc * gc[2], fc[3] * rc * gc[3]); yc.z = pk2(fc[4] * rc * gc[4], fc[5] * rc * gc[5]); yc.w = pk2(fc[6] * rc * gc[6], fc[7] * rc * gc[7]);
; }
.LBB0_119:
	s_or_b64 exec, exec, s[20:21]
	v_mov_b32_e32 v179, v178
	s_nop 1
	v_permlane32_swap_b32_e32 v178, v179
	v_add_f32_e32 v178, v178, v179
	v_fmamk_f32 v178, v178, 0x3b2aaaab, v215
	v_mul_f32_e32 v179, 0x4f800000, v178
	v_cmp_gt_f32_e32 vcc, s3, v178
	v_mov_b32_e32 v177, v176
	s_nop 1
	v_permlane32_swap_b32_e32 v176, v177
	v_add_f32_e32 v176, v176, v177
	v_fmamk_f32 v176, v176, 0x3b2aaaab, v215
	v_cndmask_b32_e32 v178, v178, v179, vcc
	v_sqrt_f32_e32 v179, v178
	v_mul_f32_e32 v177, 0x4f800000, v176
	v_mov_b32_e32 v157, v156
	s_nop 1
	v_permlane32_swap_b32_e32 v156, v157
	v_add_f32_e32 v156, v156, v157
	v_fmamk_f32 v156, v156, 0x3b800000, v215
	v_add_u32_e32 v180, -1, v179
	v_fma_f32 v182, -v180, v179, v178
	v_add_u32_e32 v181, 1, v179
	v_cmp_ge_f32_e64 s[0:1], 0, v182
	v_mul_f32_e32 v157, 0x4f800000, v156
	s_nop 0
	v_cndmask_b32_e64 v180, v179, v180, s[0:1]
	v_fma_f32 v179, -v181, v179, v178
	v_cmp_lt_f32_e64 s[0:1], 0, v179
	s_nop 1
	v_cndmask_b32_e64 v179, v180, v181, s[0:1]
	v_cmp_gt_f32_e64 s[0:1], s3, v176
	v_mul_f32_e32 v180, 0x37800000, v179
	v_cndmask_b32_e32 v179, v179, v180, vcc
	v_cndmask_b32_e64 v176, v176, v177, s[0:1]
	v_sqrt_f32_e32 v177, v176
	v_cmp_class_f32_e32 vcc, v178, v216
	s_nop 1
	v_cndmask_b32_e32 v178, v179, v178, vcc
	v_add_u32_e32 v179, -1, v177
	v_fma_f32 v180, -v179, v177, v176
	v_cmp_ge_f32_e32 vcc, 0, v180
	v_add_u32_e32 v180, 1, v177
	s_nop 0
	v_cndmask_b32_e32 v179, v177, v179, vcc
	v_fma_f32 v177, -v180, v177, v176
	v_cmp_lt_f32_e32 vcc, 0, v177
	s_nop 1
	v_cndmask_b32_e32 v177, v179, v180, vcc
	v_cmp_gt_f32_e32 vcc, s3, v156
	v_mul_f32_e32 v179, 0x37800000, v177
	v_cndmask_b32_e64 v177, v177, v179, s[0:1]
	v_cndmask_b32_e32 v156, v156, v157, vcc
	v_sqrt_f32_e32 v157, v156
	v_cmp_class_f32_e64 s[0:1], v176, v216
	s_nop 1
	v_cndmask_b32_e64 v176, v177, v176, s[0:1]
	v_add_u32_e32 v177, -1, v157
	v_fma_f32 v179, -v177, v157, v156
	v_cmp_ge_f32_e64 s[0:1], 0, v179
	v_add_u32_e32 v179, 1, v157
	s_nop 0
	v_cndmask_b32_e64 v177, v157, v177, s[0:1]
	v_fma_f32 v157, -v179, v157, v156
	v_cmp_lt_f32_e64 s[0:1], 0, v157
	s_nop 1
	v_cndmask_b32_e64 v157, v177, v179, s[0:1]
	v_div_scale_f32 v179, s[0:1], v178, v178, 1.0
	v_rcp_f32_e32 v180, v179
	v_mul_f32_e32 v177, 0x37800000, v157
	v_cndmask_b32_e32 v157, v157, v177, vcc
	v_cmp_class_f32_e32 vcc, v156, v216
	s_nop 1
	v_cndmask_b32_e32 v156, v157, v156, vcc
	v_fma_f32 v157, -v179, v180, 1.0
	v_fmac_f32_e32 v180, v157, v180
	v_div_scale_f32 v157, vcc, 1.0, v178, 1.0
	v_mul_f32_e32 v177, v157, v180
	v_fma_f32 v181, -v179, v177, v157
	v_fmac_f32_e32 v177, v181, v180
	v_fma_f32 v157, -v179, v177, v157
	v_div_scale_f32 v179, s[0:1], v176, v176, 1.0
	v_rcp_f32_e32 v181, v179
	v_div_fmas_f32 v157, v157, v180, v177
	v_div_fixup_f32 v157, v157, v178, 1.0
	v_fma_f32 v177, -v179, v181, 1.0
	v_fmac_f32_e32 v181, v177, v181
	v_div_scale_f32 v177, vcc, 1.0, v176, 1.0
	v_mul_f32_e32 v178, v177, v181
	v_fma_f32 v180, -v179, v178, v177
	v_fmac_f32_e32 v178, v180, v181
	v_fma_f32 v177, -v179, v178, v177
	v_div_scale_f32 v179, s[0:1], v156, v156, 1.0
	v_rcp_f32_e32 v180, v179
	v_div_fmas_f32 v177, v177, v181, v178
	v_div_fixup_f32 v176, v177, v176, 1.0
	s_movk_i32 s1, 0x7fff
	v_fma_f32 v177, -v179, v180, 1.0
	v_fmac_f32_e32 v180, v177, v180
	v_div_scale_f32 v177, vcc, 1.0, v156, 1.0
	v_mul_f32_e32 v178, v177, v180
	v_fma_f32 v181, -v179, v178, v177
	v_fmac_f32_e32 v178, v181, v180
	v_fma_f32 v177, -v179, v178, v177
	v_div_fmas_f32 v177, v177, v180, v178
	v_div_fixup_f32 v156, v177, v156, 1.0
	v_cndmask_b32_e64 v156, v176, v156, s[40:41]
	v_pk_mul_f32 v[132:133], v[156:157], v[132:133] op_sel_hi:[0,1]
	v_pk_mul_f32 v[134:135], v[156:157], v[134:135] op_sel_hi:[0,1]
	v_pk_mul_f32 v[138:139], v[156:157], v[138:139] op_sel_hi:[0,1]
	v_pk_mul_f32 v[132:133], v[132:133], v[150:151]
	v_pk_mul_f32 v[136:137], v[156:157], v[136:137] op_sel_hi:[0,1]
	v_pk_mul_f32 v[134:135], v[134:135], v[148:149]
	v_pk_mul_f32 v[138:139], v[138:139], v[154:155]
	v_pk_mul_f32 v[136:137], v[136:137], v[152:153]
	v_bfe_u32 v148, v135, 16, 1
	v_bfe_u32 v149, v134, 16, 1
	v_bfe_u32 v150, v133, 16, 1
	v_bfe_u32 v151, v132, 16, 1
	v_cndmask_b32_e64 v176, v157, v176, s[34:35]
	v_add3_u32 v132, v132, v151, s1
	v_add3_u32 v133, v133, v150, s1
	v_add3_u32 v134, v134, v149, s1
	v_add3_u32 v135, v135, v148, s1
	v_bfe_u32 v148, v138, 16, 1
	v_bfe_u32 v149, v139, 16, 1
	v_bfe_u32 v150, v136, 16, 1
	v_bfe_u32 v151, v137, 16, 1
	v_add3_u32 v137, v137, v151, s1
	v_add3_u32 v136, v136, v150, s1
	v_add3_u32 v139, v139, v149, s1
	v_add3_u32 v138, v138, v148, s1
	v_pk_mul_f32 v[114:115], v[114:115], v[176:177] op_sel_hi:[1,0]
	v_pk_mul_f32 v[116:117], v[116:117], v[176:177] op_sel_hi:[1,0]
	v_lshrrev_b32_e32 v138, 16, v138
	v_lshrrev_b32_e32 v139, 16, v139
	v_lshrrev_b32_e32 v136, 16, v136
	v_lshrrev_b32_e32 v137, 16, v137
	s_mov_b32 s0, 0xffff0000
	v_pk_mul_f32 v[130:131], v[130:131], v[176:177] op_sel_hi:[1,0]
	v_pk_mul_f32 v[114:115], v[114:115], v[146:147]
	v_pk_mul_f32 v[128:129], v[128:129], v[176:177] op_sel_hi:[1,0]
	v_pk_mul_f32 v[116:117], v[116:117], v[142:143]
	v_and_or_b32 v135, v135, s0, v137
	v_and_or_b32 v134, v134, s0, v136
	v_and_or_b32 v133, v133, s0, v139
	v_and_or_b32 v132, v132, s0, v138
	v_pk_mul_f32 v[130:131], v[130:131], v[140:141]
	v_pk_mul_f32 v[128:129], v[128:129], v[144:145]
	v_bfe_u32 v136, v117, 16, 1
	v_bfe_u32 v137, v116, 16, 1
	v_bfe_u32 v138, v115, 16, 1
	v_bfe_u32 v139, v114, 16, 1
	v_add3_u32 v114, v114, v139, s1
	v_add3_u32 v115, v115, v138, s1
	v_add3_u32 v116, v116, v137, s1
	v_add3_u32 v117, v117, v136, s1
	v_bfe_u32 v136, v130, 16, 1
	v_bfe_u32 v137, v131, 16, 1
	v_bfe_u32 v138, v128, 16, 1
	v_bfe_u32 v139, v129, 16, 1
	v_add3_u32 v129, v129, v139, s1
	v_add3_u32 v128, v128, v138, s1
	v_add3_u32 v131, v131, v137, s1
	v_add3_u32 v130, v130, v136, s1
	v_lshrrev_b32_e32 v130, 16, v130
	v_lshrrev_b32_e32 v131, 16, v131
	v_lshrrev_b32_e32 v128, 16, v128
	v_lshrrev_b32_e32 v129, 16, v129
	v_and_or_b32 v117, v117, s0, v129
	v_and_or_b32 v116, v116, s0, v128
	v_and_or_b32 v115, v115, s0, v131
	v_and_or_b32 v114, v114, s0, v130
	s_add_u32 s0, s24, s16
	s_addc_u32 s1, s25, s17
	global_store_dwordx4 v0, v[132:135], s[0:1]
	global_store_dwordx4 v0, v[114:117], s[0:1] offset:1024
	s_waitcnt vmcnt(30)
	s_and_saveexec_b64 s[0:1], s[38:39]
	s_xor_b64 s[0:1], exec, s[0:1]
	s_cbranch_execz .LBB0_121
; __device__ __forceinline__ void unpack8(const v4u w, float* f) { f[0] = bflo(w.x); f[1] = bfhi(w.x); f[2] = bflo(w.y); f[3] = bfhi(w.y); f[4] = bflo(w.z); f[5] = bfhi(w.z); f[6] = bflo(w.w); f[7] = bfhi(w.w); }
; __device__ __forceinline__ void norm_compute(const NormRow& R, int lane, v4u& ya, v4u& yc) {
;     ...
;     else { float f0[8], f1[8], f2[8]; unpack8(R.d0, f0); unpack8(R.d1, f1); unpack8(R.d2, f2);
;         const float inv = 1.0f / (R.l0 + R.l1 + R.l2);
; #pragma unroll
;         for (int e = 0; e < 8; ++e) fc[e] = (f0[e] + f1[e] + f2[e]) * inv; }
	v_add_f32_e32 v114, v168, v167
	v_add_f32_e32 v114, v169, v114
	v_div_scale_f32 v115, s[16:17], v114, v114, 1.0
	v_rcp_f32_e32 v130, v115
	v_lshlrev_b32_e32 v134, 16, v42
	v_and_b32_e32 v135, 0xffff0000, v42
	v_lshlrev_b32_e32 v136, 16, v43
	v_fma_f32 v131, -v115, v130, 1.0
	v_fmac_f32_e32 v130, v131, v130
	v_div_scale_f32 v131, vcc, 1.0, v114, 1.0
	v_mul_f32_e32 v132, v131, v130
	v_fma_f32 v133, -v115, v132, v131
	v_fmac_f32_e32 v132, v133, v130
	v_fma_f32 v115, -v115, v132, v131
	v_div_fmas_f32 v115, v115, v130, v132
	v_div_fixup_f32 v130, v115, v114, 1.0
	v_lshlrev_b32_e32 v114, 16, v34
	v_and_b32_e32 v115, 0xffff0000, v34
	v_lshlrev_b32_e32 v132, 16, v38
	v_and_b32_e32 v133, 0xffff0000, v38
	v_pk_add_f32 v[114:115], v[132:133], v[114:115]
	v_and_b32_e32 v137, 0xffff0000, v43
	v_pk_add_f32 v[114:115], v[114:115], v[134:135]
	v_lshlrev_b32_e32 v134, 16, v39
	v_pk_mul_f32 v[132:133], v[130:131], v[114:115] op_sel_hi:[0,1]
	v_lshlrev_b32_e32 v114, 16, v35
	v_and_b32_e32 v115, 0xffff0000, v35
	v_and_b32_e32 v135, 0xffff0000, v39
	v_pk_add_f32 v[114:115], v[134:135], v[114:115]
	v_lshlrev_b32_e32 v116, 16, v37
	v_lshlrev_b32_e32 v128, 16, v41
	v_and_b32_e32 v117, 0xffff0000, v37
	v_and_b32_e32 v129, 0xffff0000, v41
	v_pk_add_f32 v[114:115], v[114:115], v[136:137]
	v_lshlrev_b32_e32 v134, 16, v36
	v_and_b32_e32 v135, 0xffff0000, v36
	v_lshlrev_b32_e32 v136, 16, v40
	v_and_b32_e32 v137, 0xffff0000, v40
	v_lshlrev_b32_e32 v138, 16, v44
	v_and_b32_e32 v139, 0xffff0000, v44
	v_pk_add_f32 v[134:135], v[136:137], v[134:135]
	v_lshlrev_b32_e32 v136, 16, v45
	v_and_b32_e32 v137, 0xffff0000, v45
	v_pk_add_f32 v[116:117], v[128:129], v[116:117]
	v_pk_add_f32 v[134:135], v[134:135], v[138:139]
	v_pk_add_f32 v[116:117], v[116:117], v[136:137]
	v_pk_mul_f32 v[114:115], v[130:131], v[114:115] op_sel_hi:[0,1]
	v_pk_mul_f32 v[134:135], v[130:131], v[134:135] op_sel_hi:[0,1]
	v_pk_mul_f32 v[116:117], v[130:131], v[116:117] op_sel_hi:[0,1]
	v_mov_b32_e32 v129, v116
	v_mov_b32_e32 v116, v135
	v_mov_b32_e32 v128, v134
	v_mov_b32_e32 v131, v114
	v_mov_b32_e32 v114, v133
	v_mov_b32_e32 v130, v132
; __device__ __forceinline__ void unpack8(const v4u w, float* f) { f[0] = bflo(w.x); f[1] = bfhi(w.x); f[2] = bflo(w.y); f[3] = bfhi(w.y); f[4] = bflo(w.z); f[5] = bfhi(w.z); f[6] = bflo(w.w); f[7] = bfhi(w.w); }
; __device__ __forceinline__ float wave_sum(float v) {
; #pragma unroll
;     for (int o = 1; o < 64; o <<= 1) v += __shfl_xor(v, o);
;     return v;
; }
; __device__ __forceinline__ void norm_compute(const NormRow& R, int lane, v4u& ya, v4u& yc) {
;     ...
;     if (lane < 16) unpack8(R.oc, fc);
;     else { float f0[8], f1[8], f2[8]; unpack8(R.d0, f0); unpack8(R.d1, f1); unpack8(R.d2, f2);
;         const float inv = 1.0f / (R.l0 + R.l1 + R.l2);
; #pragma unroll
;         for (int e = 0; e < 8; ++e) fc[e] = (f0[e] + f1[e] + f2[e]) * inv; }
;     float sa = 0.f, sc = 0.f;
; #pragma unroll
;     for (int e = 0; e < 8; ++e) { sa += fa[e] * fa[e]; sc += fc[e] * fc[e]; }
;     const float s_moba = wave_sum(lane < 32 ? sa : 0.f), s_fox = wave_sum((lane >= 32 ? sa : 0.f) + (lane < 16 ? sc : 0.f)), s_dil = wave_sum(lane >= 16 ? sc : 0.f);
;     const float r_moba = 1.0f / sqrtf(s_moba * (1.0f / 256.0f) + EPS), r_fox = 1.0f / sqrtf(s_fox * (1.0f / 384.0f) + EPS), r_dil = 1.0f / sqrtf(s_dil * (1.0f / 384.0f) + EPS);
;     float ga[8], gc[8];
; #pragma unroll
;     for (int e = 0; e < 8; ++e) { ga[e] = 1.f; gc[e] = 1.f; }
;     if (lane >= 32) unpack8(R.ga, ga);
;     if (lane < 16) unpack8(R.gc, gc);
.LBB0_121:
	s_andn2_saveexec_b64 s[0:1], s[0:1]
	v_lshlrev_b32_e32 v130, 16, v46
	v_and_b32_e32 v114, 0xffff0000, v46
	v_lshlrev_b32_e32 v131, 16, v47
	v_and_b32_e32 v115, 0xffff0000, v47
	v_lshlrev_b32_e32 v128, 16, v48
	v_and_b32_e32 v116, 0xffff0000, v48
	v_lshlrev_b32_e32 v129, 16, v49
	v_and_b32_e32 v117, 0xffff0000, v49
	s_or_b64 exec, exec, s[0:1]
	v_lshlrev_b32_e32 v139, 16, v111
	v_lshlrev_b32_e32 v138, 16, v110
	v_and_b32_e32 v133, 0xffff0000, v111
	v_and_b32_e32 v132, 0xffff0000, v110
	v_lshlrev_b32_e32 v137, 16, v113
	v_lshlrev_b32_e32 v136, 16, v112
	v_and_b32_e32 v135, 0xffff0000, v113
	v_and_b32_e32 v134, 0xffff0000, v112
	v_pk_mul_f32 v[110:111], v[138:139], v[138:139]
	v_pk_mul_f32 v[112:113], v[132:133], v[132:133]
	v_mul_f32_e32 v144, v114, v114
	v_fmac_f32_e32 v144, v130, v130
	v_add_f32_e32 v110, v110, v112
	v_fmac_f32_e32 v144, v131, v131
	v_add_f32_e32 v110, v111, v110
	v_fmac_f32_e32 v144, v115, v115
	v_pk_mul_f32 v[140:141], v[136:137], v[136:137]
	v_add_f32_e32 v110, v113, v110
	v_fmac_f32_e32 v144, v128, v128
	v_pk_mul_f32 v[142:143], v[134:135], v[134:135]
	v_add_f32_e32 v110, v140, v110
	v_fmac_f32_e32 v144, v116, v116
	v_add_f32_e32 v110, v142, v110
	v_fmac_f32_e32 v144, v129, v129
	v_add_f32_e32 v110, v141, v110
	v_add_f32_e32 v110, v143, v110
	v_fmac_f32_e32 v144, v117, v117
	v_cndmask_b32_e64 v111, 0, v110, s[40:41]
	v_cndmask_b32_e64 v110, 0, v110, s[36:37]
	v_cndmask_b32_e64 v113, 0, v144, s[34:35]
	v_add_f32_e32 v110, v110, v113
	v_cndmask_b32_e64 v140, 0, v144, s[42:43]
	v_mov_b32_e32 v154, 1.0
	v_mov_b32_e32 v150, 1.0
	s_nop 1
	v_add_f32_dpp v111, v111, v111 quad_perm:[1,0,3,2] row_mask:0xf bank_mask:0xf
	s_nop 1
	v_add_f32_dpp v110, v110, v110 quad_perm:[1,0,3,2] row_mask:0xf bank_mask:0xf
	s_nop 1
	v_add_f32_dpp v140, v140, v140 quad_perm:[1,0,3,2] row_mask:0xf bank_mask:0xf
	v_mov_b32_e32 v155, 1.0
	v_mov_b32_e32 v151, 1.0
	s_nop 1
	v_add_f32_dpp v111, v111, v111 quad_perm:[2,3,0,1] row_mask:0xf bank_mask:0xf
	s_nop 1
	v_add_f32_dpp v110, v110, v110 quad_perm:[2,3,0,1] row_mask:0xf bank_mask:0xf
	s_nop 1
	v_add_f32_dpp v140, v140, v140 quad_perm:[2,3,0,1] row_mask:0xf bank_mask:0xf
	v_mov_b32_e32 v152, 1.0
	v_mov_b32_e32 v148, 1.0
	s_nop 1
	v_add_f32_dpp v111, v111, v111 row_half_mirror row_mask:0xf bank_mask:0xf
	s_nop 1
	v_add_f32_dpp v110, v110, v110 row_half_mirror row_mask:0xf bank_mask:0xf
	s_nop 1
	v_add_f32_dpp v140, v140, v140 row_half_mirror row_mask:0xf bank_mask:0xf
	v_mov_b32_e32 v153, 1.0
	v_mov_b32_e32 v149, 1.0
	s_nop 1
	v_add_f32_dpp v111, v111, v111 row_mirror row_mask:0xf bank_mask:0xf
	s_nop 1
	v_add_f32_dpp v110, v110, v110 row_mirror row_mask:0xf bank_mask:0xf
	s_nop 1
	v_add_f32_dpp v140, v140, v140 row_mirror row_mask:0xf bank_mask:0xf
	v_mov_b32_e32 v112, v111
	s_nop 1
	v_permlane16_swap_b32_e32 v111, v112
	v_add_f32_e32 v156, v111, v112
	v_mov_b32_e32 v113, v110
	s_nop 1
	v_permlane16_swap_b32_e32 v110, v113
	v_add_f32_e32 v176, v110, v113
	v_mov_b32_e32 v141, v140
	s_nop 1
	v_permlane16_swap_b32_e32 v140, v141
	v_add_f32_e32 v178, v140, v141
	v_mov_b32_e32 v140, 1.0
	s_and_saveexec_b64 s[0:1], s[36:37]
	v_lshlrev_b32_e32 v154, 16, v30
	v_and_b32_e32 v150, 0xffff0000, v30
	v_lshlrev_b32_e32 v155, 16, v31
	v_and_b32_e32 v151, 0xffff0000, v31
	v_lshlrev_b32_e32 v152, 16, v32
	v_and_b32_e32 v148, 0xffff0000, v32
	v_lshlrev_b32_e32 v153, 16, v33
	v_and_b32_e32 v149, 0xffff0000, v33
	s_or_b64 exec, exec, s[0:1]
	v_mov_b32_e32 v146, 1.0
	v_mov_b32_e32 v141, 1.0
	v_mov_b32_e32 v147, 1.0
	v_mov_b32_e32 v144, 1.0
	v_mov_b32_e32 v142, 1.0
	v_mov_b32_e32 v145, 1.0
	v_mov_b32_e32 v143, 1.0
	s_and_saveexec_b64 s[0:1], s[34:35]
	v_lshlrev_b32_e32 v140, 16, v26
	v_and_b32_e32 v146, 0xffff0000, v26
	v_lshlrev_b32_e32 v141, 16, v27
	v_and_b32_e32 v147, 0xffff0000, v27
	v_lshlrev_b32_e32 v144, 16, v28
	v_and_b32_e32 v142, 0xffff0000, v28
	v_lshlrev_b32_e32 v145, 16, v29
	v_and_b32_e32 v143, 0xffff0000, v29
	s_or_b64 exec, exec, s[0:1]
	s_or_b32 s0, s8, 6
	s_ashr_i32 s1, s0, 31
	s_lshl_b64 s[16:17], s[0:1], 11
	s_add_u32 s20, s29, s16
	s_addc_u32 s21, s30, s17
	global_load_dwordx4 v[110:113], v0, s[20:21] nt
	s_and_saveexec_b64 s[22:23], s[38:39]
	s_xor_b64 s[22:23], exec, s[22:23]
	s_cbranch_execz .LBB0_763
	v_mad_i64_i32 v[34:35], s[44:45], s0, v252, v[124:125]
	v_mad_i64_i32 v[38:39], s[44:45], s0, v252, v[122:123]
	v_mad_i64_i32 v[42:43], s[44:45], s0, v252, v[120:121]
	s_lshl_b64 s[44:45], s[0:1], 5
	s_add_u32 s44, s26, s44
	s_addc_u32 s45, s27, s45
	v_lshl_add_u64 v[180:181], v[118:119], 2, s[44:45]
	v_add_co_u32_e32 v168, vcc, 0x100000, v180
	global_load_dword v167, v[180:181], off
	s_nop 0
	v_addc_co_u32_e32 v169, vcc, 0, v181, vcc
	global_load_dword v168, v[168:169], off
	v_add_co_u32_e32 v180, vcc, 0x200000, v180
	global_load_dwordx4 v[34:37], v[34:35], off nt
	s_nop 0
	v_addc_co_u32_e32 v181, vcc, 0, v181, vcc
	global_load_dwordx4 v[38:41], v[38:39], off nt
	s_nop 0
	global_load_dwordx4 v[42:45], v[42:43], off nt
	s_nop 0
	global_load_dword v169, v[180:181], off
	s_andn2_saveexec_b64 s[22:23], s[22:23]
	s_cbranch_execnz .LBB0_764

; __device__ __forceinline__ unsigned pk2(float lo, float hi) { return f2bf(lo) | (f2bf(hi) << 16); }
; __device__ __forceinline__ void unpack8(const v4u w, float* f) { f[0] = bflo(w.x); f[1] = bfhi(w.x); f[2] = bflo(w.y); f[3] = bfhi(w.y); f[4] = bflo(w.z); f[5] = bfhi(w.z); f[6] = bflo(w.w); f[7] = bfhi(w.w); }
; __device__ __forceinline__ void norm_compute(const NormRow& R, int lane, v4u& ya, v4u& yc) {
;     ...
;     const float s_moba = wave_sum(lane < 32 ? sa : 0.f), s_fox = wave_sum((lane >= 32 ? sa : 0.f) + (lane < 16 ? sc : 0.f)), s_dil = wave_sum(lane >= 16 ? sc : 0.f);
;     const float r_moba = 1.0f / sqrtf(s_moba * (1.0f / 256.0f) + EPS), r_fox = 1.0f / sqrtf(s_fox * (1.0f / 384.0f) + EPS), r_dil = 1.0f / sqrtf(s_dil * (1.0f / 384.0f) + EPS);
;     float ga[8], gc[8];
; #pragma unroll
;     for (int e = 0; e < 8; ++e) { ga[e] = 1.f; gc[e] = 1.f; }
;     if (lane >= 32) unpack8(R.ga, ga);
;     if (lane < 16) unpack8(R.gc, gc);
;     const float ra = lane < 32 ? r_moba : r_fox, rc = lane < 16 ? r_fox : r_dil;
;     ya.x = pk2(fa[0] * ra * ga[0], fa[1] * ra * ga[1]); ya.y = pk2(fa[2] * ra * ga[2], fa[3] * ra * ga[3]); ya.z = pk2(fa[4] * ra * ga[4], fa[5] * ra * ga[5]); ya.w = pk2(fa[6] * ra * ga[6], fa[7] * ra * ga[7]);
;     yc.x = pk2(fc[0] * rc * gc[0], fc[1] * rc * gc[1]); yc.y = pk2(fc[2] * rc * gc[2], fc[3] * rc * gc[3]); yc.z = pk2(fc[4] * rc * gc[4], fc[5] * rc * gc[5]); yc.w = pk2(fc[6] * rc * gc[6], fc[7] * rc * gc[7]);
; }
.LBB0_131:
	s_or_b64 exec, exec, s[20:21]
	v_mov_b32_e32 v179, v178
	s_nop 1
	v_permlane32_swap_b32_e32 v178, v179
	v_add_f32_e32 v178, v178, v179
	v_fmamk_f32 v178, v178, 0x3b2aaaab, v215
	v_mul_f32_e32 v179, 0x4f800000, v178
	v_cmp_gt_f32_e32 vcc, s3, v178
	v_mov_b32_e32 v177, v176
	s_nop 1
	v_permlane32_swap_b32_e32 v176, v177
	v_add_f32_e32 v176, v176, v177
	v_fmamk_f32 v176, v176, 0x3b2aaaab, v215
	v_cndmask_b32_e32 v178, v178, v179, vcc
	v_sqrt_f32_e32 v179, v178
	v_mul_f32_e32 v177, 0x4f800000, v176
	v_mov_b32_e32 v157, v156
	s_nop 1
	v_permlane32_swap_b32_e32 v156, v157
	v_add_f32_e32 v156, v156, v157
	v_fmamk_f32 v156, v156, 0x3b800000, v215
	v_add_u32_e32 v180, -1, v179
	v_fma_f32 v182, -v180, v179, v178
	v_add_u32_e32 v181, 1, v179
	v_cmp_ge_f32_e64 s[0:1], 0, v182
	v_mul_f32_e32 v157, 0x4f800000, v156
	s_nop 0
	v_cndmask_b32_e64 v180, v179, v180, s[0:1]
	v_fma_f32 v179, -v181, v179, v178
	v_cmp_lt_f32_e64 s[0:1], 0, v179
	s_nop 1
	v_cndmask_b32_e64 v179, v180, v181, s[0:1]
	v_cmp_gt_f32_e64 s[0:1], s3, v176
	v_mul_f32_e32 v180, 0x37800000, v179
	v_cndmask_b32_e32 v179, v179, v180, vcc
	v_cndmask_b32_e64 v176, v176, v177, s[0:1]
	v_sqrt_f32_e32 v177, v176
	v_cmp_class_f32_e32 vcc, v178, v216
	s_nop 1
	v_cndmask_b32_e32 v178, v179, v178, vcc
	v_add_u32_e32 v179, -1, v177
	v_fma_f32 v180, -v179, v177, v176
	v_cmp_ge_f32_e32 vcc, 0, v180
	v_add_u32_e32 v180, 1, v177
	s_nop 0
	v_cndmask_b32_e32 v179, v177, v179, vcc
	v_fma_f32 v177, -v180, v177, v176
	v_cmp_lt_f32_e32 vcc, 0, v177
	s_nop 1
	v_cndmask_b32_e32 v177, v179, v180, vcc
	v_cmp_gt_f32_e32 vcc, s3, v156
	v_mul_f32_e32 v179, 0x37800000, v177
	v_cndmask_b32_e64 v177, v177, v179, s[0:1]
	v_cndmask_b32_e32 v156, v156, v157, vcc
	v_sqrt_f32_e32 v157, v156
	v_cmp_class_f32_e64 s[0:1], v176, v216
	s_nop 1
	v_cndmask_b32_e64 v176, v177, v176, s[0:1]
	v_add_u32_e32 v177, -1, v157
	v_fma_f32 v179, -v177, v157, v156
	v_cmp_ge_f32_e64 s[0:1], 0, v179
	v_add_u32_e32 v179, 1, v157
	s_nop 0
	v_cndmask_b32_e64 v177, v157, v177, s[0:1]
	v_fma_f32 v157, -v179, v157, v156
	v_cmp_lt_f32_e64 s[0:1], 0, v157
	s_nop 1
	v_cndmask_b32_e64 v157, v177, v179, s[0:1]
	v_div_scale_f32 v179, s[0:1], v178, v178, 1.0
	v_rcp_f32_e32 v180, v179
	v_mul_f32_e32 v177, 0x37800000, v157
	v_cndmask_b32_e32 v157, v157, v177, vcc
	v_cmp_class_f32_e32 vcc, v156, v216
	s_nop 1
	v_cndmask_b32_e32 v156, v157, v156, vcc
	v_fma_f32 v157, -v179, v180, 1.0
	v_fmac_f32_e32 v180, v157, v180
	v_div_scale_f32 v157, vcc, 1.0, v178, 1.0
	v_mul_f32_e32 v177, v157, v180
	v_fma_f32 v181, -v179, v177, v157
	v_fmac_f32_e32 v177, v181, v180
	v_fma_f32 v157, -v179, v177, v157
	v_div_scale_f32 v179, s[0:1], v176, v176, 1.0
	v_rcp_f32_e32 v181, v179
	v_div_fmas_f32 v157, v157, v180, v177
	v_div_fixup_f32 v157, v157, v178, 1.0
	v_fma_f32 v177, -v179, v181, 1.0
	v_fmac_f32_e32 v181, v177, v181
	v_div_scale_f32 v177, vcc, 1.0, v176, 1.0
	v_mul_f32_e32 v178, v177, v181
	v_fma_f32 v180, -v179, v178, v177
	v_fmac_f32_e32 v178, v180, v181
	v_fma_f32 v177, -v179, v178, v177
	v_div_scale_f32 v179, s[0:1], v156, v156, 1.0
	v_rcp_f32_e32 v180, v179
	v_div_fmas_f32 v177, v177, v181, v178
	v_div_fixup_f32 v176, v177, v176, 1.0
	s_movk_i32 s1, 0x7fff
	v_fma_f32 v177, -v179, v180, 1.0
	v_fmac_f32_e32 v180, v177, v180
	v_div_scale_f32 v177, vcc, 1.0, v156, 1.0
	v_mul_f32_e32 v178, v177, v180
	v_fma_f32 v181, -v179, v178, v177
	v_fmac_f32_e32 v178, v181, v180
	v_fma_f32 v177, -v179, v178, v177
	v_div_fmas_f32 v177, v177, v180, v178
	v_div_fixup_f32 v156, v177, v156, 1.0
	v_cndmask_b32_e64 v156, v176, v156, s[40:41]
	v_pk_mul_f32 v[132:133], v[156:157], v[132:133] op_sel_hi:[0,1]
	v_pk_mul_f32 v[134:135], v[156:157], v[134:135] op_sel_hi:[0,1]
	v_pk_mul_f32 v[138:139], v[156:157], v[138:139] op_sel_hi:[0,1]
	v_pk_mul_f32 v[132:133], v[132:133], v[150:151]
	v_pk_mul_f32 v[136:137], v[156:157], v[136:137] op_sel_hi:[0,1]
	v_pk_mul_f32 v[134:135], v[134:135], v[148:149]
	v_pk_mul_f32 v[138:139], v[138:139], v[154:155]
	v_pk_mul_f32 v[136:137], v[136:137], v[152:153]
	v_bfe_u32 v148, v135, 16, 1
	v_bfe_u32 v149, v134, 16, 1
	v_bfe_u32 v150, v133, 16, 1
	v_bfe_u32 v151, v132, 16, 1
	v_cndmask_b32_e64 v176, v157, v176, s[34:35]
	v_add3_u32 v132, v132, v151, s1
	v_add3_u32 v133, v133, v150, s1
	v_add3_u32 v134, v134, v149, s1
	v_add3_u32 v135, v135, v148, s1
	v_bfe_u32 v148, v138, 16, 1
	v_bfe_u32 v149, v139, 16, 1
	v_bfe_u32 v150, v136, 16, 1
	v_bfe_u32 v151, v137, 16, 1
	v_add3_u32 v137, v137, v151, s1
	v_add3_u32 v136, v136, v150, s1
	v_add3_u32 v139, v139, v149, s1
	v_add3_u32 v138, v138, v148, s1
	v_pk_mul_f32 v[114:115], v[114:115], v[176:177] op_sel_hi:[1,0]
	v_pk_mul_f32 v[116:117], v[116:117], v[176:177] op_sel_hi:[1,0]
	v_lshrrev_b32_e32 v138, 16, v138
	v_lshrrev_b32_e32 v139, 16, v139
	v_lshrrev_b32_e32 v136, 16, v136
	v_lshrrev_b32_e32 v137, 16, v137
	s_mov_b32 s0, 0xffff0000
	v_pk_mul_f32 v[130:131], v[130:131], v[176:177] op_sel_hi:[1,0]
	v_pk_mul_f32 v[114:115], v[114:115], v[146:147]
	v_pk_mul_f32 v[128:129], v[128:129], v[176:177] op_sel_hi:[1,0]
	v_pk_mul_f32 v[116:117], v[116:117], v[142:143]
	v_and_or_b32 v135, v135, s0, v137
	v_and_or_b32 v134, v134, s0, v136
	v_and_or_b32 v133, v133, s0, v139
	v_and_or_b32 v132, v132, s0, v138
	v_pk_mul_f32 v[130:131], v[130:131], v[140:141]
	v_pk_mul_f32 v[128:129], v[128:129], v[144:145]
	v_bfe_u32 v136, v117, 16, 1
	v_bfe_u32 v137, v116, 16, 1
	v_bfe_u32 v138, v115, 16, 1
	v_bfe_u32 v139, v114, 16, 1
	v_add3_u32 v114, v114, v139, s1
	v_add3_u32 v115, v115, v138, s1
	v_add3_u32 v116, v116, v137, s1
	v_add3_u32 v117, v117, v136, s1
	v_bfe_u32 v136, v130, 16, 1
	v_bfe_u32 v137, v131, 16, 1
	v_bfe_u32 v138, v128, 16, 1
	v_bfe_u32 v139, v129, 16, 1
	v_add3_u32 v129, v129, v139, s1
	v_add3_u32 v128, v128, v138, s1
	v_add3_u32 v131, v131, v137, s1
	v_add3_u32 v130, v130, v136, s1
	v_lshrrev_b32_e32 v130, 16, v130
	v_lshrrev_b32_e32 v131, 16, v131
	v_lshrrev_b32_e32 v128, 16, v128
	v_lshrrev_b32_e32 v129, 16, v129
	v_and_or_b32 v117, v117, s0, v129
	v_and_or_b32 v116, v116, s0, v128
	v_and_or_b32 v115, v115, s0, v131
	v_and_or_b32 v114, v114, s0, v130
	s_add_u32 s0, s24, s18
	s_addc_u32 s1, s25, s19
	global_store_dwordx4 v0, v[132:135], s[0:1]
	global_store_dwordx4 v0, v[114:117], s[0:1] offset:1024
	s_waitcnt vmcnt(32)
	s_and_saveexec_b64 s[0:1], s[38:39]
	s_xor_b64 s[0:1], exec, s[0:1]
	s_cbranch_execz .LBB0_133
; __device__ __forceinline__ void unpack8(const v4u w, float* f) { f[0] = bflo(w.x); f[1] = bfhi(w.x); f[2] = bflo(w.y); f[3] = bfhi(w.y); f[4] = bflo(w.z); f[5] = bfhi(w.z); f[6] = bflo(w.w); f[7] = bfhi(w.w); }
; __device__ __forceinline__ void norm_compute(const NormRow& R, int lane, v4u& ya, v4u& yc) {
;     ...
;     else { float f0[8], f1[8], f2[8]; unpack8(R.d0, f0); unpack8(R.d1, f1); unpack8(R.d2, f2);
;         const float inv = 1.0f / (R.l0 + R.l1 + R.l2);
; #pragma unroll
;         for (int e = 0; e < 8; ++e) fc[e] = (f0[e] + f1[e] + f2[e]) * inv; }
	v_add_f32_e32 v114, v165, v163
	v_add_f32_e32 v114, v166, v114
	v_div_scale_f32 v115, s[18:19], v114, v114, 1.0
	v_rcp_f32_e32 v130, v115
	v_lshlrev_b32_e32 v134, 16, v18
	v_and_b32_e32 v135, 0xffff0000, v18
	v_lshlrev_b32_e32 v136, 16, v19
	v_fma_f32 v131, -v115, v130, 1.0
	v_fmac_f32_e32 v130, v131, v130
	v_div_scale_f32 v131, vcc, 1.0, v114, 1.0
	v_mul_f32_e32 v132, v131, v130
	v_fma_f32 v133, -v115, v132, v131
	v_fmac_f32_e32 v132, v133, v130
	v_fma_f32 v115, -v115, v132, v131
	v_div_fmas_f32 v115, v115, v130, v132
	v_div_fixup_f32 v130, v115, v114, 1.0
	v_lshlrev_b32_e32 v114, 16, v10
	v_and_b32_e32 v115, 0xffff0000, v10
	v_lshlrev_b32_e32 v132, 16, v14
	v_and_b32_e32 v133, 0xffff0000, v14
	v_pk_add_f32 v[114:115], v[132:133], v[114:115]
	v_and_b32_e32 v137, 0xffff0000, v19
	v_pk_add_f32 v[114:115], v[114:115], v[134:135]
	v_lshlrev_b32_e32 v134, 16, v15
	v_pk_mul_f32 v[132:133], v[130:131], v[114:115] op_sel_hi:[0,1]
	v_lshlrev_b32_e32 v114, 16, v11
	v_and_b32_e32 v115, 0xffff0000, v11
	v_and_b32_e32 v135, 0xffff0000, v15
	v_pk_add_f32 v[114:115], v[134:135], v[114:115]
	v_lshlrev_b32_e32 v116, 16, v13
	v_lshlrev_b32_e32 v128, 16, v17
	v_and_b32_e32 v117, 0xffff0000, v13
	v_and_b32_e32 v129, 0xffff0000, v17
	v_pk_add_f32 v[114:115], v[114:115], v[136:137]
	v_lshlrev_b32_e32 v134, 16, v12
	v_and_b32_e32 v135, 0xffff0000, v12
	v_lshlrev_b32_e32 v136, 16, v16
	v_and_b32_e32 v137, 0xffff0000, v16
	v_lshlrev_b32_e32 v138, 16, v20
	v_and_b32_e32 v139, 0xffff0000, v20
	v_pk_add_f32 v[134:135], v[136:137], v[134:135]
	v_lshlrev_b32_e32 v136, 16, v21
	v_and_b32_e32 v137, 0xffff0000, v21
	v_pk_add_f32 v[116:117], v[128:129], v[116:117]
	v_pk_add_f32 v[134:135], v[134:135], v[138:139]
	v_pk_add_f32 v[116:117], v[116:117], v[136:137]
	v_pk_mul_f32 v[114:115], v[130:131], v[114:115] op_sel_hi:[0,1]
	v_pk_mul_f32 v[134:135], v[130:131], v[134:135] op_sel_hi:[0,1]
	v_pk_mul_f32 v[116:117], v[130:131], v[116:117] op_sel_hi:[0,1]
	v_mov_b32_e32 v129, v116
	v_mov_b32_e32 v116, v135
	v_mov_b32_e32 v128, v134
	v_mov_b32_e32 v131, v114
	v_mov_b32_e32 v114, v133
	v_mov_b32_e32 v130, v132
; __device__ __forceinline__ void unpack8(const v4u w, float* f) { f[0] = bflo(w.x); f[1] = bfhi(w.x); f[2] = bflo(w.y); f[3] = bfhi(w.y); f[4] = bflo(w.z); f[5] = bfhi(w.z); f[6] = bflo(w.w); f[7] = bfhi(w.w); }
; __device__ __forceinline__ float wave_sum(float v) {
; #pragma unroll
;     for (int o = 1; o < 64; o <<= 1) v += __shfl_xor(v, o);
;     return v;
; }
; __device__ __forceinline__ void norm_compute(const NormRow& R, int lane, v4u& ya, v4u& yc) {
;     ...
;     if (lane < 16) unpack8(R.oc, fc);
;     else { float f0[8], f1[8], f2[8]; unpack8(R.d0, f0); unpack8(R.d1, f1); unpack8(R.d2, f2);
;         const float inv = 1.0f / (R.l0 + R.l1 + R.l2);
; #pragma unroll
;         for (int e = 0; e < 8; ++e) fc[e] = (f0[e] + f1[e] + f2[e]) * inv; }
;     float sa = 0.f, sc = 0.f;
; #pragma unroll
;     for (int e = 0; e < 8; ++e) { sa += fa[e] * fa[e]; sc += fc[e] * fc[e]; }
;     const float s_moba = wave_sum(lane < 32 ? sa : 0.f), s_fox = wave_sum((lane >= 32 ? sa : 0.f) + (lane < 16 ? sc : 0.f)), s_dil = wave_sum(lane >= 16 ? sc : 0.f);
;     const float r_moba = 1.0f / sqrtf(s_moba * (1.0f / 256.0f) + EPS), r_fox = 1.0f / sqrtf(s_fox * (1.0f / 384.0f) + EPS), r_dil = 1.0f / sqrtf(s_dil * (1.0f / 384.0f) + EPS);
;     float ga[8], gc[8];
; #pragma unroll
;     for (int e = 0; e < 8; ++e) { ga[e] = 1.f; gc[e] = 1.f; }
;     if (lane >= 32) unpack8(R.ga, ga);
;     if (lane < 16) unpack8(R.gc, gc);
.LBB0_133:
	s_andn2_saveexec_b64 s[0:1], s[0:1]
	v_lshlrev_b32_e32 v130, 16, v22
	v_and_b32_e32 v114, 0xffff0000, v22
	v_lshlrev_b32_e32 v131, 16, v23
	v_and_b32_e32 v115, 0xffff0000, v23
	v_lshlrev_b32_e32 v128, 16, v24
	v_and_b32_e32 v116, 0xffff0000, v24
	v_lshlrev_b32_e32 v129, 16, v25
	v_and_b32_e32 v117, 0xffff0000, v25
	s_or_b64 exec, exec, s[0:1]
	v_lshlrev_b32_e32 v139, 16, v99
	v_lshlrev_b32_e32 v138, 16, v98
	v_and_b32_e32 v133, 0xffff0000, v99
	v_and_b32_e32 v132, 0xffff0000, v98
	v_lshlrev_b32_e32 v137, 16, v101
	v_lshlrev_b32_e32 v136, 16, v100
	v_and_b32_e32 v135, 0xffff0000, v101
	v_and_b32_e32 v134, 0xffff0000, v100
	v_pk_mul_f32 v[98:99], v[138:139], v[138:139]
	v_pk_mul_f32 v[100:101], v[132:133], v[132:133]
	v_mul_f32_e32 v144, v114, v114
	v_fmac_f32_e32 v144, v130, v130
	v_add_f32_e32 v98, v98, v100
	v_fmac_f32_e32 v144, v131, v131
	v_add_f32_e32 v98, v99, v98
	v_fmac_f32_e32 v144, v115, v115
	v_pk_mul_f32 v[140:141], v[136:137], v[136:137]
	v_add_f32_e32 v98, v101, v98
	v_fmac_f32_e32 v144, v128, v128
	v_pk_mul_f32 v[142:143], v[134:135], v[134:135]
	v_add_f32_e32 v98, v140, v98
	v_fmac_f32_e32 v144, v116, v116
	v_add_f32_e32 v98, v142, v98
	v_fmac_f32_e32 v144, v129, v129
	v_add_f32_e32 v98, v141, v98
	v_add_f32_e32 v98, v143, v98
	v_fmac_f32_e32 v144, v117, v117
	v_cndmask_b32_e64 v99, 0, v98, s[40:41]
	v_cndmask_b32_e64 v98, 0, v98, s[36:37]
	v_cndmask_b32_e64 v101, 0, v144, s[34:35]
	v_add_f32_e32 v98, v98, v101
	v_cndmask_b32_e64 v140, 0, v144, s[42:43]
	v_mov_b32_e32 v154, 1.0
	v_mov_b32_e32 v150, 1.0
	s_nop 1
	v_add_f32_dpp v99, v99, v99 quad_perm:[1,0,3,2] row_mask:0xf bank_mask:0xf
	s_nop 1
	v_add_f32_dpp v98, v98, v98 quad_perm:[1,0,3,2] row_mask:0xf bank_mask:0xf
	s_nop 1
	v_add_f32_dpp v140, v140, v140 quad_perm:[1,0,3,2] row_mask:0xf bank_mask:0xf
	v_mov_b32_e32 v155, 1.0
	v_mov_b32_e32 v151, 1.0
	s_nop 1
	v_add_f32_dpp v99, v99, v99 quad_perm:[2,3,0,1] row_mask:0xf bank_mask:0xf
	s_nop 1
	v_add_f32_dpp v98, v98, v98 quad_perm:[2,3,0,1] row_mask:0xf bank_mask:0xf
	s_nop 1
	v_add_f32_dpp v140, v140, v140 quad_perm:[2,3,0,1] row_mask:0xf bank_mask:0xf
	v_mov_b32_e32 v152, 1.0
	v_mov_b32_e32 v148, 1.0
	s_nop 1
	v_add_f32_dpp v99, v99, v99 row_half_mirror row_mask:0xf bank_mask:0xf
	s_nop 1
	v_add_f32_dpp v98, v98, v98 row_half_mirror row_mask:0xf bank_mask:0xf
	s_nop 1
	v_add_f32_dpp v140, v140, v140 row_half_mirror row_mask:0xf bank_mask:0xf
	v_mov_b32_e32 v153, 1.0
	v_mov_b32_e32 v149, 1.0
	s_nop 1
	v_add_f32_dpp v99, v99, v99 row_mirror row_mask:0xf bank_mask:0xf
	s_nop 1
	v_add_f32_dpp v98, v98, v98 row_mirror row_mask:0xf bank_mask:0xf
	s_nop 1
	v_add_f32_dpp v140, v140, v140 row_mirror row_mask:0xf bank_mask:0xf
	v_mov_b32_e32 v100, v99
	s_nop 1
	v_permlane16_swap_b32_e32 v99, v100
	v_add_f32_e32 v156, v99, v100
	v_mov_b32_e32 v101, v98
	s_nop 1
	v_permlane16_swap_b32_e32 v98, v101
	v_add_f32_e32 v176, v98, v101
	v_mov_b32_e32 v141, v140
	s_nop 1
	v_permlane16_swap_b32_e32 v140, v141
	v_add_f32_e32 v178, v140, v141
	v_mov_b32_e32 v140, 1.0
	s_and_saveexec_b64 s[0:1], s[36:37]
	v_lshlrev_b32_e32 v154, 16, v6
	v_and_b32_e32 v150, 0xffff0000, v6
	v_lshlrev_b32_e32 v155, 16, v7
	v_and_b32_e32 v151, 0xffff0000, v7
	v_lshlrev_b32_e32 v152, 16, v8
	v_and_b32_e32 v148, 0xffff0000, v8
	v_lshlrev_b32_e32 v153, 16, v9
	v_and_b32_e32 v149, 0xffff0000, v9
	s_or_b64 exec, exec, s[0:1]
	v_mov_b32_e32 v146, 1.0
	v_mov_b32_e32 v141, 1.0
	v_mov_b32_e32 v147, 1.0
	v_mov_b32_e32 v144, 1.0
	v_mov_b32_e32 v142, 1.0
	v_mov_b32_e32 v145, 1.0
	v_mov_b32_e32 v143, 1.0
	s_and_saveexec_b64 s[0:1], s[34:35]
	v_lshlrev_b32_e32 v140, 16, v2
	v_and_b32_e32 v146, 0xffff0000, v2
	v_lshlrev_b32_e32 v141, 16, v3
	v_and_b32_e32 v147, 0xffff0000, v3
	v_lshlrev_b32_e32 v144, 16, v4
	v_and_b32_e32 v142, 0xffff0000, v4
	v_lshlrev_b32_e32 v145, 16, v5
	v_and_b32_e32 v143, 0xffff0000, v5
	s_or_b64 exec, exec, s[0:1]
	s_or_b32 s0, s8, 7
	s_ashr_i32 s1, s0, 31
	s_lshl_b64 s[18:19], s[0:1], 11
	s_add_u32 s20, s29, s18
	s_addc_u32 s21, s30, s19
	global_load_dwordx4 v[98:101], v0, s[20:21] nt
	s_and_saveexec_b64 s[22:23], s[38:39]
	s_xor_b64 s[22:23], exec, s[22:23]
	s_cbranch_execz .LBB0_765
	v_mad_i64_i32 v[10:11], s[44:45], s0, v252, v[124:125]
	v_mad_i64_i32 v[14:15], s[44:45], s0, v252, v[122:123]
	v_mad_i64_i32 v[18:19], s[44:45], s0, v252, v[120:121]
	s_lshl_b64 s[44:45], s[0:1], 5
	s_add_u32 s44, s26, s44
	s_addc_u32 s45, s27, s45
	v_lshl_add_u64 v[180:181], v[118:119], 2, s[44:45]
	v_add_co_u32_e32 v182, vcc, 0x100000, v180
	global_load_dword v163, v[180:181], off
	s_nop 0
	v_addc_co_u32_e32 v183, vcc, 0, v181, vcc
	global_load_dword v165, v[182:183], off
	v_add_co_u32_e32 v180, vcc, 0x200000, v180
	global_load_dwordx4 v[10:13], v[10:11], off nt
	s_nop 0
	v_addc_co_u32_e32 v181, vcc, 0, v181, vcc
	global_load_dwordx4 v[14:17], v[14:15], off nt
	s_nop 0
	global_load_dwordx4 v[18:21], v[18:19], off nt
	s_nop 0
	global_load_dword v166, v[180:181], off
	s_andn2_saveexec_b64 s[22:23], s[22:23]
	s_cbranch_execnz .LBB0_766

; __device__ __forceinline__ unsigned pk2(float lo, float hi) { return f2bf(lo) | (f2bf(hi) << 16); }
; __device__ __forceinline__ void unpack8(const v4u w, float* f) { f[0] = bflo(w.x); f[1] = bfhi(w.x); f[2] = bflo(w.y); f[3] = bfhi(w.y); f[4] = bflo(w.z); f[5] = bfhi(w.z); f[6] = bflo(w.w); f[7] = bfhi(w.w); }
; __device__ __forceinline__ void norm_compute(const NormRow& R, int lane, v4u& ya, v4u& yc) {
;     ...
;     const float s_moba = wave_sum(lane < 32 ? sa : 0.f), s_fox = wave_sum((lane >= 32 ? sa : 0.f) + (lane < 16 ? sc : 0.f)), s_dil = wave_sum(lane >= 16 ? sc : 0.f);
;     const float r_moba = 1.0f / sqrtf(s_moba * (1.0f / 256.0f) + EPS), r_fox = 1.0f / sqrtf(s_fox * (1.0f / 384.0f) + EPS), r_dil = 1.0f / sqrtf(s_dil * (1.0f / 384.0f) + EPS);
;     float ga[8], gc[8];
; #pragma unroll
;     for (int e = 0; e < 8; ++e) { ga[e] = 1.f; gc[e] = 1.f; }
;     if (lane >= 32) unpack8(R.ga, ga);
;     if (lane < 16) unpack8(R.gc, gc);
;     const float ra = lane < 32 ? r_moba : r_fox, rc = lane < 16 ? r_fox : r_dil;
;     ya.x = pk2(fa[0] * ra * ga[0], fa[1] * ra * ga[1]); ya.y = pk2(fa[2] * ra * ga[2], fa[3] * ra * ga[3]); ya.z = pk2(fa[4] * ra * ga[4], fa[5] * ra * ga[5]); ya.w = pk2(fa[6] * ra * ga[6], fa[7] * ra * ga[7]);
;     yc.x = pk2(fc[0] * rc * gc[0], fc[1] * rc * gc[1]); yc.y = pk2(fc[2] * rc * gc[2], fc[3] * rc * gc[3]); yc.z = pk2(fc[4] * rc * gc[4], fc[5] * rc * gc[5]); yc.w = pk2(fc[6] * rc * gc[6], fc[7] * rc * gc[7]);
; }
.LBB0_143:
	s_or_b64 exec, exec, s[20:21]
	v_mov_b32_e32 v179, v178
	s_nop 1
	v_permlane32_swap_b32_e32 v178, v179
	v_add_f32_e32 v178, v178, v179
	v_fmamk_f32 v178, v178, 0x3b2aaaab, v215
	v_mul_f32_e32 v179, 0x4f800000, v178
	v_cmp_gt_f32_e32 vcc, s3, v178
	v_mov_b32_e32 v177, v176
	s_nop 1
	v_permlane32_swap_b32_e32 v176, v177
	v_add_f32_e32 v176, v176, v177
	v_fmamk_f32 v176, v176, 0x3b2aaaab, v215
	v_cndmask_b32_e32 v178, v178, v179, vcc
	v_sqrt_f32_e32 v179, v178
	v_mul_f32_e32 v177, 0x4f800000, v176
	v_mov_b32_e32 v157, v156
	s_nop 1
	v_permlane32_swap_b32_e32 v156, v157
	v_add_f32_e32 v156, v156, v157
	v_fmamk_f32 v156, v156, 0x3b800000, v215
	v_add_u32_e32 v180, -1, v179
	v_fma_f32 v182, -v180, v179, v178
	v_add_u32_e32 v181, 1, v179
	v_cmp_ge_f32_e64 s[0:1], 0, v182
	v_mul_f32_e32 v157, 0x4f800000, v156
	s_nop 0
	v_cndmask_b32_e64 v180, v179, v180, s[0:1]
	v_fma_f32 v179, -v181, v179, v178
	v_cmp_lt_f32_e64 s[0:1], 0, v179
	s_nop 1
	v_cndmask_b32_e64 v179, v180, v181, s[0:1]
	v_cmp_gt_f32_e64 s[0:1], s3, v176
	v_mul_f32_e32 v180, 0x37800000, v179
	v_cndmask_b32_e32 v179, v179, v180, vcc
	v_cndmask_b32_e64 v176, v176, v177, s[0:1]
	v_sqrt_f32_e32 v177, v176
	v_cmp_class_f32_e32 vcc, v178, v216
	s_nop 1
	v_cndmask_b32_e32 v178, v179, v178, vcc
	v_add_u32_e32 v179, -1, v177
	v_fma_f32 v180, -v179, v177, v176
	v_cmp_ge_f32_e32 vcc, 0, v180
	v_add_u32_e32 v180, 1, v177
	s_nop 0
	v_cndmask_b32_e32 v179, v177, v179, vcc
	v_fma_f32 v177, -v180, v177, v176
	v_cmp_lt_f32_e32 vcc, 0, v177
	s_nop 1
	v_cndmask_b32_e32 v177, v179, v180, vcc
	v_cmp_gt_f32_e32 vcc, s3, v156
	v_mul_f32_e32 v179, 0x37800000, v177
	v_cndmask_b32_e64 v177, v177, v179, s[0:1]
	v_cndmask_b32_e32 v156, v156, v157, vcc
	v_sqrt_f32_e32 v157, v156
	v_cmp_class_f32_e64 s[0:1], v176, v216
	s_nop 1
	v_cndmask_b32_e64 v176, v177, v176, s[0:1]
	v_add_u32_e32 v177, -1, v157
	v_fma_f32 v179, -v177, v157, v156
	v_cmp_ge_f32_e64 s[0:1], 0, v179
	v_add_u32_e32 v179, 1, v157
	s_nop 0
	v_cndmask_b32_e64 v177, v157, v177, s[0:1]
	v_fma_f32 v157, -v179, v157, v156
	v_cmp_lt_f32_e64 s[0:1], 0, v157
	s_nop 1
	v_cndmask_b32_e64 v157, v177, v179, s[0:1]
	v_div_scale_f32 v179, s[0:1], v178, v178, 1.0
	v_rcp_f32_e32 v180, v179
	v_mul_f32_e32 v177, 0x37800000, v157
	v_cndmask_b32_e32 v157, v157, v177, vcc
	v_cmp_class_f32_e32 vcc, v156, v216
	s_nop 1
	v_cndmask_b32_e32 v156, v157, v156, vcc
	v_fma_f32 v157, -v179, v180, 1.0
	v_fmac_f32_e32 v180, v157, v180
	v_div_scale_f32 v157, vcc, 1.0, v178, 1.0
	v_mul_f32_e32 v177, v157, v180
	v_fma_f32 v181, -v179, v177, v157
	v_fmac_f32_e32 v177, v181, v180
	v_fma_f32 v157, -v179, v177, v157
	v_div_scale_f32 v179, s[0:1], v176, v176, 1.0
	v_rcp_f32_e32 v181, v179
	v_div_fmas_f32 v157, v157, v180, v177
	v_div_fixup_f32 v157, v157, v178, 1.0
	v_fma_f32 v177, -v179, v181, 1.0
	v_fmac_f32_e32 v181, v177, v181
	v_div_scale_f32 v177, vcc, 1.0, v176, 1.0
	v_mul_f32_e32 v178, v177, v181
	v_fma_f32 v180, -v179, v178, v177
	v_fmac_f32_e32 v178, v180, v181
	v_fma_f32 v177, -v179, v178, v177
	v_div_scale_f32 v179, s[0:1], v156, v156, 1.0
	v_rcp_f32_e32 v180, v179
	v_div_fmas_f32 v177, v177, v181, v178
	v_div_fixup_f32 v176, v177, v176, 1.0
	s_movk_i32 s1, 0x7fff
	v_fma_f32 v177, -v179, v180, 1.0
	v_fmac_f32_e32 v180, v177, v180
	v_div_scale_f32 v177, vcc, 1.0, v156, 1.0
	v_mul_f32_e32 v178, v177, v180
	v_fma_f32 v181, -v179, v178, v177
	v_fmac_f32_e32 v178, v181, v180
	v_fma_f32 v177, -v179, v178, v177
	v_div_fmas_f32 v177, v177, v180, v178
	v_div_fixup_f32 v156, v177, v156, 1.0
	v_cndmask_b32_e64 v156, v176, v156, s[40:41]
	v_pk_mul_f32 v[132:133], v[156:157], v[132:133] op_sel_hi:[0,1]
	v_pk_mul_f32 v[134:135], v[156:157], v[134:135] op_sel_hi:[0,1]
	v_pk_mul_f32 v[138:139], v[156:157], v[138:139] op_sel_hi:[0,1]
	v_pk_mul_f32 v[132:133], v[132:133], v[150:151]
	v_pk_mul_f32 v[136:137], v[156:157], v[136:137] op_sel_hi:[0,1]
	v_pk_mul_f32 v[134:135], v[134:135], v[148:149]
	v_pk_mul_f32 v[138:139], v[138:139], v[154:155]
	v_pk_mul_f32 v[136:137], v[136:137], v[152:153]
	v_bfe_u32 v148, v135, 16, 1
	v_bfe_u32 v149, v134, 16, 1
	v_bfe_u32 v150, v133, 16, 1
	v_bfe_u32 v151, v132, 16, 1
	v_cndmask_b32_e64 v176, v157, v176, s[34:35]
	v_add3_u32 v132, v132, v151, s1
	v_add3_u32 v133, v133, v150, s1
	v_add3_u32 v134, v134, v149, s1
	v_add3_u32 v135, v135, v148, s1
	v_bfe_u32 v148, v138, 16, 1
	v_bfe_u32 v149, v139, 16, 1
	v_bfe_u32 v150, v136, 16, 1
	v_bfe_u32 v151, v137, 16, 1
	v_add3_u32 v137, v137, v151, s1
	v_add3_u32 v136, v136, v150, s1
	v_add3_u32 v139, v139, v149, s1
	v_add3_u32 v138, v138, v148, s1
	v_pk_mul_f32 v[114:115], v[114:115], v[176:177] op_sel_hi:[1,0]
	v_pk_mul_f32 v[116:117], v[116:117], v[176:177] op_sel_hi:[1,0]
	v_lshrrev_b32_e32 v138, 16, v138
	v_lshrrev_b32_e32 v139, 16, v139
	v_lshrrev_b32_e32 v136, 16, v136
	v_lshrrev_b32_e32 v137, 16, v137
	s_mov_b32 s0, 0xffff0000
	v_pk_mul_f32 v[130:131], v[130:131], v[176:177] op_sel_hi:[1,0]
	v_pk_mul_f32 v[114:115], v[114:115], v[146:147]
	v_pk_mul_f32 v[128:129], v[128:129], v[176:177] op_sel_hi:[1,0]
	v_pk_mul_f32 v[116:117], v[116:117], v[142:143]
	v_and_or_b32 v135, v135, s0, v137
	v_and_or_b32 v134, v134, s0, v136
	v_and_or_b32 v133, v133, s0, v139
	v_and_or_b32 v132, v132, s0, v138
	v_pk_mul_f32 v[130:131], v[130:131], v[140:141]
	v_pk_mul_f32 v[128:129], v[128:129], v[144:145]
	v_bfe_u32 v136, v117, 16, 1
	v_bfe_u32 v137, v116, 16, 1
	v_bfe_u32 v138, v115, 16, 1
	v_bfe_u32 v139, v114, 16, 1
	v_add3_u32 v114, v114, v139, s1
	v_add3_u32 v115, v115, v138, s1
	v_add3_u32 v116, v116, v137, s1
	v_add3_u32 v117, v117, v136, s1
	v_bfe_u32 v136, v130, 16, 1
	v_bfe_u32 v137, v131, 16, 1
	v_bfe_u32 v138, v128, 16, 1
	v_bfe_u32 v139, v129, 16, 1
	v_add3_u32 v129, v129, v139, s1
	v_add3_u32 v128, v128, v138, s1
	v_add3_u32 v131, v131, v137, s1
	v_add3_u32 v130, v130, v136, s1
	v_lshrrev_b32_e32 v130, 16, v130
	v_lshrrev_b32_e32 v131, 16, v131
	v_lshrrev_b32_e32 v128, 16, v128
	v_lshrrev_b32_e32 v129, 16, v129
	v_and_or_b32 v117, v117, s0, v129
	v_and_or_b32 v116, v116, s0, v128
	v_and_or_b32 v115, v115, s0, v131
	v_and_or_b32 v114, v114, s0, v130
	s_add_u32 s0, s24, s10
	s_addc_u32 s1, s25, s11
	global_store_dwordx4 v0, v[132:135], s[0:1]
	global_store_dwordx4 v0, v[114:117], s[0:1] offset:1024
	s_and_saveexec_b64 s[0:1], s[38:39]
	s_xor_b64 s[0:1], exec, s[0:1]
	s_cbranch_execz .LBB0_145
; __device__ __forceinline__ void unpack8(const v4u w, float* f) { f[0] = bflo(w.x); f[1] = bfhi(w.x); f[2] = bflo(w.y); f[3] = bfhi(w.y); f[4] = bflo(w.z); f[5] = bfhi(w.z); f[6] = bflo(w.w); f[7] = bfhi(w.w); }
; __device__ __forceinline__ void norm_compute(const NormRow& R, int lane, v4u& ya, v4u& yc) {
;     ...
;     if (lane < 16) unpack8(R.oc, fc);
;     else { float f0[8], f1[8], f2[8]; unpack8(R.d0, f0); unpack8(R.d1, f1); unpack8(R.d2, f2);
;         const float inv = 1.0f / (R.l0 + R.l1 + R.l2);
; #pragma unroll
;         for (int e = 0; e < 8; ++e) fc[e] = (f0[e] + f1[e] + f2[e]) * inv; }
	s_waitcnt vmcnt(34)
	v_add_f32_e32 v114, v173, v174
	v_add_f32_e32 v114, v114, v175
	v_div_scale_f32 v115, s[10:11], v114, v114, 1.0
	v_rcp_f32_e32 v130, v115
	v_lshlrev_b32_e32 v134, 16, v90
	v_and_b32_e32 v135, 0xffff0000, v90
	v_lshlrev_b32_e32 v136, 16, v91
	v_fma_f32 v131, -v115, v130, 1.0
	v_fmac_f32_e32 v130, v131, v130
	v_div_scale_f32 v131, vcc, 1.0, v114, 1.0
	v_mul_f32_e32 v132, v131, v130
	v_fma_f32 v133, -v115, v132, v131
	v_fmac_f32_e32 v132, v133, v130
	v_fma_f32 v115, -v115, v132, v131
	v_div_fmas_f32 v115, v115, v130, v132
	v_div_fixup_f32 v130, v115, v114, 1.0
	v_lshlrev_b32_e32 v114, 16, v82
	v_and_b32_e32 v115, 0xffff0000, v82
	v_lshlrev_b32_e32 v132, 16, v86
	v_and_b32_e32 v133, 0xffff0000, v86
	v_pk_add_f32 v[114:115], v[132:133], v[114:115]
	v_and_b32_e32 v137, 0xffff0000, v91
	v_pk_add_f32 v[114:115], v[114:115], v[134:135]
	v_lshlrev_b32_e32 v134, 16, v87
	v_pk_mul_f32 v[132:133], v[114:115], v[130:131] op_sel_hi:[1,0]
	v_lshlrev_b32_e32 v114, 16, v83
	v_and_b32_e32 v115, 0xffff0000, v83
	v_and_b32_e32 v135, 0xffff0000, v87
	v_pk_add_f32 v[114:115], v[134:135], v[114:115]
	v_lshlrev_b32_e32 v116, 16, v85
	v_lshlrev_b32_e32 v128, 16, v89
	v_and_b32_e32 v117, 0xffff0000, v85
	v_and_b32_e32 v129, 0xffff0000, v89
	v_pk_add_f32 v[114:115], v[114:115], v[136:137]
	v_lshlrev_b32_e32 v134, 16, v84
	v_and_b32_e32 v135, 0xffff0000, v84
	v_lshlrev_b32_e32 v136, 16, v88
	v_and_b32_e32 v137, 0xffff0000, v88
	v_lshlrev_b32_e32 v138, 16, v92
	v_and_b32_e32 v139, 0xffff0000, v92
	v_pk_add_f32 v[134:135], v[136:137], v[134:135]
	v_lshlrev_b32_e32 v136, 16, v93
	v_and_b32_e32 v137, 0xffff0000, v93
	v_pk_add_f32 v[116:117], v[128:129], v[116:117]
	v_pk_add_f32 v[134:135], v[134:135], v[138:139]
	v_pk_add_f32 v[116:117], v[116:117], v[136:137]
	v_pk_mul_f32 v[114:115], v[114:115], v[130:131] op_sel_hi:[1,0]
	v_pk_mul_f32 v[134:135], v[134:135], v[130:131] op_sel_hi:[1,0]
	v_pk_mul_f32 v[116:117], v[116:117], v[130:131] op_sel_hi:[1,0]
	v_mov_b32_e32 v128, v134
	v_mov_b32_e32 v129, v116
	v_mov_b32_e32 v116, v135
	v_mov_b32_e32 v131, v114
	v_mov_b32_e32 v114, v133
	v_mov_b32_e32 v130, v132
.LBB0_145:
	s_andn2_saveexec_b64 s[0:1], s[0:1]
	s_cbranch_execz .LBB0_147
	s_waitcnt vmcnt(34)
	v_lshlrev_b32_e32 v130, 16, v94
	v_and_b32_e32 v114, 0xffff0000, v94
	v_lshlrev_b32_e32 v131, 16, v95
	v_and_b32_e32 v115, 0xffff0000, v95
	v_lshlrev_b32_e32 v128, 16, v96
	v_and_b32_e32 v116, 0xffff0000, v96
	v_lshlrev_b32_e32 v129, 16, v97
	v_and_b32_e32 v117, 0xffff0000, v97
; #define GAS __attribute__((address_space(1)))
; __device__ __forceinline__ void unpack8(const v4u w, float* f) { f[0] = bflo(w.x); f[1] = bfhi(w.x); f[2] = bflo(w.y); f[3] = bfhi(w.y); f[4] = bflo(w.z); f[5] = bfhi(w.z); f[6] = bflo(w.w); f[7] = bfhi(w.w); }
; __device__ __forceinline__ void norm_load(NormRow& R, int m, int lane, const bf16* O, const bf16* GF, const bf16* OD, const float* LD) {
;     R.oa = __builtin_nontemporal_load((const GAS v4u*)(O + (size_t)m * DM + 8 * lane));
;     if (lane < 16) { R.oc = __builtin_nontemporal_load((const GAS v4u*)(O + (size_t)m * DM + 512 + 8 * lane)); R.gc = __builtin_nontemporal_load((const GAS v4u*)(GF + (size_t)m * 384 + 256 + 8 * lane)); }
;     else { const int dc = 8 * lane - 128, hd = dc >> 6;
;         R.d0 = __builtin_nontemporal_load((const GAS v4u*)(OD + (size_t)m * 384 + dc)); R.d1 = __builtin_nontemporal_load((const GAS v4u*)(OD + OD_BRANCH + (size_t)m * 384 + dc)); R.d2 = __builtin_nontemporal_load((const GAS v4u*)(OD + 2 * OD_BRANCH + (size_t)m * 384 + dc));
;         R.l0 = LD[(size_t)m * 8 + hd]; R.l1 = LD[LD_BRANCH + (size_t)m * 8 + hd]; R.l2 = LD[2 * LD_BRANCH + (size_t)m * 8 + hd]; }
;     if (lane >= 32) R.ga = __builtin_nontemporal_load((const GAS v4u*)(GF + (size_t)m * 384 + 8 * lane - 256));
; __device__ __forceinline__ void norm_compute(const NormRow& R, int lane, v4u& ya, v4u& yc) {
;     ...
;     float sa = 0.f, sc = 0.f;
; #pragma unroll
;     for (int e = 0; e < 8; ++e) { sa += fa[e] * fa[e]; sc += fc[e] * fc[e]; }
;     const float s_moba = wave_sum(lane < 32 ? sa : 0.f), s_fox = wave_sum((lane >= 32 ? sa : 0.f) + (lane < 16 ? sc : 0.f)), s_dil = wave_sum(lane >= 16 ? sc : 0.f);
;     const float r_moba = 1.0f / sqrtf(s_moba * (1.0f / 256.0f) + EPS), r_fox = 1.0f / sqrtf(s_fox * (1.0f / 384.0f) + EPS), r_dil = 1.0f / sqrtf(s_dil * (1.0f / 384.0f) + EPS);
;     float ga[8], gc[8];
; #pragma unroll
;     for (int e = 0; e < 8; ++e) { ga[e] = 1.f; gc[e] = 1.f; }
;     if (lane >= 32) unpack8(R.ga, ga);
;     if (lane < 16) unpack8(R.gc, gc);
.LBB0_147:
	s_or_b64 exec, exec, s[0:1]
	s_waitcnt vmcnt(34)
	v_lshlrev_b32_e32 v139, 16, v103
	v_lshlrev_b32_e32 v138, 16, v102
	v_and_b32_e32 v133, 0xffff0000, v103
	v_and_b32_e32 v132, 0xffff0000, v102
	v_lshlrev_b32_e32 v137, 16, v105
	v_lshlrev_b32_e32 v136, 16, v104
	v_and_b32_e32 v135, 0xffff0000, v105
	v_and_b32_e32 v134, 0xffff0000, v104
	v_pk_mul_f32 v[102:103], v[138:139], v[138:139]
	v_pk_mul_f32 v[104:105], v[132:133], v[132:133]
	v_mul_f32_e32 v144, v114, v114
	v_fmac_f32_e32 v144, v130, v130
	v_add_f32_e32 v102, v102, v104
	v_fmac_f32_e32 v144, v131, v131
	v_add_f32_e32 v102, v103, v102
	v_fmac_f32_e32 v144, v115, v115
	v_pk_mul_f32 v[140:141], v[136:137], v[136:137]
	v_add_f32_e32 v102, v105, v102
	v_fmac_f32_e32 v144, v128, v128
	v_pk_mul_f32 v[142:143], v[134:135], v[134:135]
	v_add_f32_e32 v102, v140, v102
	v_fmac_f32_e32 v144, v116, v116
	v_add_f32_e32 v102, v142, v102
	v_fmac_f32_e32 v144, v129, v129
	v_add_f32_e32 v102, v141, v102
	v_add_f32_e32 v102, v143, v102
	v_fmac_f32_e32 v144, v117, v117
	v_cndmask_b32_e64 v103, 0, v102, s[40:41]
	v_cndmask_b32_e64 v102, 0, v102, s[36:37]
	v_cndmask_b32_e64 v105, 0, v144, s[34:35]
	v_add_f32_e32 v102, v102, v105
	v_cndmask_b32_e64 v140, 0, v144, s[42:43]
	v_mov_b32_e32 v154, 1.0
	v_mov_b32_e32 v150, 1.0
	s_nop 1
	v_add_f32_dpp v103, v103, v103 quad_perm:[1,0,3,2] row_mask:0xf bank_mask:0xf
	s_nop 1
	v_add_f32_dpp v102, v102, v102 quad_perm:[1,0,3,2] row_mask:0xf bank_mask:0xf
	s_nop 1
	v_add_f32_dpp v140, v140, v140 quad_perm:[1,0,3,2] row_mask:0xf bank_mask:0xf
	v_mov_b32_e32 v155, 1.0
	v_mov_b32_e32 v151, 1.0
	s_nop 1
	v_add_f32_dpp v103, v103, v103 quad_perm:[2,3,0,1] row_mask:0xf bank_mask:0xf
	s_nop 1
	v_add_f32_dpp v102, v102, v102 quad_perm:[2,3,0,1] row_mask:0xf bank_mask:0xf
	s_nop 1
	v_add_f32_dpp v140, v140, v140 quad_perm:[2,3,0,1] row_mask:0xf bank_mask:0xf
	v_mov_b32_e32 v152, 1.0
	v_mov_b32_e32 v148, 1.0
	s_nop 1
	v_add_f32_dpp v103, v103, v103 row_half_mirror row_mask:0xf bank_mask:0xf
	s_nop 1
	v_add_f32_dpp v102, v102, v102 row_half_mirror row_mask:0xf bank_mask:0xf
	s_nop 1
	v_add_f32_dpp v140, v140, v140 row_half_mirror row_mask:0xf bank_mask:0xf
	v_mov_b32_e32 v153, 1.0
	v_mov_b32_e32 v149, 1.0
	s_nop 1
	v_add_f32_dpp v103, v103, v103 row_mirror row_mask:0xf bank_mask:0xf
	s_nop 1
	v_add_f32_dpp v102, v102, v102 row_mirror row_mask:0xf bank_mask:0xf
	s_nop 1
	v_add_f32_dpp v140, v140, v140 row_mirror row_mask:0xf bank_mask:0xf
	v_mov_b32_e32 v104, v103
	s_nop 1
	v_permlane16_swap_b32_e32 v103, v104
	v_add_f32_e32 v156, v103, v104
	v_mov_b32_e32 v105, v102
	s_nop 1
	v_permlane16_swap_b32_e32 v102, v105
	v_add_f32_e32 v176, v102, v105
	v_mov_b32_e32 v141, v140
	s_nop 1
	v_permlane16_swap_b32_e32 v140, v141
	v_add_f32_e32 v178, v140, v141
	v_mov_b32_e32 v140, 1.0
	s_and_saveexec_b64 s[0:1], s[36:37]
	v_lshlrev_b32_e32 v154, 16, v78
	v_and_b32_e32 v150, 0xffff0000, v78
	v_lshlrev_b32_e32 v155, 16, v79
	v_and_b32_e32 v151, 0xffff0000, v79
	v_lshlrev_b32_e32 v152, 16, v80
	v_and_b32_e32 v148, 0xffff0000, v80
	v_lshlrev_b32_e32 v153, 16, v81
	v_and_b32_e32 v149, 0xffff0000, v81
	s_or_b64 exec, exec, s[0:1]
	v_mov_b32_e32 v146, 1.0
	v_mov_b32_e32 v141, 1.0
	v_mov_b32_e32 v147, 1.0
	v_mov_b32_e32 v144, 1.0
	v_mov_b32_e32 v142, 1.0
	v_mov_b32_e32 v145, 1.0
	v_mov_b32_e32 v143, 1.0
	s_and_saveexec_b64 s[0:1], s[34:35]
	v_lshlrev_b32_e32 v140, 16, v74
	v_and_b32_e32 v146, 0xffff0000, v74
	v_lshlrev_b32_e32 v141, 16, v75
	v_and_b32_e32 v147, 0xffff0000, v75
	v_lshlrev_b32_e32 v144, 16, v76
	v_and_b32_e32 v142, 0xffff0000, v76
	v_lshlrev_b32_e32 v145, 16, v77
	v_and_b32_e32 v143, 0xffff0000, v77
	s_or_b64 exec, exec, s[0:1]
	s_or_b32 s0, s8, 8
	s_ashr_i32 s1, s0, 31
	s_lshl_b64 s[10:11], s[0:1], 11
	s_add_u32 s20, s29, s10
	s_addc_u32 s21, s30, s11
	global_load_dwordx4 v[102:105], v0, s[20:21] nt
	s_and_saveexec_b64 s[22:23], s[38:39]
	s_xor_b64 s[22:23], exec, s[22:23]
	s_cbranch_execz .LBB0_767
	v_mad_i64_i32 v[82:83], s[44:45], s0, v252, v[124:125]
	v_mad_i64_i32 v[86:87], s[44:45], s0, v252, v[122:123]
	v_mad_i64_i32 v[90:91], s[44:45], s0, v252, v[120:121]
	s_lshl_b64 s[44:45], s[0:1], 5
	s_add_u32 s44, s26, s44
	s_addc_u32 s45, s27, s45
	v_lshl_add_u64 v[180:181], v[118:119], 2, s[44:45]
	v_add_co_u32_e32 v174, vcc, 0x100000, v180
	global_load_dword v173, v[180:181], off
	s_nop 0
	v_addc_co_u32_e32 v175, vcc, 0, v181, vcc
	global_load_dword v174, v[174:175], off
	v_add_co_u32_e32 v180, vcc, 0x200000, v180
	global_load_dwordx4 v[82:85], v[82:83], off nt
	s_nop 0
	v_addc_co_u32_e32 v181, vcc, 0, v181, vcc
	global_load_dwordx4 v[86:89], v[86:87], off nt
	s_nop 0
	global_load_dwordx4 v[90:93], v[90:91], off nt
	s_nop 0
	global_load_dword v175, v[180:181], off
	s_andn2_saveexec_b64 s[22:23], s[22:23]
	s_cbranch_execnz .LBB0_768

; __device__ __forceinline__ unsigned pk2(float lo, float hi) { return f2bf(lo) | (f2bf(hi) << 16); }
; __device__ __forceinline__ void unpack8(const v4u w, float* f) { f[0] = bflo(w.x); f[1] = bfhi(w.x); f[2] = bflo(w.y); f[3] = bfhi(w.y); f[4] = bflo(w.z); f[5] = bfhi(w.z); f[6] = bflo(w.w); f[7] = bfhi(w.w); }
; __device__ __forceinline__ void norm_compute(const NormRow& R, int lane, v4u& ya, v4u& yc) {
;     ...
;     const float s_moba = wave_sum(lane < 32 ? sa : 0.f), s_fox = wave_sum((lane >= 32 ? sa : 0.f) + (lane < 16 ? sc : 0.f)), s_dil = wave_sum(lane >= 16 ? sc : 0.f);
;     const float r_moba = 1.0f / sqrtf(s_moba * (1.0f / 256.0f) + EPS), r_fox = 1.0f / sqrtf(s_fox * (1.0f / 384.0f) + EPS), r_dil = 1.0f / sqrtf(s_dil * (1.0f / 384.0f) + EPS);
;     float ga[8], gc[8];
; #pragma unroll
;     for (int e = 0; e < 8; ++e) { ga[e] = 1.f; gc[e] = 1.f; }
;     if (lane >= 32) unpack8(R.ga, ga);
;     if (lane < 16) unpack8(R.gc, gc);
;     const float ra = lane < 32 ? r_moba : r_fox, rc = lane < 16 ? r_fox : r_dil;
;     ya.x = pk2(fa[0] * ra * ga[0], fa[1] * ra * ga[1]); ya.y = pk2(fa[2] * ra * ga[2], fa[3] * ra * ga[3]); ya.z = pk2(fa[4] * ra * ga[4], fa[5] * ra * ga[5]); ya.w = pk2(fa[6] * ra * ga[6], fa[7] * ra * ga[7]);
;     yc.x = pk2(fc[0] * rc * gc[0], fc[1] * rc * gc[1]); yc.y = pk2(fc[2] * rc * gc[2], fc[3] * rc * gc[3]); yc.z = pk2(fc[4] * rc * gc[4], fc[5] * rc * gc[5]); yc.w = pk2(fc[6] * rc * gc[6], fc[7] * rc * gc[7]);
; }
.LBB0_155:
	s_or_b64 exec, exec, s[20:21]
	v_mov_b32_e32 v179, v178
	s_nop 1
	v_permlane32_swap_b32_e32 v178, v179
	v_add_f32_e32 v178, v178, v179
	v_fmamk_f32 v178, v178, 0x3b2aaaab, v215
	v_mul_f32_e32 v179, 0x4f800000, v178
	v_cmp_gt_f32_e32 vcc, s3, v178
	v_mov_b32_e32 v177, v176
	s_nop 1
	v_permlane32_swap_b32_e32 v176, v177
	v_add_f32_e32 v176, v176, v177
	v_fmamk_f32 v176, v176, 0x3b2aaaab, v215
	v_cndmask_b32_e32 v178, v178, v179, vcc
	v_sqrt_f32_e32 v179, v178
	v_mul_f32_e32 v177, 0x4f800000, v176
	v_mov_b32_e32 v157, v156
	s_nop 1
	v_permlane32_swap_b32_e32 v156, v157
	v_add_f32_e32 v156, v156, v157
	v_fmamk_f32 v156, v156, 0x3b800000, v215
	v_add_u32_e32 v180, -1, v179
	v_fma_f32 v182, -v180, v179, v178
	v_add_u32_e32 v181, 1, v179
	v_cmp_ge_f32_e64 s[0:1], 0, v182
	v_mul_f32_e32 v157, 0x4f800000, v156
	s_nop 0
	v_cndmask_b32_e64 v180, v179, v180, s[0:1]
	v_fma_f32 v179, -v181, v179, v178
	v_cmp_lt_f32_e64 s[0:1], 0, v179
	s_nop 1
	v_cndmask_b32_e64 v179, v180, v181, s[0:1]
	v_cmp_gt_f32_e64 s[0:1], s3, v176
	v_mul_f32_e32 v180, 0x37800000, v179
	v_cndmask_b32_e32 v179, v179, v180, vcc
	v_cndmask_b32_e64 v176, v176, v177, s[0:1]
	v_sqrt_f32_e32 v177, v176
	v_cmp_class_f32_e32 vcc, v178, v216
	s_nop 1
	v_cndmask_b32_e32 v178, v179, v178, vcc
	v_add_u32_e32 v179, -1, v177
	v_fma_f32 v180, -v179, v177, v176
	v_cmp_ge_f32_e32 vcc, 0, v180
	v_add_u32_e32 v180, 1, v177
	s_nop 0
	v_cndmask_b32_e32 v179, v177, v179, vcc
	v_fma_f32 v177, -v180, v177, v176
	v_cmp_lt_f32_e32 vcc, 0, v177
	s_nop 1
	v_cndmask_b32_e32 v177, v179, v180, vcc
	v_cmp_gt_f32_e32 vcc, s3, v156
	v_mul_f32_e32 v179, 0x37800000, v177
	v_cndmask_b32_e64 v177, v177, v179, s[0:1]
	v_cndmask_b32_e32 v156, v156, v157, vcc
	v_sqrt_f32_e32 v157, v156
	v_cmp_class_f32_e64 s[0:1], v176, v216
	s_nop 1
	v_cndmask_b32_e64 v176, v177, v176, s[0:1]
	v_add_u32_e32 v177, -1, v157
	v_fma_f32 v179, -v177, v157, v156
	v_cmp_ge_f32_e64 s[0:1], 0, v179
	v_add_u32_e32 v179, 1, v157
	s_nop 0
	v_cndmask_b32_e64 v177, v157, v177, s[0:1]
	v_fma_f32 v157, -v179, v157, v156
	v_cmp_lt_f32_e64 s[0:1], 0, v157
	s_nop 1
	v_cndmask_b32_e64 v157, v177, v179, s[0:1]
	v_div_scale_f32 v179, s[0:1], v178, v178, 1.0
	v_rcp_f32_e32 v180, v179
	v_mul_f32_e32 v177, 0x37800000, v157
	v_cndmask_b32_e32 v157, v157, v177, vcc
	v_cmp_class_f32_e32 vcc, v156, v216
	s_nop 1
	v_cndmask_b32_e32 v156, v157, v156, vcc
	v_fma_f32 v157, -v179, v180, 1.0
	v_fmac_f32_e32 v180, v157, v180
	v_div_scale_f32 v157, vcc, 1.0, v178, 1.0
	v_mul_f32_e32 v177, v157, v180
	v_fma_f32 v181, -v179, v177, v157
	v_fmac_f32_e32 v177, v181, v180
	v_fma_f32 v157, -v179, v177, v157
	v_div_scale_f32 v179, s[0:1], v176, v176, 1.0
	v_rcp_f32_e32 v181, v179
	v_div_fmas_f32 v157, v157, v180, v177
	v_div_fixup_f32 v157, v157, v178, 1.0
	v_fma_f32 v177, -v179, v181, 1.0
	v_fmac_f32_e32 v181, v177, v181
	v_div_scale_f32 v177, vcc, 1.0, v176, 1.0
	v_mul_f32_e32 v178, v177, v181
	v_fma_f32 v180, -v179, v178, v177
	v_fmac_f32_e32 v178, v180, v181
	v_fma_f32 v177, -v179, v178, v177
	v_div_scale_f32 v179, s[0:1], v156, v156, 1.0
	v_rcp_f32_e32 v180, v179
	v_div_fmas_f32 v177, v177, v181, v178
	v_div_fixup_f32 v176, v177, v176, 1.0
	s_movk_i32 s1, 0x7fff
	v_fma_f32 v177, -v179, v180, 1.0
	v_fmac_f32_e32 v180, v177, v180
	v_div_scale_f32 v177, vcc, 1.0, v156, 1.0
	v_mul_f32_e32 v178, v177, v180
	v_fma_f32 v181, -v179, v178, v177
	v_fmac_f32_e32 v178, v181, v180
	v_fma_f32 v177, -v179, v178, v177
	v_div_fmas_f32 v177, v177, v180, v178
	v_div_fixup_f32 v156, v177, v156, 1.0
	v_cndmask_b32_e64 v156, v176, v156, s[40:41]
	v_pk_mul_f32 v[132:133], v[156:157], v[132:133] op_sel_hi:[0,1]
	v_pk_mul_f32 v[134:135], v[156:157], v[134:135] op_sel_hi:[0,1]
	v_pk_mul_f32 v[138:139], v[156:157], v[138:139] op_sel_hi:[0,1]
	v_pk_mul_f32 v[132:133], v[132:133], v[150:151]
	v_pk_mul_f32 v[136:137], v[156:157], v[136:137] op_sel_hi:[0,1]
	v_pk_mul_f32 v[134:135], v[134:135], v[148:149]
	v_pk_mul_f32 v[138:139], v[138:139], v[154:155]
	v_pk_mul_f32 v[136:137], v[136:137], v[152:153]
	v_bfe_u32 v148, v135, 16, 1
	v_bfe_u32 v149, v134, 16, 1
	v_bfe_u32 v150, v133, 16, 1
	v_bfe_u32 v151, v132, 16, 1
	v_cndmask_b32_e64 v176, v157, v176, s[34:35]
	v_add3_u32 v132, v132, v151, s1
	v_add3_u32 v133, v133, v150, s1
	v_add3_u32 v134, v134, v149, s1
	v_add3_u32 v135, v135, v148, s1
	v_bfe_u32 v148, v138, 16, 1
	v_bfe_u32 v149, v139, 16, 1
	v_bfe_u32 v150, v136, 16, 1
	v_bfe_u32 v151, v137, 16, 1
	v_add3_u32 v137, v137, v151, s1
	v_add3_u32 v136, v136, v150, s1
	v_add3_u32 v139, v139, v149, s1
	v_add3_u32 v138, v138, v148, s1
	v_pk_mul_f32 v[114:115], v[114:115], v[176:177] op_sel_hi:[1,0]
	v_pk_mul_f32 v[116:117], v[116:117], v[176:177] op_sel_hi:[1,0]
	v_lshrrev_b32_e32 v138, 16, v138
	v_lshrrev_b32_e32 v139, 16, v139
	v_lshrrev_b32_e32 v136, 16, v136
	v_lshrrev_b32_e32 v137, 16, v137
	s_mov_b32 s0, 0xffff0000
	v_pk_mul_f32 v[130:131], v[130:131], v[176:177] op_sel_hi:[1,0]
	v_pk_mul_f32 v[114:115], v[114:115], v[146:147]
	v_pk_mul_f32 v[128:129], v[128:129], v[176:177] op_sel_hi:[1,0]
	v_pk_mul_f32 v[116:117], v[116:117], v[142:143]
	v_and_or_b32 v135, v135, s0, v137
	v_and_or_b32 v134, v134, s0, v136
	v_and_or_b32 v133, v133, s0, v139
	v_and_or_b32 v132, v132, s0, v138
	v_pk_mul_f32 v[130:131], v[130:131], v[140:141]
	v_pk_mul_f32 v[128:129], v[128:129], v[144:145]
	v_bfe_u32 v136, v117, 16, 1
	v_bfe_u32 v137, v116, 16, 1
	v_bfe_u32 v138, v115, 16, 1
	v_bfe_u32 v139, v114, 16, 1
	v_add3_u32 v114, v114, v139, s1
	v_add3_u32 v115, v115, v138, s1
	v_add3_u32 v116, v116, v137, s1
	v_add3_u32 v117, v117, v136, s1
	v_bfe_u32 v136, v130, 16, 1
	v_bfe_u32 v137, v131, 16, 1
	v_bfe_u32 v138, v128, 16, 1
	v_bfe_u32 v139, v129, 16, 1
	v_add3_u32 v129, v129, v139, s1
	v_add3_u32 v128, v128, v138, s1
	v_add3_u32 v131, v131, v137, s1
	v_add3_u32 v130, v130, v136, s1
	v_lshrrev_b32_e32 v130, 16, v130
	v_lshrrev_b32_e32 v131, 16, v131
	v_lshrrev_b32_e32 v128, 16, v128
	v_lshrrev_b32_e32 v129, 16, v129
	v_and_or_b32 v117, v117, s0, v129
	v_and_or_b32 v116, v116, s0, v128
	v_and_or_b32 v115, v115, s0, v131
	v_and_or_b32 v114, v114, s0, v130
	s_add_u32 s0, s24, s12
	s_addc_u32 s1, s25, s13
	global_store_dwordx4 v0, v[132:135], s[0:1]
	global_store_dwordx4 v0, v[114:117], s[0:1] offset:1024
	s_waitcnt vmcnt(34)
	s_and_saveexec_b64 s[0:1], s[38:39]
	s_xor_b64 s[0:1], exec, s[0:1]
	s_cbranch_execz .LBB0_157
; __device__ __forceinline__ void unpack8(const v4u w, float* f) { f[0] = bflo(w.x); f[1] = bfhi(w.x); f[2] = bflo(w.y); f[3] = bfhi(w.y); f[4] = bflo(w.z); f[5] = bfhi(w.z); f[6] = bflo(w.w); f[7] = bfhi(w.w); }
; __device__ __forceinline__ void norm_compute(const NormRow& R, int lane, v4u& ya, v4u& yc) {
;     ...
;     else { float f0[8], f1[8], f2[8]; unpack8(R.d0, f0); unpack8(R.d1, f1); unpack8(R.d2, f2);
;         const float inv = 1.0f / (R.l0 + R.l1 + R.l2);
; #pragma unroll
;         for (int e = 0; e < 8; ++e) fc[e] = (f0[e] + f1[e] + f2[e]) * inv; }
	v_add_f32_e32 v114, v171, v170
	v_add_f32_e32 v114, v172, v114
	v_div_scale_f32 v115, s[12:13], v114, v114, 1.0
	v_rcp_f32_e32 v130, v115
	v_lshlrev_b32_e32 v134, 16, v66
	v_and_b32_e32 v135, 0xffff0000, v66
	v_lshlrev_b32_e32 v136, 16, v67
	v_fma_f32 v131, -v115, v130, 1.0
	v_fmac_f32_e32 v130, v131, v130
	v_div_scale_f32 v131, vcc, 1.0, v114, 1.0
	v_mul_f32_e32 v132, v131, v130
	v_fma_f32 v133, -v115, v132, v131
	v_fmac_f32_e32 v132, v133, v130
	v_fma_f32 v115, -v115, v132, v131
	v_div_fmas_f32 v115, v115, v130, v132
	v_div_fixup_f32 v130, v115, v114, 1.0
	v_lshlrev_b32_e32 v114, 16, v58
	v_and_b32_e32 v115, 0xffff0000, v58
	v_lshlrev_b32_e32 v132, 16, v62
	v_and_b32_e32 v133, 0xffff0000, v62
	v_pk_add_f32 v[114:115], v[132:133], v[114:115]
	v_and_b32_e32 v137, 0xffff0000, v67
	v_pk_add_f32 v[114:115], v[114:115], v[134:135]
	v_lshlrev_b32_e32 v134, 16, v63
	v_pk_mul_f32 v[132:133], v[130:131], v[114:115] op_sel_hi:[0,1]
	v_lshlrev_b32_e32 v114, 16, v59
	v_and_b32_e32 v115, 0xffff0000, v59
	v_and_b32_e32 v135, 0xffff0000, v63
	v_pk_add_f32 v[114:115], v[134:135], v[114:115]
	v_lshlrev_b32_e32 v116, 16, v61
	v_lshlrev_b32_e32 v128, 16, v65
	v_and_b32_e32 v117, 0xffff0000, v61
	v_and_b32_e32 v129, 0xffff0000, v65
	v_pk_add_f32 v[114:115], v[114:115], v[136:137]
	v_lshlrev_b32_e32 v134, 16, v60
	v_and_b32_e32 v135, 0xffff0000, v60
	v_lshlrev_b32_e32 v136, 16, v64
	v_and_b32_e32 v137, 0xffff0000, v64
	v_lshlrev_b32_e32 v138, 16, v68
	v_and_b32_e32 v139, 0xffff0000, v68
	v_pk_add_f32 v[134:135], v[136:137], v[134:135]
	v_lshlrev_b32_e32 v136, 16, v69
	v_and_b32_e32 v137, 0xffff0000, v69
	v_pk_add_f32 v[116:117], v[128:129], v[116:117]
	v_pk_add_f32 v[134:135], v[134:135], v[138:139]
	v_pk_add_f32 v[116:117], v[116:117], v[136:137]
	v_pk_mul_f32 v[114:115], v[130:131], v[114:115] op_sel_hi:[0,1]
	v_pk_mul_f32 v[134:135], v[130:131], v[134:135] op_sel_hi:[0,1]
	v_pk_mul_f32 v[116:117], v[130:131], v[116:117] op_sel_hi:[0,1]
	v_mov_b32_e32 v129, v116
	v_mov_b32_e32 v116, v135
	v_mov_b32_e32 v128, v134
	v_mov_b32_e32 v131, v114
	v_mov_b32_e32 v114, v133
	v_mov_b32_e32 v130, v132
; #define GAS __attribute__((address_space(1)))
; __device__ __forceinline__ void unpack8(const v4u w, float* f) { f[0] = bflo(w.x); f[1] = bfhi(w.x); f[2] = bflo(w.y); f[3] = bfhi(w.y); f[4] = bflo(w.z); f[5] = bfhi(w.z); f[6] = bflo(w.w); f[7] = bfhi(w.w); }
; __device__ __forceinline__ void norm_load(NormRow& R, int m, int lane, const bf16* O, const bf16* GF, const bf16* OD, const float* LD) {
;     R.oa = __builtin_nontemporal_load((const GAS v4u*)(O + (size_t)m * DM + 8 * lane));
;     if (lane < 16) { R.oc = __builtin_nontemporal_load((const GAS v4u*)(O + (size_t)m * DM + 512 + 8 * lane)); R.gc = __builtin_nontemporal_load((const GAS v4u*)(GF + (size_t)m * 384 + 256 + 8 * lane)); }
;     else { const int dc = 8 * lane - 128, hd = dc >> 6;
;         R.d0 = __builtin_nontemporal_load((const GAS v4u*)(OD + (size_t)m * 384 + dc)); R.d1 = __builtin_nontemporal_load((const GAS v4u*)(OD + OD_BRANCH + (size_t)m * 384 + dc)); R.d2 = __builtin_nontemporal_load((const GAS v4u*)(OD + 2 * OD_BRANCH + (size_t)m * 384 + dc));
;         R.l0 = LD[(size_t)m * 8 + hd]; R.l1 = LD[LD_BRANCH + (size_t)m * 8 + hd]; R.l2 = LD[2 * LD_BRANCH + (size_t)m * 8 + hd]; }
;     if (lane >= 32) R.ga = __builtin_nontemporal_load((const GAS v4u*)(GF + (size_t)m * 384 + 8 * lane - 256));
; __device__ __forceinline__ void norm_compute(const NormRow& R, int lane, v4u& ya, v4u& yc) {
;     ...
;     if (lane < 16) unpack8(R.oc, fc);
;     else { float f0[8], f1[8], f2[8]; unpack8(R.d0, f0); unpack8(R.d1, f1); unpack8(R.d2, f2);
;         const float inv = 1.0f / (R.l0 + R.l1 + R.l2);
; #pragma unroll
;         for (int e = 0; e < 8; ++e) fc[e] = (f0[e] + f1[e] + f2[e]) * inv; }
;     float sa = 0.f, sc = 0.f;
; #pragma unroll
;     for (int e = 0; e < 8; ++e) { sa += fa[e] * fa[e]; sc += fc[e] * fc[e]; }
;     const float s_moba = wave_sum(lane < 32 ? sa : 0.f), s_fox = wave_sum((lane >= 32 ? sa : 0.f) + (lane < 16 ? sc : 0.f)), s_dil = wave_sum(lane >= 16 ? sc : 0.f);
;     const float r_moba = 1.0f / sqrtf(s_moba * (1.0f / 256.0f) + EPS), r_fox = 1.0f / sqrtf(s_fox * (1.0f / 384.0f) + EPS), r_dil = 1.0f / sqrtf(s_dil * (1.0f / 384.0f) + EPS);
;     float ga[8], gc[8];
; #pragma unroll
;     for (int e = 0; e < 8; ++e) { ga[e] = 1.f; gc[e] = 1.f; }
;     if (lane >= 32) unpack8(R.ga, ga);
;     if (lane < 16) unpack8(R.gc, gc);
.LBB0_157:
	s_andn2_saveexec_b64 s[0:1], s[0:1]
	v_lshlrev_b32_e32 v130, 16, v70
	v_and_b32_e32 v114, 0xffff0000, v70
	v_lshlrev_b32_e32 v131, 16, v71
	v_and_b32_e32 v115, 0xffff0000, v71
	v_lshlrev_b32_e32 v128, 16, v72
	v_and_b32_e32 v116, 0xffff0000, v72
	v_lshlrev_b32_e32 v129, 16, v73
	v_and_b32_e32 v117, 0xffff0000, v73
	s_or_b64 exec, exec, s[0:1]
	v_lshlrev_b32_e32 v139, 16, v107
	v_lshlrev_b32_e32 v138, 16, v106
	v_and_b32_e32 v133, 0xffff0000, v107
	v_and_b32_e32 v132, 0xffff0000, v106
	v_lshlrev_b32_e32 v137, 16, v109
	v_lshlrev_b32_e32 v136, 16, v108
	v_and_b32_e32 v135, 0xffff0000, v109
	v_and_b32_e32 v134, 0xffff0000, v108
	v_pk_mul_f32 v[106:107], v[138:139], v[138:139]
	v_pk_mul_f32 v[108:109], v[132:133], v[132:133]
	v_mul_f32_e32 v144, v114, v114
	v_fmac_f32_e32 v144, v130, v130
	v_add_f32_e32 v106, v106, v108
	v_fmac_f32_e32 v144, v131, v131
	v_add_f32_e32 v106, v107, v106
	v_fmac_f32_e32 v144, v115, v115
	v_pk_mul_f32 v[140:141], v[136:137], v[136:137]
	v_add_f32_e32 v106, v109, v106
	v_fmac_f32_e32 v144, v128, v128
	v_pk_mul_f32 v[142:143], v[134:135], v[134:135]
	v_add_f32_e32 v106, v140, v106
	v_fmac_f32_e32 v144, v116, v116
	v_add_f32_e32 v106, v142, v106
	v_fmac_f32_e32 v144, v129, v129
	v_add_f32_e32 v106, v141, v106
	v_add_f32_e32 v106, v143, v106
	v_fmac_f32_e32 v144, v117, v117
	v_cndmask_b32_e64 v107, 0, v106, s[40:41]
	v_cndmask_b32_e64 v106, 0, v106, s[36:37]
	v_cndmask_b32_e64 v109, 0, v144, s[34:35]
	v_add_f32_e32 v106, v106, v109
	v_cndmask_b32_e64 v140, 0, v144, s[42:43]
	v_mov_b32_e32 v154, 1.0
	v_mov_b32_e32 v150, 1.0
	s_nop 1
	v_add_f32_dpp v107, v107, v107 quad_perm:[1,0,3,2] row_mask:0xf bank_mask:0xf
	s_nop 1
	v_add_f32_dpp v106, v106, v106 quad_perm:[1,0,3,2] row_mask:0xf bank_mask:0xf
	s_nop 1
	v_add_f32_dpp v140, v140, v140 quad_perm:[1,0,3,2] row_mask:0xf bank_mask:0xf
	v_mov_b32_e32 v155, 1.0
	v_mov_b32_e32 v151, 1.0
	s_nop 1
	v_add_f32_dpp v107, v107, v107 quad_perm:[2,3,0,1] row_mask:0xf bank_mask:0xf
	s_nop 1
	v_add_f32_dpp v106, v106, v106 quad_perm:[2,3,0,1] row_mask:0xf bank_mask:0xf
	s_nop 1
	v_add_f32_dpp v140, v140, v140 quad_perm:[2,3,0,1] row_mask:0xf bank_mask:0xf
	v_mov_b32_e32 v152, 1.0
	v_mov_b32_e32 v148, 1.0
	s_nop 1
	v_add_f32_dpp v107, v107, v107 row_half_mirror row_mask:0xf bank_mask:0xf
	s_nop 1
	v_add_f32_dpp v106, v106, v106 row_half_mirror row_mask:0xf bank_mask:0xf
	s_nop 1
	v_add_f32_dpp v140, v140, v140 row_half_mirror row_mask:0xf bank_mask:0xf
	v_mov_b32_e32 v153, 1.0
	v_mov_b32_e32 v149, 1.0
	s_nop 1
	v_add_f32_dpp v107, v107, v107 row_mirror row_mask:0xf bank_mask:0xf
	s_nop 1
	v_add_f32_dpp v106, v106, v106 row_mirror row_mask:0xf bank_mask:0xf
	s_nop 1
	v_add_f32_dpp v140, v140, v140 row_mirror row_mask:0xf bank_mask:0xf
	v_mov_b32_e32 v108, v107
	s_nop 1
	v_permlane16_swap_b32_e32 v107, v108
	v_add_f32_e32 v156, v107, v108
	v_mov_b32_e32 v109, v106
	s_nop 1
	v_permlane16_swap_b32_e32 v106, v109
	v_add_f32_e32 v176, v106, v109
	v_mov_b32_e32 v141, v140
	s_nop 1
	v_permlane16_swap_b32_e32 v140, v141
	v_add_f32_e32 v178, v140, v141
	v_mov_b32_e32 v140, 1.0
	s_and_saveexec_b64 s[0:1], s[36:37]
	v_lshlrev_b32_e32 v154, 16, v54
	v_and_b32_e32 v150, 0xffff0000, v54
	v_lshlrev_b32_e32 v155, 16, v55
	v_and_b32_e32 v151, 0xffff0000, v55
	v_lshlrev_b32_e32 v152, 16, v56
	v_and_b32_e32 v148, 0xffff0000, v56
	v_lshlrev_b32_e32 v153, 16, v57
	v_and_b32_e32 v149, 0xffff0000, v57
	s_or_b64 exec, exec, s[0:1]
	v_mov_b32_e32 v146, 1.0
	v_mov_b32_e32 v141, 1.0
	v_mov_b32_e32 v147, 1.0
	v_mov_b32_e32 v144, 1.0
	v_mov_b32_e32 v142, 1.0
	v_mov_b32_e32 v145, 1.0
	v_mov_b32_e32 v143, 1.0
	s_and_saveexec_b64 s[0:1], s[34:35]
	v_lshlrev_b32_e32 v140, 16, v50
	v_and_b32_e32 v146, 0xffff0000, v50
	v_lshlrev_b32_e32 v141, 16, v51
	v_and_b32_e32 v147, 0xffff0000, v51
	v_lshlrev_b32_e32 v144, 16, v52
	v_and_b32_e32 v142, 0xffff0000, v52
	v_lshlrev_b32_e32 v145, 16, v53
	v_and_b32_e32 v143, 0xffff0000, v53
	s_or_b64 exec, exec, s[0:1]
	s_or_b32 s0, s8, 9
	s_ashr_i32 s1, s0, 31
	s_lshl_b64 s[12:13], s[0:1], 11
	s_add_u32 s20, s29, s12
	s_addc_u32 s21, s30, s13
	global_load_dwordx4 v[106:109], v0, s[20:21] nt
	s_and_saveexec_b64 s[22:23], s[38:39]
	s_xor_b64 s[22:23], exec, s[22:23]
	s_cbranch_execz .LBB0_769
	v_mad_i64_i32 v[58:59], s[44:45], s0, v252, v[124:125]
	v_mad_i64_i32 v[62:63], s[44:45], s0, v252, v[122:123]
	v_mad_i64_i32 v[66:67], s[44:45], s0, v252, v[120:121]
	s_lshl_b64 s[44:45], s[0:1], 5
	s_add_u32 s44, s26, s44
	s_addc_u32 s45, s27, s45
	v_lshl_add_u64 v[180:181], v[118:119], 2, s[44:45]
	v_add_co_u32_e32 v182, vcc, 0x100000, v180
	global_load_dword v170, v[180:181], off
	s_nop 0
	v_addc_co_u32_e32 v183, vcc, 0, v181, vcc
	global_load_dword v171, v[182:183], off
	v_add_co_u32_e32 v180, vcc, 0x200000, v180
	global_load_dwordx4 v[58:61], v[58:59], off nt
	s_nop 0
	v_addc_co_u32_e32 v181, vcc, 0, v181, vcc
	global_load_dwordx4 v[62:65], v[62:63], off nt
	s_nop 0
	global_load_dwordx4 v[66:69], v[66:67], off nt
	s_nop 0
	global_load_dword v172, v[180:181], off
	s_andn2_saveexec_b64 s[22:23], s[22:23]
	s_cbranch_execnz .LBB0_770

; __device__ __forceinline__ unsigned pk2(float lo, float hi) { return f2bf(lo) | (f2bf(hi) << 16); }
; __device__ __forceinline__ void unpack8(const v4u w, float* f) { f[0] = bflo(w.x); f[1] = bfhi(w.x); f[2] = bflo(w.y); f[3] = bfhi(w.y); f[4] = bflo(w.z); f[5] = bfhi(w.z); f[6] = bflo(w.w); f[7] = bfhi(w.w); }
; __device__ __forceinline__ void norm_compute(const NormRow& R, int lane, v4u& ya, v4u& yc) {
;     ...
;     const float s_moba = wave_sum(lane < 32 ? sa : 0.f), s_fox = wave_sum((lane >= 32 ? sa : 0.f) + (lane < 16 ? sc : 0.f)), s_dil = wave_sum(lane >= 16 ? sc : 0.f);
;     const float r_moba = 1.0f / sqrtf(s_moba * (1.0f / 256.0f) + EPS), r_fox = 1.0f / sqrtf(s_fox * (1.0f / 384.0f) + EPS), r_dil = 1.0f / sqrtf(s_dil * (1.0f / 384.0f) + EPS);
;     float ga[8], gc[8];
; #pragma unroll
;     for (int e = 0; e < 8; ++e) { ga[e] = 1.f; gc[e] = 1.f; }
;     if (lane >= 32) unpack8(R.ga, ga);
;     if (lane < 16) unpack8(R.gc, gc);
;     const float ra = lane < 32 ? r_moba : r_fox, rc = lane < 16 ? r_fox : r_dil;
;     ya.x = pk2(fa[0] * ra * ga[0], fa[1] * ra * ga[1]); ya.y = pk2(fa[2] * ra * ga[2], fa[3] * ra * ga[3]); ya.z = pk2(fa[4] * ra * ga[4], fa[5] * ra * ga[5]); ya.w = pk2(fa[6] * ra * ga[6], fa[7] * ra * ga[7]);
;     yc.x = pk2(fc[0] * rc * gc[0], fc[1] * rc * gc[1]); yc.y = pk2(fc[2] * rc * gc[2], fc[3] * rc * gc[3]); yc.z = pk2(fc[4] * rc * gc[4], fc[5] * rc * gc[5]); yc.w = pk2(fc[6] * rc * gc[6], fc[7] * rc * gc[7]);
; }
.LBB0_167:
	s_or_b64 exec, exec, s[20:21]
	v_mov_b32_e32 v179, v178
	s_nop 1
	v_permlane32_swap_b32_e32 v178, v179
	v_add_f32_e32 v178, v178, v179
	v_fmamk_f32 v178, v178, 0x3b2aaaab, v215
	v_mul_f32_e32 v179, 0x4f800000, v178
	v_cmp_gt_f32_e32 vcc, s3, v178
	v_mov_b32_e32 v177, v176
	s_nop 1
	v_permlane32_swap_b32_e32 v176, v177
	v_add_f32_e32 v176, v176, v177
	v_fmamk_f32 v176, v176, 0x3b2aaaab, v215
	v_cndmask_b32_e32 v178, v178, v179, vcc
	v_sqrt_f32_e32 v179, v178
	v_mul_f32_e32 v177, 0x4f800000, v176
	v_mov_b32_e32 v157, v156
	s_nop 1
	v_permlane32_swap_b32_e32 v156, v157
	v_add_f32_e32 v156, v156, v157
	v_fmamk_f32 v156, v156, 0x3b800000, v215
	v_add_u32_e32 v180, -1, v179
	v_fma_f32 v182, -v180, v179, v178
	v_add_u32_e32 v181, 1, v179
	v_cmp_ge_f32_e64 s[0:1], 0, v182
	v_mul_f32_e32 v157, 0x4f800000, v156
	s_nop 0
	v_cndmask_b32_e64 v180, v179, v180, s[0:1]
	v_fma_f32 v179, -v181, v179, v178
	v_cmp_lt_f32_e64 s[0:1], 0, v179
	s_nop 1
	v_cndmask_b32_e64 v179, v180, v181, s[0:1]
	v_cmp_gt_f32_e64 s[0:1], s3, v176
	v_mul_f32_e32 v180, 0x37800000, v179
	v_cndmask_b32_e32 v179, v179, v180, vcc
	v_cndmask_b32_e64 v176, v176, v177, s[0:1]
	v_sqrt_f32_e32 v177, v176
	v_cmp_class_f32_e32 vcc, v178, v216
	s_nop 1
	v_cndmask_b32_e32 v178, v179, v178, vcc
	v_add_u32_e32 v179, -1, v177
	v_fma_f32 v180, -v179, v177, v176
	v_cmp_ge_f32_e32 vcc, 0, v180
	v_add_u32_e32 v180, 1, v177
	s_nop 0
	v_cndmask_b32_e32 v179, v177, v179, vcc
	v_fma_f32 v177, -v180, v177, v176
	v_cmp_lt_f32_e32 vcc, 0, v177
	s_nop 1
	v_cndmask_b32_e32 v177, v179, v180, vcc
	v_cmp_gt_f32_e32 vcc, s3, v156
	v_mul_f32_e32 v179, 0x37800000, v177
	v_cndmask_b32_e64 v177, v177, v179, s[0:1]
	v_cndmask_b32_e32 v156, v156, v157, vcc
	v_sqrt_f32_e32 v157, v156
	v_cmp_class_f32_e64 s[0:1], v176, v216
	s_nop 1
	v_cndmask_b32_e64 v176, v177, v176, s[0:1]
	v_add_u32_e32 v177, -1, v157
	v_fma_f32 v179, -v177, v157, v156
	v_cmp_ge_f32_e64 s[0:1], 0, v179
	v_add_u32_e32 v179, 1, v157
	s_nop 0
	v_cndmask_b32_e64 v177, v157, v177, s[0:1]
	v_fma_f32 v157, -v179, v157, v156
	v_cmp_lt_f32_e64 s[0:1], 0, v157
	s_nop 1
	v_cndmask_b32_e64 v157, v177, v179, s[0:1]
	v_div_scale_f32 v179, s[0:1], v178, v178, 1.0
	v_rcp_f32_e32 v180, v179
	v_mul_f32_e32 v177, 0x37800000, v157
	v_cndmask_b32_e32 v157, v157, v177, vcc
	v_cmp_class_f32_e32 vcc, v156, v216
	s_nop 1
	v_cndmask_b32_e32 v156, v157, v156, vcc
	v_fma_f32 v157, -v179, v180, 1.0
	v_fmac_f32_e32 v180, v157, v180
	v_div_scale_f32 v157, vcc, 1.0, v178, 1.0
	v_mul_f32_e32 v177, v157, v180
	v_fma_f32 v181, -v179, v177, v157
	v_fmac_f32_e32 v177, v181, v180
	v_fma_f32 v157, -v179, v177, v157
	v_div_scale_f32 v179, s[0:1], v176, v176, 1.0
	v_rcp_f32_e32 v181, v179
	v_div_fmas_f32 v157, v157, v180, v177
	v_div_fixup_f32 v157, v157, v178, 1.0
	v_fma_f32 v177, -v179, v181, 1.0
	v_fmac_f32_e32 v181, v177, v181
	v_div_scale_f32 v177, vcc, 1.0, v176, 1.0
	v_mul_f32_e32 v178, v177, v181
	v_fma_f32 v180, -v179, v178, v177
	v_fmac_f32_e32 v178, v180, v181
	v_fma_f32 v177, -v179, v178, v177
	v_div_scale_f32 v179, s[0:1], v156, v156, 1.0
	v_rcp_f32_e32 v180, v179
	v_div_fmas_f32 v177, v177, v181, v178
	v_div_fixup_f32 v176, v177, v176, 1.0
	s_movk_i32 s1, 0x7fff
	v_fma_f32 v177, -v179, v180, 1.0
	v_fmac_f32_e32 v180, v177, v180
	v_div_scale_f32 v177, vcc, 1.0, v156, 1.0
	v_mul_f32_e32 v178, v177, v180
	v_fma_f32 v181, -v179, v178, v177
	v_fmac_f32_e32 v178, v181, v180
	v_fma_f32 v177, -v179, v178, v177
	v_div_fmas_f32 v177, v177, v180, v178
	v_div_fixup_f32 v156, v177, v156, 1.0
	v_cndmask_b32_e64 v156, v176, v156, s[40:41]
	v_pk_mul_f32 v[132:133], v[156:157], v[132:133] op_sel_hi:[0,1]
	v_pk_mul_f32 v[134:135], v[156:157], v[134:135] op_sel_hi:[0,1]
	v_pk_mul_f32 v[138:139], v[156:157], v[138:139] op_sel_hi:[0,1]
	v_pk_mul_f32 v[132:133], v[132:133], v[150:151]
	v_pk_mul_f32 v[136:137], v[156:157], v[136:137] op_sel_hi:[0,1]
	v_pk_mul_f32 v[134:135], v[134:135], v[148:149]
	v_pk_mul_f32 v[138:139], v[138:139], v[154:155]
	v_pk_mul_f32 v[136:137], v[136:137], v[152:153]
	v_bfe_u32 v148, v135, 16, 1
	v_bfe_u32 v149, v134, 16, 1
	v_bfe_u32 v150, v133, 16, 1
	v_bfe_u32 v151, v132, 16, 1
	v_cndmask_b32_e64 v176, v157, v176, s[34:35]
	v_add3_u32 v132, v132, v151, s1
	v_add3_u32 v133, v133, v150, s1
	v_add3_u32 v134, v134, v149, s1
	v_add3_u32 v135, v135, v148, s1
	v_bfe_u32 v148, v138, 16, 1
	v_bfe_u32 v149, v139, 16, 1
	v_bfe_u32 v150, v136, 16, 1
	v_bfe_u32 v151, v137, 16, 1
	v_add3_u32 v137, v137, v151, s1
	v_add3_u32 v136, v136, v150, s1
	v_add3_u32 v139, v139, v149, s1
	v_add3_u32 v138, v138, v148, s1
	v_pk_mul_f32 v[114:115], v[114:115], v[176:177] op_sel_hi:[1,0]
	v_pk_mul_f32 v[116:117], v[116:117], v[176:177] op_sel_hi:[1,0]
	v_lshrrev_b32_e32 v138, 16, v138
	v_lshrrev_b32_e32 v139, 16, v139
	v_lshrrev_b32_e32 v136, 16, v136
	v_lshrrev_b32_e32 v137, 16, v137
	s_mov_b32 s0, 0xffff0000
	v_pk_mul_f32 v[130:131], v[130:131], v[176:177] op_sel_hi:[1,0]
	v_pk_mul_f32 v[114:115], v[114:115], v[146:147]
	v_pk_mul_f32 v[128:129], v[128:129], v[176:177] op_sel_hi:[1,0]
	v_pk_mul_f32 v[116:117], v[116:117], v[142:143]
	v_and_or_b32 v135, v135, s0, v137
	v_and_or_b32 v134, v134, s0, v136
	v_and_or_b32 v133, v133, s0, v139
	v_and_or_b32 v132, v132, s0, v138
	v_pk_mul_f32 v[130:131], v[130:131], v[140:141]
	v_pk_mul_f32 v[128:129], v[128:129], v[144:145]
	v_bfe_u32 v136, v117, 16, 1
	v_bfe_u32 v137, v116, 16, 1
	v_bfe_u32 v138, v115, 16, 1
	v_bfe_u32 v139, v114, 16, 1
	v_add3_u32 v114, v114, v139, s1
	v_add3_u32 v115, v115, v138, s1
	v_add3_u32 v116, v116, v137, s1
	v_add3_u32 v117, v117, v136, s1
	v_bfe_u32 v136, v130, 16, 1
	v_bfe_u32 v137, v131, 16, 1
	v_bfe_u32 v138, v128, 16, 1
	v_bfe_u32 v139, v129, 16, 1
	v_add3_u32 v129, v129, v139, s1
	v_add3_u32 v128, v128, v138, s1
	v_add3_u32 v131, v131, v137, s1
	v_add3_u32 v130, v130, v136, s1
	v_lshrrev_b32_e32 v130, 16, v130
	v_lshrrev_b32_e32 v131, 16, v131
	v_lshrrev_b32_e32 v128, 16, v128
	v_lshrrev_b32_e32 v129, 16, v129
	v_and_or_b32 v117, v117, s0, v129
	v_and_or_b32 v116, v116, s0, v128
	v_and_or_b32 v115, v115, s0, v131
	v_and_or_b32 v114, v114, s0, v130
	s_add_u32 s0, s24, s14
	s_addc_u32 s1, s25, s15
	global_store_dwordx4 v0, v[132:135], s[0:1]
	global_store_dwordx4 v0, v[114:117], s[0:1] offset:1024
	s_waitcnt vmcnt(34)
	s_and_saveexec_b64 s[0:1], s[38:39]
	s_xor_b64 s[0:1], exec, s[0:1]
	s_cbranch_execz .LBB0_169
; __device__ __forceinline__ void unpack8(const v4u w, float* f) { f[0] = bflo(w.x); f[1] = bfhi(w.x); f[2] = bflo(w.y); f[3] = bfhi(w.y); f[4] = bflo(w.z); f[5] = bfhi(w.z); f[6] = bflo(w.w); f[7] = bfhi(w.w); }
; __device__ __forceinline__ void norm_compute(const NormRow& R, int lane, v4u& ya, v4u& yc) {
;     ...
;     else { float f0[8], f1[8], f2[8]; unpack8(R.d0, f0); unpack8(R.d1, f1); unpack8(R.d2, f2);
;         const float inv = 1.0f / (R.l0 + R.l1 + R.l2);
; #pragma unroll
;         for (int e = 0; e < 8; ++e) fc[e] = (f0[e] + f1[e] + f2[e]) * inv; }
	v_add_f32_e32 v114, v168, v167
	v_add_f32_e32 v114, v169, v114
	v_div_scale_f32 v115, s[14:15], v114, v114, 1.0
	v_rcp_f32_e32 v130, v115
	v_lshlrev_b32_e32 v134, 16, v42
	v_and_b32_e32 v135, 0xffff0000, v42
	v_lshlrev_b32_e32 v136, 16, v43
	v_fma_f32 v131, -v115, v130, 1.0
	v_fmac_f32_e32 v130, v131, v130
	v_div_scale_f32 v131, vcc, 1.0, v114, 1.0
	v_mul_f32_e32 v132, v131, v130
	v_fma_f32 v133, -v115, v132, v131
	v_fmac_f32_e32 v132, v133, v130
	v_fma_f32 v115, -v115, v132, v131
	v_div_fmas_f32 v115, v115, v130, v132
	v_div_fixup_f32 v130, v115, v114, 1.0
	v_lshlrev_b32_e32 v114, 16, v34
	v_and_b32_e32 v115, 0xffff0000, v34
	v_lshlrev_b32_e32 v132, 16, v38
	v_and_b32_e32 v133, 0xffff0000, v38
	v_pk_add_f32 v[114:115], v[132:133], v[114:115]
	v_and_b32_e32 v137, 0xffff0000, v43
	v_pk_add_f32 v[114:115], v[114:115], v[134:135]
	v_lshlrev_b32_e32 v134, 16, v39
	v_pk_mul_f32 v[132:133], v[130:131], v[114:115] op_sel_hi:[0,1]
	v_lshlrev_b32_e32 v114, 16, v35
	v_and_b32_e32 v115, 0xffff0000, v35
	v_and_b32_e32 v135, 0xffff0000, v39
	v_pk_add_f32 v[114:115], v[134:135], v[114:115]
	v_lshlrev_b32_e32 v116, 16, v37
	v_lshlrev_b32_e32 v128, 16, v41
	v_and_b32_e32 v117, 0xffff0000, v37
	v_and_b32_e32 v129, 0xffff0000, v41
	v_pk_add_f32 v[114:115], v[114:115], v[136:137]
	v_lshlrev_b32_e32 v134, 16, v36
	v_and_b32_e32 v135, 0xffff0000, v36
	v_lshlrev_b32_e32 v136, 16, v40
	v_and_b32_e32 v137, 0xffff0000, v40
	v_lshlrev_b32_e32 v138, 16, v44
	v_and_b32_e32 v139, 0xffff0000, v44
	v_pk_add_f32 v[134:135], v[136:137], v[134:135]
	v_lshlrev_b32_e32 v136, 16, v45
	v_and_b32_e32 v137, 0xffff0000, v45
	v_pk_add_f32 v[116:117], v[128:129], v[116:117]
	v_pk_add_f32 v[134:135], v[134:135], v[138:139]
	v_pk_add_f32 v[116:117], v[116:117], v[136:137]
	v_pk_mul_f32 v[114:115], v[130:131], v[114:115] op_sel_hi:[0,1]
	v_pk_mul_f32 v[134:135], v[130:131], v[134:135] op_sel_hi:[0,1]
	v_pk_mul_f32 v[116:117], v[130:131], v[116:117] op_sel_hi:[0,1]
	v_mov_b32_e32 v129, v116
	v_mov_b32_e32 v116, v135
	v_mov_b32_e32 v128, v134
	v_mov_b32_e32 v131, v114
	v_mov_b32_e32 v114, v133
	v_mov_b32_e32 v130, v132
; #define GAS __attribute__((address_space(1)))
; __device__ __forceinline__ void unpack8(const v4u w, float* f) { f[0] = bflo(w.x); f[1] = bfhi(w.x); f[2] = bflo(w.y); f[3] = bfhi(w.y); f[4] = bflo(w.z); f[5] = bfhi(w.z); f[6] = bflo(w.w); f[7] = bfhi(w.w); }
; __device__ __forceinline__ void norm_load(NormRow& R, int m, int lane, const bf16* O, const bf16* GF, const bf16* OD, const float* LD) {
;     R.oa = __builtin_nontemporal_load((const GAS v4u*)(O + (size_t)m * DM + 8 * lane));
;     if (lane < 16) { R.oc = __builtin_nontemporal_load((const GAS v4u*)(O + (size_t)m * DM + 512 + 8 * lane)); R.gc = __builtin_nontemporal_load((const GAS v4u*)(GF + (size_t)m * 384 + 256 + 8 * lane)); }
;     else { const int dc = 8 * lane - 128, hd = dc >> 6;
;         R.d0 = __builtin_nontemporal_load((const GAS v4u*)(OD + (size_t)m * 384 + dc)); R.d1 = __builtin_nontemporal_load((const GAS v4u*)(OD + OD_BRANCH + (size_t)m * 384 + dc)); R.d2 = __builtin_nontemporal_load((const GAS v4u*)(OD + 2 * OD_BRANCH + (size_t)m * 384 + dc));
;         R.l0 = LD[(size_t)m * 8 + hd]; R.l1 = LD[LD_BRANCH + (size_t)m * 8 + hd]; R.l2 = LD[2 * LD_BRANCH + (size_t)m * 8 + hd]; }
;     if (lane >= 32) R.ga = __builtin_nontemporal_load((const GAS v4u*)(GF + (size_t)m * 384 + 8 * lane - 256));
; __device__ __forceinline__ void norm_compute(const NormRow& R, int lane, v4u& ya, v4u& yc) {
;     ...
;     if (lane < 16) unpack8(R.oc, fc);
;     else { float f0[8], f1[8], f2[8]; unpack8(R.d0, f0); unpack8(R.d1, f1); unpack8(R.d2, f2);
;         const float inv = 1.0f / (R.l0 + R.l1 + R.l2);
; #pragma unroll
;         for (int e = 0; e < 8; ++e) fc[e] = (f0[e] + f1[e] + f2[e]) * inv; }
;     float sa = 0.f, sc = 0.f;
; #pragma unroll
;     for (int e = 0; e < 8; ++e) { sa += fa[e] * fa[e]; sc += fc[e] * fc[e]; }
;     const float s_moba = wave_sum(lane < 32 ? sa : 0.f), s_fox = wave_sum((lane >= 32 ? sa : 0.f) + (lane < 16 ? sc : 0.f)), s_dil = wave_sum(lane >= 16 ? sc : 0.f);
;     const float r_moba = 1.0f / sqrtf(s_moba * (1.0f / 256.0f) + EPS), r_fox = 1.0f / sqrtf(s_fox * (1.0f / 384.0f) + EPS), r_dil = 1.0f / sqrtf(s_dil * (1.0f / 384.0f) + EPS);
;     float ga[8], gc[8];
; #pragma unroll
;     for (int e = 0; e < 8; ++e) { ga[e] = 1.f; gc[e] = 1.f; }
;     if (lane >= 32) unpack8(R.ga, ga);
;     if (lane < 16) unpack8(R.gc, gc);
.LBB0_169:
	s_andn2_saveexec_b64 s[0:1], s[0:1]
	v_lshlrev_b32_e32 v130, 16, v46
	v_and_b32_e32 v114, 0xffff0000, v46
	v_lshlrev_b32_e32 v131, 16, v47
	v_and_b32_e32 v115, 0xffff0000, v47
	v_lshlrev_b32_e32 v128, 16, v48
	v_and_b32_e32 v116, 0xffff0000, v48
	v_lshlrev_b32_e32 v129, 16, v49
	v_and_b32_e32 v117, 0xffff0000, v49
	s_or_b64 exec, exec, s[0:1]
	v_lshlrev_b32_e32 v139, 16, v111
	v_lshlrev_b32_e32 v138, 16, v110
	v_and_b32_e32 v133, 0xffff0000, v111
	v_and_b32_e32 v132, 0xffff0000, v110
	v_lshlrev_b32_e32 v137, 16, v113
	v_lshlrev_b32_e32 v136, 16, v112
	v_and_b32_e32 v135, 0xffff0000, v113
	v_and_b32_e32 v134, 0xffff0000, v112
	v_pk_mul_f32 v[110:111], v[138:139], v[138:139]
	v_pk_mul_f32 v[112:113], v[132:133], v[132:133]
	v_mul_f32_e32 v144, v114, v114
	v_fmac_f32_e32 v144, v130, v130
	v_add_f32_e32 v110, v110, v112
	v_fmac_f32_e32 v144, v131, v131
	v_add_f32_e32 v110, v111, v110
	v_fmac_f32_e32 v144, v115, v115
	v_pk_mul_f32 v[140:141], v[136:137], v[136:137]
	v_add_f32_e32 v110, v113, v110
	v_fmac_f32_e32 v144, v128, v128
	v_pk_mul_f32 v[142:143], v[134:135], v[134:135]
	v_add_f32_e32 v110, v140, v110
	v_fmac_f32_e32 v144, v116, v116
	v_add_f32_e32 v110, v142, v110
	v_fmac_f32_e32 v144, v129, v129
	v_add_f32_e32 v110, v141, v110
	v_add_f32_e32 v110, v143, v110
	v_fmac_f32_e32 v144, v117, v117
	v_cndmask_b32_e64 v111, 0, v110, s[40:41]
	v_cndmask_b32_e64 v110, 0, v110, s[36:37]
	v_cndmask_b32_e64 v113, 0, v144, s[34:35]
	v_add_f32_e32 v110, v110, v113
	v_cndmask_b32_e64 v140, 0, v144, s[42:43]
	v_mov_b32_e32 v154, 1.0
	v_mov_b32_e32 v150, 1.0
	s_nop 1
	v_add_f32_dpp v111, v111, v111 quad_perm:[1,0,3,2] row_mask:0xf bank_mask:0xf
	s_nop 1
	v_add_f32_dpp v110, v110, v110 quad_perm:[1,0,3,2] row_mask:0xf bank_mask:0xf
	s_nop 1
	v_add_f32_dpp v140, v140, v140 quad_perm:[1,0,3,2] row_mask:0xf bank_mask:0xf
	v_mov_b32_e32 v155, 1.0
	v_mov_b32_e32 v151, 1.0
	s_nop 1
	v_add_f32_dpp v111, v111, v111 quad_perm:[2,3,0,1] row_mask:0xf bank_mask:0xf
	s_nop 1
	v_add_f32_dpp v110, v110, v110 quad_perm:[2,3,0,1] row_mask:0xf bank_mask:0xf
	s_nop 1
	v_add_f32_dpp v140, v140, v140 quad_perm:[2,3,0,1] row_mask:0xf bank_mask:0xf
	v_mov_b32_e32 v152, 1.0
	v_mov_b32_e32 v148, 1.0
	s_nop 1
	v_add_f32_dpp v111, v111, v111 row_half_mirror row_mask:0xf bank_mask:0xf
	s_nop 1
	v_add_f32_dpp v110, v110, v110 row_half_mirror row_mask:0xf bank_mask:0xf
	s_nop 1
	v_add_f32_dpp v140, v140, v140 row_half_mirror row_mask:0xf bank_mask:0xf
	v_mov_b32_e32 v153, 1.0
	v_mov_b32_e32 v149, 1.0
	s_nop 1
	v_add_f32_dpp v111, v111, v111 row_mirror row_mask:0xf bank_mask:0xf
	s_nop 1
	v_add_f32_dpp v110, v110, v110 row_mirror row_mask:0xf bank_mask:0xf
	s_nop 1
	v_add_f32_dpp v140, v140, v140 row_mirror row_mask:0xf bank_mask:0xf
	v_mov_b32_e32 v112, v111
	s_nop 1
	v_permlane16_swap_b32_e32 v111, v112
	v_add_f32_e32 v156, v111, v112
	v_mov_b32_e32 v113, v110
	s_nop 1
	v_permlane16_swap_b32_e32 v110, v113
	v_add_f32_e32 v176, v110, v113
	v_mov_b32_e32 v141, v140
	s_nop 1
	v_permlane16_swap_b32_e32 v140, v141
	v_add_f32_e32 v178, v140, v141
	v_mov_b32_e32 v140, 1.0
	s_and_saveexec_b64 s[0:1], s[36:37]
	v_lshlrev_b32_e32 v154, 16, v30
	v_and_b32_e32 v150, 0xffff0000, v30
	v_lshlrev_b32_e32 v155, 16, v31
	v_and_b32_e32 v151, 0xffff0000, v31
	v_lshlrev_b32_e32 v152, 16, v32
	v_and_b32_e32 v148, 0xffff0000, v32
	v_lshlrev_b32_e32 v153, 16, v33
	v_and_b32_e32 v149, 0xffff0000, v33
	s_or_b64 exec, exec, s[0:1]
	v_mov_b32_e32 v146, 1.0
	v_mov_b32_e32 v141, 1.0
	v_mov_b32_e32 v147, 1.0
	v_mov_b32_e32 v144, 1.0
	v_mov_b32_e32 v142, 1.0
	v_mov_b32_e32 v145, 1.0
	v_mov_b32_e32 v143, 1.0
	s_and_saveexec_b64 s[0:1], s[34:35]
	v_lshlrev_b32_e32 v140, 16, v26
	v_and_b32_e32 v146, 0xffff0000, v26
	v_lshlrev_b32_e32 v141, 16, v27
	v_and_b32_e32 v147, 0xffff0000, v27
	v_lshlrev_b32_e32 v144, 16, v28
	v_and_b32_e32 v142, 0xffff0000, v28
	v_lshlrev_b32_e32 v145, 16, v29
	v_and_b32_e32 v143, 0xffff0000, v29
	s_or_b64 exec, exec, s[0:1]
	s_or_b32 s0, s8, 10
	s_ashr_i32 s1, s0, 31
	s_lshl_b64 s[14:15], s[0:1], 11
	s_add_u32 s20, s29, s14
	s_addc_u32 s21, s30, s15
	global_load_dwordx4 v[110:113], v0, s[20:21] nt
	s_and_saveexec_b64 s[22:23], s[38:39]
	s_xor_b64 s[22:23], exec, s[22:23]
	s_cbranch_execz .LBB0_771
	v_mad_i64_i32 v[34:35], s[44:45], s0, v252, v[124:125]
	v_mad_i64_i32 v[38:39], s[44:45], s0, v252, v[122:123]
	v_mad_i64_i32 v[42:43], s[44:45], s0, v252, v[120:121]
	s_lshl_b64 s[44:45], s[0:1], 5
	s_add_u32 s44, s26, s44
	s_addc_u32 s45, s27, s45
	v_lshl_add_u64 v[180:181], v[118:119], 2, s[44:45]
	v_add_co_u32_e32 v168, vcc, 0x100000, v180
	global_load_dword v167, v[180:181], off
	s_nop 0
	v_addc_co_u32_e32 v169, vcc, 0, v181, vcc
	global_load_dword v168, v[168:169], off
	v_add_co_u32_e32 v180, vcc, 0x200000, v180
	global_load_dwordx4 v[34:37], v[34:35], off nt
	s_nop 0
	v_addc_co_u32_e32 v181, vcc, 0, v181, vcc
	global_load_dwordx4 v[38:41], v[38:39], off nt
	s_nop 0
	global_load_dwordx4 v[42:45], v[42:43], off nt
	s_nop 0
	global_load_dword v169, v[180:181], off
	s_andn2_saveexec_b64 s[22:23], s[22:23]
	s_cbranch_execnz .LBB0_772

; __device__ __forceinline__ unsigned pk2(float lo, float hi) { return f2bf(lo) | (f2bf(hi) << 16); }
; __device__ __forceinline__ void unpack8(const v4u w, float* f) { f[0] = bflo(w.x); f[1] = bfhi(w.x); f[2] = bflo(w.y); f[3] = bfhi(w.y); f[4] = bflo(w.z); f[5] = bfhi(w.z); f[6] = bflo(w.w); f[7] = bfhi(w.w); }
; __device__ __forceinline__ void norm_compute(const NormRow& R, int lane, v4u& ya, v4u& yc) {
;     ...
;     const float s_moba = wave_sum(lane < 32 ? sa : 0.f), s_fox = wave_sum((lane >= 32 ? sa : 0.f) + (lane < 16 ? sc : 0.f)), s_dil = wave_sum(lane >= 16 ? sc : 0.f);
;     const float r_moba = 1.0f / sqrtf(s_moba * (1.0f / 256.0f) + EPS), r_fox = 1.0f / sqrtf(s_fox * (1.0f / 384.0f) + EPS), r_dil = 1.0f / sqrtf(s_dil * (1.0f / 384.0f) + EPS);
;     float ga[8], gc[8];
; #pragma unroll
;     for (int e = 0; e < 8; ++e) { ga[e] = 1.f; gc[e] = 1.f; }
;     if (lane >= 32) unpack8(R.ga, ga);
;     if (lane < 16) unpack8(R.gc, gc);
;     const float ra = lane < 32 ? r_moba : r_fox, rc = lane < 16 ? r_fox : r_dil;
;     ya.x = pk2(fa[0] * ra * ga[0], fa[1] * ra * ga[1]); ya.y = pk2(fa[2] * ra * ga[2], fa[3] * ra * ga[3]); ya.z = pk2(fa[4] * ra * ga[4], fa[5] * ra * ga[5]); ya.w = pk2(fa[6] * ra * ga[6], fa[7] * ra * ga[7]);
;     yc.x = pk2(fc[0] * rc * gc[0], fc[1] * rc * gc[1]); yc.y = pk2(fc[2] * rc * gc[2], fc[3] * rc * gc[3]); yc.z = pk2(fc[4] * rc * gc[4], fc[5] * rc * gc[5]); yc.w = pk2(fc[6] * rc * gc[6], fc[7] * rc * gc[7]);
; }
.LBB0_179:
	s_or_b64 exec, exec, s[20:21]
	v_mov_b32_e32 v179, v178
	s_nop 1
	v_permlane32_swap_b32_e32 v178, v179
	v_add_f32_e32 v178, v178, v179
	v_fmamk_f32 v178, v178, 0x3b2aaaab, v215
	v_mul_f32_e32 v179, 0x4f800000, v178
	v_cmp_gt_f32_e32 vcc, s3, v178
	v_mov_b32_e32 v177, v176
	s_nop 1
	v_permlane32_swap_b32_e32 v176, v177
	v_add_f32_e32 v176, v176, v177
	v_fmamk_f32 v176, v176, 0x3b2aaaab, v215
	v_cndmask_b32_e32 v178, v178, v179, vcc
	v_sqrt_f32_e32 v179, v178
	v_mul_f32_e32 v177, 0x4f800000, v176
	v_mov_b32_e32 v157, v156
	s_nop 1
	v_permlane32_swap_b32_e32 v156, v157
	v_add_f32_e32 v156, v156, v157
	v_fmamk_f32 v156, v156, 0x3b800000, v215
	v_add_u32_e32 v180, -1, v179
	v_fma_f32 v182, -v180, v179, v178
	v_add_u32_e32 v181, 1, v179
	v_cmp_ge_f32_e64 s[0:1], 0, v182
	v_mul_f32_e32 v157, 0x4f800000, v156
	s_nop 0
	v_cndmask_b32_e64 v180, v179, v180, s[0:1]
	v_fma_f32 v179, -v181, v179, v178
	v_cmp_lt_f32_e64 s[0:1], 0, v179
	s_nop 1
	v_cndmask_b32_e64 v179, v180, v181, s[0:1]
	v_cmp_gt_f32_e64 s[0:1], s3, v176
	v_mul_f32_e32 v180, 0x37800000, v179
	v_cndmask_b32_e32 v179, v179, v180, vcc
	v_cndmask_b32_e64 v176, v176, v177, s[0:1]
	v_sqrt_f32_e32 v177, v176
	v_cmp_class_f32_e32 vcc, v178, v216
	s_nop 1
	v_cndmask_b32_e32 v178, v179, v178, vcc
	v_add_u32_e32 v179, -1, v177
	v_fma_f32 v180, -v179, v177, v176
	v_cmp_ge_f32_e32 vcc, 0, v180
	v_add_u32_e32 v180, 1, v177
	s_nop 0
	v_cndmask_b32_e32 v179, v177, v179, vcc
	v_fma_f32 v177, -v180, v177, v176
	v_cmp_lt_f32_e32 vcc, 0, v177
	s_nop 1
	v_cndmask_b32_e32 v177, v179, v180, vcc
	v_cmp_gt_f32_e32 vcc, s3, v156
	v_mul_f32_e32 v179, 0x37800000, v177
	v_cndmask_b32_e64 v177, v177, v179, s[0:1]
	v_cndmask_b32_e32 v156, v156, v157, vcc
	v_sqrt_f32_e32 v157, v156
	v_cmp_class_f32_e64 s[0:1], v176, v216
	s_nop 1
	v_cndmask_b32_e64 v176, v177, v176, s[0:1]
	v_add_u32_e32 v177, -1, v157
	v_fma_f32 v179, -v177, v157, v156
	v_cmp_ge_f32_e64 s[0:1], 0, v179
	v_add_u32_e32 v179, 1, v157
	s_nop 0
	v_cndmask_b32_e64 v177, v157, v177, s[0:1]
	v_fma_f32 v157, -v179, v157, v156
	v_cmp_lt_f32_e64 s[0:1], 0, v157
	s_nop 1
	v_cndmask_b32_e64 v157, v177, v179, s[0:1]
	v_div_scale_f32 v179, s[0:1], v178, v178, 1.0
	v_rcp_f32_e32 v180, v179
	v_mul_f32_e32 v177, 0x37800000, v157
	v_cndmask_b32_e32 v157, v157, v177, vcc
	v_cmp_class_f32_e32 vcc, v156, v216
	s_nop 1
	v_cndmask_b32_e32 v156, v157, v156, vcc
	v_fma_f32 v157, -v179, v180, 1.0
	v_fmac_f32_e32 v180, v157, v180
	v_div_scale_f32 v157, vcc, 1.0, v178, 1.0
	v_mul_f32_e32 v177, v157, v180
	v_fma_f32 v181, -v179, v177, v157
	v_fmac_f32_e32 v177, v181, v180
	v_fma_f32 v157, -v179, v177, v157
	v_div_scale_f32 v179, s[0:1], v176, v176, 1.0
	v_rcp_f32_e32 v181, v179
	v_div_fmas_f32 v157, v157, v180, v177
	v_div_fixup_f32 v157, v157, v178, 1.0
	v_fma_f32 v177, -v179, v181, 1.0
	v_fmac_f32_e32 v181, v177, v181
	v_div_scale_f32 v177, vcc, 1.0, v176, 1.0
	v_mul_f32_e32 v178, v177, v181
	v_fma_f32 v180, -v179, v178, v177
	v_fmac_f32_e32 v178, v180, v181
	v_fma_f32 v177, -v179, v178, v177
	v_div_scale_f32 v179, s[0:1], v156, v156, 1.0
	v_rcp_f32_e32 v180, v179
	v_div_fmas_f32 v177, v177, v181, v178
	v_div_fixup_f32 v176, v177, v176, 1.0
	s_movk_i32 s1, 0x7fff
	v_fma_f32 v177, -v179, v180, 1.0
	v_fmac_f32_e32 v180, v177, v180
	v_div_scale_f32 v177, vcc, 1.0, v156, 1.0
	v_mul_f32_e32 v178, v177, v180
	v_fma_f32 v181, -v179, v178, v177
	v_fmac_f32_e32 v178, v181, v180
	v_fma_f32 v177, -v179, v178, v177
	v_div_fmas_f32 v177, v177, v180, v178
	v_div_fixup_f32 v156, v177, v156, 1.0
	v_cndmask_b32_e64 v156, v176, v156, s[40:41]
	v_pk_mul_f32 v[132:133], v[156:157], v[132:133] op_sel_hi:[0,1]
	v_pk_mul_f32 v[134:135], v[156:157], v[134:135] op_sel_hi:[0,1]
	v_pk_mul_f32 v[138:139], v[156:157], v[138:139] op_sel_hi:[0,1]
	v_pk_mul_f32 v[132:133], v[132:133], v[150:151]
	v_pk_mul_f32 v[136:137], v[156:157], v[136:137] op_sel_hi:[0,1]
	v_pk_mul_f32 v[134:135], v[134:135], v[148:149]
	v_pk_mul_f32 v[138:139], v[138:139], v[154:155]
	v_pk_mul_f32 v[136:137], v[136:137], v[152:153]
	v_bfe_u32 v148, v135, 16, 1
	v_bfe_u32 v149, v134, 16, 1
	v_bfe_u32 v150, v133, 16, 1
	v_bfe_u32 v151, v132, 16, 1
	v_cndmask_b32_e64 v176, v157, v176, s[34:35]
	v_add3_u32 v132, v132, v151, s1
	v_add3_u32 v133, v133, v150, s1
	v_add3_u32 v134, v134, v149, s1
	v_add3_u32 v135, v135, v148, s1
	v_bfe_u32 v148, v138, 16, 1
	v_bfe_u32 v149, v139, 16, 1
	v_bfe_u32 v150, v136, 16, 1
	v_bfe_u32 v151, v137, 16, 1
	v_add3_u32 v137, v137, v151, s1
	v_add3_u32 v136, v136, v150, s1
	v_add3_u32 v139, v139, v149, s1
	v_add3_u32 v138, v138, v148, s1
	v_pk_mul_f32 v[114:115], v[114:115], v[176:177] op_sel_hi:[1,0]
	v_pk_mul_f32 v[116:117], v[116:117], v[176:177] op_sel_hi:[1,0]
	v_lshrrev_b32_e32 v138, 16, v138
	v_lshrrev_b32_e32 v139, 16, v139
	v_lshrrev_b32_e32 v136, 16, v136
	v_lshrrev_b32_e32 v137, 16, v137
	s_mov_b32 s0, 0xffff0000
	v_pk_mul_f32 v[130:131], v[130:131], v[176:177] op_sel_hi:[1,0]
	v_pk_mul_f32 v[114:115], v[114:115], v[146:147]
	v_pk_mul_f32 v[128:129], v[128:129], v[176:177] op_sel_hi:[1,0]
	v_pk_mul_f32 v[116:117], v[116:117], v[142:143]
	v_and_or_b32 v135, v135, s0, v137
	v_and_or_b32 v134, v134, s0, v136
	v_and_or_b32 v133, v133, s0, v139
	v_and_or_b32 v132, v132, s0, v138
	v_pk_mul_f32 v[130:131], v[130:131], v[140:141]
	v_pk_mul_f32 v[128:129], v[128:129], v[144:145]
	v_bfe_u32 v136, v117, 16, 1
	v_bfe_u32 v137, v116, 16, 1
	v_bfe_u32 v138, v115, 16, 1
	v_bfe_u32 v139, v114, 16, 1
	v_add3_u32 v114, v114, v139, s1
	v_add3_u32 v115, v115, v138, s1
	v_add3_u32 v116, v116, v137, s1
	v_add3_u32 v117, v117, v136, s1
	v_bfe_u32 v136, v130, 16, 1
	v_bfe_u32 v137, v131, 16, 1
	v_bfe_u32 v138, v128, 16, 1
	v_bfe_u32 v139, v129, 16, 1
	v_add3_u32 v129, v129, v139, s1
	v_add3_u32 v128, v128, v138, s1
	v_add3_u32 v131, v131, v137, s1
	v_add3_u32 v130, v130, v136, s1
	v_lshrrev_b32_e32 v130, 16, v130
	v_lshrrev_b32_e32 v131, 16, v131
	v_lshrrev_b32_e32 v128, 16, v128
	v_lshrrev_b32_e32 v129, 16, v129
	v_and_or_b32 v117, v117, s0, v129
	v_and_or_b32 v116, v116, s0, v128
	v_and_or_b32 v115, v115, s0, v131
	v_and_or_b32 v114, v114, s0, v130
	s_add_u32 s0, s24, s16
	s_addc_u32 s1, s25, s17
	global_store_dwordx4 v0, v[132:135], s[0:1]
	global_store_dwordx4 v0, v[114:117], s[0:1] offset:1024
	s_waitcnt vmcnt(34)
	s_and_saveexec_b64 s[0:1], s[38:39]
	s_xor_b64 s[0:1], exec, s[0:1]
	s_cbranch_execz .LBB0_181
; __device__ __forceinline__ void unpack8(const v4u w, float* f) { f[0] = bflo(w.x); f[1] = bfhi(w.x); f[2] = bflo(w.y); f[3] = bfhi(w.y); f[4] = bflo(w.z); f[5] = bfhi(w.z); f[6] = bflo(w.w); f[7] = bfhi(w.w); }
; __device__ __forceinline__ void norm_compute(const NormRow& R, int lane, v4u& ya, v4u& yc) {
;     ...
;     else { float f0[8], f1[8], f2[8]; unpack8(R.d0, f0); unpack8(R.d1, f1); unpack8(R.d2, f2);
;         const float inv = 1.0f / (R.l0 + R.l1 + R.l2);
; #pragma unroll
;         for (int e = 0; e < 8; ++e) fc[e] = (f0[e] + f1[e] + f2[e]) * inv; }
	v_add_f32_e32 v115, v165, v163
	v_add_f32_e32 v128, v166, v115
	v_div_scale_f32 v129, s[16:17], v128, v128, 1.0
	v_rcp_f32_e32 v130, v129
	v_lshlrev_b32_e32 v134, 16, v18
	v_and_b32_e32 v135, 0xffff0000, v18
	v_lshlrev_b32_e32 v138, 16, v20
	v_fma_f32 v131, -v129, v130, 1.0
	v_fmac_f32_e32 v130, v131, v130
	v_div_scale_f32 v131, vcc, 1.0, v128, 1.0
	v_mul_f32_e32 v132, v131, v130
	v_fma_f32 v133, -v129, v132, v131
	v_fmac_f32_e32 v132, v133, v130
	v_fma_f32 v129, -v129, v132, v131
	v_div_fmas_f32 v129, v129, v130, v132
	v_div_fixup_f32 v130, v129, v128, 1.0
	v_lshlrev_b32_e32 v128, 16, v10
	v_and_b32_e32 v129, 0xffff0000, v10
	v_lshlrev_b32_e32 v132, 16, v14
	v_and_b32_e32 v133, 0xffff0000, v14
	v_pk_add_f32 v[128:129], v[132:133], v[128:129]
	v_lshlrev_b32_e32 v132, 16, v15
	v_pk_add_f32 v[128:129], v[128:129], v[134:135]
	v_and_b32_e32 v133, 0xffff0000, v15
	v_pk_mul_f32 v[136:137], v[130:131], v[128:129] op_sel_hi:[0,1]
	v_lshlrev_b32_e32 v128, 16, v11
	v_and_b32_e32 v129, 0xffff0000, v11
	v_lshlrev_b32_e32 v134, 16, v19
	v_and_b32_e32 v135, 0xffff0000, v19
	v_pk_add_f32 v[128:129], v[132:133], v[128:129]
	v_lshlrev_b32_e32 v132, 16, v12
	v_pk_add_f32 v[128:129], v[128:129], v[134:135]
	v_and_b32_e32 v133, 0xffff0000, v12
	v_lshlrev_b32_e32 v134, 16, v16
	v_and_b32_e32 v135, 0xffff0000, v16
	v_and_b32_e32 v139, 0xffff0000, v20
	v_pk_add_f32 v[132:133], v[134:135], v[132:133]
	v_lshlrev_b32_e32 v114, 16, v13
	v_lshlrev_b32_e32 v116, 16, v17
	v_and_b32_e32 v115, 0xffff0000, v13
	v_and_b32_e32 v117, 0xffff0000, v17
	v_pk_add_f32 v[132:133], v[132:133], v[138:139]
	v_pk_add_f32 v[114:115], v[116:117], v[114:115]
	v_pk_mul_f32 v[134:135], v[130:131], v[132:133] op_sel_hi:[0,1]
	v_lshlrev_b32_e32 v132, 16, v21
	v_and_b32_e32 v133, 0xffff0000, v21
	v_pk_add_f32 v[114:115], v[114:115], v[132:133]
	v_pk_mul_f32 v[128:129], v[130:131], v[128:129] op_sel_hi:[0,1]
	v_pk_mul_f32 v[130:131], v[130:131], v[114:115] op_sel_hi:[0,1]
	v_mov_b32_e32 v133, v130
	v_mov_b32_e32 v130, v135
	v_mov_b32_e32 v132, v134
	v_mov_b32_e32 v135, v128
	v_mov_b32_e32 v128, v137
	v_mov_b32_e32 v134, v136
; #define GAS __attribute__((address_space(1)))
; __device__ __forceinline__ void unpack8(const v4u w, float* f) { f[0] = bflo(w.x); f[1] = bfhi(w.x); f[2] = bflo(w.y); f[3] = bfhi(w.y); f[4] = bflo(w.z); f[5] = bfhi(w.z); f[6] = bflo(w.w); f[7] = bfhi(w.w); }
; __device__ __forceinline__ void norm_load(NormRow& R, int m, int lane, const bf16* O, const bf16* GF, const bf16* OD, const float* LD) {
;     R.oa = __builtin_nontemporal_load((const GAS v4u*)(O + (size_t)m * DM + 8 * lane));
;     if (lane < 16) { R.oc = __builtin_nontemporal_load((const GAS v4u*)(O + (size_t)m * DM + 512 + 8 * lane)); R.gc = __builtin_nontemporal_load((const GAS v4u*)(GF + (size_t)m * 384 + 256 + 8 * lane)); }
;     else { const int dc = 8 * lane - 128, hd = dc >> 6;
;         R.d0 = __builtin_nontemporal_load((const GAS v4u*)(OD + (size_t)m * 384 + dc)); R.d1 = __builtin_nontemporal_load((const GAS v4u*)(OD + OD_BRANCH + (size_t)m * 384 + dc)); R.d2 = __builtin_nontemporal_load((const GAS v4u*)(OD + 2 * OD_BRANCH + (size_t)m * 384 + dc));
;         R.l0 = LD[(size_t)m * 8 + hd]; R.l1 = LD[LD_BRANCH + (size_t)m * 8 + hd]; R.l2 = LD[2 * LD_BRANCH + (size_t)m * 8 + hd]; }
;     if (lane >= 32) R.ga = __builtin_nontemporal_load((const GAS v4u*)(GF + (size_t)m * 384 + 8 * lane - 256));
; __device__ __forceinline__ void norm_compute(const NormRow& R, int lane, v4u& ya, v4u& yc) {
;     ...
;     if (lane < 16) unpack8(R.oc, fc);
;     else { float f0[8], f1[8], f2[8]; unpack8(R.d0, f0); unpack8(R.d1, f1); unpack8(R.d2, f2);
;         const float inv = 1.0f / (R.l0 + R.l1 + R.l2);
; #pragma unroll
;         for (int e = 0; e < 8; ++e) fc[e] = (f0[e] + f1[e] + f2[e]) * inv; }
;     float sa = 0.f, sc = 0.f;
; #pragma unroll
;     for (int e = 0; e < 8; ++e) { sa += fa[e] * fa[e]; sc += fc[e] * fc[e]; }
;     const float s_moba = wave_sum(lane < 32 ? sa : 0.f), s_fox = wave_sum((lane >= 32 ? sa : 0.f) + (lane < 16 ? sc : 0.f)), s_dil = wave_sum(lane >= 16 ? sc : 0.f);
;     const float r_moba = 1.0f / sqrtf(s_moba * (1.0f / 256.0f) + EPS), r_fox = 1.0f / sqrtf(s_fox * (1.0f / 384.0f) + EPS), r_dil = 1.0f / sqrtf(s_dil * (1.0f / 384.0f) + EPS);
;     float ga[8], gc[8];
; #pragma unroll
;     for (int e = 0; e < 8; ++e) { ga[e] = 1.f; gc[e] = 1.f; }
;     if (lane >= 32) unpack8(R.ga, ga);
;     if (lane < 16) unpack8(R.gc, gc);
.LBB0_181:
	s_andn2_saveexec_b64 s[0:1], s[0:1]
	v_lshlrev_b32_e32 v134, 16, v22
	v_and_b32_e32 v128, 0xffff0000, v22
	v_lshlrev_b32_e32 v135, 16, v23
	v_and_b32_e32 v129, 0xffff0000, v23
	v_lshlrev_b32_e32 v132, 16, v24
	v_and_b32_e32 v130, 0xffff0000, v24
	v_lshlrev_b32_e32 v133, 16, v25
	v_and_b32_e32 v131, 0xffff0000, v25
	s_or_b64 exec, exec, s[0:1]
	v_lshlrev_b32_e32 v139, 16, v99
	v_lshlrev_b32_e32 v138, 16, v98
	v_and_b32_e32 v99, 0xffff0000, v99
	v_and_b32_e32 v98, 0xffff0000, v98
	v_pk_mul_f32 v[114:115], v[138:139], v[138:139]
	v_pk_mul_f32 v[116:117], v[98:99], v[98:99]
	v_mul_f32_e32 v144, v128, v128
	v_fmac_f32_e32 v144, v134, v134
	v_add_f32_e32 v114, v114, v116
	v_lshlrev_b32_e32 v137, 16, v101
	v_lshlrev_b32_e32 v136, 16, v100
	v_fmac_f32_e32 v144, v135, v135
	v_add_f32_e32 v114, v115, v114
	v_and_b32_e32 v101, 0xffff0000, v101
	v_and_b32_e32 v100, 0xffff0000, v100
	v_fmac_f32_e32 v144, v129, v129
	v_pk_mul_f32 v[140:141], v[136:137], v[136:137]
	v_add_f32_e32 v114, v117, v114
	v_fmac_f32_e32 v144, v132, v132
	v_pk_mul_f32 v[142:143], v[100:101], v[100:101]
	v_add_f32_e32 v114, v140, v114
	v_fmac_f32_e32 v144, v130, v130
	v_add_f32_e32 v114, v142, v114
	v_fmac_f32_e32 v144, v133, v133
	v_add_f32_e32 v114, v141, v114
	v_add_f32_e32 v114, v143, v114
	v_fmac_f32_e32 v144, v131, v131
	v_cndmask_b32_e64 v115, 0, v114, s[40:41]
	v_cndmask_b32_e64 v114, 0, v114, s[36:37]
	v_cndmask_b32_e64 v117, 0, v144, s[34:35]
	v_add_f32_e32 v114, v114, v117
	v_cndmask_b32_e64 v140, 0, v144, s[42:43]
	v_mov_b32_e32 v154, 1.0
	v_mov_b32_e32 v150, 1.0
	s_nop 1
	v_add_f32_dpp v115, v115, v115 quad_perm:[1,0,3,2] row_mask:0xf bank_mask:0xf
	s_nop 1
	v_add_f32_dpp v114, v114, v114 quad_perm:[1,0,3,2] row_mask:0xf bank_mask:0xf
	s_nop 1
	v_add_f32_dpp v140, v140, v140 quad_perm:[1,0,3,2] row_mask:0xf bank_mask:0xf
	v_mov_b32_e32 v155, 1.0
	v_mov_b32_e32 v151, 1.0
	s_nop 1
	v_add_f32_dpp v115, v115, v115 quad_perm:[2,3,0,1] row_mask:0xf bank_mask:0xf
	s_nop 1
	v_add_f32_dpp v114, v114, v114 quad_perm:[2,3,0,1] row_mask:0xf bank_mask:0xf
	s_nop 1
	v_add_f32_dpp v140, v140, v140 quad_perm:[2,3,0,1] row_mask:0xf bank_mask:0xf
	v_mov_b32_e32 v152, 1.0
	v_mov_b32_e32 v148, 1.0
	s_nop 1
	v_add_f32_dpp v115, v115, v115 row_half_mirror row_mask:0xf bank_mask:0xf
	s_nop 1
	v_add_f32_dpp v114, v114, v114 row_half_mirror row_mask:0xf bank_mask:0xf
	s_nop 1
	v_add_f32_dpp v140, v140, v140 row_half_mirror row_mask:0xf bank_mask:0xf
	v_mov_b32_e32 v153, 1.0
	v_mov_b32_e32 v149, 1.0
	s_nop 1
	v_add_f32_dpp v115, v115, v115 row_mirror row_mask:0xf bank_mask:0xf
	s_nop 1
	v_add_f32_dpp v114, v114, v114 row_mirror row_mask:0xf bank_mask:0xf
	s_nop 1
	v_add_f32_dpp v140, v140, v140 row_mirror row_mask:0xf bank_mask:0xf
	v_mov_b32_e32 v116, v115
	s_nop 1
	v_permlane16_swap_b32_e32 v115, v116
	v_add_f32_e32 v156, v115, v116
	v_mov_b32_e32 v117, v114
	s_nop 1
	v_permlane16_swap_b32_e32 v114, v117
	v_add_f32_e32 v176, v114, v117
	v_mov_b32_e32 v141, v140
	s_nop 1
	v_permlane16_swap_b32_e32 v140, v141
	v_add_f32_e32 v178, v140, v141
	v_mov_b32_e32 v140, 1.0
	s_and_saveexec_b64 s[0:1], s[36:37]
	v_lshlrev_b32_e32 v154, 16, v6
	v_and_b32_e32 v150, 0xffff0000, v6
	v_lshlrev_b32_e32 v155, 16, v7
	v_and_b32_e32 v151, 0xffff0000, v7
	v_lshlrev_b32_e32 v152, 16, v8
	v_and_b32_e32 v148, 0xffff0000, v8
	v_lshlrev_b32_e32 v153, 16, v9
	v_and_b32_e32 v149, 0xffff0000, v9
	s_or_b64 exec, exec, s[0:1]
	v_mov_b32_e32 v146, 1.0
	v_mov_b32_e32 v141, 1.0
	v_mov_b32_e32 v147, 1.0
	v_mov_b32_e32 v144, 1.0
	v_mov_b32_e32 v142, 1.0
	v_mov_b32_e32 v145, 1.0
	v_mov_b32_e32 v143, 1.0
	s_and_saveexec_b64 s[0:1], s[34:35]
	v_lshlrev_b32_e32 v140, 16, v2
	v_and_b32_e32 v146, 0xffff0000, v2
	v_lshlrev_b32_e32 v141, 16, v3
	v_and_b32_e32 v147, 0xffff0000, v3
	v_lshlrev_b32_e32 v144, 16, v4
	v_and_b32_e32 v142, 0xffff0000, v4
	v_lshlrev_b32_e32 v145, 16, v5
	v_and_b32_e32 v143, 0xffff0000, v5
	s_or_b64 exec, exec, s[0:1]
	s_or_b32 s0, s8, 11
	s_ashr_i32 s1, s0, 31
	s_lshl_b64 s[16:17], s[0:1], 11
	s_add_u32 s20, s29, s16
	s_addc_u32 s21, s30, s17
	global_load_dwordx4 v[114:117], v0, s[20:21] nt
	s_and_saveexec_b64 s[22:23], s[38:39]
	s_xor_b64 s[22:23], exec, s[22:23]
	s_cbranch_execz .LBB0_773
	v_mad_i64_i32 v[10:11], s[44:45], s0, v252, v[124:125]
	v_mad_i64_i32 v[14:15], s[44:45], s0, v252, v[122:123]
	v_mad_i64_i32 v[18:19], s[44:45], s0, v252, v[120:121]
	s_lshl_b64 s[44:45], s[0:1], 5
	s_add_u32 s44, s26, s44
	s_addc_u32 s45, s27, s45
	v_lshl_add_u64 v[180:181], v[118:119], 2, s[44:45]
	v_add_co_u32_e32 v182, vcc, 0x100000, v180
	global_load_dword v163, v[180:181], off
	s_nop 0
	v_addc_co_u32_e32 v183, vcc, 0, v181, vcc
	global_load_dword v165, v[182:183], off
	v_add_co_u32_e32 v180, vcc, 0x200000, v180
	global_load_dwordx4 v[10:13], v[10:11], off nt
	s_nop 0
	v_addc_co_u32_e32 v181, vcc, 0, v181, vcc
	global_load_dwordx4 v[14:17], v[14:15], off nt
	s_nop 0
	global_load_dwordx4 v[18:21], v[18:19], off nt
	s_nop 0
	global_load_dword v166, v[180:181], off
	s_andn2_saveexec_b64 s[22:23], s[22:23]
	s_cbranch_execnz .LBB0_774

; __device__ __forceinline__ unsigned pk2(float lo, float hi) { return f2bf(lo) | (f2bf(hi) << 16); }
; __device__ __forceinline__ void unpack8(const v4u w, float* f) { f[0] = bflo(w.x); f[1] = bfhi(w.x); f[2] = bflo(w.y); f[3] = bfhi(w.y); f[4] = bflo(w.z); f[5] = bfhi(w.z); f[6] = bflo(w.w); f[7] = bfhi(w.w); }
; __device__ __forceinline__ void norm_compute(const NormRow& R, int lane, v4u& ya, v4u& yc) {
;     ...
;     const float s_moba = wave_sum(lane < 32 ? sa : 0.f), s_fox = wave_sum((lane >= 32 ? sa : 0.f) + (lane < 16 ? sc : 0.f)), s_dil = wave_sum(lane >= 16 ? sc : 0.f);
;     const float r_moba = 1.0f / sqrtf(s_moba * (1.0f / 256.0f) + EPS), r_fox = 1.0f / sqrtf(s_fox * (1.0f / 384.0f) + EPS), r_dil = 1.0f / sqrtf(s_dil * (1.0f / 384.0f) + EPS);
;     float ga[8], gc[8];
; #pragma unroll
;     for (int e = 0; e < 8; ++e) { ga[e] = 1.f; gc[e] = 1.f; }
;     if (lane >= 32) unpack8(R.ga, ga);
;     if (lane < 16) unpack8(R.gc, gc);
;     const float ra = lane < 32 ? r_moba : r_fox, rc = lane < 16 ? r_fox : r_dil;
;     ya.x = pk2(fa[0] * ra * ga[0], fa[1] * ra * ga[1]); ya.y = pk2(fa[2] * ra * ga[2], fa[3] * ra * ga[3]); ya.z = pk2(fa[4] * ra * ga[4], fa[5] * ra * ga[5]); ya.w = pk2(fa[6] * ra * ga[6], fa[7] * ra * ga[7]);
;     yc.x = pk2(fc[0] * rc * gc[0], fc[1] * rc * gc[1]); yc.y = pk2(fc[2] * rc * gc[2], fc[3] * rc * gc[3]); yc.z = pk2(fc[4] * rc * gc[4], fc[5] * rc * gc[5]); yc.w = pk2(fc[6] * rc * gc[6], fc[7] * rc * gc[7]);
; }
.LBB0_191:
	s_or_b64 exec, exec, s[20:21]
	v_mov_b32_e32 v179, v178
	s_nop 1
	v_permlane32_swap_b32_e32 v178, v179
	v_add_f32_e32 v178, v178, v179
	v_fmamk_f32 v178, v178, 0x3b2aaaab, v215
	v_mul_f32_e32 v179, 0x4f800000, v178
	v_cmp_gt_f32_e32 vcc, s3, v178
	v_mov_b32_e32 v177, v176
	s_nop 1
	v_permlane32_swap_b32_e32 v176, v177
	v_add_f32_e32 v176, v176, v177
	v_fmamk_f32 v176, v176, 0x3b2aaaab, v215
	v_cndmask_b32_e32 v178, v178, v179, vcc
	v_sqrt_f32_e32 v179, v178
	v_mul_f32_e32 v177, 0x4f800000, v176
	v_mov_b32_e32 v157, v156
	s_nop 1
	v_permlane32_swap_b32_e32 v156, v157
	v_add_f32_e32 v156, v156, v157
	v_fmamk_f32 v156, v156, 0x3b800000, v215
	v_add_u32_e32 v180, -1, v179
	v_fma_f32 v182, -v180, v179, v178
	v_add_u32_e32 v181, 1, v179
	v_cmp_ge_f32_e64 s[0:1], 0, v182
	v_mul_f32_e32 v157, 0x4f800000, v156
	s_nop 0
	v_cndmask_b32_e64 v180, v179, v180, s[0:1]
	v_fma_f32 v179, -v181, v179, v178
	v_cmp_lt_f32_e64 s[0:1], 0, v179
	s_nop 1
	v_cndmask_b32_e64 v179, v180, v181, s[0:1]
	v_cmp_gt_f32_e64 s[0:1], s3, v176
	v_mul_f32_e32 v180, 0x37800000, v179
	v_cndmask_b32_e32 v179, v179, v180, vcc
	v_cndmask_b32_e64 v176, v176, v177, s[0:1]
	v_sqrt_f32_e32 v177, v176
	v_cmp_class_f32_e32 vcc, v178, v216
	s_nop 1
	v_cndmask_b32_e32 v178, v179, v178, vcc
	v_add_u32_e32 v179, -1, v177
	v_fma_f32 v180, -v179, v177, v176
	v_cmp_ge_f32_e32 vcc, 0, v180
	v_add_u32_e32 v180, 1, v177
	s_nop 0
	v_cndmask_b32_e32 v179, v177, v179, vcc
	v_fma_f32 v177, -v180, v177, v176
	v_cmp_lt_f32_e32 vcc, 0, v177
	s_nop 1
	v_cndmask_b32_e32 v177, v179, v180, vcc
	v_cmp_gt_f32_e32 vcc, s3, v156
	v_mul_f32_e32 v179, 0x37800000, v177
	v_cndmask_b32_e64 v177, v177, v179, s[0:1]
	v_cndmask_b32_e32 v156, v156, v157, vcc
	v_sqrt_f32_e32 v157, v156
	v_cmp_class_f32_e64 s[0:1], v176, v216
	s_nop 1
	v_cndmask_b32_e64 v176, v177, v176, s[0:1]
	v_add_u32_e32 v177, -1, v157
	v_fma_f32 v179, -v177, v157, v156
	v_cmp_ge_f32_e64 s[0:1], 0, v179
	v_add_u32_e32 v179, 1, v157
	s_nop 0
	v_cndmask_b32_e64 v177, v157, v177, s[0:1]
	v_fma_f32 v157, -v179, v157, v156
	v_cmp_lt_f32_e64 s[0:1], 0, v157
	s_nop 1
	v_cndmask_b32_e64 v157, v177, v179, s[0:1]
	v_div_scale_f32 v179, s[0:1], v178, v178, 1.0
	v_rcp_f32_e32 v180, v179
	v_mul_f32_e32 v177, 0x37800000, v157
	v_cndmask_b32_e32 v157, v157, v177, vcc
	v_cmp_class_f32_e32 vcc, v156, v216
	s_nop 1
	v_cndmask_b32_e32 v156, v157, v156, vcc
	v_fma_f32 v157, -v179, v180, 1.0
	v_fmac_f32_e32 v180, v157, v180
	v_div_scale_f32 v157, vcc, 1.0, v178, 1.0
	v_mul_f32_e32 v177, v157, v180
	v_fma_f32 v181, -v179, v177, v157
	v_fmac_f32_e32 v177, v181, v180
	v_fma_f32 v157, -v179, v177, v157
	v_div_scale_f32 v179, s[0:1], v176, v176, 1.0
	v_rcp_f32_e32 v181, v179
	v_div_fmas_f32 v157, v157, v180, v177
	v_div_fixup_f32 v157, v157, v178, 1.0
	v_fma_f32 v177, -v179, v181, 1.0
	v_fmac_f32_e32 v181, v177, v181
	v_div_scale_f32 v177, vcc, 1.0, v176, 1.0
	v_mul_f32_e32 v178, v177, v181
	v_fma_f32 v180, -v179, v178, v177
	v_fmac_f32_e32 v178, v180, v181
	v_fma_f32 v177, -v179, v178, v177
	v_div_scale_f32 v179, s[0:1], v156, v156, 1.0
	v_rcp_f32_e32 v180, v179
	v_div_fmas_f32 v177, v177, v181, v178
	v_div_fixup_f32 v176, v177, v176, 1.0
	s_movk_i32 s1, 0x7fff
	v_fma_f32 v177, -v179, v180, 1.0
	v_fmac_f32_e32 v180, v177, v180
	v_div_scale_f32 v177, vcc, 1.0, v156, 1.0
	v_mul_f32_e32 v178, v177, v180
	v_fma_f32 v181, -v179, v178, v177
	v_fmac_f32_e32 v178, v181, v180
	v_fma_f32 v177, -v179, v178, v177
	v_div_fmas_f32 v177, v177, v180, v178
	v_div_fixup_f32 v156, v177, v156, 1.0
	v_cndmask_b32_e64 v156, v176, v156, s[40:41]
	v_pk_mul_f32 v[98:99], v[156:157], v[98:99] op_sel_hi:[0,1]
	v_pk_mul_f32 v[100:101], v[156:157], v[100:101] op_sel_hi:[0,1]
	v_pk_mul_f32 v[138:139], v[156:157], v[138:139] op_sel_hi:[0,1]
	v_pk_mul_f32 v[98:99], v[98:99], v[150:151]
	v_pk_mul_f32 v[136:137], v[156:157], v[136:137] op_sel_hi:[0,1]
	v_pk_mul_f32 v[100:101], v[100:101], v[148:149]
	v_pk_mul_f32 v[138:139], v[138:139], v[154:155]
	v_pk_mul_f32 v[136:137], v[136:137], v[152:153]
	v_bfe_u32 v148, v101, 16, 1
	v_bfe_u32 v149, v100, 16, 1
	v_bfe_u32 v150, v99, 16, 1
	v_bfe_u32 v151, v98, 16, 1
	v_cndmask_b32_e64 v176, v157, v176, s[34:35]
	v_add3_u32 v98, v98, v151, s1
	v_add3_u32 v99, v99, v150, s1
	v_add3_u32 v100, v100, v149, s1
	v_add3_u32 v101, v101, v148, s1
	v_bfe_u32 v148, v138, 16, 1
	v_bfe_u32 v149, v139, 16, 1
	v_bfe_u32 v150, v136, 16, 1
	v_bfe_u32 v151, v137, 16, 1
	v_add3_u32 v137, v137, v151, s1
	v_add3_u32 v136, v136, v150, s1
	v_add3_u32 v139, v139, v149, s1
	v_add3_u32 v138, v138, v148, s1
	v_pk_mul_f32 v[128:129], v[128:129], v[176:177] op_sel_hi:[1,0]
	v_pk_mul_f32 v[130:131], v[130:131], v[176:177] op_sel_hi:[1,0]
	v_lshrrev_b32_e32 v138, 16, v138
	v_lshrrev_b32_e32 v139, 16, v139
	v_lshrrev_b32_e32 v136, 16, v136
	v_lshrrev_b32_e32 v137, 16, v137
	s_mov_b32 s0, 0xffff0000
	v_pk_mul_f32 v[134:135], v[134:135], v[176:177] op_sel_hi:[1,0]
	v_pk_mul_f32 v[128:129], v[128:129], v[146:147]
	v_pk_mul_f32 v[132:133], v[132:133], v[176:177] op_sel_hi:[1,0]
	v_pk_mul_f32 v[130:131], v[130:131], v[142:143]
	v_and_or_b32 v101, v101, s0, v137
	v_and_or_b32 v100, v100, s0, v136
	v_and_or_b32 v99, v99, s0, v139
	v_and_or_b32 v98, v98, s0, v138
	v_pk_mul_f32 v[134:135], v[134:135], v[140:141]
	v_pk_mul_f32 v[132:133], v[132:133], v[144:145]
	v_bfe_u32 v136, v131, 16, 1
	v_bfe_u32 v137, v130, 16, 1
	v_bfe_u32 v138, v129, 16, 1
	v_bfe_u32 v139, v128, 16, 1
	v_add3_u32 v128, v128, v139, s1
	v_add3_u32 v129, v129, v138, s1
	v_add3_u32 v130, v130, v137, s1
	v_add3_u32 v131, v131, v136, s1
	v_bfe_u32 v136, v134, 16, 1
	v_bfe_u32 v137, v135, 16, 1
	v_bfe_u32 v138, v132, 16, 1
	v_bfe_u32 v139, v133, 16, 1
	v_add3_u32 v133, v133, v139, s1
	v_add3_u32 v132, v132, v138, s1
	v_add3_u32 v135, v135, v137, s1
	v_add3_u32 v134, v134, v136, s1
	v_lshrrev_b32_e32 v134, 16, v134
	v_lshrrev_b32_e32 v135, 16, v135
	v_lshrrev_b32_e32 v132, 16, v132
	v_lshrrev_b32_e32 v133, 16, v133
	v_and_or_b32 v131, v131, s0, v133
	v_and_or_b32 v130, v130, s0, v132
	v_and_or_b32 v129, v129, s0, v135
	v_and_or_b32 v128, v128, s0, v134
	s_add_u32 s0, s24, s18
	s_addc_u32 s1, s25, s19
	global_store_dwordx4 v0, v[98:101], s[0:1]
	global_store_dwordx4 v0, v[128:131], s[0:1] offset:1024
	s_and_saveexec_b64 s[0:1], s[38:39]
	s_xor_b64 s[0:1], exec, s[0:1]
	s_cbranch_execz .LBB0_193
; __device__ __forceinline__ void unpack8(const v4u w, float* f) { f[0] = bflo(w.x); f[1] = bfhi(w.x); f[2] = bflo(w.y); f[3] = bfhi(w.y); f[4] = bflo(w.z); f[5] = bfhi(w.z); f[6] = bflo(w.w); f[7] = bfhi(w.w); }
; __device__ __forceinline__ void norm_compute(const NormRow& R, int lane, v4u& ya, v4u& yc) {
;     ...
;     if (lane < 16) unpack8(R.oc, fc);
;     else { float f0[8], f1[8], f2[8]; unpack8(R.d0, f0); unpack8(R.d1, f1); unpack8(R.d2, f2);
;         const float inv = 1.0f / (R.l0 + R.l1 + R.l2);
; #pragma unroll
;         for (int e = 0; e < 8; ++e) fc[e] = (f0[e] + f1[e] + f2[e]) * inv; }
	s_waitcnt vmcnt(34)
	v_add_f32_e32 v99, v173, v174
	v_add_f32_e32 v128, v99, v175
	v_div_scale_f32 v129, s[18:19], v128, v128, 1.0
	v_rcp_f32_e32 v130, v129
	v_lshlrev_b32_e32 v134, 16, v90
	v_and_b32_e32 v135, 0xffff0000, v90
	v_lshlrev_b32_e32 v138, 16, v92
	v_fma_f32 v131, -v129, v130, 1.0
	v_fmac_f32_e32 v130, v131, v130
	v_div_scale_f32 v131, vcc, 1.0, v128, 1.0
	v_mul_f32_e32 v132, v131, v130
	v_fma_f32 v133, -v129, v132, v131
	v_fmac_f32_e32 v132, v133, v130
	v_fma_f32 v129, -v129, v132, v131
	v_div_fmas_f32 v129, v129, v130, v132
	v_div_fixup_f32 v130, v129, v128, 1.0
	v_lshlrev_b32_e32 v128, 16, v82
	v_and_b32_e32 v129, 0xffff0000, v82
	v_lshlrev_b32_e32 v132, 16, v86
	v_and_b32_e32 v133, 0xffff0000, v86
	v_pk_add_f32 v[128:129], v[132:133], v[128:129]
	v_lshlrev_b32_e32 v132, 16, v87
	v_pk_add_f32 v[128:129], v[128:129], v[134:135]
	v_and_b32_e32 v133, 0xffff0000, v87
	v_pk_mul_f32 v[136:137], v[128:129], v[130:131] op_sel_hi:[1,0]
	v_lshlrev_b32_e32 v128, 16, v83
	v_and_b32_e32 v129, 0xffff0000, v83
	v_lshlrev_b32_e32 v134, 16, v91
	v_and_b32_e32 v135, 0xffff0000, v91
	v_pk_add_f32 v[128:129], v[132:133], v[128:129]
	v_lshlrev_b32_e32 v132, 16, v84
	v_pk_add_f32 v[128:129], v[128:129], v[134:135]
	v_and_b32_e32 v133, 0xffff0000, v84
	v_lshlrev_b32_e32 v134, 16, v88
	v_and_b32_e32 v135, 0xffff0000, v88
	v_and_b32_e32 v139, 0xffff0000, v92
	v_pk_add_f32 v[132:133], v[134:135], v[132:133]
	v_lshlrev_b32_e32 v98, 16, v85
	v_lshlrev_b32_e32 v100, 16, v89
	v_and_b32_e32 v99, 0xffff0000, v85
	v_and_b32_e32 v101, 0xffff0000, v89
	v_pk_add_f32 v[132:133], v[132:133], v[138:139]
	v_pk_add_f32 v[98:99], v[100:101], v[98:99]
	v_pk_mul_f32 v[134:135], v[132:133], v[130:131] op_sel_hi:[1,0]
	v_lshlrev_b32_e32 v132, 16, v93
	v_and_b32_e32 v133, 0xffff0000, v93
	v_pk_add_f32 v[98:99], v[98:99], v[132:133]
	v_pk_mul_f32 v[128:129], v[128:129], v[130:131] op_sel_hi:[1,0]
	v_pk_mul_f32 v[130:131], v[98:99], v[130:131] op_sel_hi:[1,0]
	v_mov_b32_e32 v132, v134
	v_mov_b32_e32 v133, v130
	v_mov_b32_e32 v130, v135
	v_mov_b32_e32 v135, v128
	v_mov_b32_e32 v128, v137
	v_mov_b32_e32 v134, v136
.LBB0_193:
	s_andn2_saveexec_b64 s[0:1], s[0:1]
	s_cbranch_execz .LBB0_195
	s_waitcnt vmcnt(34)
	v_lshlrev_b32_e32 v134, 16, v94
	v_and_b32_e32 v128, 0xffff0000, v94
	v_lshlrev_b32_e32 v135, 16, v95
	v_and_b32_e32 v129, 0xffff0000, v95
	v_lshlrev_b32_e32 v132, 16, v96
	v_and_b32_e32 v130, 0xffff0000, v96
	v_lshlrev_b32_e32 v133, 16, v97
	v_and_b32_e32 v131, 0xffff0000, v97
; #define GAS __attribute__((address_space(1)))
; __device__ __forceinline__ void unpack8(const v4u w, float* f) { f[0] = bflo(w.x); f[1] = bfhi(w.x); f[2] = bflo(w.y); f[3] = bfhi(w.y); f[4] = bflo(w.z); f[5] = bfhi(w.z); f[6] = bflo(w.w); f[7] = bfhi(w.w); }
; __device__ __forceinline__ void norm_load(NormRow& R, int m, int lane, const bf16* O, const bf16* GF, const bf16* OD, const float* LD) {
;     R.oa = __builtin_nontemporal_load((const GAS v4u*)(O + (size_t)m * DM + 8 * lane));
;     if (lane < 16) { R.oc = __builtin_nontemporal_load((const GAS v4u*)(O + (size_t)m * DM + 512 + 8 * lane)); R.gc = __builtin_nontemporal_load((const GAS v4u*)(GF + (size_t)m * 384 + 256 + 8 * lane)); }
;     else { const int dc = 8 * lane - 128, hd = dc >> 6;
;         R.d0 = __builtin_nontemporal_load((const GAS v4u*)(OD + (size_t)m * 384 + dc)); R.d1 = __builtin_nontemporal_load((const GAS v4u*)(OD + OD_BRANCH + (size_t)m * 384 + dc)); R.d2 = __builtin_nontemporal_load((const GAS v4u*)(OD + 2 * OD_BRANCH + (size_t)m * 384 + dc));
;         R.l0 = LD[(size_t)m * 8 + hd]; R.l1 = LD[LD_BRANCH + (size_t)m * 8 + hd]; R.l2 = LD[2 * LD_BRANCH + (size_t)m * 8 + hd]; }
;     if (lane >= 32) R.ga = __builtin_nontemporal_load((const GAS v4u*)(GF + (size_t)m * 384 + 8 * lane - 256));
; __device__ __forceinline__ void norm_compute(const NormRow& R, int lane, v4u& ya, v4u& yc) {
;     ...
;     float sa = 0.f, sc = 0.f;
; #pragma unroll
;     for (int e = 0; e < 8; ++e) { sa += fa[e] * fa[e]; sc += fc[e] * fc[e]; }
;     const float s_moba = wave_sum(lane < 32 ? sa : 0.f), s_fox = wave_sum((lane >= 32 ? sa : 0.f) + (lane < 16 ? sc : 0.f)), s_dil = wave_sum(lane >= 16 ? sc : 0.f);
;     const float r_moba = 1.0f / sqrtf(s_moba * (1.0f / 256.0f) + EPS), r_fox = 1.0f / sqrtf(s_fox * (1.0f / 384.0f) + EPS), r_dil = 1.0f / sqrtf(s_dil * (1.0f / 384.0f) + EPS);
;     float ga[8], gc[8];
; #pragma unroll
;     for (int e = 0; e < 8; ++e) { ga[e] = 1.f; gc[e] = 1.f; }
;     if (lane >= 32) unpack8(R.ga, ga);
;     if (lane < 16) unpack8(R.gc, gc);
.LBB0_195:
	s_or_b64 exec, exec, s[0:1]
	s_waitcnt vmcnt(34)
	v_lshlrev_b32_e32 v139, 16, v103
	v_lshlrev_b32_e32 v138, 16, v102
	v_and_b32_e32 v103, 0xffff0000, v103
	v_and_b32_e32 v102, 0xffff0000, v102
	v_pk_mul_f32 v[98:99], v[138:139], v[138:139]
	v_pk_mul_f32 v[100:101], v[102:103], v[102:103]
	v_mul_f32_e32 v144, v128, v128
	v_fmac_f32_e32 v144, v134, v134
	v_add_f32_e32 v98, v98, v100
	v_lshlrev_b32_e32 v137, 16, v105
	v_lshlrev_b32_e32 v136, 16, v104
	v_fmac_f32_e32 v144, v135, v135
	v_add_f32_e32 v98, v99, v98
	v_and_b32_e32 v105, 0xffff0000, v105
	v_and_b32_e32 v104, 0xffff0000, v104
	v_fmac_f32_e32 v144, v129, v129
	v_pk_mul_f32 v[140:141], v[136:137], v[136:137]
	v_add_f32_e32 v98, v101, v98
	v_fmac_f32_e32 v144, v132, v132
	v_pk_mul_f32 v[142:143], v[104:105], v[104:105]
	v_add_f32_e32 v98, v140, v98
	v_fmac_f32_e32 v144, v130, v130
	v_add_f32_e32 v98, v142, v98
	v_fmac_f32_e32 v144, v133, v133
	v_add_f32_e32 v98, v141, v98
	v_add_f32_e32 v98, v143, v98
	v_fmac_f32_e32 v144, v131, v131
	v_cndmask_b32_e64 v99, 0, v98, s[40:41]
	v_cndmask_b32_e64 v98, 0, v98, s[36:37]
	v_cndmask_b32_e64 v101, 0, v144, s[34:35]
	v_add_f32_e32 v98, v98, v101
	v_cndmask_b32_e64 v140, 0, v144, s[42:43]
	v_mov_b32_e32 v154, 1.0
	v_mov_b32_e32 v150, 1.0
	s_nop 1
	v_add_f32_dpp v99, v99, v99 quad_perm:[1,0,3,2] row_mask:0xf bank_mask:0xf
	s_nop 1
	v_add_f32_dpp v98, v98, v98 quad_perm:[1,0,3,2] row_mask:0xf bank_mask:0xf
	s_nop 1
	v_add_f32_dpp v140, v140, v140 quad_perm:[1,0,3,2] row_mask:0xf bank_mask:0xf
	v_mov_b32_e32 v155, 1.0
	v_mov_b32_e32 v151, 1.0
	s_nop 1
	v_add_f32_dpp v99, v99, v99 quad_perm:[2,3,0,1] row_mask:0xf bank_mask:0xf
	s_nop 1
	v_add_f32_dpp v98, v98, v98 quad_perm:[2,3,0,1] row_mask:0xf bank_mask:0xf
	s_nop 1
	v_add_f32_dpp v140, v140, v140 quad_perm:[2,3,0,1] row_mask:0xf bank_mask:0xf
	v_mov_b32_e32 v152, 1.0
	v_mov_b32_e32 v148, 1.0
	s_nop 1
	v_add_f32_dpp v99, v99, v99 row_half_mirror row_mask:0xf bank_mask:0xf
	s_nop 1
	v_add_f32_dpp v98, v98, v98 row_half_mirror row_mask:0xf bank_mask:0xf
	s_nop 1
	v_add_f32_dpp v140, v140, v140 row_half_mirror row_mask:0xf bank_mask:0xf
	v_mov_b32_e32 v153, 1.0
	v_mov_b32_e32 v149, 1.0
	s_nop 1
	v_add_f32_dpp v99, v99, v99 row_mirror row_mask:0xf bank_mask:0xf
	s_nop 1
	v_add_f32_dpp v98, v98, v98 row_mirror row_mask:0xf bank_mask:0xf
	s_nop 1
	v_add_f32_dpp v140, v140, v140 row_mirror row_mask:0xf bank_mask:0xf
	v_mov_b32_e32 v100, v99
	s_nop 1
	v_permlane16_swap_b32_e32 v99, v100
	v_add_f32_e32 v156, v99, v100
	v_mov_b32_e32 v101, v98
	s_nop 1
	v_permlane16_swap_b32_e32 v98, v101
	v_add_f32_e32 v176, v98, v101
	v_mov_b32_e32 v141, v140
	s_nop 1
	v_permlane16_swap_b32_e32 v140, v141
	v_add_f32_e32 v178, v140, v141
	v_mov_b32_e32 v140, 1.0
	s_and_saveexec_b64 s[0:1], s[36:37]
	v_lshlrev_b32_e32 v154, 16, v78
	v_and_b32_e32 v150, 0xffff0000, v78
	v_lshlrev_b32_e32 v155, 16, v79
	v_and_b32_e32 v151, 0xffff0000, v79
	v_lshlrev_b32_e32 v152, 16, v80
	v_and_b32_e32 v148, 0xffff0000, v80
	v_lshlrev_b32_e32 v153, 16, v81
	v_and_b32_e32 v149, 0xffff0000, v81
	s_or_b64 exec, exec, s[0:1]
	v_mov_b32_e32 v146, 1.0
	v_mov_b32_e32 v141, 1.0
	v_mov_b32_e32 v147, 1.0
	v_mov_b32_e32 v144, 1.0
	v_mov_b32_e32 v142, 1.0
	v_mov_b32_e32 v145, 1.0
	v_mov_b32_e32 v143, 1.0
	s_and_saveexec_b64 s[0:1], s[34:35]
	v_lshlrev_b32_e32 v140, 16, v74
	v_and_b32_e32 v146, 0xffff0000, v74
	v_lshlrev_b32_e32 v141, 16, v75
	v_and_b32_e32 v147, 0xffff0000, v75
	v_lshlrev_b32_e32 v144, 16, v76
	v_and_b32_e32 v142, 0xffff0000, v76
	v_lshlrev_b32_e32 v145, 16, v77
	v_and_b32_e32 v143, 0xffff0000, v77
	s_or_b64 exec, exec, s[0:1]
	s_or_b32 s0, s8, 12
	s_ashr_i32 s1, s0, 31
	s_lshl_b64 s[18:19], s[0:1], 11
	s_add_u32 s20, s29, s18
	s_addc_u32 s21, s30, s19
	global_load_dwordx4 v[98:101], v0, s[20:21] nt
	s_and_saveexec_b64 s[22:23], s[38:39]
	s_xor_b64 s[22:23], exec, s[22:23]
	s_cbranch_execz .LBB0_775
	v_mad_i64_i32 v[82:83], s[44:45], s0, v252, v[124:125]
	v_mad_i64_i32 v[86:87], s[44:45], s0, v252, v[122:123]
	v_mad_i64_i32 v[90:91], s[44:45], s0, v252, v[120:121]
	s_lshl_b64 s[44:45], s[0:1], 5
	s_add_u32 s44, s26, s44
	s_addc_u32 s45, s27, s45
	v_lshl_add_u64 v[180:181], v[118:119], 2, s[44:45]
	v_add_co_u32_e32 v174, vcc, 0x100000, v180
	global_load_dword v173, v[180:181], off
	s_nop 0
	v_addc_co_u32_e32 v175, vcc, 0, v181, vcc
	global_load_dword v174, v[174:175], off
	v_add_co_u32_e32 v180, vcc, 0x200000, v180
	global_load_dwordx4 v[82:85], v[82:83], off nt
	s_nop 0
	v_addc_co_u32_e32 v181, vcc, 0, v181, vcc
	global_load_dwordx4 v[86:89], v[86:87], off nt
	s_nop 0
	global_load_dwordx4 v[90:93], v[90:91], off nt
	s_nop 0
	global_load_dword v175, v[180:181], off
	s_andn2_saveexec_b64 s[22:23], s[22:23]
	s_cbranch_execnz .LBB0_776

; __device__ __forceinline__ unsigned pk2(float lo, float hi) { return f2bf(lo) | (f2bf(hi) << 16); }
; __device__ __forceinline__ void unpack8(const v4u w, float* f) { f[0] = bflo(w.x); f[1] = bfhi(w.x); f[2] = bflo(w.y); f[3] = bfhi(w.y); f[4] = bflo(w.z); f[5] = bfhi(w.z); f[6] = bflo(w.w); f[7] = bfhi(w.w); }
; __device__ __forceinline__ void norm_compute(const NormRow& R, int lane, v4u& ya, v4u& yc) {
;     ...
;     const float s_moba = wave_sum(lane < 32 ? sa : 0.f), s_fox = wave_sum((lane >= 32 ? sa : 0.f) + (lane < 16 ? sc : 0.f)), s_dil = wave_sum(lane >= 16 ? sc : 0.f);
;     const float r_moba = 1.0f / sqrtf(s_moba * (1.0f / 256.0f) + EPS), r_fox = 1.0f / sqrtf(s_fox * (1.0f / 384.0f) + EPS), r_dil = 1.0f / sqrtf(s_dil * (1.0f / 384.0f) + EPS);
;     float ga[8], gc[8];
; #pragma unroll
;     for (int e = 0; e < 8; ++e) { ga[e] = 1.f; gc[e] = 1.f; }
;     if (lane >= 32) unpack8(R.ga, ga);
;     if (lane < 16) unpack8(R.gc, gc);
;     const float ra = lane < 32 ? r_moba : r_fox, rc = lane < 16 ? r_fox : r_dil;
;     ya.x = pk2(fa[0] * ra * ga[0], fa[1] * ra * ga[1]); ya.y = pk2(fa[2] * ra * ga[2], fa[3] * ra * ga[3]); ya.z = pk2(fa[4] * ra * ga[4], fa[5] * ra * ga[5]); ya.w = pk2(fa[6] * ra * ga[6], fa[7] * ra * ga[7]);
;     yc.x = pk2(fc[0] * rc * gc[0], fc[1] * rc * gc[1]); yc.y = pk2(fc[2] * rc * gc[2], fc[3] * rc * gc[3]); yc.z = pk2(fc[4] * rc * gc[4], fc[5] * rc * gc[5]); yc.w = pk2(fc[6] * rc * gc[6], fc[7] * rc * gc[7]);
; }
.LBB0_203:
	s_or_b64 exec, exec, s[20:21]
	v_mov_b32_e32 v179, v178
	s_nop 1
	v_permlane32_swap_b32_e32 v178, v179
	v_add_f32_e32 v178, v178, v179
	v_fmamk_f32 v178, v178, 0x3b2aaaab, v215
	v_mul_f32_e32 v179, 0x4f800000, v178
	v_cmp_gt_f32_e32 vcc, s3, v178
	v_mov_b32_e32 v177, v176
	s_nop 1
	v_permlane32_swap_b32_e32 v176, v177
	v_add_f32_e32 v176, v176, v177
	v_fmamk_f32 v176, v176, 0x3b2aaaab, v215
	v_cndmask_b32_e32 v178, v178, v179, vcc
	v_sqrt_f32_e32 v179, v178
	v_mul_f32_e32 v177, 0x4f800000, v176
	v_mov_b32_e32 v157, v156
	s_nop 1
	v_permlane32_swap_b32_e32 v156, v157
	v_add_f32_e32 v156, v156, v157
	v_fmamk_f32 v156, v156, 0x3b800000, v215
	v_add_u32_e32 v180, -1, v179
	v_fma_f32 v182, -v180, v179, v178
	v_add_u32_e32 v181, 1, v179
	v_cmp_ge_f32_e64 s[0:1], 0, v182
	v_mul_f32_e32 v157, 0x4f800000, v156
	s_nop 0
	v_cndmask_b32_e64 v180, v179, v180, s[0:1]
	v_fma_f32 v179, -v181, v179, v178
	v_cmp_lt_f32_e64 s[0:1], 0, v179
	s_nop 1
	v_cndmask_b32_e64 v179, v180, v181, s[0:1]
	v_cmp_gt_f32_e64 s[0:1], s3, v176
	v_mul_f32_e32 v180, 0x37800000, v179
	v_cndmask_b32_e32 v179, v179, v180, vcc
	v_cndmask_b32_e64 v176, v176, v177, s[0:1]
	v_sqrt_f32_e32 v177, v176
	v_cmp_class_f32_e32 vcc, v178, v216
	s_nop 1
	v_cndmask_b32_e32 v178, v179, v178, vcc
	v_add_u32_e32 v179, -1, v177
	v_fma_f32 v180, -v179, v177, v176
	v_cmp_ge_f32_e32 vcc, 0, v180
	v_add_u32_e32 v180, 1, v177
	s_nop 0
	v_cndmask_b32_e32 v179, v177, v179, vcc
	v_fma_f32 v177, -v180, v177, v176
	v_cmp_lt_f32_e32 vcc, 0, v177
	s_nop 1
	v_cndmask_b32_e32 v177, v179, v180, vcc
	v_cmp_gt_f32_e32 vcc, s3, v156
	v_mul_f32_e32 v179, 0x37800000, v177
	v_cndmask_b32_e64 v177, v177, v179, s[0:1]
	v_cndmask_b32_e32 v156, v156, v157, vcc
	v_sqrt_f32_e32 v157, v156
	v_cmp_class_f32_e64 s[0:1], v176, v216
	s_nop 1
	v_cndmask_b32_e64 v176, v177, v176, s[0:1]
	v_add_u32_e32 v177, -1, v157
	v_fma_f32 v179, -v177, v157, v156
	v_cmp_ge_f32_e64 s[0:1], 0, v179
	v_add_u32_e32 v179, 1, v157
	s_nop 0
	v_cndmask_b32_e64 v177, v157, v177, s[0:1]
	v_fma_f32 v157, -v179, v157, v156
	v_cmp_lt_f32_e64 s[0:1], 0, v157
	s_nop 1
	v_cndmask_b32_e64 v157, v177, v179, s[0:1]
	v_div_scale_f32 v179, s[0:1], v178, v178, 1.0
	v_rcp_f32_e32 v180, v179
	v_mul_f32_e32 v177, 0x37800000, v157
	v_cndmask_b32_e32 v157, v157, v177, vcc
	v_cmp_class_f32_e32 vcc, v156, v216
	s_nop 1
	v_cndmask_b32_e32 v156, v157, v156, vcc
	v_fma_f32 v157, -v179, v180, 1.0
	v_fmac_f32_e32 v180, v157, v180
	v_div_scale_f32 v157, vcc, 1.0, v178, 1.0
	v_mul_f32_e32 v177, v157, v180
	v_fma_f32 v181, -v179, v177, v157
	v_fmac_f32_e32 v177, v181, v180
	v_fma_f32 v157, -v179, v177, v157
	v_div_scale_f32 v179, s[0:1], v176, v176, 1.0
	v_rcp_f32_e32 v181, v179
	v_div_fmas_f32 v157, v157, v180, v177
	v_div_fixup_f32 v157, v157, v178, 1.0
	v_fma_f32 v177, -v179, v181, 1.0
	v_fmac_f32_e32 v181, v177, v181
	v_div_scale_f32 v177, vcc, 1.0, v176, 1.0
	v_mul_f32_e32 v178, v177, v181
	v_fma_f32 v180, -v179, v178, v177
	v_fmac_f32_e32 v178, v180, v181
	v_fma_f32 v177, -v179, v178, v177
	v_div_scale_f32 v179, s[0:1], v156, v156, 1.0
	v_rcp_f32_e32 v180, v179
	v_div_fmas_f32 v177, v177, v181, v178
	v_div_fixup_f32 v176, v177, v176, 1.0
	s_movk_i32 s1, 0x7fff
	v_fma_f32 v177, -v179, v180, 1.0
	v_fmac_f32_e32 v180, v177, v180
	v_div_scale_f32 v177, vcc, 1.0, v156, 1.0
	v_mul_f32_e32 v178, v177, v180
	v_fma_f32 v181, -v179, v178, v177
	v_fmac_f32_e32 v178, v181, v180
	v_fma_f32 v177, -v179, v178, v177
	v_div_fmas_f32 v177, v177, v180, v178
	v_div_fixup_f32 v156, v177, v156, 1.0
	v_cndmask_b32_e64 v156, v176, v156, s[40:41]
	v_pk_mul_f32 v[102:103], v[156:157], v[102:103] op_sel_hi:[0,1]
	v_pk_mul_f32 v[104:105], v[156:157], v[104:105] op_sel_hi:[0,1]
	v_pk_mul_f32 v[138:139], v[156:157], v[138:139] op_sel_hi:[0,1]
	v_pk_mul_f32 v[102:103], v[102:103], v[150:151]
	v_pk_mul_f32 v[136:137], v[156:157], v[136:137] op_sel_hi:[0,1]
	v_pk_mul_f32 v[104:105], v[104:105], v[148:149]
	v_pk_mul_f32 v[138:139], v[138:139], v[154:155]
	v_pk_mul_f32 v[136:137], v[136:137], v[152:153]
	v_bfe_u32 v148, v105, 16, 1
	v_bfe_u32 v149, v104, 16, 1
	v_bfe_u32 v150, v103, 16, 1
	v_bfe_u32 v151, v102, 16, 1
	v_cndmask_b32_e64 v176, v157, v176, s[34:35]
	v_add3_u32 v102, v102, v151, s1
	v_add3_u32 v103, v103, v150, s1
	v_add3_u32 v104, v104, v149, s1
	v_add3_u32 v105, v105, v148, s1
	v_bfe_u32 v148, v138, 16, 1
	v_bfe_u32 v149, v139, 16, 1
	v_bfe_u32 v150, v136, 16, 1
	v_bfe_u32 v151, v137, 16, 1
	v_add3_u32 v137, v137, v151, s1
	v_add3_u32 v136, v136, v150, s1
	v_add3_u32 v139, v139, v149, s1
	v_add3_u32 v138, v138, v148, s1
	v_pk_mul_f32 v[128:129], v[128:129], v[176:177] op_sel_hi:[1,0]
	v_pk_mul_f32 v[130:131], v[130:131], v[176:177] op_sel_hi:[1,0]
	v_lshrrev_b32_e32 v138, 16, v138
	v_lshrrev_b32_e32 v139, 16, v139
	v_lshrrev_b32_e32 v136, 16, v136
	v_lshrrev_b32_e32 v137, 16, v137
	s_mov_b32 s0, 0xffff0000
	v_pk_mul_f32 v[134:135], v[134:135], v[176:177] op_sel_hi:[1,0]
	v_pk_mul_f32 v[128:129], v[128:129], v[146:147]
	v_pk_mul_f32 v[132:133], v[132:133], v[176:177] op_sel_hi:[1,0]
	v_pk_mul_f32 v[130:131], v[130:131], v[142:143]
	v_and_or_b32 v105, v105, s0, v137
	v_and_or_b32 v104, v104, s0, v136
	v_and_or_b32 v103, v103, s0, v139
	v_and_or_b32 v102, v102, s0, v138
	v_pk_mul_f32 v[134:135], v[134:135], v[140:141]
	v_pk_mul_f32 v[132:133], v[132:133], v[144:145]
	v_bfe_u32 v136, v131, 16, 1
	v_bfe_u32 v137, v130, 16, 1
	v_bfe_u32 v138, v129, 16, 1
	v_bfe_u32 v139, v128, 16, 1
	v_add3_u32 v128, v128, v139, s1
	v_add3_u32 v129, v129, v138, s1
	v_add3_u32 v130, v130, v137, s1
	v_add3_u32 v131, v131, v136, s1
	v_bfe_u32 v136, v134, 16, 1
	v_bfe_u32 v137, v135, 16, 1
	v_bfe_u32 v138, v132, 16, 1
	v_bfe_u32 v139, v133, 16, 1
	v_add3_u32 v133, v133, v139, s1
	v_add3_u32 v132, v132, v138, s1
	v_add3_u32 v135, v135, v137, s1
	v_add3_u32 v134, v134, v136, s1
	v_lshrrev_b32_e32 v134, 16, v134
	v_lshrrev_b32_e32 v135, 16, v135
	v_lshrrev_b32_e32 v132, 16, v132
	v_lshrrev_b32_e32 v133, 16, v133
	v_and_or_b32 v131, v131, s0, v133
	v_and_or_b32 v130, v130, s0, v132
	v_and_or_b32 v129, v129, s0, v135
	v_and_or_b32 v128, v128, s0, v134
	s_add_u32 s0, s24, s10
	s_addc_u32 s1, s25, s11
	global_store_dwordx4 v0, v[102:105], s[0:1]
	global_store_dwordx4 v0, v[128:131], s[0:1] offset:1024
	s_waitcnt vmcnt(34)
	s_and_saveexec_b64 s[0:1], s[38:39]
	s_xor_b64 s[0:1], exec, s[0:1]
	s_cbranch_execz .LBB0_205
; __device__ __forceinline__ void unpack8(const v4u w, float* f) { f[0] = bflo(w.x); f[1] = bfhi(w.x); f[2] = bflo(w.y); f[3] = bfhi(w.y); f[4] = bflo(w.z); f[5] = bfhi(w.z); f[6] = bflo(w.w); f[7] = bfhi(w.w); }
; __device__ __forceinline__ void norm_compute(const NormRow& R, int lane, v4u& ya, v4u& yc) {
;     ...
;     else { float f0[8], f1[8], f2[8]; unpack8(R.d0, f0); unpack8(R.d1, f1); unpack8(R.d2, f2);
;         const float inv = 1.0f / (R.l0 + R.l1 + R.l2);
; #pragma unroll
;         for (int e = 0; e < 8; ++e) fc[e] = (f0[e] + f1[e] + f2[e]) * inv; }
	v_add_f32_e32 v103, v171, v170
	v_add_f32_e32 v128, v172, v103
	v_div_scale_f32 v129, s[10:11], v128, v128, 1.0
	v_rcp_f32_e32 v130, v129
	v_lshlrev_b32_e32 v134, 16, v66
	v_and_b32_e32 v135, 0xffff0000, v66
	v_lshlrev_b32_e32 v138, 16, v68
	v_fma_f32 v131, -v129, v130, 1.0
	v_fmac_f32_e32 v130, v131, v130
	v_div_scale_f32 v131, vcc, 1.0, v128, 1.0
	v_mul_f32_e32 v132, v131, v130
	v_fma_f32 v133, -v129, v132, v131
	v_fmac_f32_e32 v132, v133, v130
	v_fma_f32 v129, -v129, v132, v131
	v_div_fmas_f32 v129, v129, v130, v132
	v_div_fixup_f32 v130, v129, v128, 1.0
	v_lshlrev_b32_e32 v128, 16, v58
	v_and_b32_e32 v129, 0xffff0000, v58
	v_lshlrev_b32_e32 v132, 16, v62
	v_and_b32_e32 v133, 0xffff0000, v62
	v_pk_add_f32 v[128:129], v[132:133], v[128:129]
	v_lshlrev_b32_e32 v132, 16, v63
	v_pk_add_f32 v[128:129], v[128:129], v[134:135]
	v_and_b32_e32 v133, 0xffff0000, v63
	v_pk_mul_f32 v[136:137], v[130:131], v[128:129] op_sel_hi:[0,1]
	v_lshlrev_b32_e32 v128, 16, v59
	v_and_b32_e32 v129, 0xffff0000, v59
	v_lshlrev_b32_e32 v134, 16, v67
	v_and_b32_e32 v135, 0xffff0000, v67
	v_pk_add_f32 v[128:129], v[132:133], v[128:129]
	v_lshlrev_b32_e32 v132, 16, v60
	v_pk_add_f32 v[128:129], v[128:129], v[134:135]
	v_and_b32_e32 v133, 0xffff0000, v60
	v_lshlrev_b32_e32 v134, 16, v64
	v_and_b32_e32 v135, 0xffff0000, v64
	v_and_b32_e32 v139, 0xffff0000, v68
	v_pk_add_f32 v[132:133], v[134:135], v[132:133]
	v_lshlrev_b32_e32 v102, 16, v61
	v_lshlrev_b32_e32 v104, 16, v65
	v_and_b32_e32 v103, 0xffff0000, v61
	v_and_b32_e32 v105, 0xffff0000, v65
	v_pk_add_f32 v[132:133], v[132:133], v[138:139]
	v_pk_add_f32 v[102:103], v[104:105], v[102:103]
	v_pk_mul_f32 v[134:135], v[130:131], v[132:133] op_sel_hi:[0,1]
	v_lshlrev_b32_e32 v132, 16, v69
	v_and_b32_e32 v133, 0xffff0000, v69
	v_pk_add_f32 v[102:103], v[102:103], v[132:133]
	v_pk_mul_f32 v[128:129], v[130:131], v[128:129] op_sel_hi:[0,1]
	v_pk_mul_f32 v[130:131], v[130:131], v[102:103] op_sel_hi:[0,1]
	v_mov_b32_e32 v133, v130
	v_mov_b32_e32 v130, v135
	v_mov_b32_e32 v132, v134
	v_mov_b32_e32 v135, v128
	v_mov_b32_e32 v128, v137
	v_mov_b32_e32 v134, v136
; #define GAS __attribute__((address_space(1)))
; __device__ __forceinline__ void unpack8(const v4u w, float* f) { f[0] = bflo(w.x); f[1] = bfhi(w.x); f[2] = bflo(w.y); f[3] = bfhi(w.y); f[4] = bflo(w.z); f[5] = bfhi(w.z); f[6] = bflo(w.w); f[7] = bfhi(w.w); }
; __device__ __forceinline__ void norm_load(NormRow& R, int m, int lane, const bf16* O, const bf16* GF, const bf16* OD, const float* LD) {
;     R.oa = __builtin_nontemporal_load((const GAS v4u*)(O + (size_t)m * DM + 8 * lane));
;     if (lane < 16) { R.oc = __builtin_nontemporal_load((const GAS v4u*)(O + (size_t)m * DM + 512 + 8 * lane)); R.gc = __builtin_nontemporal_load((const GAS v4u*)(GF + (size_t)m * 384 + 256 + 8 * lane)); }
;     else { const int dc = 8 * lane - 128, hd = dc >> 6;
;         R.d0 = __builtin_nontemporal_load((const GAS v4u*)(OD + (size_t)m * 384 + dc)); R.d1 = __builtin_nontemporal_load((const GAS v4u*)(OD + OD_BRANCH + (size_t)m * 384 + dc)); R.d2 = __builtin_nontemporal_load((const GAS v4u*)(OD + 2 * OD_BRANCH + (size_t)m * 384 + dc));
;         R.l0 = LD[(size_t)m * 8 + hd]; R.l1 = LD[LD_BRANCH + (size_t)m * 8 + hd]; R.l2 = LD[2 * LD_BRANCH + (size_t)m * 8 + hd]; }
;     if (lane >= 32) R.ga = __builtin_nontemporal_load((const GAS v4u*)(GF + (size_t)m * 384 + 8 * lane - 256));
; __device__ __forceinline__ void norm_compute(const NormRow& R, int lane, v4u& ya, v4u& yc) {
;     ...
;     if (lane < 16) unpack8(R.oc, fc);
;     else { float f0[8], f1[8], f2[8]; unpack8(R.d0, f0); unpack8(R.d1, f1); unpack8(R.d2, f2);
;         const float inv = 1.0f / (R.l0 + R.l1 + R.l2);
; #pragma unroll
;         for (int e = 0; e < 8; ++e) fc[e] = (f0[e] + f1[e] + f2[e]) * inv; }
;     float sa = 0.f, sc = 0.f;
; #pragma unroll
;     for (int e = 0; e < 8; ++e) { sa += fa[e] * fa[e]; sc += fc[e] * fc[e]; }
;     const float s_moba = wave_sum(lane < 32 ? sa : 0.f), s_fox = wave_sum((lane >= 32 ? sa : 0.f) + (lane < 16 ? sc : 0.f)), s_dil = wave_sum(lane >= 16 ? sc : 0.f);
;     const float r_moba = 1.0f / sqrtf(s_moba * (1.0f / 256.0f) + EPS), r_fox = 1.0f / sqrtf(s_fox * (1.0f / 384.0f) + EPS), r_dil = 1.0f / sqrtf(s_dil * (1.0f / 384.0f) + EPS);
;     float ga[8], gc[8];
; #pragma unroll
;     for (int e = 0; e < 8; ++e) { ga[e] = 1.f; gc[e] = 1.f; }
;     if (lane >= 32) unpack8(R.ga, ga);
;     if (lane < 16) unpack8(R.gc, gc);
.LBB0_205:
	s_andn2_saveexec_b64 s[0:1], s[0:1]
	v_lshlrev_b32_e32 v134, 16, v70
	v_and_b32_e32 v128, 0xffff0000, v70
	v_lshlrev_b32_e32 v135, 16, v71
	v_and_b32_e32 v129, 0xffff0000, v71
	v_lshlrev_b32_e32 v132, 16, v72
	v_and_b32_e32 v130, 0xffff0000, v72
	v_lshlrev_b32_e32 v133, 16, v73
	v_and_b32_e32 v131, 0xffff0000, v73
	s_or_b64 exec, exec, s[0:1]
	v_lshlrev_b32_e32 v139, 16, v107
	v_lshlrev_b32_e32 v138, 16, v106
	v_and_b32_e32 v107, 0xffff0000, v107
	v_and_b32_e32 v106, 0xffff0000, v106
	v_pk_mul_f32 v[102:103], v[138:139], v[138:139]
	v_pk_mul_f32 v[104:105], v[106:107], v[106:107]
	v_mul_f32_e32 v144, v128, v128
	v_fmac_f32_e32 v144, v134, v134
	v_add_f32_e32 v102, v102, v104
	v_lshlrev_b32_e32 v137, 16, v109
	v_lshlrev_b32_e32 v136, 16, v108
	v_fmac_f32_e32 v144, v135, v135
	v_add_f32_e32 v102, v103, v102
	v_and_b32_e32 v109, 0xffff0000, v109
	v_and_b32_e32 v108, 0xffff0000, v108
	v_fmac_f32_e32 v144, v129, v129
	v_pk_mul_f32 v[140:141], v[136:137], v[136:137]
	v_add_f32_e32 v102, v105, v102
	v_fmac_f32_e32 v144, v132, v132
	v_pk_mul_f32 v[142:143], v[108:109], v[108:109]
	v_add_f32_e32 v102, v140, v102
	v_fmac_f32_e32 v144, v130, v130
	v_add_f32_e32 v102, v142, v102
	v_fmac_f32_e32 v144, v133, v133
	v_add_f32_e32 v102, v141, v102
	v_add_f32_e32 v102, v143, v102
	v_fmac_f32_e32 v144, v131, v131
	v_cndmask_b32_e64 v103, 0, v102, s[40:41]
	v_cndmask_b32_e64 v102, 0, v102, s[36:37]
	v_cndmask_b32_e64 v105, 0, v144, s[34:35]
	v_add_f32_e32 v102, v102, v105
	v_cndmask_b32_e64 v140, 0, v144, s[42:43]
	v_mov_b32_e32 v154, 1.0
	v_mov_b32_e32 v150, 1.0
	s_nop 1
	v_add_f32_dpp v103, v103, v103 quad_perm:[1,0,3,2] row_mask:0xf bank_mask:0xf
	s_nop 1
	v_add_f32_dpp v102, v102, v102 quad_perm:[1,0,3,2] row_mask:0xf bank_mask:0xf
	s_nop 1
	v_add_f32_dpp v140, v140, v140 quad_perm:[1,0,3,2] row_mask:0xf bank_mask:0xf
	v_mov_b32_e32 v155, 1.0
	v_mov_b32_e32 v151, 1.0
	s_nop 1
	v_add_f32_dpp v103, v103, v103 quad_perm:[2,3,0,1] row_mask:0xf bank_mask:0xf
	s_nop 1
	v_add_f32_dpp v102, v102, v102 quad_perm:[2,3,0,1] row_mask:0xf bank_mask:0xf
	s_nop 1
	v_add_f32_dpp v140, v140, v140 quad_perm:[2,3,0,1] row_mask:0xf bank_mask:0xf
	v_mov_b32_e32 v152, 1.0
	v_mov_b32_e32 v148, 1.0
	s_nop 1
	v_add_f32_dpp v103, v103, v103 row_half_mirror row_mask:0xf bank_mask:0xf
	s_nop 1
	v_add_f32_dpp v102, v102, v102 row_half_mirror row_mask:0xf bank_mask:0xf
	s_nop 1
	v_add_f32_dpp v140, v140, v140 row_half_mirror row_mask:0xf bank_mask:0xf
	v_mov_b32_e32 v153, 1.0
	v_mov_b32_e32 v149, 1.0
	s_nop 1
	v_add_f32_dpp v103, v103, v103 row_mirror row_mask:0xf bank_mask:0xf
	s_nop 1
	v_add_f32_dpp v102, v102, v102 row_mirror row_mask:0xf bank_mask:0xf
	s_nop 1
	v_add_f32_dpp v140, v140, v140 row_mirror row_mask:0xf bank_mask:0xf
	v_mov_b32_e32 v104, v103
	s_nop 1
	v_permlane16_swap_b32_e32 v103, v104
	v_add_f32_e32 v156, v103, v104
	v_mov_b32_e32 v105, v102
	s_nop 1
	v_permlane16_swap_b32_e32 v102, v105
	v_add_f32_e32 v176, v102, v105
	v_mov_b32_e32 v141, v140
	s_nop 1
	v_permlane16_swap_b32_e32 v140, v141
	v_add_f32_e32 v178, v140, v141
	v_mov_b32_e32 v140, 1.0
	s_and_saveexec_b64 s[0:1], s[36:37]
	v_lshlrev_b32_e32 v154, 16, v54
	v_and_b32_e32 v150, 0xffff0000, v54
	v_lshlrev_b32_e32 v155, 16, v55
	v_and_b32_e32 v151, 0xffff0000, v55
	v_lshlrev_b32_e32 v152, 16, v56
	v_and_b32_e32 v148, 0xffff0000, v56
	v_lshlrev_b32_e32 v153, 16, v57
	v_and_b32_e32 v149, 0xffff0000, v57
	s_or_b64 exec, exec, s[0:1]
	v_mov_b32_e32 v146, 1.0
	v_mov_b32_e32 v141, 1.0
	v_mov_b32_e32 v147, 1.0
	v_mov_b32_e32 v144, 1.0
	v_mov_b32_e32 v142, 1.0
	v_mov_b32_e32 v145, 1.0
	v_mov_b32_e32 v143, 1.0
	s_and_saveexec_b64 s[0:1], s[34:35]
	v_lshlrev_b32_e32 v140, 16, v50
	v_and_b32_e32 v146, 0xffff0000, v50
	v_lshlrev_b32_e32 v141, 16, v51
	v_and_b32_e32 v147, 0xffff0000, v51
	v_lshlrev_b32_e32 v144, 16, v52
	v_and_b32_e32 v142, 0xffff0000, v52
	v_lshlrev_b32_e32 v145, 16, v53
	v_and_b32_e32 v143, 0xffff0000, v53
	s_or_b64 exec, exec, s[0:1]
	s_or_b32 s0, s8, 13
	s_ashr_i32 s1, s0, 31
	s_lshl_b64 s[10:11], s[0:1], 11
	s_add_u32 s20, s29, s10
	s_addc_u32 s21, s30, s11
	global_load_dwordx4 v[102:105], v0, s[20:21] nt
	s_and_saveexec_b64 s[22:23], s[38:39]
	s_xor_b64 s[22:23], exec, s[22:23]
	s_cbranch_execz .LBB0_777
	v_mad_i64_i32 v[58:59], s[44:45], s0, v252, v[124:125]
	v_mad_i64_i32 v[62:63], s[44:45], s0, v252, v[122:123]
	v_mad_i64_i32 v[66:67], s[44:45], s0, v252, v[120:121]
	s_lshl_b64 s[44:45], s[0:1], 5
	s_add_u32 s44, s26, s44
	s_addc_u32 s45, s27, s45
	v_lshl_add_u64 v[180:181], v[118:119], 2, s[44:45]
	v_add_co_u32_e32 v182, vcc, 0x100000, v180
	global_load_dword v170, v[180:181], off
	s_nop 0
	v_addc_co_u32_e32 v183, vcc, 0, v181, vcc
	global_load_dword v171, v[182:183], off
	v_add_co_u32_e32 v180, vcc, 0x200000, v180
	global_load_dwordx4 v[58:61], v[58:59], off nt
	s_nop 0
	v_addc_co_u32_e32 v181, vcc, 0, v181, vcc
	global_load_dwordx4 v[62:65], v[62:63], off nt
	s_nop 0
	global_load_dwordx4 v[66:69], v[66:67], off nt
	s_nop 0
	global_load_dword v172, v[180:181], off
	s_andn2_saveexec_b64 s[22:23], s[22:23]
	s_cbranch_execnz .LBB0_778

; __device__ __forceinline__ unsigned pk2(float lo, float hi) { return f2bf(lo) | (f2bf(hi) << 16); }
; __device__ __forceinline__ void unpack8(const v4u w, float* f) { f[0] = bflo(w.x); f[1] = bfhi(w.x); f[2] = bflo(w.y); f[3] = bfhi(w.y); f[4] = bflo(w.z); f[5] = bfhi(w.z); f[6] = bflo(w.w); f[7] = bfhi(w.w); }
; __device__ __forceinline__ void norm_compute(const NormRow& R, int lane, v4u& ya, v4u& yc) {
;     ...
;     const float s_moba = wave_sum(lane < 32 ? sa : 0.f), s_fox = wave_sum((lane >= 32 ? sa : 0.f) + (lane < 16 ? sc : 0.f)), s_dil = wave_sum(lane >= 16 ? sc : 0.f);
;     const float r_moba = 1.0f / sqrtf(s_moba * (1.0f / 256.0f) + EPS), r_fox = 1.0f / sqrtf(s_fox * (1.0f / 384.0f) + EPS), r_dil = 1.0f / sqrtf(s_dil * (1.0f / 384.0f) + EPS);
;     float ga[8], gc[8];
; #pragma unroll
;     for (int e = 0; e < 8; ++e) { ga[e] = 1.f; gc[e] = 1.f; }
;     if (lane >= 32) unpack8(R.ga, ga);
;     if (lane < 16) unpack8(R.gc, gc);
;     const float ra = lane < 32 ? r_moba : r_fox, rc = lane < 16 ? r_fox : r_dil;
;     ya.x = pk2(fa[0] * ra * ga[0], fa[1] * ra * ga[1]); ya.y = pk2(fa[2] * ra * ga[2], fa[3] * ra * ga[3]); ya.z = pk2(fa[4] * ra * ga[4], fa[5] * ra * ga[5]); ya.w = pk2(fa[6] * ra * ga[6], fa[7] * ra * ga[7]);
;     yc.x = pk2(fc[0] * rc * gc[0], fc[1] * rc * gc[1]); yc.y = pk2(fc[2] * rc * gc[2], fc[3] * rc * gc[3]); yc.z = pk2(fc[4] * rc * gc[4], fc[5] * rc * gc[5]); yc.w = pk2(fc[6] * rc * gc[6], fc[7] * rc * gc[7]);
; }
.LBB0_215:
	s_or_b64 exec, exec, s[20:21]
	v_mov_b32_e32 v179, v178
	s_nop 1
	v_permlane32_swap_b32_e32 v178, v179
	v_add_f32_e32 v178, v178, v179
	v_fmamk_f32 v178, v178, 0x3b2aaaab, v215
	v_mul_f32_e32 v179, 0x4f800000, v178
	v_cmp_gt_f32_e32 vcc, s3, v178
	v_mov_b32_e32 v177, v176
	s_nop 1
	v_permlane32_swap_b32_e32 v176, v177
	v_add_f32_e32 v176, v176, v177
	v_fmamk_f32 v176, v176, 0x3b2aaaab, v215
	v_cndmask_b32_e32 v178, v178, v179, vcc
	v_sqrt_f32_e32 v179, v178
	v_mul_f32_e32 v177, 0x4f800000, v176
	v_mov_b32_e32 v157, v156
	s_nop 1
	v_permlane32_swap_b32_e32 v156, v157
	v_add_f32_e32 v156, v156, v157
	v_fmamk_f32 v156, v156, 0x3b800000, v215
	v_add_u32_e32 v180, -1, v179
	v_fma_f32 v182, -v180, v179, v178
	v_add_u32_e32 v181, 1, v179
	v_cmp_ge_f32_e64 s[0:1], 0, v182
	v_mul_f32_e32 v157, 0x4f800000, v156
	s_nop 0
	v_cndmask_b32_e64 v180, v179, v180, s[0:1]
	v_fma_f32 v179, -v181, v179, v178
	v_cmp_lt_f32_e64 s[0:1], 0, v179
	s_nop 1
	v_cndmask_b32_e64 v179, v180, v181, s[0:1]
	v_cmp_gt_f32_e64 s[0:1], s3, v176
	v_mul_f32_e32 v180, 0x37800000, v179
	v_cndmask_b32_e32 v179, v179, v180, vcc
	v_cndmask_b32_e64 v176, v176, v177, s[0:1]
	v_sqrt_f32_e32 v177, v176
	v_cmp_class_f32_e32 vcc, v178, v216
	s_nop 1
	v_cndmask_b32_e32 v178, v179, v178, vcc
	v_add_u32_e32 v179, -1, v177
	v_fma_f32 v180, -v179, v177, v176
	v_cmp_ge_f32_e32 vcc, 0, v180
	v_add_u32_e32 v180, 1, v177
	s_nop 0
	v_cndmask_b32_e32 v179, v177, v179, vcc
	v_fma_f32 v177, -v180, v177, v176
	v_cmp_lt_f32_e32 vcc, 0, v177
	s_nop 1
	v_cndmask_b32_e32 v177, v179, v180, vcc
	v_cmp_gt_f32_e32 vcc, s3, v156
	v_mul_f32_e32 v179, 0x37800000, v177
	v_cndmask_b32_e64 v177, v177, v179, s[0:1]
	v_cndmask_b32_e32 v156, v156, v157, vcc
	v_sqrt_f32_e32 v157, v156
	v_cmp_class_f32_e64 s[0:1], v176, v216
	s_nop 1
	v_cndmask_b32_e64 v176, v177, v176, s[0:1]
	v_add_u32_e32 v177, -1, v157
	v_fma_f32 v179, -v177, v157, v156
	v_cmp_ge_f32_e64 s[0:1], 0, v179
	v_add_u32_e32 v179, 1, v157
	s_nop 0
	v_cndmask_b32_e64 v177, v157, v177, s[0:1]
	v_fma_f32 v157, -v179, v157, v156
	v_cmp_lt_f32_e64 s[0:1], 0, v157
	s_nop 1
	v_cndmask_b32_e64 v157, v177, v179, s[0:1]
	v_div_scale_f32 v179, s[0:1], v178, v178, 1.0
	v_rcp_f32_e32 v180, v179
	v_mul_f32_e32 v177, 0x37800000, v157
	v_cndmask_b32_e32 v157, v157, v177, vcc
	v_cmp_class_f32_e32 vcc, v156, v216
	s_nop 1
	v_cndmask_b32_e32 v156, v157, v156, vcc
	v_fma_f32 v157, -v179, v180, 1.0
	v_fmac_f32_e32 v180, v157, v180
	v_div_scale_f32 v157, vcc, 1.0, v178, 1.0
	v_mul_f32_e32 v177, v157, v180
	v_fma_f32 v181, -v179, v177, v157
	v_fmac_f32_e32 v177, v181, v180
	v_fma_f32 v157, -v179, v177, v157
	v_div_scale_f32 v179, s[0:1], v176, v176, 1.0
	v_rcp_f32_e32 v181, v179
	v_div_fmas_f32 v157, v157, v180, v177
	v_div_fixup_f32 v157, v157, v178, 1.0
	v_fma_f32 v177, -v179, v181, 1.0
	v_fmac_f32_e32 v181, v177, v181
	v_div_scale_f32 v177, vcc, 1.0, v176, 1.0
	v_mul_f32_e32 v178, v177, v181
	v_fma_f32 v180, -v179, v178, v177
	v_fmac_f32_e32 v178, v180, v181
	v_fma_f32 v177, -v179, v178, v177
	v_div_scale_f32 v179, s[0:1], v156, v156, 1.0
	v_rcp_f32_e32 v180, v179
	v_div_fmas_f32 v177, v177, v181, v178
	v_div_fixup_f32 v176, v177, v176, 1.0
	s_movk_i32 s1, 0x7fff
	v_fma_f32 v177, -v179, v180, 1.0
	v_fmac_f32_e32 v180, v177, v180
	v_div_scale_f32 v177, vcc, 1.0, v156, 1.0
	v_mul_f32_e32 v178, v177, v180
	v_fma_f32 v181, -v179, v178, v177
	v_fmac_f32_e32 v178, v181, v180
	v_fma_f32 v177, -v179, v178, v177
	v_div_fmas_f32 v177, v177, v180, v178
	v_div_fixup_f32 v156, v177, v156, 1.0
	v_cndmask_b32_e64 v156, v176, v156, s[40:41]
	v_pk_mul_f32 v[106:107], v[156:157], v[106:107] op_sel_hi:[0,1]
	v_pk_mul_f32 v[108:109], v[156:157], v[108:109] op_sel_hi:[0,1]
	v_pk_mul_f32 v[138:139], v[156:157], v[138:139] op_sel_hi:[0,1]
	v_pk_mul_f32 v[106:107], v[106:107], v[150:151]
	v_pk_mul_f32 v[136:137], v[156:157], v[136:137] op_sel_hi:[0,1]
	v_pk_mul_f32 v[108:109], v[108:109], v[148:149]
	v_pk_mul_f32 v[138:139], v[138:139], v[154:155]
	v_pk_mul_f32 v[136:137], v[136:137], v[152:153]
	v_bfe_u32 v148, v109, 16, 1
	v_bfe_u32 v149, v108, 16, 1
	v_bfe_u32 v150, v107, 16, 1
	v_bfe_u32 v151, v106, 16, 1
	v_cndmask_b32_e64 v176, v157, v176, s[34:35]
	v_add3_u32 v106, v106, v151, s1
	v_add3_u32 v107, v107, v150, s1
	v_add3_u32 v108, v108, v149, s1
	v_add3_u32 v109, v109, v148, s1
	v_bfe_u32 v148, v138, 16, 1
	v_bfe_u32 v149, v139, 16, 1
	v_bfe_u32 v150, v136, 16, 1
	v_bfe_u32 v151, v137, 16, 1
	v_add3_u32 v137, v137, v151, s1
	v_add3_u32 v136, v136, v150, s1
	v_add3_u32 v139, v139, v149, s1
	v_add3_u32 v138, v138, v148, s1
	v_pk_mul_f32 v[128:129], v[128:129], v[176:177] op_sel_hi:[1,0]
	v_pk_mul_f32 v[130:131], v[130:131], v[176:177] op_sel_hi:[1,0]
	v_lshrrev_b32_e32 v138, 16, v138
	v_lshrrev_b32_e32 v139, 16, v139
	v_lshrrev_b32_e32 v136, 16, v136
	v_lshrrev_b32_e32 v137, 16, v137
	s_mov_b32 s0, 0xffff0000
	v_pk_mul_f32 v[134:135], v[134:135], v[176:177] op_sel_hi:[1,0]
	v_pk_mul_f32 v[128:129], v[128:129], v[146:147]
	v_pk_mul_f32 v[132:133], v[132:133], v[176:177] op_sel_hi:[1,0]
	v_pk_mul_f32 v[130:131], v[130:131], v[142:143]
	v_and_or_b32 v109, v109, s0, v137
	v_and_or_b32 v108, v108, s0, v136
	v_and_or_b32 v107, v107, s0, v139
	v_and_or_b32 v106, v106, s0, v138
	v_pk_mul_f32 v[134:135], v[134:135], v[140:141]
	v_pk_mul_f32 v[132:133], v[132:133], v[144:145]
	v_bfe_u32 v136, v131, 16, 1
	v_bfe_u32 v137, v130, 16, 1
	v_bfe_u32 v138, v129, 16, 1
	v_bfe_u32 v139, v128, 16, 1
	v_add3_u32 v128, v128, v139, s1
	v_add3_u32 v129, v129, v138, s1
	v_add3_u32 v130, v130, v137, s1
	v_add3_u32 v131, v131, v136, s1
	v_bfe_u32 v136, v134, 16, 1
	v_bfe_u32 v137, v135, 16, 1
	v_bfe_u32 v138, v132, 16, 1
	v_bfe_u32 v139, v133, 16, 1
	v_add3_u32 v133, v133, v139, s1
	v_add3_u32 v132, v132, v138, s1
	v_add3_u32 v135, v135, v137, s1
	v_add3_u32 v134, v134, v136, s1
	v_lshrrev_b32_e32 v134, 16, v134
	v_lshrrev_b32_e32 v135, 16, v135
	v_lshrrev_b32_e32 v132, 16, v132
	v_lshrrev_b32_e32 v133, 16, v133
	v_and_or_b32 v131, v131, s0, v133
	v_and_or_b32 v130, v130, s0, v132
	v_and_or_b32 v129, v129, s0, v135
	v_and_or_b32 v128, v128, s0, v134
	s_add_u32 s0, s24, s12
	s_addc_u32 s1, s25, s13
	global_store_dwordx4 v0, v[106:109], s[0:1]
	global_store_dwordx4 v0, v[128:131], s[0:1] offset:1024
	s_waitcnt vmcnt(34)
	s_and_saveexec_b64 s[0:1], s[38:39]
	s_xor_b64 s[0:1], exec, s[0:1]
	s_cbranch_execz .LBB0_217
; __device__ __forceinline__ void unpack8(const v4u w, float* f) { f[0] = bflo(w.x); f[1] = bfhi(w.x); f[2] = bflo(w.y); f[3] = bfhi(w.y); f[4] = bflo(w.z); f[5] = bfhi(w.z); f[6] = bflo(w.w); f[7] = bfhi(w.w); }
; __device__ __forceinline__ void norm_compute(const NormRow& R, int lane, v4u& ya, v4u& yc) {
;     ...
;     else { float f0[8], f1[8], f2[8]; unpack8(R.d0, f0); unpack8(R.d1, f1); unpack8(R.d2, f2);
;         const float inv = 1.0f / (R.l0 + R.l1 + R.l2);
; #pragma unroll
;         for (int e = 0; e < 8; ++e) fc[e] = (f0[e] + f1[e] + f2[e]) * inv; }
	v_add_f32_e32 v107, v168, v167
	v_add_f32_e32 v128, v169, v107
	v_div_scale_f32 v129, s[12:13], v128, v128, 1.0
	v_rcp_f32_e32 v130, v129
	v_lshlrev_b32_e32 v134, 16, v42
	v_and_b32_e32 v135, 0xffff0000, v42
	v_lshlrev_b32_e32 v138, 16, v44
	v_fma_f32 v131, -v129, v130, 1.0
	v_fmac_f32_e32 v130, v131, v130
	v_div_scale_f32 v131, vcc, 1.0, v128, 1.0
	v_mul_f32_e32 v132, v131, v130
	v_fma_f32 v133, -v129, v132, v131
	v_fmac_f32_e32 v132, v133, v130
	v_fma_f32 v129, -v129, v132, v131
	v_div_fmas_f32 v129, v129, v130, v132
	v_div_fixup_f32 v130, v129, v128, 1.0
	v_lshlrev_b32_e32 v128, 16, v34
	v_and_b32_e32 v129, 0xffff0000, v34
	v_lshlrev_b32_e32 v132, 16, v38
	v_and_b32_e32 v133, 0xffff0000, v38
	v_pk_add_f32 v[128:129], v[132:133], v[128:129]
	v_lshlrev_b32_e32 v132, 16, v39
	v_pk_add_f32 v[128:129], v[128:129], v[134:135]
	v_and_b32_e32 v133, 0xffff0000, v39
	v_pk_mul_f32 v[136:137], v[130:131], v[128:129] op_sel_hi:[0,1]
	v_lshlrev_b32_e32 v128, 16, v35
	v_and_b32_e32 v129, 0xffff0000, v35
	v_lshlrev_b32_e32 v134, 16, v43
	v_and_b32_e32 v135, 0xffff0000, v43
	v_pk_add_f32 v[128:129], v[132:133], v[128:129]
	v_lshlrev_b32_e32 v132, 16, v36
	v_pk_add_f32 v[128:129], v[128:129], v[134:135]
	v_and_b32_e32 v133, 0xffff0000, v36
	v_lshlrev_b32_e32 v134, 16, v40
	v_and_b32_e32 v135, 0xffff0000, v40
	v_and_b32_e32 v139, 0xffff0000, v44
	v_pk_add_f32 v[132:133], v[134:135], v[132:133]
	v_lshlrev_b32_e32 v106, 16, v37
	v_lshlrev_b32_e32 v108, 16, v41
	v_and_b32_e32 v107, 0xffff0000, v37
	v_and_b32_e32 v109, 0xffff0000, v41
	v_pk_add_f32 v[132:133], v[132:133], v[138:139]
	v_pk_add_f32 v[106:107], v[108:109], v[106:107]
	v_pk_mul_f32 v[134:135], v[130:131], v[132:133] op_sel_hi:[0,1]
	v_lshlrev_b32_e32 v132, 16, v45
	v_and_b32_e32 v133, 0xffff0000, v45
	v_pk_add_f32 v[106:107], v[106:107], v[132:133]
	v_pk_mul_f32 v[128:129], v[130:131], v[128:129] op_sel_hi:[0,1]
	v_pk_mul_f32 v[130:131], v[130:131], v[106:107] op_sel_hi:[0,1]
	v_mov_b32_e32 v133, v130
	v_mov_b32_e32 v130, v135
	v_mov_b32_e32 v132, v134
	v_mov_b32_e32 v135, v128
	v_mov_b32_e32 v128, v137
	v_mov_b32_e32 v134, v136
; #define GAS __attribute__((address_space(1)))
; __device__ __forceinline__ void unpack8(const v4u w, float* f) { f[0] = bflo(w.x); f[1] = bfhi(w.x); f[2] = bflo(w.y); f[3] = bfhi(w.y); f[4] = bflo(w.z); f[5] = bfhi(w.z); f[6] = bflo(w.w); f[7] = bfhi(w.w); }
; __device__ __forceinline__ void norm_load(NormRow& R, int m, int lane, const bf16* O, const bf16* GF, const bf16* OD, const float* LD) {
;     R.oa = __builtin_nontemporal_load((const GAS v4u*)(O + (size_t)m * DM + 8 * lane));
;     if (lane < 16) { R.oc = __builtin_nontemporal_load((const GAS v4u*)(O + (size_t)m * DM + 512 + 8 * lane)); R.gc = __builtin_nontemporal_load((const GAS v4u*)(GF + (size_t)m * 384 + 256 + 8 * lane)); }
;     else { const int dc = 8 * lane - 128, hd = dc >> 6;
;         R.d0 = __builtin_nontemporal_load((const GAS v4u*)(OD + (size_t)m * 384 + dc)); R.d1 = __builtin_nontemporal_load((const GAS v4u*)(OD + OD_BRANCH + (size_t)m * 384 + dc)); R.d2 = __builtin_nontemporal_load((const GAS v4u*)(OD + 2 * OD_BRANCH + (size_t)m * 384 + dc));
;         R.l0 = LD[(size_t)m * 8 + hd]; R.l1 = LD[LD_BRANCH + (size_t)m * 8 + hd]; R.l2 = LD[2 * LD_BRANCH + (size_t)m * 8 + hd]; }
;     if (lane >= 32) R.ga = __builtin_nontemporal_load((const GAS v4u*)(GF + (size_t)m * 384 + 8 * lane - 256));
; __device__ __forceinline__ void norm_compute(const NormRow& R, int lane, v4u& ya, v4u& yc) {
;     ...
;     if (lane < 16) unpack8(R.oc, fc);
;     else { float f0[8], f1[8], f2[8]; unpack8(R.d0, f0); unpack8(R.d1, f1); unpack8(R.d2, f2);
;         const float inv = 1.0f / (R.l0 + R.l1 + R.l2);
; #pragma unroll
;         for (int e = 0; e < 8; ++e) fc[e] = (f0[e] + f1[e] + f2[e]) * inv; }
;     float sa = 0.f, sc = 0.f;
; #pragma unroll
;     for (int e = 0; e < 8; ++e) { sa += fa[e] * fa[e]; sc += fc[e] * fc[e]; }
;     const float s_moba = wave_sum(lane < 32 ? sa : 0.f), s_fox = wave_sum((lane >= 32 ? sa : 0.f) + (lane < 16 ? sc : 0.f)), s_dil = wave_sum(lane >= 16 ? sc : 0.f);
;     const float r_moba = 1.0f / sqrtf(s_moba * (1.0f / 256.0f) + EPS), r_fox = 1.0f / sqrtf(s_fox * (1.0f / 384.0f) + EPS), r_dil = 1.0f / sqrtf(s_dil * (1.0f / 384.0f) + EPS);
;     float ga[8], gc[8];
; #pragma unroll
;     for (int e = 0; e < 8; ++e) { ga[e] = 1.f; gc[e] = 1.f; }
;     if (lane >= 32) unpack8(R.ga, ga);
;     if (lane < 16) unpack8(R.gc, gc);
.LBB0_217:
	s_andn2_saveexec_b64 s[0:1], s[0:1]
	v_lshlrev_b32_e32 v134, 16, v46
	v_and_b32_e32 v128, 0xffff0000, v46
	v_lshlrev_b32_e32 v135, 16, v47
	v_and_b32_e32 v129, 0xffff0000, v47
	v_lshlrev_b32_e32 v132, 16, v48
	v_and_b32_e32 v130, 0xffff0000, v48
	v_lshlrev_b32_e32 v133, 16, v49
	v_and_b32_e32 v131, 0xffff0000, v49
	s_or_b64 exec, exec, s[0:1]
	v_lshlrev_b32_e32 v139, 16, v111
	v_lshlrev_b32_e32 v138, 16, v110
	v_and_b32_e32 v111, 0xffff0000, v111
	v_and_b32_e32 v110, 0xffff0000, v110
	v_pk_mul_f32 v[106:107], v[138:139], v[138:139]
	v_pk_mul_f32 v[108:109], v[110:111], v[110:111]
	v_mul_f32_e32 v144, v128, v128
	v_fmac_f32_e32 v144, v134, v134
	v_add_f32_e32 v106, v106, v108
	v_lshlrev_b32_e32 v137, 16, v113
	v_lshlrev_b32_e32 v136, 16, v112
	v_fmac_f32_e32 v144, v135, v135
	v_add_f32_e32 v106, v107, v106
	v_and_b32_e32 v113, 0xffff0000, v113
	v_and_b32_e32 v112, 0xffff0000, v112
	v_fmac_f32_e32 v144, v129, v129
	v_pk_mul_f32 v[140:141], v[136:137], v[136:137]
	v_add_f32_e32 v106, v109, v106
	v_fmac_f32_e32 v144, v132, v132
	v_pk_mul_f32 v[142:143], v[112:113], v[112:113]
	v_add_f32_e32 v106, v140, v106
	v_fmac_f32_e32 v144, v130, v130
	v_add_f32_e32 v106, v142, v106
	v_fmac_f32_e32 v144, v133, v133
	v_add_f32_e32 v106, v141, v106
	v_add_f32_e32 v106, v143, v106
	v_fmac_f32_e32 v144, v131, v131
	v_cndmask_b32_e64 v107, 0, v106, s[40:41]
	v_cndmask_b32_e64 v106, 0, v106, s[36:37]
	v_cndmask_b32_e64 v109, 0, v144, s[34:35]
	v_add_f32_e32 v106, v106, v109
	v_cndmask_b32_e64 v140, 0, v144, s[42:43]
	v_mov_b32_e32 v154, 1.0
	v_mov_b32_e32 v150, 1.0
	s_nop 1
	v_add_f32_dpp v107, v107, v107 quad_perm:[1,0,3,2] row_mask:0xf bank_mask:0xf
	s_nop 1
	v_add_f32_dpp v106, v106, v106 quad_perm:[1,0,3,2] row_mask:0xf bank_mask:0xf
	s_nop 1
	v_add_f32_dpp v140, v140, v140 quad_perm:[1,0,3,2] row_mask:0xf bank_mask:0xf
	v_mov_b32_e32 v155, 1.0
	v_mov_b32_e32 v151, 1.0
	s_nop 1
	v_add_f32_dpp v107, v107, v107 quad_perm:[2,3,0,1] row_mask:0xf bank_mask:0xf
	s_nop 1
	v_add_f32_dpp v106, v106, v106 quad_perm:[2,3,0,1] row_mask:0xf bank_mask:0xf
	s_nop 1
	v_add_f32_dpp v140, v140, v140 quad_perm:[2,3,0,1] row_mask:0xf bank_mask:0xf
	v_mov_b32_e32 v152, 1.0
	v_mov_b32_e32 v148, 1.0
	s_nop 1
	v_add_f32_dpp v107, v107, v107 row_half_mirror row_mask:0xf bank_mask:0xf
	s_nop 1
	v_add_f32_dpp v106, v106, v106 row_half_mirror row_mask:0xf bank_mask:0xf
	s_nop 1
	v_add_f32_dpp v140, v140, v140 row_half_mirror row_mask:0xf bank_mask:0xf
	v_mov_b32_e32 v153, 1.0
	v_mov_b32_e32 v149, 1.0
	s_nop 1
	v_add_f32_dpp v107, v107, v107 row_mirror row_mask:0xf bank_mask:0xf
	s_nop 1
	v_add_f32_dpp v106, v106, v106 row_mirror row_mask:0xf bank_mask:0xf
	s_nop 1
	v_add_f32_dpp v140, v140, v140 row_mirror row_mask:0xf bank_mask:0xf
	v_mov_b32_e32 v108, v107
	s_nop 1
	v_permlane16_swap_b32_e32 v107, v108
	v_add_f32_e32 v156, v107, v108
	v_mov_b32_e32 v109, v106
	s_nop 1
	v_permlane16_swap_b32_e32 v106, v109
	v_add_f32_e32 v176, v106, v109
	v_mov_b32_e32 v141, v140
	s_nop 1
	v_permlane16_swap_b32_e32 v140, v141
	v_add_f32_e32 v178, v140, v141
	v_mov_b32_e32 v140, 1.0
	s_and_saveexec_b64 s[0:1], s[36:37]
	v_lshlrev_b32_e32 v154, 16, v30
	v_and_b32_e32 v150, 0xffff0000, v30
	v_lshlrev_b32_e32 v155, 16, v31
	v_and_b32_e32 v151, 0xffff0000, v31
	v_lshlrev_b32_e32 v152, 16, v32
	v_and_b32_e32 v148, 0xffff0000, v32
	v_lshlrev_b32_e32 v153, 16, v33
	v_and_b32_e32 v149, 0xffff0000, v33
	s_or_b64 exec, exec, s[0:1]
	v_mov_b32_e32 v146, 1.0
	v_mov_b32_e32 v141, 1.0
	v_mov_b32_e32 v147, 1.0
	v_mov_b32_e32 v144, 1.0
	v_mov_b32_e32 v142, 1.0
	v_mov_b32_e32 v145, 1.0
	v_mov_b32_e32 v143, 1.0
	s_and_saveexec_b64 s[0:1], s[34:35]
	v_lshlrev_b32_e32 v140, 16, v26
	v_and_b32_e32 v146, 0xffff0000, v26
	v_lshlrev_b32_e32 v141, 16, v27
	v_and_b32_e32 v147, 0xffff0000, v27
	v_lshlrev_b32_e32 v144, 16, v28
	v_and_b32_e32 v142, 0xffff0000, v28
	v_lshlrev_b32_e32 v145, 16, v29
	v_and_b32_e32 v143, 0xffff0000, v29
	s_or_b64 exec, exec, s[0:1]
	s_or_b32 s0, s8, 14
	s_ashr_i32 s1, s0, 31
	s_lshl_b64 s[12:13], s[0:1], 11
	s_add_u32 s20, s29, s12
	s_addc_u32 s21, s30, s13
	global_load_dwordx4 v[106:109], v0, s[20:21] nt
	s_and_saveexec_b64 s[22:23], s[38:39]
	s_xor_b64 s[22:23], exec, s[22:23]
	s_cbranch_execz .LBB0_779
	v_mad_i64_i32 v[34:35], s[44:45], s0, v252, v[124:125]
	v_mad_i64_i32 v[38:39], s[44:45], s0, v252, v[122:123]
	v_mad_i64_i32 v[42:43], s[44:45], s0, v252, v[120:121]
	s_lshl_b64 s[44:45], s[0:1], 5
	s_add_u32 s44, s26, s44
	s_addc_u32 s45, s27, s45
	v_lshl_add_u64 v[180:181], v[118:119], 2, s[44:45]
	v_add_co_u32_e32 v168, vcc, 0x100000, v180
	global_load_dword v167, v[180:181], off
	s_nop 0
	v_addc_co_u32_e32 v169, vcc, 0, v181, vcc
	global_load_dword v168, v[168:169], off
	v_add_co_u32_e32 v180, vcc, 0x200000, v180
	global_load_dwordx4 v[34:37], v[34:35], off nt
	s_nop 0
	v_addc_co_u32_e32 v181, vcc, 0, v181, vcc
	global_load_dwordx4 v[38:41], v[38:39], off nt
	s_nop 0
	global_load_dwordx4 v[42:45], v[42:43], off nt
	s_nop 0
	global_load_dword v169, v[180:181], off
	s_andn2_saveexec_b64 s[22:23], s[22:23]
	s_cbranch_execnz .LBB0_780

; __device__ __forceinline__ unsigned pk2(float lo, float hi) { return f2bf(lo) | (f2bf(hi) << 16); }
; __device__ __forceinline__ void unpack8(const v4u w, float* f) { f[0] = bflo(w.x); f[1] = bfhi(w.x); f[2] = bflo(w.y); f[3] = bfhi(w.y); f[4] = bflo(w.z); f[5] = bfhi(w.z); f[6] = bflo(w.w); f[7] = bfhi(w.w); }
; __device__ __forceinline__ void norm_compute(const NormRow& R, int lane, v4u& ya, v4u& yc) {
;     ...
;     const float s_moba = wave_sum(lane < 32 ? sa : 0.f), s_fox = wave_sum((lane >= 32 ? sa : 0.f) + (lane < 16 ? sc : 0.f)), s_dil = wave_sum(lane >= 16 ? sc : 0.f);
;     const float r_moba = 1.0f / sqrtf(s_moba * (1.0f / 256.0f) + EPS), r_fox = 1.0f / sqrtf(s_fox * (1.0f / 384.0f) + EPS), r_dil = 1.0f / sqrtf(s_dil * (1.0f / 384.0f) + EPS);
;     float ga[8], gc[8];
; #pragma unroll
;     for (int e = 0; e < 8; ++e) { ga[e] = 1.f; gc[e] = 1.f; }
;     if (lane >= 32) unpack8(R.ga, ga);
;     if (lane < 16) unpack8(R.gc, gc);
;     const float ra = lane < 32 ? r_moba : r_fox, rc = lane < 16 ? r_fox : r_dil;
;     ya.x = pk2(fa[0] * ra * ga[0], fa[1] * ra * ga[1]); ya.y = pk2(fa[2] * ra * ga[2], fa[3] * ra * ga[3]); ya.z = pk2(fa[4] * ra * ga[4], fa[5] * ra * ga[5]); ya.w = pk2(fa[6] * ra * ga[6], fa[7] * ra * ga[7]);
;     yc.x = pk2(fc[0] * rc * gc[0], fc[1] * rc * gc[1]); yc.y = pk2(fc[2] * rc * gc[2], fc[3] * rc * gc[3]); yc.z = pk2(fc[4] * rc * gc[4], fc[5] * rc * gc[5]); yc.w = pk2(fc[6] * rc * gc[6], fc[7] * rc * gc[7]);
; }
.LBB0_227:
	s_or_b64 exec, exec, s[20:21]
	v_mov_b32_e32 v179, v178
	s_nop 1
	v_permlane32_swap_b32_e32 v178, v179
	v_add_f32_e32 v178, v178, v179
	v_fmamk_f32 v178, v178, 0x3b2aaaab, v215
	v_mul_f32_e32 v179, 0x4f800000, v178
	v_cmp_gt_f32_e32 vcc, s3, v178
	v_mov_b32_e32 v177, v176
	s_nop 1
	v_permlane32_swap_b32_e32 v176, v177
	v_add_f32_e32 v176, v176, v177
	v_fmamk_f32 v176, v176, 0x3b2aaaab, v215
	v_cndmask_b32_e32 v178, v178, v179, vcc
	v_sqrt_f32_e32 v179, v178
	v_mul_f32_e32 v177, 0x4f800000, v176
	v_mov_b32_e32 v157, v156
	s_nop 1
	v_permlane32_swap_b32_e32 v156, v157
	v_add_f32_e32 v156, v156, v157
	v_fmamk_f32 v156, v156, 0x3b800000, v215
	v_add_u32_e32 v180, -1, v179
	v_fma_f32 v182, -v180, v179, v178
	v_add_u32_e32 v181, 1, v179
	v_cmp_ge_f32_e64 s[0:1], 0, v182
	v_mul_f32_e32 v157, 0x4f800000, v156
	s_nop 0
	v_cndmask_b32_e64 v180, v179, v180, s[0:1]
	v_fma_f32 v179, -v181, v179, v178
	v_cmp_lt_f32_e64 s[0:1], 0, v179
	s_nop 1
	v_cndmask_b32_e64 v179, v180, v181, s[0:1]
	v_cmp_gt_f32_e64 s[0:1], s3, v176
	v_mul_f32_e32 v180, 0x37800000, v179
	v_cndmask_b32_e32 v179, v179, v180, vcc
	v_cndmask_b32_e64 v176, v176, v177, s[0:1]
	v_sqrt_f32_e32 v177, v176
	v_cmp_class_f32_e32 vcc, v178, v216
	s_nop 1
	v_cndmask_b32_e32 v178, v179, v178, vcc
	v_add_u32_e32 v179, -1, v177
	v_fma_f32 v180, -v179, v177, v176
	v_cmp_ge_f32_e32 vcc, 0, v180
	v_add_u32_e32 v180, 1, v177
	s_nop 0
	v_cndmask_b32_e32 v179, v177, v179, vcc
	v_fma_f32 v177, -v180, v177, v176
	v_cmp_lt_f32_e32 vcc, 0, v177
	s_nop 1
	v_cndmask_b32_e32 v177, v179, v180, vcc
	v_cmp_gt_f32_e32 vcc, s3, v156
	v_mul_f32_e32 v179, 0x37800000, v177
	v_cndmask_b32_e64 v177, v177, v179, s[0:1]
	v_cndmask_b32_e32 v156, v156, v157, vcc
	v_sqrt_f32_e32 v157, v156
	v_cmp_class_f32_e64 s[0:1], v176, v216
	s_nop 1
	v_cndmask_b32_e64 v176, v177, v176, s[0:1]
	v_add_u32_e32 v177, -1, v157
	v_fma_f32 v179, -v177, v157, v156
	v_cmp_ge_f32_e64 s[0:1], 0, v179
	v_add_u32_e32 v179, 1, v157
	s_nop 0
	v_cndmask_b32_e64 v177, v157, v177, s[0:1]
	v_fma_f32 v157, -v179, v157, v156
	v_cmp_lt_f32_e64 s[0:1], 0, v157
	s_nop 1
	v_cndmask_b32_e64 v157, v177, v179, s[0:1]
	v_div_scale_f32 v179, s[0:1], v178, v178, 1.0
	v_rcp_f32_e32 v180, v179
	v_mul_f32_e32 v177, 0x37800000, v157
	v_cndmask_b32_e32 v157, v157, v177, vcc
	v_cmp_class_f32_e32 vcc, v156, v216
	s_nop 1
	v_cndmask_b32_e32 v156, v157, v156, vcc
	v_fma_f32 v157, -v179, v180, 1.0
	v_fmac_f32_e32 v180, v157, v180
	v_div_scale_f32 v157, vcc, 1.0, v178, 1.0
	v_mul_f32_e32 v177, v157, v180
	v_fma_f32 v181, -v179, v177, v157
	v_fmac_f32_e32 v177, v181, v180
	v_fma_f32 v157, -v179, v177, v157
	v_div_scale_f32 v179, s[0:1], v176, v176, 1.0
	v_rcp_f32_e32 v181, v179
	v_div_fmas_f32 v157, v157, v180, v177
	v_div_fixup_f32 v157, v157, v178, 1.0
	v_fma_f32 v177, -v179, v181, 1.0
	v_fmac_f32_e32 v181, v177, v181
	v_div_scale_f32 v177, vcc, 1.0, v176, 1.0
	v_mul_f32_e32 v178, v177, v181
	v_fma_f32 v180, -v179, v178, v177
	v_fmac_f32_e32 v178, v180, v181
	v_fma_f32 v177, -v179, v178, v177
	v_div_scale_f32 v179, s[0:1], v156, v156, 1.0
	v_rcp_f32_e32 v180, v179
	v_div_fmas_f32 v177, v177, v181, v178
	v_div_fixup_f32 v176, v177, v176, 1.0
	s_movk_i32 s1, 0x7fff
	v_fma_f32 v177, -v179, v180, 1.0
	v_fmac_f32_e32 v180, v177, v180
	v_div_scale_f32 v177, vcc, 1.0, v156, 1.0
	v_mul_f32_e32 v178, v177, v180
	v_fma_f32 v181, -v179, v178, v177
	v_fmac_f32_e32 v178, v181, v180
	v_fma_f32 v177, -v179, v178, v177
	v_div_fmas_f32 v177, v177, v180, v178
	v_div_fixup_f32 v156, v177, v156, 1.0
	v_cndmask_b32_e64 v156, v176, v156, s[40:41]
	v_pk_mul_f32 v[110:111], v[156:157], v[110:111] op_sel_hi:[0,1]
	v_pk_mul_f32 v[112:113], v[156:157], v[112:113] op_sel_hi:[0,1]
	v_pk_mul_f32 v[138:139], v[156:157], v[138:139] op_sel_hi:[0,1]
	v_pk_mul_f32 v[110:111], v[110:111], v[150:151]
	v_pk_mul_f32 v[136:137], v[156:157], v[136:137] op_sel_hi:[0,1]
	v_pk_mul_f32 v[112:113], v[112:113], v[148:149]
	v_pk_mul_f32 v[138:139], v[138:139], v[154:155]
	v_pk_mul_f32 v[136:137], v[136:137], v[152:153]
	v_bfe_u32 v148, v113, 16, 1
	v_bfe_u32 v149, v112, 16, 1
	v_bfe_u32 v150, v111, 16, 1
	v_bfe_u32 v151, v110, 16, 1
	v_cndmask_b32_e64 v176, v157, v176, s[34:35]
	v_add3_u32 v110, v110, v151, s1
	v_add3_u32 v111, v111, v150, s1
	v_add3_u32 v112, v112, v149, s1
	v_add3_u32 v113, v113, v148, s1
	v_bfe_u32 v148, v138, 16, 1
	v_bfe_u32 v149, v139, 16, 1
	v_bfe_u32 v150, v136, 16, 1
	v_bfe_u32 v151, v137, 16, 1
	v_add3_u32 v137, v137, v151, s1
	v_add3_u32 v136, v136, v150, s1
	v_add3_u32 v139, v139, v149, s1
	v_add3_u32 v138, v138, v148, s1
	v_pk_mul_f32 v[128:129], v[128:129], v[176:177] op_sel_hi:[1,0]
	v_pk_mul_f32 v[130:131], v[130:131], v[176:177] op_sel_hi:[1,0]
	v_lshrrev_b32_e32 v138, 16, v138
	v_lshrrev_b32_e32 v139, 16, v139
	v_lshrrev_b32_e32 v136, 16, v136
	v_lshrrev_b32_e32 v137, 16, v137
	s_mov_b32 s0, 0xffff0000
	v_pk_mul_f32 v[134:135], v[134:135], v[176:177] op_sel_hi:[1,0]
	v_pk_mul_f32 v[128:129], v[128:129], v[146:147]
	v_pk_mul_f32 v[132:133], v[132:133], v[176:177] op_sel_hi:[1,0]
	v_pk_mul_f32 v[130:131], v[130:131], v[142:143]
	v_and_or_b32 v113, v113, s0, v137
	v_and_or_b32 v112, v112, s0, v136
	v_and_or_b32 v111, v111, s0, v139
	v_and_or_b32 v110, v110, s0, v138
	v_pk_mul_f32 v[134:135], v[134:135], v[140:141]
	v_pk_mul_f32 v[132:133], v[132:133], v[144:145]
	v_bfe_u32 v136, v131, 16, 1
	v_bfe_u32 v137, v130, 16, 1
	v_bfe_u32 v138, v129, 16, 1
	v_bfe_u32 v139, v128, 16, 1
	v_add3_u32 v128, v128, v139, s1
	v_add3_u32 v129, v129, v138, s1
	v_add3_u32 v130, v130, v137, s1
	v_add3_u32 v131, v131, v136, s1
	v_bfe_u32 v136, v134, 16, 1
	v_bfe_u32 v137, v135, 16, 1
	v_bfe_u32 v138, v132, 16, 1
	v_bfe_u32 v139, v133, 16, 1
	v_add3_u32 v133, v133, v139, s1
	v_add3_u32 v132, v132, v138, s1
	v_add3_u32 v135, v135, v137, s1
	v_add3_u32 v134, v134, v136, s1
	v_lshrrev_b32_e32 v134, 16, v134
	v_lshrrev_b32_e32 v135, 16, v135
	v_lshrrev_b32_e32 v132, 16, v132
	v_lshrrev_b32_e32 v133, 16, v133
	v_and_or_b32 v131, v131, s0, v133
	v_and_or_b32 v130, v130, s0, v132
	v_and_or_b32 v129, v129, s0, v135
	v_and_or_b32 v128, v128, s0, v134
	s_add_u32 s0, s24, s14
	s_addc_u32 s1, s25, s15
	global_store_dwordx4 v0, v[110:113], s[0:1]
	global_store_dwordx4 v0, v[128:131], s[0:1] offset:1024
	s_waitcnt vmcnt(34)
	s_and_saveexec_b64 s[0:1], s[38:39]
	s_xor_b64 s[0:1], exec, s[0:1]
	s_cbranch_execz .LBB0_229
; __device__ __forceinline__ void unpack8(const v4u w, float* f) { f[0] = bflo(w.x); f[1] = bfhi(w.x); f[2] = bflo(w.y); f[3] = bfhi(w.y); f[4] = bflo(w.z); f[5] = bfhi(w.z); f[6] = bflo(w.w); f[7] = bfhi(w.w); }
; __device__ __forceinline__ void norm_compute(const NormRow& R, int lane, v4u& ya, v4u& yc) {
;     ...
;     else { float f0[8], f1[8], f2[8]; unpack8(R.d0, f0); unpack8(R.d1, f1); unpack8(R.d2, f2);
;         const float inv = 1.0f / (R.l0 + R.l1 + R.l2);
; #pragma unroll
;         for (int e = 0; e < 8; ++e) fc[e] = (f0[e] + f1[e] + f2[e]) * inv; }
	v_add_f32_e32 v111, v165, v163
	v_add_f32_e32 v128, v166, v111
	v_div_scale_f32 v129, s[14:15], v128, v128, 1.0
	v_rcp_f32_e32 v130, v129
	v_lshlrev_b32_e32 v134, 16, v18
	v_and_b32_e32 v135, 0xffff0000, v18
	v_lshlrev_b32_e32 v138, 16, v20
	v_fma_f32 v131, -v129, v130, 1.0
	v_fmac_f32_e32 v130, v131, v130
	v_div_scale_f32 v131, vcc, 1.0, v128, 1.0
	v_mul_f32_e32 v132, v131, v130
	v_fma_f32 v133, -v129, v132, v131
	v_fmac_f32_e32 v132, v133, v130
	v_fma_f32 v129, -v129, v132, v131
	v_div_fmas_f32 v129, v129, v130, v132
	v_div_fixup_f32 v130, v129, v128, 1.0
	v_lshlrev_b32_e32 v128, 16, v10
	v_and_b32_e32 v129, 0xffff0000, v10
	v_lshlrev_b32_e32 v132, 16, v14
	v_and_b32_e32 v133, 0xffff0000, v14
	v_pk_add_f32 v[128:129], v[132:133], v[128:129]
	v_lshlrev_b32_e32 v132, 16, v15
	v_pk_add_f32 v[128:129], v[128:129], v[134:135]
	v_and_b32_e32 v133, 0xffff0000, v15
	v_pk_mul_f32 v[136:137], v[130:131], v[128:129] op_sel_hi:[0,1]
	v_lshlrev_b32_e32 v128, 16, v11
	v_and_b32_e32 v129, 0xffff0000, v11
	v_lshlrev_b32_e32 v134, 16, v19
	v_and_b32_e32 v135, 0xffff0000, v19
	v_pk_add_f32 v[128:129], v[132:133], v[128:129]
	v_lshlrev_b32_e32 v132, 16, v12
	v_pk_add_f32 v[128:129], v[128:129], v[134:135]
	v_and_b32_e32 v133, 0xffff0000, v12
	v_lshlrev_b32_e32 v134, 16, v16
	v_and_b32_e32 v135, 0xffff0000, v16
	v_and_b32_e32 v139, 0xffff0000, v20
	v_pk_add_f32 v[132:133], v[134:135], v[132:133]
	v_lshlrev_b32_e32 v110, 16, v13
	v_lshlrev_b32_e32 v112, 16, v17
	v_and_b32_e32 v111, 0xffff0000, v13
	v_and_b32_e32 v113, 0xffff0000, v17
	v_pk_add_f32 v[132:133], v[132:133], v[138:139]
	v_pk_add_f32 v[110:111], v[112:113], v[110:111]
	v_pk_mul_f32 v[134:135], v[130:131], v[132:133] op_sel_hi:[0,1]
	v_lshlrev_b32_e32 v132, 16, v21
	v_and_b32_e32 v133, 0xffff0000, v21
	v_pk_add_f32 v[110:111], v[110:111], v[132:133]
	v_pk_mul_f32 v[128:129], v[130:131], v[128:129] op_sel_hi:[0,1]
	v_pk_mul_f32 v[130:131], v[130:131], v[110:111] op_sel_hi:[0,1]
	v_mov_b32_e32 v133, v130
	v_mov_b32_e32 v130, v135
	v_mov_b32_e32 v132, v134
	v_mov_b32_e32 v135, v128
	v_mov_b32_e32 v128, v137
	v_mov_b32_e32 v134, v136
; #define GAS __attribute__((address_space(1)))
; __device__ __forceinline__ void unpack8(const v4u w, float* f) { f[0] = bflo(w.x); f[1] = bfhi(w.x); f[2] = bflo(w.y); f[3] = bfhi(w.y); f[4] = bflo(w.z); f[5] = bfhi(w.z); f[6] = bflo(w.w); f[7] = bfhi(w.w); }
; __device__ __forceinline__ void norm_load(NormRow& R, int m, int lane, const bf16* O, const bf16* GF, const bf16* OD, const float* LD) {
;     R.oa = __builtin_nontemporal_load((const GAS v4u*)(O + (size_t)m * DM + 8 * lane));
;     if (lane < 16) { R.oc = __builtin_nontemporal_load((const GAS v4u*)(O + (size_t)m * DM + 512 + 8 * lane)); R.gc = __builtin_nontemporal_load((const GAS v4u*)(GF + (size_t)m * 384 + 256 + 8 * lane)); }
;     else { const int dc = 8 * lane - 128, hd = dc >> 6;
;         R.d0 = __builtin_nontemporal_load((const GAS v4u*)(OD + (size_t)m * 384 + dc)); R.d1 = __builtin_nontemporal_load((const GAS v4u*)(OD + OD_BRANCH + (size_t)m * 384 + dc)); R.d2 = __builtin_nontemporal_load((const GAS v4u*)(OD + 2 * OD_BRANCH + (size_t)m * 384 + dc));
;         R.l0 = LD[(size_t)m * 8 + hd]; R.l1 = LD[LD_BRANCH + (size_t)m * 8 + hd]; R.l2 = LD[2 * LD_BRANCH + (size_t)m * 8 + hd]; }
;     if (lane >= 32) R.ga = __builtin_nontemporal_load((const GAS v4u*)(GF + (size_t)m * 384 + 8 * lane - 256));
; __device__ __forceinline__ void norm_compute(const NormRow& R, int lane, v4u& ya, v4u& yc) {
;     ...
;     if (lane < 16) unpack8(R.oc, fc);
;     else { float f0[8], f1[8], f2[8]; unpack8(R.d0, f0); unpack8(R.d1, f1); unpack8(R.d2, f2);
;         const float inv = 1.0f / (R.l0 + R.l1 + R.l2);
; #pragma unroll
;         for (int e = 0; e < 8; ++e) fc[e] = (f0[e] + f1[e] + f2[e]) * inv; }
;     float sa = 0.f, sc = 0.f;
; #pragma unroll
;     for (int e = 0; e < 8; ++e) { sa += fa[e] * fa[e]; sc += fc[e] * fc[e]; }
;     const float s_moba = wave_sum(lane < 32 ? sa : 0.f), s_fox = wave_sum((lane >= 32 ? sa : 0.f) + (lane < 16 ? sc : 0.f)), s_dil = wave_sum(lane >= 16 ? sc : 0.f);
;     const float r_moba = 1.0f / sqrtf(s_moba * (1.0f / 256.0f) + EPS), r_fox = 1.0f / sqrtf(s_fox * (1.0f / 384.0f) + EPS), r_dil = 1.0f / sqrtf(s_dil * (1.0f / 384.0f) + EPS);
;     float ga[8], gc[8];
; #pragma unroll
;     for (int e = 0; e < 8; ++e) { ga[e] = 1.f; gc[e] = 1.f; }
;     if (lane >= 32) unpack8(R.ga, ga);
;     if (lane < 16) unpack8(R.gc, gc);
.LBB0_229:
	s_andn2_saveexec_b64 s[0:1], s[0:1]
	v_lshlrev_b32_e32 v134, 16, v22
	v_and_b32_e32 v128, 0xffff0000, v22
	v_lshlrev_b32_e32 v135, 16, v23
	v_and_b32_e32 v129, 0xffff0000, v23
	v_lshlrev_b32_e32 v132, 16, v24
	v_and_b32_e32 v130, 0xffff0000, v24
	v_lshlrev_b32_e32 v133, 16, v25
	v_and_b32_e32 v131, 0xffff0000, v25
	s_or_b64 exec, exec, s[0:1]
	v_lshlrev_b32_e32 v139, 16, v115
	v_lshlrev_b32_e32 v138, 16, v114
	v_and_b32_e32 v115, 0xffff0000, v115
	v_and_b32_e32 v114, 0xffff0000, v114
	v_pk_mul_f32 v[110:111], v[138:139], v[138:139]
	v_pk_mul_f32 v[112:113], v[114:115], v[114:115]
	v_mul_f32_e32 v144, v128, v128
	v_fmac_f32_e32 v144, v134, v134
	v_add_f32_e32 v110, v110, v112
	v_lshlrev_b32_e32 v137, 16, v117
	v_lshlrev_b32_e32 v136, 16, v116
	v_fmac_f32_e32 v144, v135, v135
	v_add_f32_e32 v110, v111, v110
	v_and_b32_e32 v117, 0xffff0000, v117
	v_and_b32_e32 v116, 0xffff0000, v116
	v_fmac_f32_e32 v144, v129, v129
	v_pk_mul_f32 v[140:141], v[136:137], v[136:137]
	v_add_f32_e32 v110, v113, v110
	v_fmac_f32_e32 v144, v132, v132
	v_pk_mul_f32 v[142:143], v[116:117], v[116:117]
	v_add_f32_e32 v110, v140, v110
	v_fmac_f32_e32 v144, v130, v130
	v_add_f32_e32 v110, v142, v110
	v_fmac_f32_e32 v144, v133, v133
	v_add_f32_e32 v110, v141, v110
	v_add_f32_e32 v110, v143, v110
	v_fmac_f32_e32 v144, v131, v131
	v_cndmask_b32_e64 v111, 0, v110, s[40:41]
	v_cndmask_b32_e64 v110, 0, v110, s[36:37]
	v_cndmask_b32_e64 v113, 0, v144, s[34:35]
	v_add_f32_e32 v110, v110, v113
	v_cndmask_b32_e64 v140, 0, v144, s[42:43]
	v_mov_b32_e32 v154, 1.0
	v_mov_b32_e32 v150, 1.0
	s_nop 1
	v_add_f32_dpp v111, v111, v111 quad_perm:[1,0,3,2] row_mask:0xf bank_mask:0xf
	s_nop 1
	v_add_f32_dpp v110, v110, v110 quad_perm:[1,0,3,2] row_mask:0xf bank_mask:0xf
	s_nop 1
	v_add_f32_dpp v140, v140, v140 quad_perm:[1,0,3,2] row_mask:0xf bank_mask:0xf
	v_mov_b32_e32 v155, 1.0
	v_mov_b32_e32 v151, 1.0
	s_nop 1
	v_add_f32_dpp v111, v111, v111 quad_perm:[2,3,0,1] row_mask:0xf bank_mask:0xf
	s_nop 1
	v_add_f32_dpp v110, v110, v110 quad_perm:[2,3,0,1] row_mask:0xf bank_mask:0xf
	s_nop 1
	v_add_f32_dpp v140, v140, v140 quad_perm:[2,3,0,1] row_mask:0xf bank_mask:0xf
	v_mov_b32_e32 v152, 1.0
	v_mov_b32_e32 v148, 1.0
	s_nop 1
	v_add_f32_dpp v111, v111, v111 row_half_mirror row_mask:0xf bank_mask:0xf
	s_nop 1
	v_add_f32_dpp v110, v110, v110 row_half_mirror row_mask:0xf bank_mask:0xf
	s_nop 1
	v_add_f32_dpp v140, v140, v140 row_half_mirror row_mask:0xf bank_mask:0xf
	v_mov_b32_e32 v153, 1.0
	v_mov_b32_e32 v149, 1.0
	s_nop 1
	v_add_f32_dpp v111, v111, v111 row_mirror row_mask:0xf bank_mask:0xf
	s_nop 1
	v_add_f32_dpp v110, v110, v110 row_mirror row_mask:0xf bank_mask:0xf
	s_nop 1
	v_add_f32_dpp v140, v140, v140 row_mirror row_mask:0xf bank_mask:0xf
	v_mov_b32_e32 v112, v111
	s_nop 1
	v_permlane16_swap_b32_e32 v111, v112
	v_add_f32_e32 v156, v111, v112
	v_mov_b32_e32 v113, v110
	s_nop 1
	v_permlane16_swap_b32_e32 v110, v113
	v_add_f32_e32 v176, v110, v113
	v_mov_b32_e32 v141, v140
	s_nop 1
	v_permlane16_swap_b32_e32 v140, v141
	v_add_f32_e32 v178, v140, v141
	v_mov_b32_e32 v140, 1.0
	s_and_saveexec_b64 s[0:1], s[36:37]
	v_lshlrev_b32_e32 v154, 16, v6
	v_and_b32_e32 v150, 0xffff0000, v6
	v_lshlrev_b32_e32 v155, 16, v7
	v_and_b32_e32 v151, 0xffff0000, v7
	v_lshlrev_b32_e32 v152, 16, v8
	v_and_b32_e32 v148, 0xffff0000, v8
	v_lshlrev_b32_e32 v153, 16, v9
	v_and_b32_e32 v149, 0xffff0000, v9
	s_or_b64 exec, exec, s[0:1]
	v_mov_b32_e32 v146, 1.0
	v_mov_b32_e32 v141, 1.0
	v_mov_b32_e32 v147, 1.0
	v_mov_b32_e32 v144, 1.0
	v_mov_b32_e32 v142, 1.0
	v_mov_b32_e32 v145, 1.0
	v_mov_b32_e32 v143, 1.0
	s_and_saveexec_b64 s[0:1], s[34:35]
	v_lshlrev_b32_e32 v140, 16, v2
	v_and_b32_e32 v146, 0xffff0000, v2
	v_lshlrev_b32_e32 v141, 16, v3
	v_and_b32_e32 v147, 0xffff0000, v3
	v_lshlrev_b32_e32 v144, 16, v4
	v_and_b32_e32 v142, 0xffff0000, v4
	v_lshlrev_b32_e32 v145, 16, v5
	v_and_b32_e32 v143, 0xffff0000, v5
	s_or_b64 exec, exec, s[0:1]
	s_or_b32 s0, s8, 15
	s_ashr_i32 s1, s0, 31
	s_lshl_b64 s[8:9], s[0:1], 11
	s_add_u32 s14, s29, s8
	s_addc_u32 s15, s30, s9
	global_load_dwordx4 v[110:113], v0, s[14:15] nt
	s_and_saveexec_b64 s[20:21], s[38:39]
	s_xor_b64 s[20:21], exec, s[20:21]
	s_cbranch_execz .LBB0_781
	v_mad_i64_i32 v[10:11], s[22:23], s0, v252, v[124:125]
	v_mad_i64_i32 v[14:15], s[22:23], s0, v252, v[122:123]
	v_mad_i64_i32 v[18:19], s[22:23], s0, v252, v[120:121]
	s_lshl_b64 s[22:23], s[0:1], 5
	s_add_u32 s22, s26, s22
	s_addc_u32 s23, s27, s23
	v_lshl_add_u64 v[118:119], v[118:119], 2, s[22:23]
	v_add_co_u32_e32 v120, vcc, 0x100000, v118
	global_load_dword v163, v[118:119], off
	s_nop 0
	v_addc_co_u32_e32 v121, vcc, 0, v119, vcc
	global_load_dword v165, v[120:121], off
	v_add_co_u32_e32 v118, vcc, 0x200000, v118
	global_load_dwordx4 v[10:13], v[10:11], off nt
	s_nop 0
	v_addc_co_u32_e32 v119, vcc, 0, v119, vcc
	global_load_dwordx4 v[14:17], v[14:15], off nt
	s_nop 0
	global_load_dwordx4 v[18:21], v[18:19], off nt
	s_nop 0
	global_load_dword v166, v[118:119], off
	s_andn2_saveexec_b64 s[20:21], s[20:21]
	s_cbranch_execnz .LBB0_782

; __device__ __forceinline__ unsigned pk2(float lo, float hi) { return f2bf(lo) | (f2bf(hi) << 16); }
; __device__ __forceinline__ void unpack8(const v4u w, float* f) { f[0] = bflo(w.x); f[1] = bfhi(w.x); f[2] = bflo(w.y); f[3] = bfhi(w.y); f[4] = bflo(w.z); f[5] = bfhi(w.z); f[6] = bflo(w.w); f[7] = bfhi(w.w); }
; __device__ __forceinline__ void norm_compute(const NormRow& R, int lane, v4u& ya, v4u& yc) {
;     float fa[8], fc[8];
;     unpack8(R.oa, fa);
;     if (lane < 16) unpack8(R.oc, fc);
;     else { float f0[8], f1[8], f2[8]; unpack8(R.d0, f0); unpack8(R.d1, f1); unpack8(R.d2, f2);
;         const float inv = 1.0f / (R.l0 + R.l1 + R.l2);
; #pragma unroll
;         for (int e = 0; e < 8; ++e) fc[e] = (f0[e] + f1[e] + f2[e]) * inv; }
;     float sa = 0.f, sc = 0.f;
; #pragma unroll
;     for (int e = 0; e < 8; ++e) { sa += fa[e] * fa[e]; sc += fc[e] * fc[e]; }
;     const float s_moba = wave_sum(lane < 32 ? sa : 0.f), s_fox = wave_sum((lane >= 32 ? sa : 0.f) + (lane < 16 ? sc : 0.f)), s_dil = wave_sum(lane >= 16 ? sc : 0.f);
;     const float r_moba = 1.0f / sqrtf(s_moba * (1.0f / 256.0f) + EPS), r_fox = 1.0f / sqrtf(s_fox * (1.0f / 384.0f) + EPS), r_dil = 1.0f / sqrtf(s_dil * (1.0f / 384.0f) + EPS);
;     float ga[8], gc[8];
; #pragma unroll
;     for (int e = 0; e < 8; ++e) { ga[e] = 1.f; gc[e] = 1.f; }
;     if (lane >= 32) unpack8(R.ga, ga);
;     if (lane < 16) unpack8(R.gc, gc);
;     const float ra = lane < 32 ? r_moba : r_fox, rc = lane < 16 ? r_fox : r_dil;
;     ya.x = pk2(fa[0] * ra * ga[0], fa[1] * ra * ga[1]); ya.y = pk2(fa[2] * ra * ga[2], fa[3] * ra * ga[3]); ya.z = pk2(fa[4] * ra * ga[4], fa[5] * ra * ga[5]); ya.w = pk2(fa[6] * ra * ga[6], fa[7] * ra * ga[7]);
;     yc.x = pk2(fc[0] * rc * gc[0], fc[1] * rc * gc[1]); yc.y = pk2(fc[2] * rc * gc[2], fc[3] * rc * gc[3]); yc.z = pk2(fc[4] * rc * gc[4], fc[5] * rc * gc[5]); yc.w = pk2(fc[6] * rc * gc[6], fc[7] * rc * gc[7]);
; }
.LBB0_239:
	s_or_b64 exec, exec, s[6:7]
	v_mov_b32_e32 v179, v178
	s_nop 1
	v_permlane32_swap_b32_e32 v178, v179
	v_add_f32_e32 v118, v178, v179
	v_fmamk_f32 v118, v118, 0x3b2aaaab, v215
	v_mul_f32_e32 v119, 0x4f800000, v118
	v_cmp_gt_f32_e32 vcc, s3, v118
	s_nop 1
	v_cndmask_b32_e32 v118, v118, v119, vcc
	v_sqrt_f32_e32 v119, v118
	s_nop 0
	v_add_u32_e32 v120, -1, v119
	v_fma_f32 v122, -v120, v119, v118
	v_add_u32_e32 v121, 1, v119
	v_cmp_ge_f32_e64 s[0:1], 0, v122
	s_nop 1
	v_cndmask_b32_e64 v120, v119, v120, s[0:1]
	v_fma_f32 v119, -v121, v119, v118
	v_cmp_lt_f32_e64 s[0:1], 0, v119
	s_nop 1
	v_cndmask_b32_e64 v119, v120, v121, s[0:1]
	v_mov_b32_e32 v177, v176
	s_nop 1
	v_permlane32_swap_b32_e32 v176, v177
	v_add_f32_e32 v121, v176, v177
	v_fmamk_f32 v121, v121, 0x3b2aaaab, v215
	v_mul_f32_e32 v122, 0x4f800000, v121
	v_cmp_gt_f32_e64 s[0:1], s3, v121
	v_mul_f32_e32 v120, 0x37800000, v119
	v_cndmask_b32_e32 v119, v119, v120, vcc
	v_cndmask_b32_e64 v121, v121, v122, s[0:1]
	v_sqrt_f32_e32 v122, v121
	v_cmp_class_f32_e32 vcc, v118, v216
	s_nop 1
	v_cndmask_b32_e32 v118, v119, v118, vcc
	v_add_u32_e32 v119, -1, v122
	v_fma_f32 v120, -v119, v122, v121
	v_cmp_ge_f32_e32 vcc, 0, v120
	v_add_u32_e32 v120, 1, v122
	s_nop 0
	v_cndmask_b32_e32 v119, v122, v119, vcc
	v_fma_f32 v122, -v120, v122, v121
	v_cmp_lt_f32_e32 vcc, 0, v122
	v_mov_b32_e32 v157, v156
	s_nop 1
	v_permlane32_swap_b32_e32 v156, v157
	v_add_f32_e32 v122, v156, v157
	v_fmamk_f32 v122, v122, 0x3b800000, v215
	v_cndmask_b32_e32 v119, v119, v120, vcc
	v_mul_f32_e32 v123, 0x4f800000, v122
	v_cmp_gt_f32_e32 vcc, s3, v122
	v_mul_f32_e32 v120, 0x37800000, v119
	v_cndmask_b32_e64 v119, v119, v120, s[0:1]
	v_cndmask_b32_e32 v122, v122, v123, vcc
	v_sqrt_f32_e32 v123, v122
	v_cmp_class_f32_e64 s[0:1], v121, v216
	v_add_u32_e32 v120, -1, v123
	s_nop 0
	v_cndmask_b32_e64 v119, v119, v121, s[0:1]
	v_fma_f32 v121, -v120, v123, v122
	v_cmp_ge_f32_e64 s[0:1], 0, v121
	v_add_u32_e32 v121, 1, v123
	s_nop 0
	v_cndmask_b32_e64 v120, v123, v120, s[0:1]
	v_fma_f32 v123, -v121, v123, v122
	v_cmp_lt_f32_e64 s[0:1], 0, v123
	s_nop 1
	v_cndmask_b32_e64 v120, v120, v121, s[0:1]
	v_div_scale_f32 v123, s[0:1], v118, v118, 1.0
	v_rcp_f32_e32 v124, v123
	v_mul_f32_e32 v121, 0x37800000, v120
	v_cndmask_b32_e32 v120, v120, v121, vcc
	v_cmp_class_f32_e32 vcc, v122, v216
	v_fma_f32 v121, -v123, v124, 1.0
	v_fmac_f32_e32 v124, v121, v124
	v_cndmask_b32_e32 v120, v120, v122, vcc
	v_div_scale_f32 v121, vcc, 1.0, v118, 1.0
	v_mul_f32_e32 v122, v121, v124
	v_fma_f32 v125, -v123, v122, v121
	v_fmac_f32_e32 v122, v125, v124
	v_fma_f32 v121, -v123, v122, v121
	v_div_scale_f32 v123, s[0:1], v119, v119, 1.0
	v_rcp_f32_e32 v125, v123
	v_div_fmas_f32 v121, v121, v124, v122
	v_div_fixup_f32 v121, v121, v118, 1.0
	v_fma_f32 v118, -v123, v125, 1.0
	v_fmac_f32_e32 v125, v118, v125
	v_div_scale_f32 v118, vcc, 1.0, v119, 1.0
	v_mul_f32_e32 v122, v118, v125
	v_fma_f32 v124, -v123, v122, v118
	v_fmac_f32_e32 v122, v124, v125
	v_fma_f32 v118, -v123, v122, v118
	v_div_scale_f32 v123, s[0:1], v120, v120, 1.0
	v_rcp_f32_e32 v124, v123
	v_div_fmas_f32 v118, v118, v125, v122
	v_div_fixup_f32 v119, v118, v119, 1.0
	s_movk_i32 s1, 0x7fff
	v_fma_f32 v118, -v123, v124, 1.0
	v_fmac_f32_e32 v124, v118, v124
	v_div_scale_f32 v118, vcc, 1.0, v120, 1.0
	v_mul_f32_e32 v122, v118, v124
	v_fma_f32 v125, -v123, v122, v118
	v_fmac_f32_e32 v122, v125, v124
	v_fma_f32 v118, -v123, v122, v118
	v_div_fmas_f32 v118, v118, v124, v122
	v_div_fixup_f32 v118, v118, v120, 1.0
	v_cndmask_b32_e64 v118, v119, v118, s[40:41]
	v_pk_mul_f32 v[114:115], v[118:119], v[114:115] op_sel_hi:[0,1]
	v_pk_mul_f32 v[116:117], v[118:119], v[116:117] op_sel_hi:[0,1]
	v_pk_mul_f32 v[122:123], v[118:119], v[138:139] op_sel_hi:[0,1]
	v_pk_mul_f32 v[114:115], v[114:115], v[150:151]
	v_pk_mul_f32 v[124:125], v[118:119], v[136:137] op_sel_hi:[0,1]
	v_pk_mul_f32 v[116:117], v[116:117], v[148:149]
	v_cndmask_b32_e64 v120, v121, v119, s[34:35]
	v_pk_mul_f32 v[122:123], v[122:123], v[154:155]
	v_pk_mul_f32 v[124:125], v[124:125], v[152:153]
	v_bfe_u32 v118, v117, 16, 1
	v_bfe_u32 v119, v116, 16, 1
	v_bfe_u32 v121, v115, 16, 1
	v_bfe_u32 v126, v114, 16, 1
	v_add3_u32 v114, v114, v126, s1
	v_add3_u32 v115, v115, v121, s1
	v_add3_u32 v116, v116, v119, s1
	v_add3_u32 v117, v117, v118, s1
	v_bfe_u32 v118, v122, 16, 1
	v_bfe_u32 v119, v123, 16, 1
	v_bfe_u32 v121, v124, 16, 1
	v_bfe_u32 v126, v125, 16, 1
	v_add3_u32 v125, v125, v126, s1
	v_add3_u32 v121, v124, v121, s1
	v_add3_u32 v119, v123, v119, s1
	v_add3_u32 v118, v122, v118, s1
	v_lshrrev_b32_e32 v118, 16, v118
	v_lshrrev_b32_e32 v119, 16, v119
	v_lshrrev_b32_e32 v121, 16, v121
	v_lshrrev_b32_e32 v122, 16, v125
	s_mov_b32 s0, 0xffff0000
	v_and_or_b32 v117, v117, s0, v122
	v_and_or_b32 v116, v116, s0, v121
	v_and_or_b32 v115, v115, s0, v119
	v_and_or_b32 v114, v114, s0, v118
	v_pk_mul_f32 v[118:119], v[134:135], v[120:121] op_sel_hi:[1,0]
	v_pk_mul_f32 v[122:123], v[128:129], v[120:121] op_sel_hi:[1,0]
	v_pk_mul_f32 v[124:125], v[132:133], v[120:121] op_sel_hi:[1,0]
	v_pk_mul_f32 v[120:121], v[130:131], v[120:121] op_sel_hi:[1,0]
	v_pk_mul_f32 v[122:123], v[122:123], v[146:147]
	v_pk_mul_f32 v[120:121], v[120:121], v[142:143]
	v_pk_mul_f32 v[118:119], v[118:119], v[140:141]
	v_pk_mul_f32 v[124:125], v[124:125], v[144:145]
	v_bfe_u32 v126, v121, 16, 1
	v_bfe_u32 v127, v120, 16, 1
	v_bfe_u32 v128, v123, 16, 1
	v_bfe_u32 v129, v122, 16, 1
	v_add3_u32 v122, v122, v129, s1
	v_add3_u32 v123, v123, v128, s1
	v_add3_u32 v120, v120, v127, s1
	v_add3_u32 v121, v121, v126, s1
	v_bfe_u32 v126, v118, 16, 1
	v_bfe_u32 v127, v119, 16, 1
	v_bfe_u32 v128, v124, 16, 1
	v_bfe_u32 v129, v125, 16, 1
	v_add3_u32 v125, v125, v129, s1
	v_add3_u32 v124, v124, v128, s1
	v_add3_u32 v119, v119, v127, s1
	v_add3_u32 v118, v118, v126, s1
	v_lshrrev_b32_e32 v118, 16, v118
	v_lshrrev_b32_e32 v119, 16, v119
	v_lshrrev_b32_e32 v124, 16, v124
	v_lshrrev_b32_e32 v125, 16, v125
	v_and_or_b32 v121, v121, s0, v125
	v_and_or_b32 v120, v120, s0, v124
	v_and_or_b32 v119, v123, s0, v119
	v_and_or_b32 v118, v122, s0, v118
	s_add_u32 s0, s24, s16
	s_addc_u32 s1, s25, s17
	global_store_dwordx4 v0, v[114:117], s[0:1]
	global_store_dwordx4 v0, v[118:121], s[0:1] offset:1024
	s_and_saveexec_b64 s[0:1], s[38:39]
	s_xor_b64 s[0:1], exec, s[0:1]
	s_cbranch_execz .LBB0_241
; __device__ __forceinline__ void unpack8(const v4u w, float* f) { f[0] = bflo(w.x); f[1] = bfhi(w.x); f[2] = bflo(w.y); f[3] = bfhi(w.y); f[4] = bflo(w.z); f[5] = bfhi(w.z); f[6] = bflo(w.w); f[7] = bfhi(w.w); }
; __device__ __forceinline__ void norm_compute(const NormRow& R, int lane, v4u& ya, v4u& yc) {
;     ...
;     if (lane < 16) unpack8(R.oc, fc);
;     else { float f0[8], f1[8], f2[8]; unpack8(R.d0, f0); unpack8(R.d1, f1); unpack8(R.d2, f2);
;         const float inv = 1.0f / (R.l0 + R.l1 + R.l2);
; #pragma unroll
;         for (int e = 0; e < 8; ++e) fc[e] = (f0[e] + f1[e] + f2[e]) * inv; }
;     float sa = 0.f, sc = 0.f;
; #pragma unroll
;     for (int e = 0; e < 8; ++e) { sa += fa[e] * fa[e]; sc += fc[e] * fc[e]; }
;     const float s_moba = wave_sum(lane < 32 ? sa : 0.f), s_fox = wave_sum((lane >= 32 ? sa : 0.f) + (lane < 16 ? sc : 0.f)), s_dil = wave_sum(lane >= 16 ? sc : 0.f);
;     const float r_moba = 1.0f / sqrtf(s_moba * (1.0f / 256.0f) + EPS), r_fox = 1.0f / sqrtf(s_fox * (1.0f / 384.0f) + EPS), r_dil = 1.0f / sqrtf(s_dil * (1.0f / 384.0f) + EPS);
;     float ga[8], gc[8];
; #pragma unroll
;     for (int e = 0; e < 8; ++e) { ga[e] = 1.f; gc[e] = 1.f; }
;     if (lane >= 32) unpack8(R.ga, ga);
;     if (lane < 16) unpack8(R.gc, gc);
	s_waitcnt vmcnt(34)
	v_add_f32_e32 v95, v173, v174
	v_add_f32_e32 v114, v95, v175
	v_div_scale_f32 v115, s[6:7], v114, v114, 1.0
	v_rcp_f32_e32 v116, v115
	v_lshlrev_b32_e32 v94, 16, v85
	v_and_b32_e32 v95, 0xffff0000, v85
	v_lshlrev_b32_e32 v96, 16, v89
	v_fma_f32 v85, -v115, v116, 1.0
	v_fmac_f32_e32 v116, v85, v116
	v_div_scale_f32 v85, vcc, 1.0, v114, 1.0
	v_and_b32_e32 v97, 0xffff0000, v89
	v_mul_f32_e32 v89, v85, v116
	v_fma_f32 v117, -v115, v89, v85
	v_fmac_f32_e32 v89, v117, v116
	v_fma_f32 v85, -v115, v89, v85
	v_div_fmas_f32 v85, v85, v116, v89
	v_div_fixup_f32 v116, v85, v114, 1.0
	v_lshlrev_b32_e32 v114, 16, v82
	v_and_b32_e32 v115, 0xffff0000, v82
	v_lshlrev_b32_e32 v118, 16, v86
	v_and_b32_e32 v119, 0xffff0000, v86
	v_lshlrev_b32_e32 v82, 16, v83
	v_and_b32_e32 v83, 0xffff0000, v83
	v_lshlrev_b32_e32 v86, 16, v87
	v_and_b32_e32 v87, 0xffff0000, v87
	v_lshlrev_b32_e32 v120, 16, v90
	v_and_b32_e32 v121, 0xffff0000, v90
	v_pk_add_f32 v[114:115], v[118:119], v[114:115]
	v_lshlrev_b32_e32 v90, 16, v91
	v_and_b32_e32 v91, 0xffff0000, v91
	v_pk_add_f32 v[82:83], v[86:87], v[82:83]
	v_pk_add_f32 v[114:115], v[114:115], v[120:121]
	v_pk_add_f32 v[82:83], v[82:83], v[90:91]
	v_pk_mul_f32 v[122:123], v[114:115], v[116:117] op_sel_hi:[1,0]
	v_pk_mul_f32 v[114:115], v[82:83], v[116:117] op_sel_hi:[1,0]
	v_lshlrev_b32_e32 v82, 16, v84
	v_and_b32_e32 v83, 0xffff0000, v84
	v_lshlrev_b32_e32 v84, 16, v88
	v_and_b32_e32 v85, 0xffff0000, v88
	v_lshlrev_b32_e32 v86, 16, v92
	v_and_b32_e32 v87, 0xffff0000, v92
	v_pk_add_f32 v[82:83], v[84:85], v[82:83]
	v_lshlrev_b32_e32 v84, 16, v93
	v_pk_add_f32 v[82:83], v[82:83], v[86:87]
	v_and_b32_e32 v85, 0xffff0000, v93
	v_pk_add_f32 v[86:87], v[96:97], v[94:95]
	v_pk_mul_f32 v[82:83], v[82:83], v[116:117] op_sel_hi:[1,0]
	v_pk_add_f32 v[84:85], v[86:87], v[84:85]
	v_mov_b32_e32 v118, v82
	v_pk_mul_f32 v[116:117], v[84:85], v[116:117] op_sel_hi:[1,0]
	v_mov_b32_e32 v121, v114
	v_mov_b32_e32 v119, v116
	v_mov_b32_e32 v116, v83
	v_mov_b32_e32 v114, v123
	v_mov_b32_e32 v120, v122
.LBB0_241:
	s_andn2_saveexec_b64 s[0:1], s[0:1]
	s_cbranch_execz .LBB0_243
	s_waitcnt vmcnt(34)
	v_lshlrev_b32_e32 v120, 16, v94
	v_and_b32_e32 v114, 0xffff0000, v94
	v_lshlrev_b32_e32 v121, 16, v95
	v_and_b32_e32 v115, 0xffff0000, v95
	v_lshlrev_b32_e32 v118, 16, v96
	v_and_b32_e32 v116, 0xffff0000, v96
	v_lshlrev_b32_e32 v119, 16, v97
	v_and_b32_e32 v117, 0xffff0000, v97
.LBB0_243:
	s_or_b64 exec, exec, s[0:1]
	s_waitcnt vmcnt(34)
	v_lshlrev_b32_e32 v85, 16, v99
	v_lshlrev_b32_e32 v84, 16, v98
	v_and_b32_e32 v87, 0xffff0000, v99
	v_and_b32_e32 v86, 0xffff0000, v98
	v_pk_mul_f32 v[90:91], v[84:85], v[84:85]
	v_pk_mul_f32 v[92:93], v[86:87], v[86:87]
	v_mul_f32_e32 v98, v114, v114
	v_fmac_f32_e32 v98, v120, v120
	v_add_f32_e32 v90, v90, v92
	v_lshlrev_b32_e32 v83, 16, v101
	v_lshlrev_b32_e32 v82, 16, v100
	v_fmac_f32_e32 v98, v121, v121
	v_add_f32_e32 v90, v91, v90
	v_and_b32_e32 v89, 0xffff0000, v101
	v_and_b32_e32 v88, 0xffff0000, v100
	v_fmac_f32_e32 v98, v115, v115
	v_pk_mul_f32 v[94:95], v[82:83], v[82:83]
	v_add_f32_e32 v90, v93, v90
	v_fmac_f32_e32 v98, v118, v118
	v_pk_mul_f32 v[96:97], v[88:89], v[88:89]
	v_add_f32_e32 v90, v94, v90
	v_fmac_f32_e32 v98, v116, v116
	v_add_f32_e32 v90, v96, v90
	v_fmac_f32_e32 v98, v119, v119
	v_add_f32_e32 v90, v95, v90
	v_add_f32_e32 v90, v97, v90
	v_fmac_f32_e32 v98, v117, v117
	v_cndmask_b32_e64 v91, 0, v90, s[40:41]
	v_cndmask_b32_e64 v90, 0, v90, s[36:37]
	v_cndmask_b32_e64 v93, 0, v98, s[34:35]
	v_add_f32_e32 v90, v90, v93
	v_cndmask_b32_e64 v94, 0, v98, s[42:43]
	v_mov_b32_e32 v98, 1.0
	v_mov_b32_e32 v96, 1.0
	s_nop 1
	v_add_f32_dpp v91, v91, v91 quad_perm:[1,0,3,2] row_mask:0xf bank_mask:0xf
	s_nop 1
	v_add_f32_dpp v90, v90, v90 quad_perm:[1,0,3,2] row_mask:0xf bank_mask:0xf
	s_nop 1
	v_add_f32_dpp v94, v94, v94 quad_perm:[1,0,3,2] row_mask:0xf bank_mask:0xf
	v_mov_b32_e32 v97, 1.0
	s_nop 1
	v_add_f32_dpp v91, v91, v91 quad_perm:[2,3,0,1] row_mask:0xf bank_mask:0xf
	s_nop 1
	v_add_f32_dpp v90, v90, v90 quad_perm:[2,3,0,1] row_mask:0xf bank_mask:0xf
	s_nop 1
	v_add_f32_dpp v94, v94, v94 quad_perm:[2,3,0,1] row_mask:0xf bank_mask:0xf
	s_nop 1
	v_add_f32_dpp v91, v91, v91 row_half_mirror row_mask:0xf bank_mask:0xf
	s_nop 1
	v_add_f32_dpp v90, v90, v90 row_half_mirror row_mask:0xf bank_mask:0xf
	s_nop 1
	v_add_f32_dpp v94, v94, v94 row_half_mirror row_mask:0xf bank_mask:0xf
	s_nop 1
	v_add_f32_dpp v91, v91, v91 row_mirror row_mask:0xf bank_mask:0xf
	s_nop 1
	v_add_f32_dpp v90, v90, v90 row_mirror row_mask:0xf bank_mask:0xf
	s_nop 1
	v_add_f32_dpp v94, v94, v94 row_mirror row_mask:0xf bank_mask:0xf
	v_mov_b32_e32 v92, v91
	s_nop 1
	v_permlane16_swap_b32_e32 v91, v92
	v_add_f32_e32 v122, v91, v92
	v_mov_b32_e32 v93, v90
	s_nop 1
	v_permlane16_swap_b32_e32 v90, v93
	v_add_f32_e32 v126, v90, v93
	v_mov_b32_e32 v95, v94
	s_nop 1
	v_permlane16_swap_b32_e32 v94, v95
	v_add_f32_e32 v124, v94, v95
	v_mov_b32_e32 v92, 1.0
	v_mov_b32_e32 v93, 1.0
	v_mov_b32_e32 v90, 1.0
	v_mov_b32_e32 v94, 1.0
	v_mov_b32_e32 v91, 1.0
	v_mov_b32_e32 v95, 1.0
	s_and_saveexec_b64 s[0:1], s[36:37]
	v_lshlrev_b32_e32 v92, 16, v78
	v_and_b32_e32 v96, 0xffff0000, v78
	v_lshlrev_b32_e32 v93, 16, v79
	v_and_b32_e32 v97, 0xffff0000, v79
	v_lshlrev_b32_e32 v90, 16, v80
	v_and_b32_e32 v94, 0xffff0000, v80
	v_lshlrev_b32_e32 v91, 16, v81
	v_and_b32_e32 v95, 0xffff0000, v81
	s_or_b64 exec, exec, s[0:1]
	v_mov_b32_e32 v100, 1.0
	v_mov_b32_e32 v99, 1.0
	v_mov_b32_e32 v101, 1.0
	v_mov_b32_e32 v78, 1.0
	v_mov_b32_e32 v80, 1.0
	v_mov_b32_e32 v79, 1.0
	v_mov_b32_e32 v81, 1.0
	s_and_saveexec_b64 s[0:1], s[34:35]
	v_lshlrev_b32_e32 v98, 16, v74
; __device__ __forceinline__ unsigned pk2(float lo, float hi) { return f2bf(lo) | (f2bf(hi) << 16); }
; __device__ __forceinline__ void unpack8(const v4u w, float* f) { f[0] = bflo(w.x); f[1] = bfhi(w.x); f[2] = bflo(w.y); f[3] = bfhi(w.y); f[4] = bflo(w.z); f[5] = bfhi(w.z); f[6] = bflo(w.w); f[7] = bfhi(w.w); }
; __device__ __forceinline__ void norm_compute(const NormRow& R, int lane, v4u& ya, v4u& yc) {
;     ...
;     for (int e = 0; e < 8; ++e) { sa += fa[e] * fa[e]; sc += fc[e] * fc[e]; }
;     const float s_moba = wave_sum(lane < 32 ? sa : 0.f), s_fox = wave_sum((lane >= 32 ? sa : 0.f) + (lane < 16 ? sc : 0.f)), s_dil = wave_sum(lane >= 16 ? sc : 0.f);
;     const float r_moba = 1.0f / sqrtf(s_moba * (1.0f / 256.0f) + EPS), r_fox = 1.0f / sqrtf(s_fox * (1.0f / 384.0f) + EPS), r_dil = 1.0f / sqrtf(s_dil * (1.0f / 384.0f) + EPS);
;     float ga[8], gc[8];
; #pragma unroll
;     for (int e = 0; e < 8; ++e) { ga[e] = 1.f; gc[e] = 1.f; }
;     if (lane >= 32) unpack8(R.ga, ga);
;     if (lane < 16) unpack8(R.gc, gc);
;     const float ra = lane < 32 ? r_moba : r_fox, rc = lane < 16 ? r_fox : r_dil;
;     ya.x = pk2(fa[0] * ra * ga[0], fa[1] * ra * ga[1]); ya.y = pk2(fa[2] * ra * ga[2], fa[3] * ra * ga[3]); ya.z = pk2(fa[4] * ra * ga[4], fa[5] * ra * ga[5]); ya.w = pk2(fa[6] * ra * ga[6], fa[7] * ra * ga[7]);
;     yc.x = pk2(fc[0] * rc * gc[0], fc[1] * rc * gc[1]); yc.y = pk2(fc[2] * rc * gc[2], fc[3] * rc * gc[3]); yc.z = pk2(fc[4] * rc * gc[4], fc[5] * rc * gc[5]); yc.w = pk2(fc[6] * rc * gc[6], fc[7] * rc * gc[7]);
; }
	v_and_b32_e32 v100, 0xffff0000, v74
	v_lshlrev_b32_e32 v99, 16, v75
	v_and_b32_e32 v101, 0xffff0000, v75
	v_lshlrev_b32_e32 v78, 16, v76
	v_and_b32_e32 v80, 0xffff0000, v76
	v_lshlrev_b32_e32 v79, 16, v77
	v_and_b32_e32 v81, 0xffff0000, v77
	s_or_b64 exec, exec, s[0:1]
	v_mov_b32_e32 v127, v126
	s_nop 1
	v_permlane32_swap_b32_e32 v126, v127
	v_add_f32_e32 v74, v126, v127
	v_fmamk_f32 v74, v74, 0x3b2aaaab, v215
	v_cmp_gt_f32_e32 vcc, s3, v74
	v_mul_f32_e32 v75, 0x4f800000, v74
	s_movk_i32 s7, 0x7fff
	v_cndmask_b32_e32 v74, v74, v75, vcc
	v_sqrt_f32_e32 v75, v74
	s_mov_b32 s6, 0xffff0000
	v_add_u32_e32 v76, -1, v75
	v_fma_f32 v77, -v76, v75, v74
	v_cmp_ge_f32_e64 s[0:1], 0, v77
	v_add_u32_e32 v77, 1, v75
	s_nop 0
	v_cndmask_b32_e64 v76, v75, v76, s[0:1]
	v_fma_f32 v75, -v77, v75, v74
	v_cmp_lt_f32_e64 s[0:1], 0, v75
	s_nop 1
	v_cndmask_b32_e64 v75, v76, v77, s[0:1]
	v_mul_f32_e32 v76, 0x37800000, v75
	v_cndmask_b32_e32 v75, v75, v76, vcc
	v_cmp_class_f32_e32 vcc, v74, v216
	s_nop 1
	v_cndmask_b32_e32 v74, v75, v74, vcc
	v_div_scale_f32 v75, s[0:1], v74, v74, 1.0
	v_rcp_f32_e32 v76, v75
	s_nop 0
	v_fma_f32 v77, -v75, v76, 1.0
	v_fmac_f32_e32 v76, v77, v76
	v_div_scale_f32 v77, vcc, 1.0, v74, 1.0
	v_mul_f32_e32 v126, v77, v76
	v_fma_f32 v127, -v75, v126, v77
	v_fmac_f32_e32 v126, v127, v76
	v_fma_f32 v75, -v75, v126, v77
	v_div_fmas_f32 v75, v75, v76, v126
	v_div_fixup_f32 v126, v75, v74, 1.0
	v_mov_b32_e32 v125, v124
	s_nop 1
	v_permlane32_swap_b32_e32 v124, v125
	v_add_f32_e32 v74, v124, v125
	v_fmamk_f32 v74, v74, 0x3b2aaaab, v215
	v_cmp_gt_f32_e32 vcc, s3, v74
	v_mul_f32_e32 v75, 0x4f800000, v74
	s_nop 0
	v_cndmask_b32_e32 v74, v74, v75, vcc
	v_sqrt_f32_e32 v75, v74
	s_nop 0
	v_add_u32_e32 v76, -1, v75
	v_fma_f32 v77, -v76, v75, v74
	v_cmp_ge_f32_e64 s[0:1], 0, v77
	v_add_u32_e32 v77, 1, v75
	s_nop 0
	v_cndmask_b32_e64 v76, v75, v76, s[0:1]
	v_fma_f32 v75, -v77, v75, v74
	v_cmp_lt_f32_e64 s[0:1], 0, v75
	s_nop 1
	v_cndmask_b32_e64 v75, v76, v77, s[0:1]
	v_mul_f32_e32 v76, 0x37800000, v75
	v_cndmask_b32_e32 v75, v75, v76, vcc
	v_cmp_class_f32_e32 vcc, v74, v216
	s_nop 1
	v_cndmask_b32_e32 v74, v75, v74, vcc
	v_div_scale_f32 v75, s[0:1], v74, v74, 1.0
	v_rcp_f32_e32 v76, v75
	s_nop 0
	v_fma_f32 v77, -v75, v76, 1.0
	v_fmac_f32_e32 v76, v77, v76
	v_div_scale_f32 v77, vcc, 1.0, v74, 1.0
	v_mul_f32_e32 v124, v77, v76
	v_fma_f32 v125, -v75, v124, v77
	v_fmac_f32_e32 v124, v125, v76
	v_fma_f32 v75, -v75, v124, v77
	v_div_fmas_f32 v75, v75, v76, v124
	v_div_fixup_f32 v74, v75, v74, 1.0
	v_cndmask_b32_e64 v74, v74, v126, s[34:35]
	v_pk_mul_f32 v[76:77], v[114:115], v[74:75] op_sel_hi:[1,0]
	s_nop 0
	v_pk_mul_f32 v[76:77], v[76:77], v[100:101]
	v_pk_mul_f32 v[100:101], v[120:121], v[74:75] op_sel_hi:[1,0]
	s_nop 0
	v_pk_mul_f32 v[98:99], v[100:101], v[98:99]
	v_pk_mul_f32 v[100:101], v[116:117], v[74:75] op_sel_hi:[1,0]
	v_pk_mul_f32 v[74:75], v[118:119], v[74:75] op_sel_hi:[1,0]
	v_pk_mul_f32 v[80:81], v[100:101], v[80:81]
	v_pk_mul_f32 v[74:75], v[74:75], v[78:79]
	v_bfe_u32 v78, v81, 16, 1
	v_bfe_u32 v79, v80, 16, 1
	v_bfe_u32 v100, v77, 16, 1
	v_bfe_u32 v101, v76, 16, 1
	v_add3_u32 v101, v76, v101, s7
	v_add3_u32 v100, v77, v100, s7
	v_add3_u32 v76, v80, v79, s7
	v_add3_u32 v77, v81, v78, s7
	v_bfe_u32 v78, v98, 16, 1
	v_bfe_u32 v80, v74, 16, 1
	v_add3_u32 v74, v74, v80, s7
	v_add3_u32 v78, v98, v78, s7
	v_bfe_u32 v79, v99, 16, 1
	v_bfe_u32 v81, v75, 16, 1
	v_lshrrev_b32_e32 v78, 16, v78
	v_lshrrev_b32_e32 v74, 16, v74
	v_add3_u32 v75, v75, v81, s7
	v_add3_u32 v79, v99, v79, s7
	v_and_or_b32 v76, v76, s6, v74
	v_and_or_b32 v74, v101, s6, v78
	v_mov_b32_e32 v123, v122
	s_nop 1
	v_permlane32_swap_b32_e32 v122, v123
	v_add_f32_e32 v78, v122, v123
	v_lshrrev_b32_e32 v79, 16, v79
	v_lshrrev_b32_e32 v75, 16, v75
	v_fmamk_f32 v78, v78, 0x3b800000, v215
	v_and_or_b32 v77, v77, s6, v75
	v_and_or_b32 v75, v100, s6, v79
	v_cmp_gt_f32_e32 vcc, s3, v78
	v_mul_f32_e32 v79, 0x4f800000, v78
	s_nop 0
	v_cndmask_b32_e32 v78, v78, v79, vcc
	v_sqrt_f32_e32 v79, v78
	s_nop 0
	v_add_u32_e32 v80, -1, v79
	v_fma_f32 v81, -v80, v79, v78
	v_cmp_ge_f32_e64 s[0:1], 0, v81
	v_add_u32_e32 v81, 1, v79
	s_nop 0
	v_cndmask_b32_e64 v80, v79, v80, s[0:1]
	v_fma_f32 v79, -v81, v79, v78
	v_cmp_lt_f32_e64 s[0:1], 0, v79
	s_nop 1
	v_cndmask_b32_e64 v79, v80, v81, s[0:1]
	v_mul_f32_e32 v80, 0x37800000, v79
	v_cndmask_b32_e32 v79, v79, v80, vcc
	v_cmp_class_f32_e32 vcc, v78, v216
	s_nop 1
	v_cndmask_b32_e32 v78, v79, v78, vcc
	v_div_scale_f32 v79, s[0:1], v78, v78, 1.0
	v_rcp_f32_e32 v80, v79
	s_add_u32 s0, s24, s18
	s_addc_u32 s1, s25, s19
	v_fma_f32 v81, -v79, v80, 1.0
	v_fmac_f32_e32 v80, v81, v80
	v_div_scale_f32 v81, vcc, 1.0, v78, 1.0
	v_mul_f32_e32 v98, v81, v80
	v_fma_f32 v99, -v79, v98, v81
	v_fmac_f32_e32 v98, v99, v80
	v_fma_f32 v79, -v79, v98, v81
	v_div_fmas_f32 v79, v79, v80, v98
	v_div_fixup_f32 v78, v79, v78, 1.0
	v_cndmask_b32_e64 v78, v126, v78, s[40:41]
	v_pk_mul_f32 v[80:81], v[78:79], v[86:87] op_sel_hi:[0,1]
	v_pk_mul_f32 v[86:87], v[78:79], v[88:89] op_sel_hi:[0,1]
	v_pk_mul_f32 v[80:81], v[80:81], v[96:97]
	v_pk_mul_f32 v[84:85], v[78:79], v[84:85] op_sel_hi:[0,1]
	v_pk_mul_f32 v[86:87], v[86:87], v[94:95]
	v_pk_mul_f32 v[78:79], v[78:79], v[82:83] op_sel_hi:[0,1]
	v_pk_mul_f32 v[84:85], v[84:85], v[92:93]
	v_pk_mul_f32 v[78:79], v[78:79], v[90:91]
	v_bfe_u32 v82, v87, 16, 1
	v_bfe_u32 v83, v86, 16, 1
	v_bfe_u32 v88, v81, 16, 1
	v_bfe_u32 v89, v80, 16, 1
	v_add3_u32 v89, v80, v89, s7
	v_add3_u32 v88, v81, v88, s7
	v_add3_u32 v80, v86, v83, s7
	v_add3_u32 v81, v87, v82, s7
	v_bfe_u32 v82, v84, 16, 1
	v_bfe_u32 v83, v85, 16, 1
	v_bfe_u32 v86, v78, 16, 1
	v_bfe_u32 v87, v79, 16, 1
	v_add3_u32 v79, v79, v87, s7
	v_add3_u32 v78, v78, v86, s7
	v_add3_u32 v83, v85, v83, s7
	v_add3_u32 v82, v84, v82, s7
	v_lshrrev_b32_e32 v82, 16, v82
	v_lshrrev_b32_e32 v83, 16, v83
	v_lshrrev_b32_e32 v78, 16, v78
	v_lshrrev_b32_e32 v79, 16, v79
	v_and_or_b32 v81, v81, s6, v79
	v_and_or_b32 v80, v80, s6, v78
	v_and_or_b32 v79, v88, s6, v83
	v_and_or_b32 v78, v89, s6, v82
	global_store_dwordx4 v0, v[78:81], s[0:1]
	global_store_dwordx4 v0, v[74:77], s[0:1] offset:1024
	s_waitcnt vmcnt(24)
	s_and_saveexec_b64 s[0:1], s[38:39]
	s_xor_b64 s[0:1], exec, s[0:1]
	s_cbranch_execz .LBB0_249
; __device__ __forceinline__ void unpack8(const v4u w, float* f) { f[0] = bflo(w.x); f[1] = bfhi(w.x); f[2] = bflo(w.y); f[3] = bfhi(w.y); f[4] = bflo(w.z); f[5] = bfhi(w.z); f[6] = bflo(w.w); f[7] = bfhi(w.w); }
; __device__ __forceinline__ void norm_compute(const NormRow& R, int lane, v4u& ya, v4u& yc) {
;     ...
;     if (lane < 16) unpack8(R.oc, fc);
;     else { float f0[8], f1[8], f2[8]; unpack8(R.d0, f0); unpack8(R.d1, f1); unpack8(R.d2, f2);
;         const float inv = 1.0f / (R.l0 + R.l1 + R.l2);
; #pragma unroll
;         for (int e = 0; e < 8; ++e) fc[e] = (f0[e] + f1[e] + f2[e]) * inv; }
;     float sa = 0.f, sc = 0.f;
; #pragma unroll
;     for (int e = 0; e < 8; ++e) { sa += fa[e] * fa[e]; sc += fc[e] * fc[e]; }
;     const float s_moba = wave_sum(lane < 32 ? sa : 0.f), s_fox = wave_sum((lane >= 32 ? sa : 0.f) + (lane < 16 ? sc : 0.f)), s_dil = wave_sum(lane >= 16 ? sc : 0.f);
;     const float r_moba = 1.0f / sqrtf(s_moba * (1.0f / 256.0f) + EPS), r_fox = 1.0f / sqrtf(s_fox * (1.0f / 384.0f) + EPS), r_dil = 1.0f / sqrtf(s_dil * (1.0f / 384.0f) + EPS);
;     float ga[8], gc[8];
; #pragma unroll
;     for (int e = 0; e < 8; ++e) { ga[e] = 1.f; gc[e] = 1.f; }
;     if (lane >= 32) unpack8(R.ga, ga);
;     if (lane < 16) unpack8(R.gc, gc);
	v_add_f32_e32 v71, v171, v170
	v_add_f32_e32 v74, v172, v71
	v_div_scale_f32 v75, s[6:7], v74, v74, 1.0
	v_rcp_f32_e32 v76, v75
	v_lshlrev_b32_e32 v70, 16, v61
	v_and_b32_e32 v71, 0xffff0000, v61
	v_lshlrev_b32_e32 v72, 16, v65
	v_fma_f32 v61, -v75, v76, 1.0
	v_fmac_f32_e32 v76, v61, v76
	v_div_scale_f32 v61, vcc, 1.0, v74, 1.0
	v_and_b32_e32 v73, 0xffff0000, v65
	v_mul_f32_e32 v65, v61, v76
	v_fma_f32 v77, -v75, v65, v61
	v_fmac_f32_e32 v65, v77, v76
	v_fma_f32 v61, -v75, v65, v61
	v_div_fmas_f32 v61, v61, v76, v65
	v_div_fixup_f32 v76, v61, v74, 1.0
	v_lshlrev_b32_e32 v74, 16, v58
	v_and_b32_e32 v75, 0xffff0000, v58
	v_lshlrev_b32_e32 v78, 16, v62
	v_and_b32_e32 v79, 0xffff0000, v62
	v_lshlrev_b32_e32 v58, 16, v59
	v_and_b32_e32 v59, 0xffff0000, v59
	v_lshlrev_b32_e32 v62, 16, v63
	v_and_b32_e32 v63, 0xffff0000, v63
	v_lshlrev_b32_e32 v80, 16, v66
	v_and_b32_e32 v81, 0xffff0000, v66
	v_pk_add_f32 v[74:75], v[78:79], v[74:75]
	v_lshlrev_b32_e32 v66, 16, v67
	v_and_b32_e32 v67, 0xffff0000, v67
	v_pk_add_f32 v[58:59], v[62:63], v[58:59]
	v_pk_add_f32 v[74:75], v[74:75], v[80:81]
	v_pk_add_f32 v[58:59], v[58:59], v[66:67]
	v_pk_mul_f32 v[82:83], v[76:77], v[74:75] op_sel_hi:[0,1]
	v_pk_mul_f32 v[74:75], v[76:77], v[58:59] op_sel_hi:[0,1]
	v_lshlrev_b32_e32 v58, 16, v60
	v_and_b32_e32 v59, 0xffff0000, v60
	v_lshlrev_b32_e32 v60, 16, v64
	v_and_b32_e32 v61, 0xffff0000, v64
	v_lshlrev_b32_e32 v62, 16, v68
	v_and_b32_e32 v63, 0xffff0000, v68
	v_pk_add_f32 v[58:59], v[60:61], v[58:59]
	v_lshlrev_b32_e32 v60, 16, v69
	v_pk_add_f32 v[58:59], v[58:59], v[62:63]
	v_and_b32_e32 v61, 0xffff0000, v69
	v_pk_add_f32 v[62:63], v[72:73], v[70:71]
	v_pk_mul_f32 v[58:59], v[76:77], v[58:59] op_sel_hi:[0,1]
	v_pk_add_f32 v[60:61], v[62:63], v[60:61]
	v_mov_b32_e32 v78, v58
	v_pk_mul_f32 v[76:77], v[76:77], v[60:61] op_sel_hi:[0,1]
	v_mov_b32_e32 v79, v76
	v_mov_b32_e32 v76, v59
	v_mov_b32_e32 v81, v74
	v_mov_b32_e32 v74, v83
	v_mov_b32_e32 v80, v82
.LBB0_249:
	s_andn2_saveexec_b64 s[0:1], s[0:1]
	v_lshlrev_b32_e32 v80, 16, v70
	v_and_b32_e32 v74, 0xffff0000, v70
	v_lshlrev_b32_e32 v81, 16, v71
	v_and_b32_e32 v75, 0xffff0000, v71
	v_lshlrev_b32_e32 v78, 16, v72
	v_and_b32_e32 v76, 0xffff0000, v72
	v_lshlrev_b32_e32 v79, 16, v73
	v_and_b32_e32 v77, 0xffff0000, v73
	s_or_b64 exec, exec, s[0:1]
	v_lshlrev_b32_e32 v61, 16, v103
	v_lshlrev_b32_e32 v60, 16, v102
	v_and_b32_e32 v63, 0xffff0000, v103
	v_and_b32_e32 v62, 0xffff0000, v102
	v_pk_mul_f32 v[66:67], v[60:61], v[60:61]
	v_pk_mul_f32 v[68:69], v[62:63], v[62:63]
	v_mul_f32_e32 v82, v74, v74
	v_fmac_f32_e32 v82, v80, v80
	v_add_f32_e32 v66, v66, v68
	v_lshlrev_b32_e32 v59, 16, v105
	v_lshlrev_b32_e32 v58, 16, v104
	v_fmac_f32_e32 v82, v81, v81
	v_add_f32_e32 v66, v67, v66
	v_and_b32_e32 v65, 0xffff0000, v105
	v_and_b32_e32 v64, 0xffff0000, v104
	v_fmac_f32_e32 v82, v75, v75
	v_pk_mul_f32 v[70:71], v[58:59], v[58:59]
	v_add_f32_e32 v66, v69, v66
	v_fmac_f32_e32 v82, v78, v78
	v_pk_mul_f32 v[72:73], v[64:65], v[64:65]
	v_add_f32_e32 v66, v70, v66
	v_fmac_f32_e32 v82, v76, v76
	v_add_f32_e32 v66, v72, v66
	v_fmac_f32_e32 v82, v79, v79
	v_add_f32_e32 v66, v71, v66
	v_add_f32_e32 v66, v73, v66
	v_fmac_f32_e32 v82, v77, v77
	v_cndmask_b32_e64 v67, 0, v66, s[40:41]
	v_cndmask_b32_e64 v66, 0, v66, s[36:37]
	v_cndmask_b32_e64 v69, 0, v82, s[34:35]
	v_add_f32_e32 v66, v66, v69
	v_cndmask_b32_e64 v70, 0, v82, s[42:43]
	v_mov_b32_e32 v82, 1.0
	v_mov_b32_e32 v72, 1.0
	s_nop 1
	v_add_f32_dpp v67, v67, v67 quad_perm:[1,0,3,2] row_mask:0xf bank_mask:0xf
	s_nop 1
	v_add_f32_dpp v66, v66, v66 quad_perm:[1,0,3,2] row_mask:0xf bank_mask:0xf
	s_nop 1
	v_add_f32_dpp v70, v70, v70 quad_perm:[1,0,3,2] row_mask:0xf bank_mask:0xf
	v_mov_b32_e32 v73, 1.0
	s_nop 1
	v_add_f32_dpp v67, v67, v67 quad_perm:[2,3,0,1] row_mask:0xf bank_mask:0xf
	s_nop 1
	v_add_f32_dpp v66, v66, v66 quad_perm:[2,3,0,1] row_mask:0xf bank_mask:0xf
	s_nop 1
	v_add_f32_dpp v70, v70, v70 quad_perm:[2,3,0,1] row_mask:0xf bank_mask:0xf
	s_nop 1
	v_add_f32_dpp v67, v67, v67 row_half_mirror row_mask:0xf bank_mask:0xf
	s_nop 1
	v_add_f32_dpp v66, v66, v66 row_half_mirror row_mask:0xf bank_mask:0xf
	s_nop 1
	v_add_f32_dpp v70, v70, v70 row_half_mirror row_mask:0xf bank_mask:0xf
	s_nop 1
	v_add_f32_dpp v67, v67, v67 row_mirror row_mask:0xf bank_mask:0xf
	s_nop 1
	v_add_f32_dpp v66, v66, v66 row_mirror row_mask:0xf bank_mask:0xf
	s_nop 1
	v_add_f32_dpp v70, v70, v70 row_mirror row_mask:0xf bank_mask:0xf
	v_mov_b32_e32 v68, v67
	s_nop 1
	v_permlane16_swap_b32_e32 v67, v68
	v_add_f32_e32 v86, v67, v68
	v_mov_b32_e32 v69, v66
	s_nop 1
	v_permlane16_swap_b32_e32 v66, v69
	v_add_f32_e32 v90, v66, v69
	v_mov_b32_e32 v71, v70
	s_nop 1
	v_permlane16_swap_b32_e32 v70, v71
	v_add_f32_e32 v88, v70, v71
	v_mov_b32_e32 v68, 1.0
	v_mov_b32_e32 v69, 1.0
	v_mov_b32_e32 v66, 1.0
	v_mov_b32_e32 v70, 1.0
	v_mov_b32_e32 v67, 1.0
	v_mov_b32_e32 v71, 1.0
	s_and_saveexec_b64 s[0:1], s[36:37]
	v_lshlrev_b32_e32 v68, 16, v54
	v_and_b32_e32 v72, 0xffff0000, v54
	v_lshlrev_b32_e32 v69, 16, v55
	v_and_b32_e32 v73, 0xffff0000, v55
	v_lshlrev_b32_e32 v66, 16, v56
	v_and_b32_e32 v70, 0xffff0000, v56
	v_lshlrev_b32_e32 v67, 16, v57
	v_and_b32_e32 v71, 0xffff0000, v57
	s_or_b64 exec, exec, s[0:1]
	v_mov_b32_e32 v84, 1.0
	v_mov_b32_e32 v83, 1.0
	v_mov_b32_e32 v85, 1.0
	v_mov_b32_e32 v54, 1.0
	v_mov_b32_e32 v56, 1.0
	v_mov_b32_e32 v55, 1.0
	v_mov_b32_e32 v57, 1.0
	s_and_saveexec_b64 s[0:1], s[34:35]
	v_lshlrev_b32_e32 v82, 16, v50
	v_and_b32_e32 v84, 0xffff0000, v50
	v_lshlrev_b32_e32 v83, 16, v51
	v_and_b32_e32 v85, 0xffff0000, v51
	v_lshlrev_b32_e32 v54, 16, v52
	v_and_b32_e32 v56, 0xffff0000, v52
; __device__ __forceinline__ unsigned pk2(float lo, float hi) { return f2bf(lo) | (f2bf(hi) << 16); }
; __device__ __forceinline__ void unpack8(const v4u w, float* f) { f[0] = bflo(w.x); f[1] = bfhi(w.x); f[2] = bflo(w.y); f[3] = bfhi(w.y); f[4] = bflo(w.z); f[5] = bfhi(w.z); f[6] = bflo(w.w); f[7] = bfhi(w.w); }
; __device__ __forceinline__ void norm_compute(const NormRow& R, int lane, v4u& ya, v4u& yc) {
;     ...
;     for (int e = 0; e < 8; ++e) { sa += fa[e] * fa[e]; sc += fc[e] * fc[e]; }
;     const float s_moba = wave_sum(lane < 32 ? sa : 0.f), s_fox = wave_sum((lane >= 32 ? sa : 0.f) + (lane < 16 ? sc : 0.f)), s_dil = wave_sum(lane >= 16 ? sc : 0.f);
;     const float r_moba = 1.0f / sqrtf(s_moba * (1.0f / 256.0f) + EPS), r_fox = 1.0f / sqrtf(s_fox * (1.0f / 384.0f) + EPS), r_dil = 1.0f / sqrtf(s_dil * (1.0f / 384.0f) + EPS);
;     float ga[8], gc[8];
; #pragma unroll
;     for (int e = 0; e < 8; ++e) { ga[e] = 1.f; gc[e] = 1.f; }
;     if (lane >= 32) unpack8(R.ga, ga);
;     if (lane < 16) unpack8(R.gc, gc);
;     const float ra = lane < 32 ? r_moba : r_fox, rc = lane < 16 ? r_fox : r_dil;
;     ya.x = pk2(fa[0] * ra * ga[0], fa[1] * ra * ga[1]); ya.y = pk2(fa[2] * ra * ga[2], fa[3] * ra * ga[3]); ya.z = pk2(fa[4] * ra * ga[4], fa[5] * ra * ga[5]); ya.w = pk2(fa[6] * ra * ga[6], fa[7] * ra * ga[7]);
;     yc.x = pk2(fc[0] * rc * gc[0], fc[1] * rc * gc[1]); yc.y = pk2(fc[2] * rc * gc[2], fc[3] * rc * gc[3]); yc.z = pk2(fc[4] * rc * gc[4], fc[5] * rc * gc[5]); yc.w = pk2(fc[6] * rc * gc[6], fc[7] * rc * gc[7]);
; }
	v_lshlrev_b32_e32 v55, 16, v53
	v_and_b32_e32 v57, 0xffff0000, v53
	s_or_b64 exec, exec, s[0:1]
	v_mov_b32_e32 v91, v90
	s_nop 1
	v_permlane32_swap_b32_e32 v90, v91
	v_add_f32_e32 v50, v90, v91
	v_fmamk_f32 v50, v50, 0x3b2aaaab, v215
	v_cmp_gt_f32_e32 vcc, s3, v50
	v_mul_f32_e32 v51, 0x4f800000, v50
	s_movk_i32 s7, 0x7fff
	v_cndmask_b32_e32 v50, v50, v51, vcc
	v_sqrt_f32_e32 v51, v50
	s_mov_b32 s6, 0xffff0000
	v_add_u32_e32 v52, -1, v51
	v_fma_f32 v53, -v52, v51, v50
	v_cmp_ge_f32_e64 s[0:1], 0, v53
	v_add_u32_e32 v53, 1, v51
	s_nop 0
	v_cndmask_b32_e64 v52, v51, v52, s[0:1]
	v_fma_f32 v51, -v53, v51, v50
	v_cmp_lt_f32_e64 s[0:1], 0, v51
	s_nop 1
	v_cndmask_b32_e64 v51, v52, v53, s[0:1]
	v_mul_f32_e32 v52, 0x37800000, v51
	v_cndmask_b32_e32 v51, v51, v52, vcc
	v_cmp_class_f32_e32 vcc, v50, v216
	s_nop 1
	v_cndmask_b32_e32 v50, v51, v50, vcc
	v_div_scale_f32 v51, s[0:1], v50, v50, 1.0
	v_rcp_f32_e32 v52, v51
	s_nop 0
	v_fma_f32 v53, -v51, v52, 1.0
	v_fmac_f32_e32 v52, v53, v52
	v_div_scale_f32 v53, vcc, 1.0, v50, 1.0
	v_mul_f32_e32 v90, v53, v52
	v_fma_f32 v91, -v51, v90, v53
	v_fmac_f32_e32 v90, v91, v52
	v_fma_f32 v51, -v51, v90, v53
	v_div_fmas_f32 v51, v51, v52, v90
	v_div_fixup_f32 v90, v51, v50, 1.0
	v_mov_b32_e32 v89, v88
	s_nop 1
	v_permlane32_swap_b32_e32 v88, v89
	v_add_f32_e32 v50, v88, v89
	v_fmamk_f32 v50, v50, 0x3b2aaaab, v215
	v_cmp_gt_f32_e32 vcc, s3, v50
	v_mul_f32_e32 v51, 0x4f800000, v50
	s_nop 0
	v_cndmask_b32_e32 v50, v50, v51, vcc
	v_sqrt_f32_e32 v51, v50
	s_nop 0
	v_add_u32_e32 v52, -1, v51
	v_fma_f32 v53, -v52, v51, v50
	v_cmp_ge_f32_e64 s[0:1], 0, v53
	v_add_u32_e32 v53, 1, v51
	s_nop 0
	v_cndmask_b32_e64 v52, v51, v52, s[0:1]
	v_fma_f32 v51, -v53, v51, v50
	v_cmp_lt_f32_e64 s[0:1], 0, v51
	s_nop 1
	v_cndmask_b32_e64 v51, v52, v53, s[0:1]
	v_mul_f32_e32 v52, 0x37800000, v51
	v_cndmask_b32_e32 v51, v51, v52, vcc
	v_cmp_class_f32_e32 vcc, v50, v216
	s_nop 1
	v_cndmask_b32_e32 v50, v51, v50, vcc
	v_div_scale_f32 v51, s[0:1], v50, v50, 1.0
	v_rcp_f32_e32 v52, v51
	s_nop 0
	v_fma_f32 v53, -v51, v52, 1.0
	v_fmac_f32_e32 v52, v53, v52
	v_div_scale_f32 v53, vcc, 1.0, v50, 1.0
	v_mul_f32_e32 v88, v53, v52
	v_fma_f32 v89, -v51, v88, v53
	v_fmac_f32_e32 v88, v89, v52
	v_fma_f32 v51, -v51, v88, v53
	v_div_fmas_f32 v51, v51, v52, v88
	v_div_fixup_f32 v50, v51, v50, 1.0
	v_cndmask_b32_e64 v50, v50, v90, s[34:35]
	v_pk_mul_f32 v[52:53], v[74:75], v[50:51] op_sel_hi:[1,0]
	v_pk_mul_f32 v[76:77], v[76:77], v[50:51] op_sel_hi:[1,0]
	v_pk_mul_f32 v[52:53], v[52:53], v[84:85]
	v_pk_mul_f32 v[74:75], v[80:81], v[50:51] op_sel_hi:[1,0]
	v_pk_mul_f32 v[56:57], v[76:77], v[56:57]
	v_pk_mul_f32 v[50:51], v[78:79], v[50:51] op_sel_hi:[1,0]
	v_pk_mul_f32 v[74:75], v[74:75], v[82:83]
	v_pk_mul_f32 v[50:51], v[50:51], v[54:55]
	v_bfe_u32 v54, v57, 16, 1
	v_bfe_u32 v55, v56, 16, 1
	v_bfe_u32 v76, v53, 16, 1
	v_bfe_u32 v77, v52, 16, 1
	v_add3_u32 v77, v52, v77, s7
	v_add3_u32 v76, v53, v76, s7
	v_add3_u32 v52, v56, v55, s7
	v_add3_u32 v53, v57, v54, s7
	v_bfe_u32 v54, v74, 16, 1
	v_bfe_u32 v56, v50, 16, 1
	v_add3_u32 v50, v50, v56, s7
	v_add3_u32 v54, v74, v54, s7
	v_bfe_u32 v55, v75, 16, 1
	v_bfe_u32 v57, v51, 16, 1
	v_lshrrev_b32_e32 v54, 16, v54
	v_lshrrev_b32_e32 v50, 16, v50
	v_add3_u32 v51, v51, v57, s7
	v_add3_u32 v55, v75, v55, s7
	v_and_or_b32 v52, v52, s6, v50
	v_and_or_b32 v50, v77, s6, v54
	v_mov_b32_e32 v87, v86
	s_nop 1
	v_permlane32_swap_b32_e32 v86, v87
	v_add_f32_e32 v54, v86, v87
	v_lshrrev_b32_e32 v55, 16, v55
	v_lshrrev_b32_e32 v51, 16, v51
	v_fmamk_f32 v54, v54, 0x3b800000, v215
	v_and_or_b32 v53, v53, s6, v51
	v_and_or_b32 v51, v76, s6, v55
	v_cmp_gt_f32_e32 vcc, s3, v54
	v_mul_f32_e32 v55, 0x4f800000, v54
	s_nop 0
	v_cndmask_b32_e32 v54, v54, v55, vcc
	v_sqrt_f32_e32 v55, v54
	s_nop 0
	v_add_u32_e32 v56, -1, v55
	v_fma_f32 v57, -v56, v55, v54
	v_cmp_ge_f32_e64 s[0:1], 0, v57
	v_add_u32_e32 v57, 1, v55
	s_nop 0
	v_cndmask_b32_e64 v56, v55, v56, s[0:1]
	v_fma_f32 v55, -v57, v55, v54
	v_cmp_lt_f32_e64 s[0:1], 0, v55
	s_nop 1
	v_cndmask_b32_e64 v55, v56, v57, s[0:1]
	v_mul_f32_e32 v56, 0x37800000, v55
	v_cndmask_b32_e32 v55, v55, v56, vcc
	v_cmp_class_f32_e32 vcc, v54, v216
	s_nop 1
	v_cndmask_b32_e32 v54, v55, v54, vcc
	v_div_scale_f32 v55, s[0:1], v54, v54, 1.0
	v_rcp_f32_e32 v56, v55
	s_add_u32 s0, s24, s10
	s_addc_u32 s1, s25, s11
	v_fma_f32 v57, -v55, v56, 1.0
	v_fmac_f32_e32 v56, v57, v56
	v_div_scale_f32 v57, vcc, 1.0, v54, 1.0
	v_mul_f32_e32 v74, v57, v56
	v_fma_f32 v75, -v55, v74, v57
	v_fmac_f32_e32 v74, v75, v56
	v_fma_f32 v55, -v55, v74, v57
	v_div_fmas_f32 v55, v55, v56, v74
	v_div_fixup_f32 v54, v55, v54, 1.0
	v_cndmask_b32_e64 v54, v90, v54, s[40:41]
	v_pk_mul_f32 v[56:57], v[54:55], v[62:63] op_sel_hi:[0,1]
	v_pk_mul_f32 v[62:63], v[54:55], v[64:65] op_sel_hi:[0,1]
	v_pk_mul_f32 v[56:57], v[56:57], v[72:73]
	v_pk_mul_f32 v[60:61], v[54:55], v[60:61] op_sel_hi:[0,1]
	v_pk_mul_f32 v[62:63], v[62:63], v[70:71]
	v_pk_mul_f32 v[54:55], v[54:55], v[58:59] op_sel_hi:[0,1]
	v_pk_mul_f32 v[60:61], v[60:61], v[68:69]
	v_pk_mul_f32 v[54:55], v[54:55], v[66:67]
	v_bfe_u32 v58, v63, 16, 1
	v_bfe_u32 v59, v62, 16, 1
	v_bfe_u32 v64, v57, 16, 1
	v_bfe_u32 v65, v56, 16, 1
	v_add3_u32 v65, v56, v65, s7
	v_add3_u32 v64, v57, v64, s7
	v_add3_u32 v56, v62, v59, s7
	v_add3_u32 v57, v63, v58, s7
	v_bfe_u32 v58, v60, 16, 1
	v_bfe_u32 v59, v61, 16, 1
	v_bfe_u32 v62, v54, 16, 1
	v_bfe_u32 v63, v55, 16, 1
	v_add3_u32 v55, v55, v63, s7
	v_add3_u32 v54, v54, v62, s7
	v_add3_u32 v59, v61, v59, s7
	v_add3_u32 v58, v60, v58, s7
	v_lshrrev_b32_e32 v58, 16, v58
	v_lshrrev_b32_e32 v59, 16, v59
	v_lshrrev_b32_e32 v54, 16, v54
	v_lshrrev_b32_e32 v55, 16, v55
	v_and_or_b32 v57, v57, s6, v55
	v_and_or_b32 v56, v56, s6, v54
	v_and_or_b32 v55, v64, s6, v59
	v_and_or_b32 v54, v65, s6, v58
	global_store_dwordx4 v0, v[54:57], s[0:1]
	global_store_dwordx4 v0, v[50:53], s[0:1] offset:1024
	s_waitcnt vmcnt(14)
	s_and_saveexec_b64 s[0:1], s[38:39]
	s_xor_b64 s[0:1], exec, s[0:1]
	s_cbranch_execz .LBB0_257
; __device__ __forceinline__ void unpack8(const v4u w, float* f) { f[0] = bflo(w.x); f[1] = bfhi(w.x); f[2] = bflo(w.y); f[3] = bfhi(w.y); f[4] = bflo(w.z); f[5] = bfhi(w.z); f[6] = bflo(w.w); f[7] = bfhi(w.w); }
; __device__ __forceinline__ void norm_compute(const NormRow& R, int lane, v4u& ya, v4u& yc) {
;     ...
;     if (lane < 16) unpack8(R.oc, fc);
;     else { float f0[8], f1[8], f2[8]; unpack8(R.d0, f0); unpack8(R.d1, f1); unpack8(R.d2, f2);
;         const float inv = 1.0f / (R.l0 + R.l1 + R.l2);
; #pragma unroll
;         for (int e = 0; e < 8; ++e) fc[e] = (f0[e] + f1[e] + f2[e]) * inv; }
;     float sa = 0.f, sc = 0.f;
; #pragma unroll
;     for (int e = 0; e < 8; ++e) { sa += fa[e] * fa[e]; sc += fc[e] * fc[e]; }
;     const float s_moba = wave_sum(lane < 32 ? sa : 0.f), s_fox = wave_sum((lane >= 32 ? sa : 0.f) + (lane < 16 ? sc : 0.f)), s_dil = wave_sum(lane >= 16 ? sc : 0.f);
;     const float r_moba = 1.0f / sqrtf(s_moba * (1.0f / 256.0f) + EPS), r_fox = 1.0f / sqrtf(s_fox * (1.0f / 384.0f) + EPS), r_dil = 1.0f / sqrtf(s_dil * (1.0f / 384.0f) + EPS);
;     float ga[8], gc[8];
; #pragma unroll
;     for (int e = 0; e < 8; ++e) { ga[e] = 1.f; gc[e] = 1.f; }
;     if (lane >= 32) unpack8(R.ga, ga);
;     if (lane < 16) unpack8(R.gc, gc);
	v_add_f32_e32 v47, v168, v167
	v_add_f32_e32 v50, v169, v47
	v_div_scale_f32 v51, s[6:7], v50, v50, 1.0
	v_rcp_f32_e32 v52, v51
	v_lshlrev_b32_e32 v46, 16, v37
	v_and_b32_e32 v47, 0xffff0000, v37
	v_lshlrev_b32_e32 v48, 16, v41
	v_fma_f32 v37, -v51, v52, 1.0
	v_fmac_f32_e32 v52, v37, v52
	v_div_scale_f32 v37, vcc, 1.0, v50, 1.0
	v_and_b32_e32 v49, 0xffff0000, v41
	v_mul_f32_e32 v41, v37, v52
	v_fma_f32 v53, -v51, v41, v37
	v_fmac_f32_e32 v41, v53, v52
	v_fma_f32 v37, -v51, v41, v37
	v_div_fmas_f32 v37, v37, v52, v41
	v_div_fixup_f32 v52, v37, v50, 1.0
	v_lshlrev_b32_e32 v50, 16, v34
	v_and_b32_e32 v51, 0xffff0000, v34
	v_lshlrev_b32_e32 v54, 16, v38
	v_and_b32_e32 v55, 0xffff0000, v38
	v_lshlrev_b32_e32 v34, 16, v35
	v_and_b32_e32 v35, 0xffff0000, v35
	v_lshlrev_b32_e32 v38, 16, v39
	v_and_b32_e32 v39, 0xffff0000, v39
	v_lshlrev_b32_e32 v56, 16, v42
	v_and_b32_e32 v57, 0xffff0000, v42
	v_pk_add_f32 v[50:51], v[54:55], v[50:51]
	v_lshlrev_b32_e32 v42, 16, v43
	v_and_b32_e32 v43, 0xffff0000, v43
	v_pk_add_f32 v[34:35], v[38:39], v[34:35]
	v_pk_add_f32 v[50:51], v[50:51], v[56:57]
	v_pk_add_f32 v[34:35], v[34:35], v[42:43]
	v_pk_mul_f32 v[58:59], v[52:53], v[50:51] op_sel_hi:[0,1]
	v_pk_mul_f32 v[50:51], v[52:53], v[34:35] op_sel_hi:[0,1]
	v_lshlrev_b32_e32 v34, 16, v36
	v_and_b32_e32 v35, 0xffff0000, v36
	v_lshlrev_b32_e32 v36, 16, v40
	v_and_b32_e32 v37, 0xffff0000, v40
	v_lshlrev_b32_e32 v38, 16, v44
	v_and_b32_e32 v39, 0xffff0000, v44
	v_pk_add_f32 v[34:35], v[36:37], v[34:35]
	v_lshlrev_b32_e32 v36, 16, v45
	v_pk_add_f32 v[34:35], v[34:35], v[38:39]
	v_and_b32_e32 v37, 0xffff0000, v45
	v_pk_add_f32 v[38:39], v[48:49], v[46:47]
	v_pk_mul_f32 v[34:35], v[52:53], v[34:35] op_sel_hi:[0,1]
	v_pk_add_f32 v[36:37], v[38:39], v[36:37]
	v_mov_b32_e32 v54, v34
	v_pk_mul_f32 v[52:53], v[52:53], v[36:37] op_sel_hi:[0,1]
	v_mov_b32_e32 v55, v52
	v_mov_b32_e32 v52, v35
	v_mov_b32_e32 v57, v50
	v_mov_b32_e32 v50, v59
	v_mov_b32_e32 v56, v58
.LBB0_257:
	s_andn2_saveexec_b64 s[0:1], s[0:1]
	v_lshlrev_b32_e32 v56, 16, v46
	v_and_b32_e32 v50, 0xffff0000, v46
	v_lshlrev_b32_e32 v57, 16, v47
	v_and_b32_e32 v51, 0xffff0000, v47
	v_lshlrev_b32_e32 v54, 16, v48
	v_and_b32_e32 v52, 0xffff0000, v48
	v_lshlrev_b32_e32 v55, 16, v49
	v_and_b32_e32 v53, 0xffff0000, v49
	s_or_b64 exec, exec, s[0:1]
	v_lshlrev_b32_e32 v37, 16, v107
	v_lshlrev_b32_e32 v36, 16, v106
	v_and_b32_e32 v39, 0xffff0000, v107
	v_and_b32_e32 v38, 0xffff0000, v106
	v_pk_mul_f32 v[42:43], v[36:37], v[36:37]
	v_pk_mul_f32 v[44:45], v[38:39], v[38:39]
	v_mul_f32_e32 v58, v50, v50
	v_fmac_f32_e32 v58, v56, v56
	v_add_f32_e32 v42, v42, v44
	v_lshlrev_b32_e32 v35, 16, v109
	v_lshlrev_b32_e32 v34, 16, v108
	v_fmac_f32_e32 v58, v57, v57
	v_add_f32_e32 v42, v43, v42
	v_and_b32_e32 v41, 0xffff0000, v109
	v_and_b32_e32 v40, 0xffff0000, v108
	v_fmac_f32_e32 v58, v51, v51
	v_pk_mul_f32 v[46:47], v[34:35], v[34:35]
	v_add_f32_e32 v42, v45, v42
	v_fmac_f32_e32 v58, v54, v54
	v_pk_mul_f32 v[48:49], v[40:41], v[40:41]
	v_add_f32_e32 v42, v46, v42
	v_fmac_f32_e32 v58, v52, v52
	v_add_f32_e32 v42, v48, v42
	v_fmac_f32_e32 v58, v55, v55
	v_add_f32_e32 v42, v47, v42
	v_add_f32_e32 v42, v49, v42
	v_fmac_f32_e32 v58, v53, v53
	v_cndmask_b32_e64 v43, 0, v42, s[40:41]
	v_cndmask_b32_e64 v42, 0, v42, s[36:37]
	v_cndmask_b32_e64 v45, 0, v58, s[34:35]
	v_add_f32_e32 v42, v42, v45
	v_cndmask_b32_e64 v46, 0, v58, s[42:43]
	v_mov_b32_e32 v58, 1.0
	v_mov_b32_e32 v48, 1.0
	s_nop 1
	v_add_f32_dpp v43, v43, v43 quad_perm:[1,0,3,2] row_mask:0xf bank_mask:0xf
	s_nop 1
	v_add_f32_dpp v42, v42, v42 quad_perm:[1,0,3,2] row_mask:0xf bank_mask:0xf
	s_nop 1
	v_add_f32_dpp v46, v46, v46 quad_perm:[1,0,3,2] row_mask:0xf bank_mask:0xf
	v_mov_b32_e32 v49, 1.0
	s_nop 1
	v_add_f32_dpp v43, v43, v43 quad_perm:[2,3,0,1] row_mask:0xf bank_mask:0xf
	s_nop 1
	v_add_f32_dpp v42, v42, v42 quad_perm:[2,3,0,1] row_mask:0xf bank_mask:0xf
	s_nop 1
	v_add_f32_dpp v46, v46, v46 quad_perm:[2,3,0,1] row_mask:0xf bank_mask:0xf
	s_nop 1
	v_add_f32_dpp v43, v43, v43 row_half_mirror row_mask:0xf bank_mask:0xf
	s_nop 1
	v_add_f32_dpp v42, v42, v42 row_half_mirror row_mask:0xf bank_mask:0xf
	s_nop 1
	v_add_f32_dpp v46, v46, v46 row_half_mirror row_mask:0xf bank_mask:0xf
	s_nop 1
	v_add_f32_dpp v43, v43, v43 row_mirror row_mask:0xf bank_mask:0xf
	s_nop 1
	v_add_f32_dpp v42, v42, v42 row_mirror row_mask:0xf bank_mask:0xf
	s_nop 1
	v_add_f32_dpp v46, v46, v46 row_mirror row_mask:0xf bank_mask:0xf
	v_mov_b32_e32 v44, v43
	s_nop 1
	v_permlane16_swap_b32_e32 v43, v44
	v_add_f32_e32 v62, v43, v44
	v_mov_b32_e32 v45, v42
	s_nop 1
	v_permlane16_swap_b32_e32 v42, v45
	v_add_f32_e32 v66, v42, v45
	v_mov_b32_e32 v47, v46
	s_nop 1
	v_permlane16_swap_b32_e32 v46, v47
	v_add_f32_e32 v64, v46, v47
	v_mov_b32_e32 v44, 1.0
	v_mov_b32_e32 v45, 1.0
	v_mov_b32_e32 v42, 1.0
	v_mov_b32_e32 v46, 1.0
	v_mov_b32_e32 v43, 1.0
	v_mov_b32_e32 v47, 1.0
	s_and_saveexec_b64 s[0:1], s[36:37]
	v_lshlrev_b32_e32 v44, 16, v30
	v_and_b32_e32 v48, 0xffff0000, v30
	v_lshlrev_b32_e32 v45, 16, v31
	v_and_b32_e32 v49, 0xffff0000, v31
	v_lshlrev_b32_e32 v42, 16, v32
	v_and_b32_e32 v46, 0xffff0000, v32
	v_lshlrev_b32_e32 v43, 16, v33
	v_and_b32_e32 v47, 0xffff0000, v33
	s_or_b64 exec, exec, s[0:1]
	v_mov_b32_e32 v60, 1.0
	v_mov_b32_e32 v59, 1.0
	v_mov_b32_e32 v61, 1.0
	v_mov_b32_e32 v30, 1.0
	v_mov_b32_e32 v32, 1.0
	v_mov_b32_e32 v31, 1.0
	v_mov_b32_e32 v33, 1.0
	s_and_saveexec_b64 s[0:1], s[34:35]
	v_lshlrev_b32_e32 v58, 16, v26
	v_and_b32_e32 v60, 0xffff0000, v26
	v_lshlrev_b32_e32 v59, 16, v27
	v_and_b32_e32 v61, 0xffff0000, v27
	v_lshlrev_b32_e32 v30, 16, v28
	v_and_b32_e32 v32, 0xffff0000, v28
; __device__ __forceinline__ unsigned pk2(float lo, float hi) { return f2bf(lo) | (f2bf(hi) << 16); }
; __device__ __forceinline__ void unpack8(const v4u w, float* f) { f[0] = bflo(w.x); f[1] = bfhi(w.x); f[2] = bflo(w.y); f[3] = bfhi(w.y); f[4] = bflo(w.z); f[5] = bfhi(w.z); f[6] = bflo(w.w); f[7] = bfhi(w.w); }
; __device__ __forceinline__ void norm_compute(const NormRow& R, int lane, v4u& ya, v4u& yc) {
;     ...
;     for (int e = 0; e < 8; ++e) { sa += fa[e] * fa[e]; sc += fc[e] * fc[e]; }
;     const float s_moba = wave_sum(lane < 32 ? sa : 0.f), s_fox = wave_sum((lane >= 32 ? sa : 0.f) + (lane < 16 ? sc : 0.f)), s_dil = wave_sum(lane >= 16 ? sc : 0.f);
;     const float r_moba = 1.0f / sqrtf(s_moba * (1.0f / 256.0f) + EPS), r_fox = 1.0f / sqrtf(s_fox * (1.0f / 384.0f) + EPS), r_dil = 1.0f / sqrtf(s_dil * (1.0f / 384.0f) + EPS);
;     float ga[8], gc[8];
; #pragma unroll
;     for (int e = 0; e < 8; ++e) { ga[e] = 1.f; gc[e] = 1.f; }
;     if (lane >= 32) unpack8(R.ga, ga);
;     if (lane < 16) unpack8(R.gc, gc);
;     const float ra = lane < 32 ? r_moba : r_fox, rc = lane < 16 ? r_fox : r_dil;
;     ya.x = pk2(fa[0] * ra * ga[0], fa[1] * ra * ga[1]); ya.y = pk2(fa[2] * ra * ga[2], fa[3] * ra * ga[3]); ya.z = pk2(fa[4] * ra * ga[4], fa[5] * ra * ga[5]); ya.w = pk2(fa[6] * ra * ga[6], fa[7] * ra * ga[7]);
;     yc.x = pk2(fc[0] * rc * gc[0], fc[1] * rc * gc[1]); yc.y = pk2(fc[2] * rc * gc[2], fc[3] * rc * gc[3]); yc.z = pk2(fc[4] * rc * gc[4], fc[5] * rc * gc[5]); yc.w = pk2(fc[6] * rc * gc[6], fc[7] * rc * gc[7]);
; }
	v_lshlrev_b32_e32 v31, 16, v29
	v_and_b32_e32 v33, 0xffff0000, v29
	s_or_b64 exec, exec, s[0:1]
	v_mov_b32_e32 v67, v66
	s_nop 1
	v_permlane32_swap_b32_e32 v66, v67
	v_add_f32_e32 v26, v66, v67
	v_fmamk_f32 v26, v26, 0x3b2aaaab, v215
	v_cmp_gt_f32_e32 vcc, s3, v26
	v_mul_f32_e32 v27, 0x4f800000, v26
	s_movk_i32 s7, 0x7fff
	v_cndmask_b32_e32 v26, v26, v27, vcc
	v_sqrt_f32_e32 v27, v26
	s_mov_b32 s6, 0xffff0000
	v_add_u32_e32 v28, -1, v27
	v_fma_f32 v29, -v28, v27, v26
	v_cmp_ge_f32_e64 s[0:1], 0, v29
	v_add_u32_e32 v29, 1, v27
	s_nop 0
	v_cndmask_b32_e64 v28, v27, v28, s[0:1]
	v_fma_f32 v27, -v29, v27, v26
	v_cmp_lt_f32_e64 s[0:1], 0, v27
	s_nop 1
	v_cndmask_b32_e64 v27, v28, v29, s[0:1]
	v_mul_f32_e32 v28, 0x37800000, v27
	v_cndmask_b32_e32 v27, v27, v28, vcc
	v_cmp_class_f32_e32 vcc, v26, v216
	s_nop 1
	v_cndmask_b32_e32 v26, v27, v26, vcc
	v_div_scale_f32 v27, s[0:1], v26, v26, 1.0
	v_rcp_f32_e32 v28, v27
	s_nop 0
	v_fma_f32 v29, -v27, v28, 1.0
	v_fmac_f32_e32 v28, v29, v28
	v_div_scale_f32 v29, vcc, 1.0, v26, 1.0
	v_mul_f32_e32 v66, v29, v28
	v_fma_f32 v67, -v27, v66, v29
	v_fmac_f32_e32 v66, v67, v28
	v_fma_f32 v27, -v27, v66, v29
	v_div_fmas_f32 v27, v27, v28, v66
	v_div_fixup_f32 v66, v27, v26, 1.0
	v_mov_b32_e32 v65, v64
	s_nop 1
	v_permlane32_swap_b32_e32 v64, v65
	v_add_f32_e32 v26, v64, v65
	v_fmamk_f32 v26, v26, 0x3b2aaaab, v215
	v_cmp_gt_f32_e32 vcc, s3, v26
	v_mul_f32_e32 v27, 0x4f800000, v26
	s_nop 0
	v_cndmask_b32_e32 v26, v26, v27, vcc
	v_sqrt_f32_e32 v27, v26
	s_nop 0
	v_add_u32_e32 v28, -1, v27
	v_fma_f32 v29, -v28, v27, v26
	v_cmp_ge_f32_e64 s[0:1], 0, v29
	v_add_u32_e32 v29, 1, v27
	s_nop 0
	v_cndmask_b32_e64 v28, v27, v28, s[0:1]
	v_fma_f32 v27, -v29, v27, v26
	v_cmp_lt_f32_e64 s[0:1], 0, v27
	s_nop 1
	v_cndmask_b32_e64 v27, v28, v29, s[0:1]
	v_mul_f32_e32 v28, 0x37800000, v27
	v_cndmask_b32_e32 v27, v27, v28, vcc
	v_cmp_class_f32_e32 vcc, v26, v216
	s_nop 1
	v_cndmask_b32_e32 v26, v27, v26, vcc
	v_div_scale_f32 v27, s[0:1], v26, v26, 1.0
	v_rcp_f32_e32 v28, v27
	s_nop 0
	v_fma_f32 v29, -v27, v28, 1.0
	v_fmac_f32_e32 v28, v29, v28
	v_div_scale_f32 v29, vcc, 1.0, v26, 1.0
	v_mul_f32_e32 v64, v29, v28
	v_fma_f32 v65, -v27, v64, v29
	v_fmac_f32_e32 v64, v65, v28
	v_fma_f32 v27, -v27, v64, v29
	v_div_fmas_f32 v27, v27, v28, v64
	v_div_fixup_f32 v26, v27, v26, 1.0
	v_cndmask_b32_e64 v26, v26, v66, s[34:35]
	v_pk_mul_f32 v[28:29], v[50:51], v[26:27] op_sel_hi:[1,0]
	v_pk_mul_f32 v[52:53], v[52:53], v[26:27] op_sel_hi:[1,0]
	v_pk_mul_f32 v[28:29], v[28:29], v[60:61]
	v_pk_mul_f32 v[50:51], v[56:57], v[26:27] op_sel_hi:[1,0]
	v_pk_mul_f32 v[32:33], v[52:53], v[32:33]
	v_pk_mul_f32 v[26:27], v[54:55], v[26:27] op_sel_hi:[1,0]
	v_pk_mul_f32 v[50:51], v[50:51], v[58:59]
	v_pk_mul_f32 v[26:27], v[26:27], v[30:31]
	v_bfe_u32 v30, v33, 16, 1
	v_bfe_u32 v31, v32, 16, 1
	v_bfe_u32 v52, v29, 16, 1
	v_bfe_u32 v53, v28, 16, 1
	v_add3_u32 v53, v28, v53, s7
	v_add3_u32 v52, v29, v52, s7
	v_add3_u32 v28, v32, v31, s7
	v_add3_u32 v29, v33, v30, s7
	v_bfe_u32 v30, v50, 16, 1
	v_bfe_u32 v32, v26, 16, 1
	v_add3_u32 v26, v26, v32, s7
	v_add3_u32 v30, v50, v30, s7
	v_bfe_u32 v31, v51, 16, 1
	v_bfe_u32 v33, v27, 16, 1
	v_lshrrev_b32_e32 v30, 16, v30
	v_lshrrev_b32_e32 v26, 16, v26
	v_add3_u32 v27, v27, v33, s7
	v_add3_u32 v31, v51, v31, s7
	v_and_or_b32 v28, v28, s6, v26
	v_and_or_b32 v26, v53, s6, v30
	v_mov_b32_e32 v63, v62
	s_nop 1
	v_permlane32_swap_b32_e32 v62, v63
	v_add_f32_e32 v30, v62, v63
	v_lshrrev_b32_e32 v31, 16, v31
	v_lshrrev_b32_e32 v27, 16, v27
	v_fmamk_f32 v30, v30, 0x3b800000, v215
	v_and_or_b32 v29, v29, s6, v27
	v_and_or_b32 v27, v52, s6, v31
	v_cmp_gt_f32_e32 vcc, s3, v30
	v_mul_f32_e32 v31, 0x4f800000, v30
	s_nop 0
	v_cndmask_b32_e32 v30, v30, v31, vcc
	v_sqrt_f32_e32 v31, v30
	s_nop 0
	v_add_u32_e32 v32, -1, v31
	v_fma_f32 v33, -v32, v31, v30
	v_cmp_ge_f32_e64 s[0:1], 0, v33
	v_add_u32_e32 v33, 1, v31
	s_nop 0
	v_cndmask_b32_e64 v32, v31, v32, s[0:1]
	v_fma_f32 v31, -v33, v31, v30
	v_cmp_lt_f32_e64 s[0:1], 0, v31
	s_nop 1
	v_cndmask_b32_e64 v31, v32, v33, s[0:1]
	v_mul_f32_e32 v32, 0x37800000, v31
	v_cndmask_b32_e32 v31, v31, v32, vcc
	v_cmp_class_f32_e32 vcc, v30, v216
	s_nop 1
	v_cndmask_b32_e32 v30, v31, v30, vcc
	v_div_scale_f32 v31, s[0:1], v30, v30, 1.0
	v_rcp_f32_e32 v32, v31
	s_add_u32 s0, s24, s12
	s_addc_u32 s1, s25, s13
	v_fma_f32 v33, -v31, v32, 1.0
	v_fmac_f32_e32 v32, v33, v32
	v_div_scale_f32 v33, vcc, 1.0, v30, 1.0
	v_mul_f32_e32 v50, v33, v32
	v_fma_f32 v51, -v31, v50, v33
	v_fmac_f32_e32 v50, v51, v32
	v_fma_f32 v31, -v31, v50, v33
	v_div_fmas_f32 v31, v31, v32, v50
	v_div_fixup_f32 v30, v31, v30, 1.0
	v_cndmask_b32_e64 v30, v66, v30, s[40:41]
	v_pk_mul_f32 v[32:33], v[30:31], v[38:39] op_sel_hi:[0,1]
	v_pk_mul_f32 v[38:39], v[30:31], v[40:41] op_sel_hi:[0,1]
	v_pk_mul_f32 v[32:33], v[32:33], v[48:49]
	v_pk_mul_f32 v[36:37], v[30:31], v[36:37] op_sel_hi:[0,1]
	v_pk_mul_f32 v[38:39], v[38:39], v[46:47]
	v_pk_mul_f32 v[30:31], v[30:31], v[34:35] op_sel_hi:[0,1]
	v_pk_mul_f32 v[36:37], v[36:37], v[44:45]
	v_pk_mul_f32 v[30:31], v[30:31], v[42:43]
	v_bfe_u32 v34, v39, 16, 1
	v_bfe_u32 v35, v38, 16, 1
	v_bfe_u32 v40, v33, 16, 1
	v_bfe_u32 v41, v32, 16, 1
	v_add3_u32 v41, v32, v41, s7
	v_add3_u32 v40, v33, v40, s7
	v_add3_u32 v32, v38, v35, s7
	v_add3_u32 v33, v39, v34, s7
	v_bfe_u32 v34, v36, 16, 1
	v_bfe_u32 v35, v37, 16, 1
	v_bfe_u32 v38, v30, 16, 1
	v_bfe_u32 v39, v31, 16, 1
	v_add3_u32 v31, v31, v39, s7
	v_add3_u32 v30, v30, v38, s7
	v_add3_u32 v35, v37, v35, s7
	v_add3_u32 v34, v36, v34, s7
	v_lshrrev_b32_e32 v34, 16, v34
	v_lshrrev_b32_e32 v35, 16, v35
	v_lshrrev_b32_e32 v30, 16, v30
	v_lshrrev_b32_e32 v31, 16, v31
	v_and_or_b32 v33, v33, s6, v31
	v_and_or_b32 v32, v32, s6, v30
	v_and_or_b32 v31, v40, s6, v35
	v_and_or_b32 v30, v41, s6, v34
	global_store_dwordx4 v0, v[30:33], s[0:1]
	global_store_dwordx4 v0, v[26:29], s[0:1] offset:1024
	s_waitcnt vmcnt(4)
	s_and_saveexec_b64 s[0:1], s[38:39]
	s_xor_b64 s[0:1], exec, s[0:1]
	s_cbranch_execz .LBB0_265
; __device__ __forceinline__ void unpack8(const v4u w, float* f) { f[0] = bflo(w.x); f[1] = bfhi(w.x); f[2] = bflo(w.y); f[3] = bfhi(w.y); f[4] = bflo(w.z); f[5] = bfhi(w.z); f[6] = bflo(w.w); f[7] = bfhi(w.w); }
; __device__ __forceinline__ void norm_compute(const NormRow& R, int lane, v4u& ya, v4u& yc) {
;     ...
;     if (lane < 16) unpack8(R.oc, fc);
;     else { float f0[8], f1[8], f2[8]; unpack8(R.d0, f0); unpack8(R.d1, f1); unpack8(R.d2, f2);
;         const float inv = 1.0f / (R.l0 + R.l1 + R.l2);
; #pragma unroll
;         for (int e = 0; e < 8; ++e) fc[e] = (f0[e] + f1[e] + f2[e]) * inv; }
;     float sa = 0.f, sc = 0.f;
; #pragma unroll
;     for (int e = 0; e < 8; ++e) { sa += fa[e] * fa[e]; sc += fc[e] * fc[e]; }
;     const float s_moba = wave_sum(lane < 32 ? sa : 0.f), s_fox = wave_sum((lane >= 32 ? sa : 0.f) + (lane < 16 ? sc : 0.f)), s_dil = wave_sum(lane >= 16 ? sc : 0.f);
;     const float r_moba = 1.0f / sqrtf(s_moba * (1.0f / 256.0f) + EPS), r_fox = 1.0f / sqrtf(s_fox * (1.0f / 384.0f) + EPS), r_dil = 1.0f / sqrtf(s_dil * (1.0f / 384.0f) + EPS);
;     float ga[8], gc[8];
; #pragma unroll
;     for (int e = 0; e < 8; ++e) { ga[e] = 1.f; gc[e] = 1.f; }
;     if (lane >= 32) unpack8(R.ga, ga);
;     if (lane < 16) unpack8(R.gc, gc);
	v_add_f32_e32 v23, v165, v163
	v_add_f32_e32 v26, v166, v23
	v_div_scale_f32 v27, s[6:7], v26, v26, 1.0
	v_rcp_f32_e32 v28, v27
	v_lshlrev_b32_e32 v22, 16, v13
	v_and_b32_e32 v23, 0xffff0000, v13
	v_lshlrev_b32_e32 v24, 16, v17
	v_fma_f32 v13, -v27, v28, 1.0
	v_fmac_f32_e32 v28, v13, v28
	v_div_scale_f32 v13, vcc, 1.0, v26, 1.0
	v_and_b32_e32 v25, 0xffff0000, v17
	v_mul_f32_e32 v17, v13, v28
	v_fma_f32 v29, -v27, v17, v13
	v_fmac_f32_e32 v17, v29, v28
	v_fma_f32 v13, -v27, v17, v13
	v_div_fmas_f32 v13, v13, v28, v17
	v_div_fixup_f32 v28, v13, v26, 1.0
	v_lshlrev_b32_e32 v26, 16, v10
	v_and_b32_e32 v27, 0xffff0000, v10
	v_lshlrev_b32_e32 v30, 16, v14
	v_and_b32_e32 v31, 0xffff0000, v14
	v_lshlrev_b32_e32 v10, 16, v11
	v_and_b32_e32 v11, 0xffff0000, v11
	v_lshlrev_b32_e32 v14, 16, v15
	v_and_b32_e32 v15, 0xffff0000, v15
	v_lshlrev_b32_e32 v32, 16, v18
	v_and_b32_e32 v33, 0xffff0000, v18
	v_pk_add_f32 v[26:27], v[30:31], v[26:27]
	v_lshlrev_b32_e32 v18, 16, v19
	v_and_b32_e32 v19, 0xffff0000, v19
	v_pk_add_f32 v[10:11], v[14:15], v[10:11]
	v_pk_add_f32 v[26:27], v[26:27], v[32:33]
	v_pk_add_f32 v[10:11], v[10:11], v[18:19]
	v_pk_mul_f32 v[34:35], v[28:29], v[26:27] op_sel_hi:[0,1]
	v_pk_mul_f32 v[26:27], v[28:29], v[10:11] op_sel_hi:[0,1]
	v_lshlrev_b32_e32 v10, 16, v12
	v_and_b32_e32 v11, 0xffff0000, v12
	v_lshlrev_b32_e32 v12, 16, v16
	v_and_b32_e32 v13, 0xffff0000, v16
	v_lshlrev_b32_e32 v14, 16, v20
	v_and_b32_e32 v15, 0xffff0000, v20
	v_pk_add_f32 v[10:11], v[12:13], v[10:11]
	v_lshlrev_b32_e32 v12, 16, v21
	v_pk_add_f32 v[10:11], v[10:11], v[14:15]
	v_and_b32_e32 v13, 0xffff0000, v21
	v_pk_add_f32 v[14:15], v[24:25], v[22:23]
	v_pk_mul_f32 v[10:11], v[28:29], v[10:11] op_sel_hi:[0,1]
	v_pk_add_f32 v[12:13], v[14:15], v[12:13]
	v_mov_b32_e32 v30, v10
	v_pk_mul_f32 v[28:29], v[28:29], v[12:13] op_sel_hi:[0,1]
	v_mov_b32_e32 v31, v28
	v_mov_b32_e32 v28, v11
	v_mov_b32_e32 v33, v26
	v_mov_b32_e32 v26, v35
	v_mov_b32_e32 v32, v34
.LBB0_265:
	s_andn2_saveexec_b64 s[0:1], s[0:1]
	v_lshlrev_b32_e32 v32, 16, v22
	v_and_b32_e32 v26, 0xffff0000, v22
	v_lshlrev_b32_e32 v33, 16, v23
	v_and_b32_e32 v27, 0xffff0000, v23
	v_lshlrev_b32_e32 v30, 16, v24
	v_and_b32_e32 v28, 0xffff0000, v24
	v_lshlrev_b32_e32 v31, 16, v25
	v_and_b32_e32 v29, 0xffff0000, v25
	s_or_b64 exec, exec, s[0:1]
	v_lshlrev_b32_e32 v13, 16, v111
	v_lshlrev_b32_e32 v12, 16, v110
	v_and_b32_e32 v15, 0xffff0000, v111
	v_and_b32_e32 v14, 0xffff0000, v110
	v_pk_mul_f32 v[18:19], v[12:13], v[12:13]
	v_pk_mul_f32 v[20:21], v[14:15], v[14:15]
	v_mul_f32_e32 v34, v26, v26
	v_fmac_f32_e32 v34, v32, v32
	v_add_f32_e32 v18, v18, v20
	v_lshlrev_b32_e32 v11, 16, v113
	v_lshlrev_b32_e32 v10, 16, v112
	v_fmac_f32_e32 v34, v33, v33
	v_add_f32_e32 v18, v19, v18
	v_and_b32_e32 v17, 0xffff0000, v113
	v_and_b32_e32 v16, 0xffff0000, v112
	v_fmac_f32_e32 v34, v27, v27
	v_pk_mul_f32 v[22:23], v[10:11], v[10:11]
	v_add_f32_e32 v18, v21, v18
	v_fmac_f32_e32 v34, v30, v30
	v_pk_mul_f32 v[24:25], v[16:17], v[16:17]
	v_add_f32_e32 v18, v22, v18
	v_fmac_f32_e32 v34, v28, v28
	v_add_f32_e32 v18, v24, v18
	v_fmac_f32_e32 v34, v31, v31
	v_add_f32_e32 v18, v23, v18
	v_add_f32_e32 v18, v25, v18
	v_fmac_f32_e32 v34, v29, v29
	v_cndmask_b32_e64 v19, 0, v18, s[40:41]
	v_cndmask_b32_e64 v18, 0, v18, s[36:37]
	v_cndmask_b32_e64 v21, 0, v34, s[34:35]
	v_add_f32_e32 v18, v18, v21
	v_cndmask_b32_e64 v22, 0, v34, s[42:43]
	v_mov_b32_e32 v34, 1.0
	v_mov_b32_e32 v24, 1.0
	s_nop 1
	v_add_f32_dpp v19, v19, v19 quad_perm:[1,0,3,2] row_mask:0xf bank_mask:0xf
	s_nop 1
	v_add_f32_dpp v18, v18, v18 quad_perm:[1,0,3,2] row_mask:0xf bank_mask:0xf
	s_nop 1
	v_add_f32_dpp v22, v22, v22 quad_perm:[1,0,3,2] row_mask:0xf bank_mask:0xf
	v_mov_b32_e32 v25, 1.0
	s_nop 1
	v_add_f32_dpp v19, v19, v19 quad_perm:[2,3,0,1] row_mask:0xf bank_mask:0xf
	s_nop 1
	v_add_f32_dpp v18, v18, v18 quad_perm:[2,3,0,1] row_mask:0xf bank_mask:0xf
	s_nop 1
	v_add_f32_dpp v22, v22, v22 quad_perm:[2,3,0,1] row_mask:0xf bank_mask:0xf
	s_nop 1
	v_add_f32_dpp v19, v19, v19 row_half_mirror row_mask:0xf bank_mask:0xf
	s_nop 1
	v_add_f32_dpp v18, v18, v18 row_half_mirror row_mask:0xf bank_mask:0xf
	s_nop 1
	v_add_f32_dpp v22, v22, v22 row_half_mirror row_mask:0xf bank_mask:0xf
	s_nop 1
	v_add_f32_dpp v19, v19, v19 row_mirror row_mask:0xf bank_mask:0xf
	s_nop 1
	v_add_f32_dpp v18, v18, v18 row_mirror row_mask:0xf bank_mask:0xf
	s_nop 1
	v_add_f32_dpp v22, v22, v22 row_mirror row_mask:0xf bank_mask:0xf
	v_mov_b32_e32 v20, v19
	s_nop 1
	v_permlane16_swap_b32_e32 v19, v20
	v_add_f32_e32 v38, v19, v20
	v_mov_b32_e32 v21, v18
	s_nop 1
	v_permlane16_swap_b32_e32 v18, v21
	v_add_f32_e32 v42, v18, v21
	v_mov_b32_e32 v23, v22
	s_nop 1
	v_permlane16_swap_b32_e32 v22, v23
	v_add_f32_e32 v40, v22, v23
	v_mov_b32_e32 v20, 1.0
	v_mov_b32_e32 v21, 1.0
	v_mov_b32_e32 v18, 1.0
	v_mov_b32_e32 v22, 1.0
	v_mov_b32_e32 v19, 1.0
	v_mov_b32_e32 v23, 1.0
	s_and_saveexec_b64 s[0:1], s[36:37]
	v_lshlrev_b32_e32 v20, 16, v6
	v_and_b32_e32 v24, 0xffff0000, v6
	v_lshlrev_b32_e32 v21, 16, v7
	v_and_b32_e32 v25, 0xffff0000, v7
	v_lshlrev_b32_e32 v18, 16, v8
	v_and_b32_e32 v22, 0xffff0000, v8
	v_lshlrev_b32_e32 v19, 16, v9
	v_and_b32_e32 v23, 0xffff0000, v9
	s_or_b64 exec, exec, s[0:1]
	v_mov_b32_e32 v36, 1.0
	v_mov_b32_e32 v35, 1.0
	v_mov_b32_e32 v37, 1.0
	v_mov_b32_e32 v6, 1.0
	v_mov_b32_e32 v8, 1.0
	v_mov_b32_e32 v7, 1.0
	v_mov_b32_e32 v9, 1.0
	s_and_saveexec_b64 s[0:1], s[34:35]
	v_lshlrev_b32_e32 v34, 16, v2
	v_and_b32_e32 v36, 0xffff0000, v2
	v_lshlrev_b32_e32 v35, 16, v3
	v_and_b32_e32 v37, 0xffff0000, v3
	v_lshlrev_b32_e32 v6, 16, v4
; __device__ __forceinline__ unsigned pk2(float lo, float hi) { return f2bf(lo) | (f2bf(hi) << 16); }
; __device__ __forceinline__ void unpack8(const v4u w, float* f) { f[0] = bflo(w.x); f[1] = bfhi(w.x); f[2] = bflo(w.y); f[3] = bfhi(w.y); f[4] = bflo(w.z); f[5] = bfhi(w.z); f[6] = bflo(w.w); f[7] = bfhi(w.w); }
; __device__ __forceinline__ void norm_compute(const NormRow& R, int lane, v4u& ya, v4u& yc) {
;     ...
;     for (int e = 0; e < 8; ++e) { sa += fa[e] * fa[e]; sc += fc[e] * fc[e]; }
;     const float s_moba = wave_sum(lane < 32 ? sa : 0.f), s_fox = wave_sum((lane >= 32 ? sa : 0.f) + (lane < 16 ? sc : 0.f)), s_dil = wave_sum(lane >= 16 ? sc : 0.f);
;     const float r_moba = 1.0f / sqrtf(s_moba * (1.0f / 256.0f) + EPS), r_fox = 1.0f / sqrtf(s_fox * (1.0f / 384.0f) + EPS), r_dil = 1.0f / sqrtf(s_dil * (1.0f / 384.0f) + EPS);
;     float ga[8], gc[8];
; #pragma unroll
;     for (int e = 0; e < 8; ++e) { ga[e] = 1.f; gc[e] = 1.f; }
;     if (lane >= 32) unpack8(R.ga, ga);
;     if (lane < 16) unpack8(R.gc, gc);
;     const float ra = lane < 32 ? r_moba : r_fox, rc = lane < 16 ? r_fox : r_dil;
;     ya.x = pk2(fa[0] * ra * ga[0], fa[1] * ra * ga[1]); ya.y = pk2(fa[2] * ra * ga[2], fa[3] * ra * ga[3]); ya.z = pk2(fa[4] * ra * ga[4], fa[5] * ra * ga[5]); ya.w = pk2(fa[6] * ra * ga[6], fa[7] * ra * ga[7]);
;     yc.x = pk2(fc[0] * rc * gc[0], fc[1] * rc * gc[1]); yc.y = pk2(fc[2] * rc * gc[2], fc[3] * rc * gc[3]); yc.z = pk2(fc[4] * rc * gc[4], fc[5] * rc * gc[5]); yc.w = pk2(fc[6] * rc * gc[6], fc[7] * rc * gc[7]);
; }
	v_and_b32_e32 v8, 0xffff0000, v4
	v_lshlrev_b32_e32 v7, 16, v5
	v_and_b32_e32 v9, 0xffff0000, v5
	s_or_b64 exec, exec, s[0:1]
	v_mov_b32_e32 v43, v42
	s_nop 1
	v_permlane32_swap_b32_e32 v42, v43
	v_add_f32_e32 v2, v42, v43
	v_fmamk_f32 v2, v2, 0x3b2aaaab, v215
	v_cmp_gt_f32_e32 vcc, s3, v2
	v_mul_f32_e32 v3, 0x4f800000, v2
	s_movk_i32 s7, 0x7fff
	v_cndmask_b32_e32 v2, v2, v3, vcc
	v_sqrt_f32_e32 v3, v2
	s_mov_b32 s6, 0xffff0000
	v_add_u32_e32 v4, -1, v3
	v_fma_f32 v5, -v4, v3, v2
	v_cmp_ge_f32_e64 s[0:1], 0, v5
	v_add_u32_e32 v5, 1, v3
	s_nop 0
	v_cndmask_b32_e64 v4, v3, v4, s[0:1]
	v_fma_f32 v3, -v5, v3, v2
	v_cmp_lt_f32_e64 s[0:1], 0, v3
	s_nop 1
	v_cndmask_b32_e64 v3, v4, v5, s[0:1]
	v_mul_f32_e32 v4, 0x37800000, v3
	v_cndmask_b32_e32 v3, v3, v4, vcc
	v_cmp_class_f32_e32 vcc, v2, v216
	s_nop 1
	v_cndmask_b32_e32 v2, v3, v2, vcc
	v_div_scale_f32 v3, s[0:1], v2, v2, 1.0
	v_rcp_f32_e32 v4, v3
	s_nop 0
	v_fma_f32 v5, -v3, v4, 1.0
	v_fmac_f32_e32 v4, v5, v4
	v_div_scale_f32 v5, vcc, 1.0, v2, 1.0
	v_mul_f32_e32 v42, v5, v4
	v_fma_f32 v43, -v3, v42, v5
	v_fmac_f32_e32 v42, v43, v4
	v_fma_f32 v3, -v3, v42, v5
	v_div_fmas_f32 v3, v3, v4, v42
	v_div_fixup_f32 v42, v3, v2, 1.0
	v_mov_b32_e32 v41, v40
	s_nop 1
	v_permlane32_swap_b32_e32 v40, v41
	v_add_f32_e32 v2, v40, v41
	v_fmamk_f32 v2, v2, 0x3b2aaaab, v215
	v_cmp_gt_f32_e32 vcc, s3, v2
	v_mul_f32_e32 v3, 0x4f800000, v2
	s_nop 0
	v_cndmask_b32_e32 v2, v2, v3, vcc
	v_sqrt_f32_e32 v3, v2
	s_nop 0
	v_add_u32_e32 v4, -1, v3
	v_fma_f32 v5, -v4, v3, v2
	v_cmp_ge_f32_e64 s[0:1], 0, v5
	v_add_u32_e32 v5, 1, v3
	s_nop 0
	v_cndmask_b32_e64 v4, v3, v4, s[0:1]
	v_fma_f32 v3, -v5, v3, v2
	v_cmp_lt_f32_e64 s[0:1], 0, v3
	s_nop 1
	v_cndmask_b32_e64 v3, v4, v5, s[0:1]
	v_mul_f32_e32 v4, 0x37800000, v3
	v_cndmask_b32_e32 v3, v3, v4, vcc
	v_cmp_class_f32_e32 vcc, v2, v216
	s_nop 1
	v_cndmask_b32_e32 v2, v3, v2, vcc
	v_div_scale_f32 v3, s[0:1], v2, v2, 1.0
	v_rcp_f32_e32 v4, v3
	s_nop 0
	v_fma_f32 v5, -v3, v4, 1.0
	v_fmac_f32_e32 v4, v5, v4
	v_div_scale_f32 v5, vcc, 1.0, v2, 1.0
	v_mul_f32_e32 v40, v5, v4
	v_fma_f32 v41, -v3, v40, v5
	v_fmac_f32_e32 v40, v41, v4
	v_fma_f32 v3, -v3, v40, v5
	v_div_fmas_f32 v3, v3, v4, v40
	v_div_fixup_f32 v2, v3, v2, 1.0
	v_cndmask_b32_e64 v2, v2, v42, s[34:35]
	v_pk_mul_f32 v[4:5], v[26:27], v[2:3] op_sel_hi:[1,0]
	v_pk_mul_f32 v[28:29], v[28:29], v[2:3] op_sel_hi:[1,0]
	v_pk_mul_f32 v[4:5], v[4:5], v[36:37]
	v_pk_mul_f32 v[26:27], v[32:33], v[2:3] op_sel_hi:[1,0]
	v_pk_mul_f32 v[8:9], v[28:29], v[8:9]
	v_pk_mul_f32 v[2:3], v[30:31], v[2:3] op_sel_hi:[1,0]
	v_pk_mul_f32 v[26:27], v[26:27], v[34:35]
	v_pk_mul_f32 v[2:3], v[2:3], v[6:7]
	v_bfe_u32 v6, v9, 16, 1
	v_bfe_u32 v7, v8, 16, 1
	v_bfe_u32 v28, v5, 16, 1
	v_bfe_u32 v29, v4, 16, 1
	v_add3_u32 v29, v4, v29, s7
	v_add3_u32 v28, v5, v28, s7
	v_add3_u32 v4, v8, v7, s7
	v_add3_u32 v5, v9, v6, s7
	v_bfe_u32 v6, v26, 16, 1
	v_bfe_u32 v8, v2, 16, 1
	v_add3_u32 v2, v2, v8, s7
	v_add3_u32 v6, v26, v6, s7
	v_bfe_u32 v7, v27, 16, 1
	v_bfe_u32 v9, v3, 16, 1
	v_lshrrev_b32_e32 v6, 16, v6
	v_lshrrev_b32_e32 v2, 16, v2
	v_add3_u32 v3, v3, v9, s7
	v_add3_u32 v7, v27, v7, s7
	v_and_or_b32 v4, v4, s6, v2
	v_and_or_b32 v2, v29, s6, v6
	v_mov_b32_e32 v39, v38
	s_nop 1
	v_permlane32_swap_b32_e32 v38, v39
	v_add_f32_e32 v6, v38, v39
	v_lshrrev_b32_e32 v7, 16, v7
	v_lshrrev_b32_e32 v3, 16, v3
	v_fmamk_f32 v6, v6, 0x3b800000, v215
	v_and_or_b32 v5, v5, s6, v3
	v_and_or_b32 v3, v28, s6, v7
	v_cmp_gt_f32_e32 vcc, s3, v6
	v_mul_f32_e32 v7, 0x4f800000, v6
	s_nop 0
	v_cndmask_b32_e32 v6, v6, v7, vcc
	v_sqrt_f32_e32 v7, v6
	s_nop 0
	v_add_u32_e32 v8, -1, v7
	v_fma_f32 v9, -v8, v7, v6
	v_cmp_ge_f32_e64 s[0:1], 0, v9
	v_add_u32_e32 v9, 1, v7
	s_nop 0
	v_cndmask_b32_e64 v8, v7, v8, s[0:1]
	v_fma_f32 v7, -v9, v7, v6
	v_cmp_lt_f32_e64 s[0:1], 0, v7
	s_nop 1
	v_cndmask_b32_e64 v7, v8, v9, s[0:1]
	v_mul_f32_e32 v8, 0x37800000, v7
	v_cndmask_b32_e32 v7, v7, v8, vcc
	v_cmp_class_f32_e32 vcc, v6, v216
	s_nop 1
	v_cndmask_b32_e32 v6, v7, v6, vcc
	v_div_scale_f32 v7, s[0:1], v6, v6, 1.0
	v_rcp_f32_e32 v8, v7
	s_add_u32 s0, s24, s8
	s_addc_u32 s1, s25, s9
	v_fma_f32 v9, -v7, v8, 1.0
	v_fmac_f32_e32 v8, v9, v8
	v_div_scale_f32 v9, vcc, 1.0, v6, 1.0
	v_mul_f32_e32 v26, v9, v8
	v_fma_f32 v27, -v7, v26, v9
	v_fmac_f32_e32 v26, v27, v8
	v_fma_f32 v7, -v7, v26, v9
	v_div_fmas_f32 v7, v7, v8, v26
	v_div_fixup_f32 v6, v7, v6, 1.0
	v_cndmask_b32_e64 v6, v42, v6, s[40:41]
	v_pk_mul_f32 v[8:9], v[6:7], v[14:15] op_sel_hi:[0,1]
	v_pk_mul_f32 v[14:15], v[6:7], v[16:17] op_sel_hi:[0,1]
	v_pk_mul_f32 v[8:9], v[8:9], v[24:25]
	v_pk_mul_f32 v[12:13], v[6:7], v[12:13] op_sel_hi:[0,1]
	v_pk_mul_f32 v[14:15], v[14:15], v[22:23]
	v_pk_mul_f32 v[6:7], v[6:7], v[10:11] op_sel_hi:[0,1]
	v_pk_mul_f32 v[12:13], v[12:13], v[20:21]
	v_pk_mul_f32 v[6:7], v[6:7], v[18:19]
	v_bfe_u32 v10, v15, 16, 1
	v_bfe_u32 v11, v14, 16, 1
	v_bfe_u32 v16, v9, 16, 1
	v_bfe_u32 v17, v8, 16, 1
	v_add3_u32 v17, v8, v17, s7
	v_add3_u32 v16, v9, v16, s7
	v_add3_u32 v8, v14, v11, s7
	v_add3_u32 v9, v15, v10, s7
	v_bfe_u32 v10, v12, 16, 1
	v_bfe_u32 v11, v13, 16, 1
	v_bfe_u32 v14, v6, 16, 1
	v_bfe_u32 v15, v7, 16, 1
	v_add3_u32 v7, v7, v15, s7
	v_add3_u32 v6, v6, v14, s7
	v_add3_u32 v11, v13, v11, s7
	v_add3_u32 v10, v12, v10, s7
	v_lshrrev_b32_e32 v10, 16, v10
	v_lshrrev_b32_e32 v11, 16, v11
	v_lshrrev_b32_e32 v6, 16, v6
	v_lshrrev_b32_e32 v7, 16, v7
	v_and_or_b32 v9, v9, s6, v7
	v_and_or_b32 v8, v8, s6, v6
	v_and_or_b32 v7, v16, s6, v11
	v_and_or_b32 v6, v17, s6, v10
	global_store_dwordx4 v0, v[6:9], s[0:1]
	global_store_dwordx4 v0, v[2:5], s[0:1] offset:1024
	s_mov_b64 s[0:1], 0
